# adds write-through sc1 on bulk dwordx4 stores (prologue conv, proj/dyn/wout epilogues, prep, scan y, final)
# speedup vs baseline: 1.0047x; 1.0047x over previous
.LBB0_28:
	s_or_b64 exec, exec, s[10:11]
	s_waitcnt lgkmcnt(5)
	v_mul_f32_e32 v7, 0x42000000, v20
	v_mul_f32_e32 v20, 0x42000000, v22
	v_med3_f32 v22, v20, s48, v47
	v_mul_f32_e32 v20, 0x42000000, v23
	v_med3_f32 v23, v20, s48, v47
	v_mov_b32_e32 v20, v1
	v_cvt_pk_fp8_f32 v20, v22, v23
	v_mul_f32_e32 v21, 0x42000000, v21
	v_med3_f32 v7, v7, s48, v47
	v_med3_f32 v21, v21, s48, v47
	v_cvt_pk_fp8_f32 v20, v7, v21 op_sel:[0,0,1]
	s_waitcnt lgkmcnt(1)
	v_mul_f32_e32 v7, 0x42000000, v16
	v_mul_f32_e32 v16, 0x42000000, v18
	v_mul_f32_e32 v18, 0x42000000, v19
	v_med3_f32 v16, v16, s48, v47
	v_med3_f32 v18, v18, s48, v47
	v_mov_b32_e32 v21, v1
	v_cvt_pk_fp8_f32 v21, v16, v18
	v_mul_f32_e32 v16, 0x42000000, v17
	v_med3_f32 v7, v7, s48, v47
	v_med3_f32 v16, v16, s48, v47
	v_cvt_pk_fp8_f32 v21, v7, v16 op_sel:[0,0,1]
	v_mul_f32_e32 v7, 0x42000000, v12
	v_mul_f32_e32 v12, 0x42000000, v14
	v_mul_f32_e32 v14, 0x42000000, v15
	v_med3_f32 v12, v12, s48, v47
	v_med3_f32 v14, v14, s48, v47
	v_mov_b32_e32 v22, v1
	v_cvt_pk_fp8_f32 v22, v12, v14
	v_mul_f32_e32 v12, 0x42000000, v13
	v_med3_f32 v7, v7, s48, v47
	v_med3_f32 v12, v12, s48, v47
	v_cvt_pk_fp8_f32 v22, v7, v12 op_sel:[0,0,1]
	s_waitcnt lgkmcnt(0)
	v_mul_f32_e32 v7, 0x42000000, v8
	v_mul_f32_e32 v8, 0x42000000, v10
	v_mul_f32_e32 v10, 0x42000000, v11
	v_med3_f32 v8, v8, s48, v47
	v_med3_f32 v10, v10, s48, v47
	v_mov_b32_e32 v23, v1
	v_cvt_pk_fp8_f32 v23, v8, v10
	v_mul_f32_e32 v8, 0x42000000, v9
	v_med3_f32 v7, v7, s48, v47
	v_med3_f32 v8, v8, s48, v47
	v_cvt_pk_fp8_f32 v23, v7, v8 op_sel:[0,0,1]
	v_ashrrev_i32_e32 v7, 31, v6
	v_lshlrev_b64 v[6:7], 11, v[6:7]
	v_lshl_add_u64 v[6:7], v[4:5], 0, v[6:7]
	ds_read2_b32 v[8:9], v32 offset1:32
	global_store_dwordx4 v[6:7], v[20:23], off sc1
	ds_read2_b32 v[6:7], v32 offset0:64 offset1:96
	ds_read2_b32 v[10:11], v49 offset1:32
	ds_read2_b32 v[12:13], v49 offset0:64 offset1:96
	s_waitcnt lgkmcnt(3)
	v_mul_f32_e32 v14, 0x42000000, v8
	v_mul_f32_e32 v16, 0x42000000, v9
	s_waitcnt lgkmcnt(2)
	v_mul_f32_e32 v18, 0x42000000, v6
	ds_read2_b32 v[8:9], v32 offset0:128 offset1:160
	v_mul_f32_e32 v20, 0x42000000, v7
	ds_read2_b32 v[6:7], v49 offset0:128 offset1:160
	s_waitcnt lgkmcnt(3)
	v_mul_f32_e32 v15, 0x42000000, v10
	v_mul_f32_e32 v17, 0x42000000, v11
	s_waitcnt lgkmcnt(2)
	v_mul_f32_e32 v19, 0x42000000, v12
	v_mul_f32_e32 v21, 0x42000000, v13
	s_waitcnt lgkmcnt(1)
	v_mul_f32_e32 v8, 0x42000000, v8
	ds_read2_b32 v[10:11], v32 offset0:192 offset1:224
	ds_read2_b32 v[12:13], v49 offset0:192 offset1:224
	s_waitcnt lgkmcnt(2)
	v_mul_f32_e32 v22, 0x42000000, v6
	v_mul_f32_e32 v9, 0x42000000, v9
	v_mul_f32_e32 v23, 0x42000000, v7
	v_med3_f32 v7, v14, s48, v47
	v_med3_f32 v14, v16, s48, v47
	v_mov_b32_e32 v6, v1
	v_cvt_pk_fp8_f32 v6, v7, v14
	v_med3_f32 v8, v8, s48, v47
	v_med3_f32 v9, v9, s48, v47
	v_mov_b32_e32 v7, v1
	v_cvt_pk_fp8_f32 v7, v8, v9
	s_waitcnt lgkmcnt(1)
	v_mul_f32_e32 v10, 0x42000000, v10
	v_mul_f32_e32 v11, 0x42000000, v11
	v_med3_f32 v8, v10, s48, v47
	v_med3_f32 v9, v11, s48, v47
	v_med3_f32 v14, v18, s48, v47
	v_med3_f32 v16, v20, s48, v47
	v_cvt_pk_fp8_f32 v7, v8, v9 op_sel:[0,0,1]
	v_med3_f32 v9, v15, s48, v47
	v_med3_f32 v10, v17, s48, v47
	v_mov_b32_e32 v8, v1
	v_cvt_pk_fp8_f32 v6, v14, v16 op_sel:[0,0,1]
	v_cvt_pk_fp8_f32 v8, v9, v10
	v_med3_f32 v14, v22, s48, v47
	v_med3_f32 v15, v23, s48, v47
	v_mov_b32_e32 v9, v1
	v_cvt_pk_fp8_f32 v9, v14, v15
	s_waitcnt lgkmcnt(0)
	v_mul_f32_e32 v12, 0x42000000, v12
	v_mul_f32_e32 v13, 0x42000000, v13
	v_med3_f32 v10, v19, s48, v47
	v_med3_f32 v11, v21, s48, v47
	v_cvt_pk_fp8_f32 v8, v10, v11 op_sel:[0,0,1]
	v_med3_f32 v10, v12, s48, v47
	v_med3_f32 v11, v13, s48, v47
	v_cvt_pk_fp8_f32 v9, v10, v11 op_sel:[0,0,1]
	v_or_b32_e32 v10, s8, v31
	v_ashrrev_i32_e32 v11, 31, v10
	v_lshlrev_b64 v[10:11], 11, v[10:11]
	v_lshl_add_u64 v[10:11], v[4:5], 0, v[10:11]
	global_store_dwordx4 v[10:11], v[6:9], off sc1
	ds_read2_b32 v[6:7], v35 offset1:32
	ds_read2_b32 v[8:9], v50 offset1:32
	ds_read2_b32 v[10:11], v35 offset0:64 offset1:96
	ds_read2_b32 v[12:13], v50 offset0:64 offset1:96
	ds_read2_b32 v[14:15], v35 offset0:128 offset1:160
	ds_read2_b32 v[16:17], v50 offset0:128 offset1:160
	ds_read2_b32 v[18:19], v35 offset0:192 offset1:224
	ds_read2_b32 v[20:21], v50 offset0:192 offset1:224
	s_waitcnt lgkmcnt(7)
	v_mul_f32_e32 v6, 0x42000000, v6
	v_med3_f32 v23, v6, s48, v47
	v_mul_f32_e32 v6, 0x42000000, v7
	v_med3_f32 v7, v6, s48, v47
	v_mov_b32_e32 v6, v1
	v_cvt_pk_fp8_f32 v6, v23, v7
	s_waitcnt lgkmcnt(5)
	v_mul_f32_e32 v10, 0x42000000, v10
	v_med3_f32 v7, v10, s48, v47
	v_mul_f32_e32 v10, 0x42000000, v11
	v_med3_f32 v10, v10, s48, v47
	v_cvt_pk_fp8_f32 v6, v7, v10 op_sel:[0,0,1]
	s_waitcnt lgkmcnt(3)
	v_mul_f32_e32 v7, 0x42000000, v14
	v_med3_f32 v11, v7, s48, v47
	v_mul_f32_e32 v7, 0x42000000, v15
	v_med3_f32 v14, v7, s48, v47
	v_mov_b32_e32 v7, v1
	v_cvt_pk_fp8_f32 v7, v11, v14
	s_waitcnt lgkmcnt(1)
	v_mul_f32_e32 v10, 0x42000000, v18
	v_mul_f32_e32 v11, 0x42000000, v19
	v_med3_f32 v10, v10, s48, v47
	v_med3_f32 v11, v11, s48, v47
	v_mul_f32_e32 v8, 0x42000000, v8
	v_cvt_pk_fp8_f32 v7, v10, v11 op_sel:[0,0,1]
	v_med3_f32 v11, v8, s48, v47
	v_mul_f32_e32 v8, 0x42000000, v9
	v_med3_f32 v9, v8, s48, v47
	v_mov_b32_e32 v8, v1
	v_cvt_pk_fp8_f32 v8, v11, v9
	v_mul_f32_e32 v10, 0x42000000, v12
	v_med3_f32 v9, v10, s48, v47
	v_mul_f32_e32 v10, 0x42000000, v13
	v_med3_f32 v10, v10, s48, v47
	v_cvt_pk_fp8_f32 v8, v9, v10 op_sel:[0,0,1]
	v_mul_f32_e32 v9, 0x42000000, v16
	v_med3_f32 v11, v9, s48, v47
	v_mul_f32_e32 v9, 0x42000000, v17
	v_med3_f32 v12, v9, s48, v47
	v_mov_b32_e32 v9, v1
	v_cvt_pk_fp8_f32 v9, v11, v12
	s_waitcnt lgkmcnt(0)
	v_mul_f32_e32 v10, 0x42000000, v20
	v_mul_f32_e32 v11, 0x42000000, v21
	v_med3_f32 v10, v10, s48, v47
	v_med3_f32 v11, v11, s48, v47
	v_or_b32_e32 v22, s8, v33
	v_cvt_pk_fp8_f32 v9, v10, v11 op_sel:[0,0,1]
	v_ashrrev_i32_e32 v23, 31, v22
	v_lshlrev_b64 v[10:11], 11, v[22:23]
	v_lshl_add_u64 v[4:5], v[4:5], 0, v[10:11]
	global_store_dwordx4 v[4:5], v[6:9], off sc1
	s_waitcnt lgkmcnt(0)

.LBB0_30:
	s_mul_hi_i32 s4, s67, 0x7a44c6b
	s_lshr_b32 s6, s4, 31
	s_ashr_i32 s4, s4, 7
	s_add_i32 s6, s4, s6
	s_mul_i32 s4, s6, 0xffffef40
	s_add_i32 s10, s67, s4
	s_ashr_i32 s7, s6, 31
	s_cmpk_gt_i32 s10, 0xcbf
	s_mov_b64 s[8:9], -1
	s_cbranch_scc0 .LBB0_32
	s_load_dwordx2 s[8:9], s[14:15], 0x38
	s_lshl_b64 s[18:19], s[6:7], 22
	s_lshl_b64 s[68:69], s[6:7], 24
	s_mul_i32 s4, s6, 0xffffde80
	v_mov_b32_e32 v5, v1
	s_waitcnt lgkmcnt(0)
	s_add_u32 s8, s8, s68
	s_addc_u32 s9, s9, s69
	s_add_u32 s11, s20, s18
	s_addc_u32 s18, s21, s19
	s_add_i32 s4, s26, s4
	s_and_b32 s19, s4, 0x780
	v_or_b32_e32 v4, s19, v24
	s_and_b32 s7, s24, 0x7e0
	v_lshlrev_b32_e32 v4, 13, v4
	v_lshl_add_u64 v[4:5], s[8:9], 0, v[4:5]
	s_lshl_b32 s4, s7, 2
	v_lshl_add_u64 v[4:5], v[4:5], 0, s[4:5]
	v_lshl_add_u64 v[88:89], v[4:5], 0, v[0:1]
	v_add_co_u32_e32 v8, vcc, s28, v88
	s_add_u32 s8, s11, s19
	s_nop 0
	v_addc_co_u32_e32 v9, vcc, 0, v89, vcc
	v_add_co_u32_e32 v12, vcc, s29, v88
	global_load_dwordx4 v[4:7], v[88:89], off
	s_nop 0
	global_load_dwordx4 v[8:11], v[8:9], off
	v_addc_co_u32_e32 v13, vcc, 0, v89, vcc
	v_add_co_u32_e32 v16, vcc, s30, v88
	s_addc_u32 s9, s18, 0
	s_nop 0
	v_addc_co_u32_e32 v17, vcc, 0, v89, vcc
	v_add_co_u32_e32 v20, vcc, s31, v88
	global_load_dwordx4 v[12:15], v[12:13], off
	s_nop 0
	global_load_dwordx4 v[16:19], v[16:17], off
	v_addc_co_u32_e32 v21, vcc, 0, v89, vcc
	v_add_co_u32_e32 v52, vcc, s37, v88
	s_nop 1
	v_addc_co_u32_e32 v53, vcc, 0, v89, vcc
	v_add_co_u32_e32 v56, vcc, s38, v88
	global_load_dwordx4 v[20:23], v[20:21], off
	s_nop 0
	global_load_dwordx4 v[52:55], v[52:53], off
	v_addc_co_u32_e32 v57, vcc, 0, v89, vcc
	v_add_co_u32_e32 v60, vcc, s39, v88
	s_nop 1
	v_addc_co_u32_e32 v61, vcc, 0, v89, vcc
	v_add_co_u32_e32 v64, vcc, s40, v88
	global_load_dwordx4 v[56:59], v[56:57], off
	s_nop 0
	global_load_dwordx4 v[60:63], v[60:61], off
	v_addc_co_u32_e32 v65, vcc, 0, v89, vcc
	v_add_co_u32_e32 v68, vcc, s41, v88
	s_nop 1
	v_addc_co_u32_e32 v69, vcc, 0, v89, vcc
	v_add_co_u32_e32 v72, vcc, s42, v88
	global_load_dwordx4 v[64:67], v[64:65], off
	s_nop 0
	global_load_dwordx4 v[68:71], v[68:69], off
	v_addc_co_u32_e32 v73, vcc, 0, v89, vcc
	v_add_co_u32_e32 v76, vcc, s43, v88
	s_nop 1
	v_addc_co_u32_e32 v77, vcc, 0, v89, vcc
	v_add_co_u32_e32 v80, vcc, s44, v88
	global_load_dwordx4 v[72:75], v[72:73], off
	s_nop 0
	global_load_dwordx4 v[76:79], v[76:77], off
	v_addc_co_u32_e32 v81, vcc, 0, v89, vcc
	v_add_co_u32_e32 v84, vcc, s45, v88
	s_nop 1
	v_addc_co_u32_e32 v85, vcc, 0, v89, vcc
	v_add_co_u32_e32 v90, vcc, s46, v88
	global_load_dwordx4 v[80:83], v[80:81], off
	s_nop 0
	global_load_dwordx4 v[84:87], v[84:85], off
	v_addc_co_u32_e32 v91, vcc, 0, v89, vcc
	v_add_co_u32_e32 v92, vcc, s47, v88
	s_nop 1
	v_addc_co_u32_e32 v93, vcc, 0, v89, vcc
	global_load_dwordx4 v[88:91], v[90:91], off
	s_nop 0
	global_load_dwordx4 v[92:95], v[92:93], off
	s_waitcnt vmcnt(15)
	ds_write_b128 v45, v[4:7]
	s_waitcnt vmcnt(14)
	ds_write_b128 v45, v[8:11] offset:1024
	s_waitcnt vmcnt(13)
	ds_write_b128 v38, v[12:15] offset:2048
	s_waitcnt vmcnt(12)
	ds_write_b128 v38, v[16:19] offset:3072
	s_waitcnt vmcnt(11)
	ds_write_b128 v39, v[20:23] offset:4096
	s_waitcnt vmcnt(10)
	ds_write_b128 v39, v[52:55] offset:5120
	s_waitcnt vmcnt(9)
	ds_write_b128 v40, v[56:59] offset:6144
	s_waitcnt vmcnt(8)
	ds_write_b128 v40, v[60:63] offset:7168
	s_waitcnt vmcnt(7)
	ds_write_b128 v41, v[64:67] offset:8192
	s_waitcnt vmcnt(6)
	ds_write_b128 v41, v[68:71] offset:9216
	s_waitcnt vmcnt(5)
	ds_write_b128 v42, v[72:75] offset:10240
	s_waitcnt vmcnt(4)
	ds_write_b128 v42, v[76:79] offset:11264
	s_waitcnt vmcnt(3)
	ds_write_b128 v43, v[80:83] offset:12288
	s_waitcnt vmcnt(2)
	ds_write_b128 v43, v[84:87] offset:13312
	s_waitcnt vmcnt(1)
	ds_write_b128 v44, v[88:91] offset:14336
	s_waitcnt vmcnt(0)
	ds_write_b128 v44, v[92:95] offset:15360
	s_waitcnt lgkmcnt(0)
	ds_read2_b32 v[6:7], v28 offset1:32
	ds_read2_b32 v[8:9], v46 offset1:32
	ds_read2_b32 v[10:11], v28 offset0:64 offset1:96
	ds_read2_b32 v[12:13], v46 offset0:64 offset1:96
	v_lshl_add_u64 v[4:5], s[8:9], 0, v[2:3]
	s_waitcnt lgkmcnt(3)
	v_mul_f32_e32 v14, 0x42000000, v6
	s_waitcnt lgkmcnt(2)
	v_mul_f32_e32 v15, 0x42000000, v8
	v_mul_f32_e32 v16, 0x42000000, v7
	v_mul_f32_e32 v17, 0x42000000, v9
	s_waitcnt lgkmcnt(1)
	v_mul_f32_e32 v18, 0x42000000, v10
	ds_read2_b32 v[6:7], v28 offset0:128 offset1:160
	s_waitcnt lgkmcnt(1)
	v_mul_f32_e32 v19, 0x42000000, v12
	v_mul_f32_e32 v20, 0x42000000, v11
	ds_read2_b32 v[8:9], v46 offset0:128 offset1:160
	v_mul_f32_e32 v21, 0x42000000, v13
	ds_read2_b32 v[10:11], v28 offset0:192 offset1:224
	ds_read2_b32 v[12:13], v46 offset0:192 offset1:224
	s_waitcnt lgkmcnt(3)
	v_mul_f32_e32 v22, 0x42000000, v6
	v_mul_f32_e32 v7, 0x42000000, v7
	s_waitcnt lgkmcnt(2)
	v_mul_f32_e32 v23, 0x42000000, v8
	s_waitcnt lgkmcnt(1)
	v_mul_f32_e32 v8, 0x42000000, v10
	s_waitcnt lgkmcnt(0)
	v_mul_f32_e32 v10, 0x42000000, v12
	v_mul_f32_e32 v12, 0x42000000, v13
	v_med3_f32 v13, v14, s48, v47
	v_med3_f32 v14, v16, s48, v47
	v_mov_b32_e32 v6, v1
	v_cvt_pk_fp8_f32 v6, v13, v14
	v_med3_f32 v13, v18, s48, v47
	v_med3_f32 v16, v22, s48, v47
	v_med3_f32 v18, v7, s48, v47
	v_mov_b32_e32 v7, v1
	v_cvt_pk_fp8_f32 v7, v16, v18
	v_mul_f32_e32 v11, 0x42000000, v11
	v_med3_f32 v14, v20, s48, v47
	v_med3_f32 v8, v8, s48, v47
	v_med3_f32 v11, v11, s48, v47
	v_mul_f32_e32 v9, 0x42000000, v9
	v_cvt_pk_fp8_f32 v6, v13, v14 op_sel:[0,0,1]
	v_cvt_pk_fp8_f32 v7, v8, v11 op_sel:[0,0,1]
	v_med3_f32 v11, v15, s48, v47
	v_med3_f32 v13, v17, s48, v47
	v_mov_b32_e32 v8, v1
	v_cvt_pk_fp8_f32 v8, v11, v13
	v_med3_f32 v14, v23, s48, v47
	v_med3_f32 v15, v9, s48, v47
	v_mov_b32_e32 v9, v1
	v_cvt_pk_fp8_f32 v9, v14, v15
	v_med3_f32 v11, v19, s48, v47
	v_med3_f32 v13, v21, s48, v47
	v_cvt_pk_fp8_f32 v8, v11, v13 op_sel:[0,0,1]
	v_med3_f32 v10, v10, s48, v47
	v_med3_f32 v11, v12, s48, v47
	v_cvt_pk_fp8_f32 v9, v10, v11 op_sel:[0,0,1]
	v_or_b32_e32 v10, s7, v24
	v_lshlrev_b32_e32 v10, 11, v10
	v_mov_b32_e32 v11, v1
	v_lshl_add_u64 v[10:11], v[4:5], 0, v[10:11]
	global_store_dwordx4 v[10:11], v[6:9], off sc1
	ds_read2_b32 v[6:7], v30 offset0:64 offset1:96
	ds_read2_b32 v[12:13], v30 offset1:32
	ds_read2_b32 v[8:9], v48 offset0:64 offset1:96
	ds_read2_b32 v[10:11], v30 offset0:128 offset1:160
	ds_read2_b32 v[14:15], v48 offset1:32
	s_waitcnt lgkmcnt(4)
	v_mul_f32_e32 v18, 0x42000000, v6
	v_mul_f32_e32 v20, 0x42000000, v7
	ds_read2_b32 v[6:7], v48 offset0:128 offset1:160
	s_waitcnt lgkmcnt(4)
	v_mul_f32_e32 v16, 0x42000000, v12
	v_mul_f32_e32 v17, 0x42000000, v13
	s_waitcnt lgkmcnt(3)
	v_mul_f32_e32 v19, 0x42000000, v8
	v_mul_f32_e32 v21, 0x42000000, v9
	s_waitcnt lgkmcnt(2)
	v_mul_f32_e32 v10, 0x42000000, v10
	ds_read2_b32 v[8:9], v30 offset0:192 offset1:224
	ds_read2_b32 v[12:13], v48 offset0:192 offset1:224
	s_waitcnt lgkmcnt(2)
	v_mul_f32_e32 v22, 0x42000000, v6
	v_mul_f32_e32 v11, 0x42000000, v11
	v_mul_f32_e32 v23, 0x42000000, v7
	v_med3_f32 v7, v16, s48, v47
	v_med3_f32 v16, v17, s48, v47
	v_mov_b32_e32 v6, v1
	v_cvt_pk_fp8_f32 v6, v7, v16
	v_med3_f32 v10, v10, s48, v47
	v_med3_f32 v11, v11, s48, v47
	v_mov_b32_e32 v7, v1
	v_cvt_pk_fp8_f32 v7, v10, v11
	s_waitcnt lgkmcnt(1)
	v_mul_f32_e32 v8, 0x42000000, v8
	v_mul_f32_e32 v9, 0x42000000, v9
	v_mul_f32_e32 v14, 0x42000000, v14
	v_mul_f32_e32 v15, 0x42000000, v15
	v_med3_f32 v8, v8, s48, v47
	v_med3_f32 v9, v9, s48, v47
	v_cvt_pk_fp8_f32 v7, v8, v9 op_sel:[0,0,1]
	v_med3_f32 v9, v14, s48, v47
	v_med3_f32 v10, v15, s48, v47
	v_mov_b32_e32 v8, v1
	v_cvt_pk_fp8_f32 v8, v9, v10
	v_med3_f32 v14, v22, s48, v47
	v_med3_f32 v15, v23, s48, v47
	v_mov_b32_e32 v9, v1
	v_cvt_pk_fp8_f32 v9, v14, v15
	s_waitcnt lgkmcnt(0)
	v_mul_f32_e32 v12, 0x42000000, v12
	v_mul_f32_e32 v13, 0x42000000, v13
	v_med3_f32 v10, v19, s48, v47
	v_med3_f32 v11, v21, s48, v47
	v_med3_f32 v16, v18, s48, v47
	v_med3_f32 v17, v20, s48, v47
	v_cvt_pk_fp8_f32 v8, v10, v11 op_sel:[0,0,1]
	v_med3_f32 v10, v12, s48, v47
	v_med3_f32 v11, v13, s48, v47
	v_cvt_pk_fp8_f32 v6, v16, v17 op_sel:[0,0,1]
	v_cvt_pk_fp8_f32 v9, v10, v11 op_sel:[0,0,1]
	v_or_b32_e32 v10, s7, v29
	v_lshlrev_b32_e32 v10, 11, v10
	v_mov_b32_e32 v11, v1
	v_lshl_add_u64 v[10:11], v[4:5], 0, v[10:11]
	global_store_dwordx4 v[10:11], v[6:9], off sc1
	ds_read2_b32 v[6:7], v32 offset0:64 offset1:96
	ds_read2_b32 v[12:13], v32 offset1:32
	ds_read2_b32 v[8:9], v49 offset0:64 offset1:96
	ds_read2_b32 v[10:11], v32 offset0:128 offset1:160
	ds_read2_b32 v[14:15], v49 offset1:32
	s_waitcnt lgkmcnt(4)
	v_mul_f32_e32 v18, 0x42000000, v6
	v_mul_f32_e32 v20, 0x42000000, v7
	ds_read2_b32 v[6:7], v49 offset0:128 offset1:160
	s_waitcnt lgkmcnt(4)
	v_mul_f32_e32 v16, 0x42000000, v12
	v_mul_f32_e32 v17, 0x42000000, v13
	s_waitcnt lgkmcnt(3)
	v_mul_f32_e32 v19, 0x42000000, v8
	v_mul_f32_e32 v21, 0x42000000, v9
	s_waitcnt lgkmcnt(2)
	v_mul_f32_e32 v10, 0x42000000, v10
	ds_read2_b32 v[8:9], v32 offset0:192 offset1:224
	ds_read2_b32 v[12:13], v49 offset0:192 offset1:224
	s_waitcnt lgkmcnt(2)
	v_mul_f32_e32 v22, 0x42000000, v6
	v_mul_f32_e32 v11, 0x42000000, v11
	v_mul_f32_e32 v23, 0x42000000, v7
	v_med3_f32 v7, v16, s48, v47
	v_med3_f32 v16, v17, s48, v47
	v_mov_b32_e32 v6, v1
	v_cvt_pk_fp8_f32 v6, v7, v16
	v_med3_f32 v10, v10, s48, v47
	v_med3_f32 v11, v11, s48, v47
	v_mov_b32_e32 v7, v1
	v_cvt_pk_fp8_f32 v7, v10, v11
	s_waitcnt lgkmcnt(1)
	v_mul_f32_e32 v8, 0x42000000, v8
	v_mul_f32_e32 v9, 0x42000000, v9
	v_mul_f32_e32 v14, 0x42000000, v14
	v_mul_f32_e32 v15, 0x42000000, v15
	v_med3_f32 v8, v8, s48, v47
	v_med3_f32 v9, v9, s48, v47
	v_cvt_pk_fp8_f32 v7, v8, v9 op_sel:[0,0,1]
	v_med3_f32 v9, v14, s48, v47
	v_med3_f32 v10, v15, s48, v47
	v_mov_b32_e32 v8, v1
	v_cvt_pk_fp8_f32 v8, v9, v10
	v_med3_f32 v14, v22, s48, v47
	v_med3_f32 v15, v23, s48, v47
	v_mov_b32_e32 v9, v1
	v_cvt_pk_fp8_f32 v9, v14, v15
	s_waitcnt lgkmcnt(0)
	v_mul_f32_e32 v12, 0x42000000, v12
	v_mul_f32_e32 v13, 0x42000000, v13
	v_med3_f32 v10, v19, s48, v47
	v_med3_f32 v11, v21, s48, v47
	v_med3_f32 v16, v18, s48, v47
	v_med3_f32 v17, v20, s48, v47
	v_cvt_pk_fp8_f32 v8, v10, v11 op_sel:[0,0,1]
	v_med3_f32 v10, v12, s48, v47
	v_med3_f32 v11, v13, s48, v47
	v_cvt_pk_fp8_f32 v6, v16, v17 op_sel:[0,0,1]
	v_cvt_pk_fp8_f32 v9, v10, v11 op_sel:[0,0,1]
	v_or_b32_e32 v10, s7, v31
	v_lshlrev_b32_e32 v10, 11, v10
	v_mov_b32_e32 v11, v1
	v_lshl_add_u64 v[10:11], v[4:5], 0, v[10:11]
	global_store_dwordx4 v[10:11], v[6:9], off sc1
	ds_read2_b32 v[6:7], v35 offset0:64 offset1:96
	ds_read2_b32 v[12:13], v35 offset1:32
	ds_read2_b32 v[8:9], v50 offset0:64 offset1:96
	ds_read2_b32 v[10:11], v35 offset0:128 offset1:160
	ds_read2_b32 v[14:15], v50 offset1:32
	s_waitcnt lgkmcnt(4)
	v_mul_f32_e32 v18, 0x42000000, v6
	v_mul_f32_e32 v20, 0x42000000, v7
	ds_read2_b32 v[6:7], v50 offset0:128 offset1:160
	s_waitcnt lgkmcnt(4)
	v_mul_f32_e32 v16, 0x42000000, v12
	v_mul_f32_e32 v17, 0x42000000, v13
	s_waitcnt lgkmcnt(3)
	v_mul_f32_e32 v19, 0x42000000, v8
	v_mul_f32_e32 v21, 0x42000000, v9
	s_waitcnt lgkmcnt(2)
	v_mul_f32_e32 v10, 0x42000000, v10
	ds_read2_b32 v[8:9], v35 offset0:192 offset1:224
	ds_read2_b32 v[12:13], v50 offset0:192 offset1:224
	s_waitcnt lgkmcnt(2)
	v_mul_f32_e32 v22, 0x42000000, v6
	v_mul_f32_e32 v11, 0x42000000, v11
	v_mul_f32_e32 v23, 0x42000000, v7
	v_med3_f32 v7, v16, s48, v47
	v_med3_f32 v16, v17, s48, v47
	v_mov_b32_e32 v6, v1
	v_cvt_pk_fp8_f32 v6, v7, v16
	v_med3_f32 v10, v10, s48, v47
	v_med3_f32 v11, v11, s48, v47
	v_mov_b32_e32 v7, v1
	v_cvt_pk_fp8_f32 v7, v10, v11
	s_waitcnt lgkmcnt(1)
	v_mul_f32_e32 v8, 0x42000000, v8
	v_mul_f32_e32 v9, 0x42000000, v9
	v_mul_f32_e32 v14, 0x42000000, v14
	v_mul_f32_e32 v15, 0x42000000, v15
	v_med3_f32 v8, v8, s48, v47
	v_med3_f32 v9, v9, s48, v47
	v_cvt_pk_fp8_f32 v7, v8, v9 op_sel:[0,0,1]
	v_med3_f32 v9, v14, s48, v47
	v_med3_f32 v10, v15, s48, v47
	v_mov_b32_e32 v8, v1
	v_cvt_pk_fp8_f32 v8, v9, v10
	v_med3_f32 v14, v22, s48, v47
	v_med3_f32 v15, v23, s48, v47
	v_mov_b32_e32 v9, v1
	v_cvt_pk_fp8_f32 v9, v14, v15
	s_waitcnt lgkmcnt(0)
	v_mul_f32_e32 v12, 0x42000000, v12
	v_mul_f32_e32 v13, 0x42000000, v13
	v_med3_f32 v10, v19, s48, v47
	v_med3_f32 v11, v21, s48, v47
	v_med3_f32 v16, v18, s48, v47
	v_med3_f32 v17, v20, s48, v47
	v_cvt_pk_fp8_f32 v8, v10, v11 op_sel:[0,0,1]
	v_med3_f32 v10, v12, s48, v47
	v_med3_f32 v11, v13, s48, v47
	v_cvt_pk_fp8_f32 v6, v16, v17 op_sel:[0,0,1]
	v_cvt_pk_fp8_f32 v9, v10, v11 op_sel:[0,0,1]
	v_or_b32_e32 v10, s7, v33
	v_lshlrev_b32_e32 v10, 11, v10
	v_mov_b32_e32 v11, v1
	v_lshl_add_u64 v[4:5], v[4:5], 0, v[10:11]
	global_store_dwordx4 v[4:5], v[6:9], off sc1
	s_waitcnt lgkmcnt(0)
	s_mov_b64 s[8:9], 0
.LBB0_32:
	s_andn2_b64 vcc, exec, s[8:9]
	s_cbranch_vccnz .LBB0_29
	s_load_dwordx2 s[8:9], s[14:15], 0x30
	s_mul_i32 s7, s6, 0x3300000
	s_mul_hi_i32 s4, s6, 0x3300000
	s_mul_i32 s11, s10, 0xffffa0a1
	s_waitcnt lgkmcnt(0)
	s_add_u32 s18, s8, s7
	s_addc_u32 s19, s9, s4
	s_lshr_b32 s4, s11, 16
	s_add_i32 s4, s4, s10
	s_sext_i32_i16 s7, s4
	s_ashr_i32 s7, s7, 7
	s_bfe_u32 s4, s4, 0x1000f
	s_add_i32 s4, s7, s4
	s_sext_i32_i16 s7, s4
	s_mulk_i32 s4, 0xcc
	s_lshl_b32 s7, s7, 7
	s_sub_i32 s4, s10, s4
	v_or_b32_e32 v4, s7, v24
	s_sext_i32_i16 s8, s4
	v_mul_i32_i24_e32 v4, 0x6600, v4
	s_lshl_b32 s8, s8, 5
	v_ashrrev_i32_e32 v5, 31, v4
	v_lshl_add_u64 v[4:5], s[18:19], 0, v[4:5]
	s_ashr_i32 s9, s8, 31
	v_lshl_add_u64 v[4:5], s[8:9], 2, v[4:5]
	v_lshl_add_u64 v[12:13], v[4:5], 0, v[0:1]
	v_add_co_u32_e32 v8, vcc, s49, v12
	s_nop 1
	v_addc_co_u32_e32 v9, vcc, 0, v13, vcc
	v_add_co_u32_e32 v14, vcc, s50, v12
	global_load_dwordx4 v[4:7], v[12:13], off
	s_nop 0
	global_load_dwordx4 v[8:11], v[8:9], off
	v_addc_co_u32_e32 v15, vcc, 0, v13, vcc
	v_add_co_u32_e32 v16, vcc, s51, v12
	s_nop 1
	v_addc_co_u32_e32 v17, vcc, 0, v13, vcc
	v_add_co_u32_e32 v20, vcc, s52, v12
	s_nop 1
	v_addc_co_u32_e32 v21, vcc, 0, v13, vcc
	v_add_co_u32_e32 v52, vcc, s53, v12
	s_nop 1
	v_addc_co_u32_e32 v53, vcc, 0, v13, vcc
	v_add_co_u32_e32 v56, vcc, s54, v12
	s_nop 1
	v_addc_co_u32_e32 v57, vcc, 0, v13, vcc
	v_add_co_u32_e32 v60, vcc, s55, v12
	s_nop 1
	v_addc_co_u32_e32 v61, vcc, 0, v13, vcc
	v_add_co_u32_e32 v64, vcc, s56, v12
	s_nop 1
	v_addc_co_u32_e32 v65, vcc, 0, v13, vcc
	v_add_co_u32_e32 v68, vcc, s57, v12
	s_nop 1
	v_addc_co_u32_e32 v69, vcc, 0, v13, vcc
	v_add_co_u32_e32 v72, vcc, s58, v12
	s_nop 1
	v_addc_co_u32_e32 v73, vcc, 0, v13, vcc
	v_add_co_u32_e32 v76, vcc, s59, v12
	s_nop 1
	v_addc_co_u32_e32 v77, vcc, 0, v13, vcc
	v_add_co_u32_e32 v80, vcc, s60, v12
	s_nop 1
	v_addc_co_u32_e32 v81, vcc, 0, v13, vcc
	v_add_co_u32_e32 v84, vcc, s61, v12
	s_nop 1
	v_addc_co_u32_e32 v85, vcc, 0, v13, vcc
	v_add_co_u32_e32 v88, vcc, s62, v12
	s_nop 1
	v_addc_co_u32_e32 v89, vcc, 0, v13, vcc
	v_add_co_u32_e32 v92, vcc, s63, v12
	s_nop 1
	v_addc_co_u32_e32 v93, vcc, 0, v13, vcc
	global_load_dwordx4 v[12:15], v[14:15], off
	s_nop 0
	global_load_dwordx4 v[16:19], v[16:17], off
	s_nop 0
	global_load_dwordx4 v[20:23], v[20:21], off
	s_nop 0
	global_load_dwordx4 v[52:55], v[52:53], off
	s_nop 0
	global_load_dwordx4 v[56:59], v[56:57], off
	s_nop 0
	global_load_dwordx4 v[60:63], v[60:61], off
	s_nop 0
	global_load_dwordx4 v[64:67], v[64:65], off
	s_nop 0
	global_load_dwordx4 v[68:71], v[68:69], off
	s_nop 0
	global_load_dwordx4 v[72:75], v[72:73], off
	s_nop 0
	global_load_dwordx4 v[76:79], v[76:77], off
	s_nop 0
	global_load_dwordx4 v[80:83], v[80:81], off
	s_nop 0
	global_load_dwordx4 v[84:87], v[84:85], off
	s_nop 0
	global_load_dwordx4 v[88:91], v[88:89], off
	s_nop 0
	global_load_dwordx4 v[92:95], v[92:93], off
	s_waitcnt vmcnt(15)
	ds_write_b128 v45, v[4:7]
	s_waitcnt vmcnt(14)
	ds_write_b128 v45, v[8:11] offset:1024
	s_waitcnt vmcnt(13)
	ds_write_b128 v38, v[12:15] offset:2048
	s_waitcnt vmcnt(12)
	ds_write_b128 v38, v[16:19] offset:3072
	s_waitcnt vmcnt(11)
	ds_write_b128 v39, v[20:23] offset:4096
	s_waitcnt vmcnt(10)
	ds_write_b128 v39, v[52:55] offset:5120
	s_waitcnt vmcnt(9)
	ds_write_b128 v40, v[56:59] offset:6144
	s_waitcnt vmcnt(8)
	ds_write_b128 v40, v[60:63] offset:7168
	s_waitcnt vmcnt(7)
	ds_write_b128 v41, v[64:67] offset:8192
	s_waitcnt vmcnt(6)
	ds_write_b128 v41, v[68:71] offset:9216
	s_waitcnt vmcnt(5)
	ds_write_b128 v42, v[72:75] offset:10240
	s_waitcnt vmcnt(4)
	ds_write_b128 v42, v[76:79] offset:11264
	s_waitcnt vmcnt(3)
	ds_write_b128 v43, v[80:83] offset:12288
	s_waitcnt vmcnt(2)
	ds_write_b128 v43, v[84:87] offset:13312
	s_waitcnt vmcnt(1)
	ds_write_b128 v44, v[88:91] offset:14336
	s_waitcnt vmcnt(0)
	ds_write_b128 v44, v[92:95] offset:15360
	s_waitcnt lgkmcnt(0)
	ds_read2_b32 v[20:21], v28 offset1:32
	ds_read2_b32 v[22:23], v46 offset1:32
	ds_read2_b32 v[16:17], v28 offset0:64 offset1:96
	ds_read2_b32 v[18:19], v46 offset0:64 offset1:96
	ds_read2_b32 v[12:13], v28 offset0:128 offset1:160
	ds_read2_b32 v[14:15], v46 offset0:128 offset1:160
	ds_read2_b32 v[8:9], v28 offset0:192 offset1:224
	ds_read2_b32 v[10:11], v46 offset0:192 offset1:224
	v_or_b32_e32 v4, s8, v24
	v_cmp_lt_i32_e64 s[10:11], s64, v4
	v_cmp_gt_i32_e32 vcc, s65, v4
	s_and_saveexec_b64 s[18:19], vcc
	s_bitcmp1_b32 s4, 0
	s_cselect_b64 s[68:69], -1, 0
	s_andn2_b64 s[10:11], s[10:11], exec
	s_and_b64 s[68:69], s[68:69], exec
	v_and_or_b32 v6, v4, s66, v36
	s_or_b64 s[10:11], s[10:11], s[68:69]
	s_or_b64 exec, exec, s[18:19]
	s_and_saveexec_b64 s[18:19], s[10:11]
	v_mov_b32_e32 v6, v4
	s_or_b64 exec, exec, s[18:19]
	s_waitcnt lgkmcnt(7)
	v_mul_f32_e32 v7, 0x42000000, v20
	v_mul_f32_e32 v21, 0x42000000, v21
	s_waitcnt lgkmcnt(3)
	v_mul_f32_e32 v12, 0x42000000, v12
	v_mul_f32_e32 v13, 0x42000000, v13
	v_med3_f32 v7, v7, s48, v47
	v_med3_f32 v21, v21, s48, v47
	v_mov_b32_e32 v52, 0
	v_cvt_pk_fp8_f32 v52, v7, v21
	v_med3_f32 v12, v12, s48, v47
	v_med3_f32 v13, v13, s48, v47
	v_mov_b32_e32 v53, 0
	v_cvt_pk_fp8_f32 v53, v12, v13
	v_mul_f32_e32 v16, 0x42000000, v16
	v_mul_f32_e32 v17, 0x42000000, v17
	s_waitcnt lgkmcnt(1)
	v_mul_f32_e32 v8, 0x42000000, v8
	v_mul_f32_e32 v9, 0x42000000, v9
	v_med3_f32 v7, v16, s48, v47
	v_med3_f32 v16, v17, s48, v47
	v_mul_f32_e32 v20, 0x42000000, v22
	v_mul_f32_e32 v22, 0x42000000, v23
	v_cvt_pk_fp8_f32 v52, v7, v16 op_sel:[0,0,1]
	v_med3_f32 v7, v8, s48, v47
	v_med3_f32 v8, v9, s48, v47
	v_mul_f32_e32 v14, 0x42000000, v14
	v_mul_f32_e32 v15, 0x42000000, v15
	v_cvt_pk_fp8_f32 v53, v7, v8 op_sel:[0,0,1]
	v_med3_f32 v7, v20, s48, v47
	v_med3_f32 v8, v22, s48, v47
	v_mov_b32_e32 v54, 0
	v_cvt_pk_fp8_f32 v54, v7, v8
	v_med3_f32 v9, v14, s48, v47
	v_med3_f32 v12, v15, s48, v47
	v_mov_b32_e32 v55, 0
	v_cvt_pk_fp8_f32 v55, v9, v12
	v_mul_f32_e32 v18, 0x42000000, v18
	v_mul_f32_e32 v19, 0x42000000, v19
	s_waitcnt lgkmcnt(0)
	v_mul_f32_e32 v10, 0x42000000, v10
	v_mul_f32_e32 v11, 0x42000000, v11
	v_med3_f32 v7, v18, s48, v47
	v_med3_f32 v8, v19, s48, v47
	v_cvt_pk_fp8_f32 v54, v7, v8 op_sel:[0,0,1]
	v_med3_f32 v7, v10, s48, v47
	v_med3_f32 v8, v11, s48, v47
	v_cvt_pk_fp8_f32 v55, v7, v8 op_sel:[0,0,1]
	ds_read2_b32 v[22:23], v30 offset1:32
	ds_read2_b32 v[14:15], v48 offset1:32
	ds_read2_b32 v[20:21], v30 offset0:64 offset1:96
	ds_read2_b32 v[12:13], v48 offset0:64 offset1:96
	ds_read2_b32 v[18:19], v30 offset0:128 offset1:160
	ds_read2_b32 v[10:11], v48 offset0:128 offset1:160
	ds_read2_b32 v[16:17], v30 offset0:192 offset1:224
	ds_read2_b32 v[8:9], v48 offset0:192 offset1:224
	s_mul_hi_i32 s9, s6, 0xd00000
	s_mul_i32 s6, s6, 0xd00000
	s_add_u32 s6, s22, s6
	s_addc_u32 s9, s23, s9
	s_ashr_i32 s10, s7, 31
	s_add_u32 s6, s6, s7
	s_addc_u32 s7, s9, s10
	v_ashrrev_i32_e32 v7, 31, v6
	v_lshl_add_u64 v[4:5], s[6:7], 0, v[2:3]
	v_lshlrev_b64 v[6:7], 11, v[6:7]
	v_lshl_add_u64 v[6:7], v[4:5], 0, v[6:7]
	global_store_dwordx4 v[6:7], v[52:55], off sc1
	v_or_b32_e32 v7, s8, v29
	v_cmp_lt_i32_e64 s[6:7], s64, v7
	v_cmp_gt_i32_e32 vcc, s65, v7
	s_and_saveexec_b64 s[10:11], vcc
	s_bitcmp1_b32 s4, 0
	s_cselect_b64 s[18:19], -1, 0
	s_andn2_b64 s[6:7], s[6:7], exec
	s_and_b64 s[18:19], s[18:19], exec
	v_and_or_b32 v6, v7, s66, v37
	s_or_b64 s[6:7], s[6:7], s[18:19]
	s_or_b64 exec, exec, s[10:11]
	s_and_saveexec_b64 s[10:11], s[6:7]
	s_cbranch_execz .LBB0_28
	v_mov_b32_e32 v6, v7
	s_branch .LBB0_28

.LBB0_43:
	v_ashrrev_i32_e32 v5, 31, v4
	v_lshrrev_b32_e32 v5, 18, v5
	v_add_u32_e32 v5, v4, v5
	v_ashrrev_i32_e32 v5, 14, v5
	v_mul_i32_i24_e32 v7, 0x4000, v5
	v_mul_i32_i24_e32 v6, 0x1a00, v5
	v_sub_u32_e32 v8, v4, v7
	v_ashrrev_i32_e32 v7, 31, v6
	v_add_u32_e32 v4, s35, v4
	v_lshlrev_b64 v[6:7], 11, v[6:7]
	v_ashrrev_i32_e32 v9, 31, v8
	v_cmp_lt_i32_e32 vcc, s10, v4
	v_lshl_add_u64 v[6:7], s[6:7], 0, v[6:7]
	s_or_b64 s[8:9], vcc, s[8:9]
	v_lshl_add_u64 v[6:7], v[8:9], 4, v[6:7]
	global_store_dwordx4 v[6:7], v[0:3], off sc1
	s_andn2_b64 exec, exec, s[8:9]
	s_cbranch_execnz .LBB0_43

.LBB0_46:
	s_or_b64 exec, exec, s[4:5]
	v_sub_u32_e32 v0, 0, v3
	v_mul_i32_i24_e32 v3, 0x1400, v4
	s_waitcnt vmcnt(0)
	v_cvt_pk_bf16_f32 v6, v14, v15
	v_cvt_pk_bf16_f32 v7, v16, v17
	v_cvt_pk_bf16_f32 v8, v18, v19
	v_cvt_pk_bf16_f32 v9, v20, v5
	v_add3_u32 v0, v3, v26, v0
	v_mov_b64_e32 v[4:5], s[10:11]
	v_add_u32_e32 v26, s35, v26
	v_mad_i64_i32 v[4:5], s[4:5], v0, s41, v[4:5]
	v_ashrrev_i32_e32 v3, 31, v2
	v_cmp_lt_i32_e32 vcc, s42, v26
	v_lshl_add_u64 v[2:3], v[2:3], 1, v[4:5]
	s_or_b64 s[18:19], vcc, s[18:19]
	global_store_dwordx4 v[2:3], v[6:9], off sc1
	s_andn2_b64 exec, exec, s[18:19]
	s_cbranch_execz .LBB0_175

.LBB0_178:
	s_mul_hi_i32 s10, s34, 0x2aaaaaab
	s_lshr_b32 s14, s10, 31
	s_ashr_i32 s10, s10, 8
	s_add_i32 s14, s10, s14
	s_mul_i32 s10, s14, 0xfffffa00
	s_add_i32 s65, s34, s10
	s_cmpk_gt_i32 s65, 0x1ff
	s_mov_b64 s[16:17], -1
	s_cbranch_scc0 .LBB0_184
	s_ashr_i32 s15, s14, 31
	s_lshl_b64 s[16:17], s[14:15], 23
	s_cmpk_gt_u32 s65, 0x3ff
	s_mov_b64 s[18:19], -1
	s_cbranch_scc0 .LBB0_181
	s_waitcnt lgkmcnt(0)
	s_add_u32 s66, s8, s16
	s_addc_u32 s67, s9, s17
	s_lshl_b64 s[18:19], s[14:15], 21
	s_add_u32 s68, s22, s18
	s_addc_u32 s19, s23, s19
	s_lshl_b32 s10, s14, 10
	s_sub_i32 s10, s29, s10
	s_and_b32 s69, s10, 0x780
	s_add_i32 s10, s25, 0xffffc000
	v_or_b32_e32 v4, s69, v24
	s_and_b32 s18, s10, 0x7e0
	v_lshlrev_b32_e32 v4, 13, v4
	v_mov_b32_e32 v5, v1
	v_lshl_add_u64 v[4:5], s[66:67], 0, v[4:5]
	s_lshl_b32 s10, s18, 2
	v_lshl_add_u64 v[4:5], v[4:5], 0, s[10:11]
	v_lshl_add_u64 v[4:5], v[4:5], 0, v[0:1]
	v_add_co_u32_e32 v34, vcc, s31, v4
	s_add_u32 s66, s68, s69
	s_nop 0
	v_addc_co_u32_e32 v35, vcc, 0, v5, vcc
	v_add_co_u32_e32 v38, vcc, s35, v4
	global_load_dwordx4 v[30:33], v[4:5], off
	s_nop 0
	global_load_dwordx4 v[34:37], v[34:35], off
	v_addc_co_u32_e32 v39, vcc, 0, v5, vcc
	v_add_co_u32_e32 v42, vcc, s36, v4
	s_addc_u32 s67, s19, 0
	s_nop 0
	v_addc_co_u32_e32 v43, vcc, 0, v5, vcc
	v_add_co_u32_e32 v46, vcc, s37, v4
	global_load_dwordx4 v[38:41], v[38:39], off
	s_nop 0
	global_load_dwordx4 v[42:45], v[42:43], off
	v_addc_co_u32_e32 v47, vcc, 0, v5, vcc
	v_add_co_u32_e32 v50, vcc, s38, v4
	s_nop 1
	v_addc_co_u32_e32 v51, vcc, 0, v5, vcc
	v_add_co_u32_e32 v54, vcc, s39, v4
	global_load_dwordx4 v[46:49], v[46:47], off
	s_nop 0
	global_load_dwordx4 v[50:53], v[50:51], off
	v_addc_co_u32_e32 v55, vcc, 0, v5, vcc
	v_add_co_u32_e32 v58, vcc, s40, v4
	s_nop 1
	v_addc_co_u32_e32 v59, vcc, 0, v5, vcc
	v_add_co_u32_e32 v62, vcc, s41, v4
	global_load_dwordx4 v[54:57], v[54:55], off
	s_nop 0
	global_load_dwordx4 v[58:61], v[58:59], off
	v_addc_co_u32_e32 v63, vcc, 0, v5, vcc
	v_add_co_u32_e32 v66, vcc, s42, v4
	s_nop 1
	v_addc_co_u32_e32 v67, vcc, 0, v5, vcc
	v_add_co_u32_e32 v70, vcc, s43, v4
	global_load_dwordx4 v[62:65], v[62:63], off
	s_nop 0
	global_load_dwordx4 v[66:69], v[66:67], off
	v_addc_co_u32_e32 v71, vcc, 0, v5, vcc
	v_add_co_u32_e32 v74, vcc, s44, v4
	s_nop 1
	v_addc_co_u32_e32 v75, vcc, 0, v5, vcc
	v_add_co_u32_e32 v78, vcc, s45, v4
	global_load_dwordx4 v[70:73], v[70:71], off
	s_nop 0
	global_load_dwordx4 v[74:77], v[74:75], off
	v_addc_co_u32_e32 v79, vcc, 0, v5, vcc
	v_add_co_u32_e32 v82, vcc, s46, v4
	s_nop 1
	v_addc_co_u32_e32 v83, vcc, 0, v5, vcc
	v_add_co_u32_e32 v86, vcc, s47, v4
	global_load_dwordx4 v[78:81], v[78:79], off
	s_nop 0
	global_load_dwordx4 v[82:85], v[82:83], off
	v_addc_co_u32_e32 v87, vcc, 0, v5, vcc
	v_add_co_u32_e32 v4, vcc, s48, v4
	s_nop 1
	v_addc_co_u32_e32 v5, vcc, 0, v5, vcc
	global_load_dwordx4 v[86:89], v[86:87], off
	s_nop 0
	global_load_dwordx4 v[90:93], v[4:5], off
	v_lshl_add_u64 v[4:5], s[66:67], 0, v[2:3]
	v_readlane_b32 s66, v253, 2
	s_waitcnt vmcnt(15)
	ds_write_b128 v22, v[30:33]
	s_waitcnt vmcnt(14)
	ds_write_b128 v22, v[34:37] offset:1024
	s_waitcnt vmcnt(13)
	ds_write_b128 v15, v[38:41] offset:2048
	s_waitcnt vmcnt(12)
	ds_write_b128 v15, v[42:45] offset:3072
	s_waitcnt vmcnt(11)
	ds_write_b128 v16, v[46:49] offset:4096
	s_waitcnt vmcnt(10)
	ds_write_b128 v16, v[50:53] offset:5120
	s_waitcnt vmcnt(9)
	ds_write_b128 v17, v[54:57] offset:6144
	s_waitcnt vmcnt(8)
	ds_write_b128 v17, v[58:61] offset:7168
	s_waitcnt vmcnt(7)
	ds_write_b128 v18, v[62:65] offset:8192
	s_waitcnt vmcnt(6)
	ds_write_b128 v18, v[66:69] offset:9216
	s_waitcnt vmcnt(5)
	ds_write_b128 v19, v[70:73] offset:10240
	s_waitcnt vmcnt(4)
	ds_write_b128 v19, v[74:77] offset:11264
	s_waitcnt vmcnt(3)
	ds_write_b128 v20, v[78:81] offset:12288
	s_waitcnt vmcnt(2)
	ds_write_b128 v20, v[82:85] offset:13312
	s_waitcnt vmcnt(1)
	ds_write_b128 v21, v[86:89] offset:14336
	s_waitcnt vmcnt(0)
	ds_write_b128 v21, v[90:93] offset:15360
	s_waitcnt lgkmcnt(0)
	ds_read2_b32 v[30:31], v7 offset1:32
	ds_read2_b32 v[32:33], v23 offset1:32
	ds_read2_b32 v[34:35], v7 offset0:64 offset1:96
	ds_read2_b32 v[36:37], v23 offset0:64 offset1:96
	s_waitcnt lgkmcnt(3)
	v_mul_f32_e32 v38, 0x41800000, v30
	s_waitcnt lgkmcnt(2)
	v_mul_f32_e32 v39, 0x41800000, v32
	v_mul_f32_e32 v40, 0x41800000, v31
	v_mul_f32_e32 v41, 0x41800000, v33
	s_waitcnt lgkmcnt(1)
	v_mul_f32_e32 v42, 0x41800000, v34
	ds_read2_b32 v[30:31], v7 offset0:128 offset1:160
	s_waitcnt lgkmcnt(1)
	v_mul_f32_e32 v43, 0x41800000, v36
	v_mul_f32_e32 v44, 0x41800000, v35
	ds_read2_b32 v[32:33], v23 offset0:128 offset1:160
	v_mul_f32_e32 v45, 0x41800000, v37
	ds_read2_b32 v[34:35], v7 offset0:192 offset1:224
	ds_read2_b32 v[36:37], v23 offset0:192 offset1:224
	s_waitcnt lgkmcnt(3)
	v_mul_f32_e32 v46, 0x41800000, v30
	v_mul_f32_e32 v31, 0x41800000, v31
	s_waitcnt lgkmcnt(2)
	v_mul_f32_e32 v47, 0x41800000, v32
	s_waitcnt lgkmcnt(1)
	v_mul_f32_e32 v32, 0x41800000, v34
	s_waitcnt lgkmcnt(0)
	v_mul_f32_e32 v34, 0x41800000, v36
	v_mul_f32_e32 v36, 0x41800000, v37
	v_med3_f32 v37, v38, s49, v25
	v_med3_f32 v38, v40, s49, v25
	v_mov_b32_e32 v30, v1
	v_cvt_pk_fp8_f32 v30, v37, v38
	v_med3_f32 v37, v42, s49, v25
	v_med3_f32 v40, v46, s49, v25
	v_med3_f32 v42, v31, s49, v25
	v_mov_b32_e32 v31, v1
	v_cvt_pk_fp8_f32 v31, v40, v42
	v_mul_f32_e32 v35, 0x41800000, v35
	v_med3_f32 v38, v44, s49, v25
	v_med3_f32 v32, v32, s49, v25
	v_med3_f32 v35, v35, s49, v25
	v_mul_f32_e32 v33, 0x41800000, v33
	v_cvt_pk_fp8_f32 v30, v37, v38 op_sel:[0,0,1]
	v_cvt_pk_fp8_f32 v31, v32, v35 op_sel:[0,0,1]
	v_med3_f32 v35, v39, s49, v25
	v_med3_f32 v37, v41, s49, v25
	v_mov_b32_e32 v32, v1
	v_cvt_pk_fp8_f32 v32, v35, v37
	v_med3_f32 v38, v47, s49, v25
	v_med3_f32 v39, v33, s49, v25
	v_mov_b32_e32 v33, v1
	v_cvt_pk_fp8_f32 v33, v38, v39
	v_med3_f32 v35, v43, s49, v25
	v_med3_f32 v37, v45, s49, v25
	v_cvt_pk_fp8_f32 v32, v35, v37 op_sel:[0,0,1]
	v_med3_f32 v34, v34, s49, v25
	v_med3_f32 v35, v36, s49, v25
	v_cvt_pk_fp8_f32 v33, v34, v35 op_sel:[0,0,1]
	v_or_b32_e32 v34, s18, v24
	v_lshlrev_b32_e32 v34, 10, v34
	v_mov_b32_e32 v35, v1
	v_lshl_add_u64 v[34:35], v[4:5], 0, v[34:35]
	global_store_dwordx4 v[34:35], v[30:33], off sc1
	ds_read2_b32 v[30:31], v9 offset0:64 offset1:96
	ds_read2_b32 v[36:37], v9 offset1:32
	ds_read2_b32 v[32:33], v26 offset0:64 offset1:96
	ds_read2_b32 v[34:35], v9 offset0:128 offset1:160
	ds_read2_b32 v[38:39], v26 offset1:32
	s_waitcnt lgkmcnt(4)
	v_mul_f32_e32 v42, 0x41800000, v30
	v_mul_f32_e32 v44, 0x41800000, v31
	ds_read2_b32 v[30:31], v26 offset0:128 offset1:160
	s_waitcnt lgkmcnt(4)
	v_mul_f32_e32 v40, 0x41800000, v36
	v_mul_f32_e32 v41, 0x41800000, v37
	s_waitcnt lgkmcnt(3)
	v_mul_f32_e32 v43, 0x41800000, v32
	v_mul_f32_e32 v45, 0x41800000, v33
	s_waitcnt lgkmcnt(2)
	v_mul_f32_e32 v34, 0x41800000, v34
	ds_read2_b32 v[32:33], v9 offset0:192 offset1:224
	ds_read2_b32 v[36:37], v26 offset0:192 offset1:224
	s_waitcnt lgkmcnt(2)
	v_mul_f32_e32 v46, 0x41800000, v30
	v_mul_f32_e32 v35, 0x41800000, v35
	v_mul_f32_e32 v47, 0x41800000, v31
	v_med3_f32 v31, v40, s49, v25
	v_med3_f32 v40, v41, s49, v25
	v_mov_b32_e32 v30, v1
	v_cvt_pk_fp8_f32 v30, v31, v40
	v_med3_f32 v34, v34, s49, v25
	v_med3_f32 v35, v35, s49, v25
	v_mov_b32_e32 v31, v1
	v_cvt_pk_fp8_f32 v31, v34, v35
	s_waitcnt lgkmcnt(1)
	v_mul_f32_e32 v32, 0x41800000, v32
	v_mul_f32_e32 v33, 0x41800000, v33
	v_mul_f32_e32 v38, 0x41800000, v38
	v_mul_f32_e32 v39, 0x41800000, v39
	v_med3_f32 v32, v32, s49, v25
	v_med3_f32 v33, v33, s49, v25
	v_cvt_pk_fp8_f32 v31, v32, v33 op_sel:[0,0,1]
	v_med3_f32 v33, v38, s49, v25
	v_med3_f32 v34, v39, s49, v25
	v_mov_b32_e32 v32, v1
	v_cvt_pk_fp8_f32 v32, v33, v34
	v_med3_f32 v38, v46, s49, v25
	v_med3_f32 v39, v47, s49, v25
	v_mov_b32_e32 v33, v1
	v_cvt_pk_fp8_f32 v33, v38, v39
	s_waitcnt lgkmcnt(0)
	v_mul_f32_e32 v36, 0x41800000, v36
	v_mul_f32_e32 v37, 0x41800000, v37
	v_med3_f32 v34, v43, s49, v25
	v_med3_f32 v35, v45, s49, v25
	v_med3_f32 v40, v42, s49, v25
	v_med3_f32 v41, v44, s49, v25
	v_cvt_pk_fp8_f32 v32, v34, v35 op_sel:[0,0,1]
	v_med3_f32 v34, v36, s49, v25
	v_med3_f32 v35, v37, s49, v25
	v_cvt_pk_fp8_f32 v30, v40, v41 op_sel:[0,0,1]
	v_cvt_pk_fp8_f32 v33, v34, v35 op_sel:[0,0,1]
	v_or_b32_e32 v34, s18, v8
	v_lshlrev_b32_e32 v34, 10, v34
	v_mov_b32_e32 v35, v1
	v_lshl_add_u64 v[34:35], v[4:5], 0, v[34:35]
	global_store_dwordx4 v[34:35], v[30:33], off sc1
	ds_read2_b32 v[30:31], v11 offset0:64 offset1:96
	ds_read2_b32 v[36:37], v11 offset1:32
	ds_read2_b32 v[32:33], v27 offset0:64 offset1:96
	ds_read2_b32 v[34:35], v11 offset0:128 offset1:160
	ds_read2_b32 v[38:39], v27 offset1:32
	s_waitcnt lgkmcnt(4)
	v_mul_f32_e32 v42, 0x41800000, v30
	v_mul_f32_e32 v44, 0x41800000, v31
	ds_read2_b32 v[30:31], v27 offset0:128 offset1:160
	s_waitcnt lgkmcnt(4)
	v_mul_f32_e32 v40, 0x41800000, v36
	v_mul_f32_e32 v41, 0x41800000, v37
	s_waitcnt lgkmcnt(3)
	v_mul_f32_e32 v43, 0x41800000, v32
	v_mul_f32_e32 v45, 0x41800000, v33
	s_waitcnt lgkmcnt(2)
	v_mul_f32_e32 v34, 0x41800000, v34
	ds_read2_b32 v[32:33], v11 offset0:192 offset1:224
	ds_read2_b32 v[36:37], v27 offset0:192 offset1:224
	s_waitcnt lgkmcnt(2)
	v_mul_f32_e32 v46, 0x41800000, v30
	v_mul_f32_e32 v35, 0x41800000, v35
	v_mul_f32_e32 v47, 0x41800000, v31
	v_med3_f32 v31, v40, s49, v25
	v_med3_f32 v40, v41, s49, v25
	v_mov_b32_e32 v30, v1
	v_cvt_pk_fp8_f32 v30, v31, v40
	v_med3_f32 v34, v34, s49, v25
	v_med3_f32 v35, v35, s49, v25
	v_mov_b32_e32 v31, v1
	v_cvt_pk_fp8_f32 v31, v34, v35
	s_waitcnt lgkmcnt(1)
	v_mul_f32_e32 v32, 0x41800000, v32
	v_mul_f32_e32 v33, 0x41800000, v33
	v_mul_f32_e32 v38, 0x41800000, v38
	v_mul_f32_e32 v39, 0x41800000, v39
	v_med3_f32 v32, v32, s49, v25
	v_med3_f32 v33, v33, s49, v25
	v_cvt_pk_fp8_f32 v31, v32, v33 op_sel:[0,0,1]
	v_med3_f32 v33, v38, s49, v25
	v_med3_f32 v34, v39, s49, v25
	v_mov_b32_e32 v32, v1
	v_cvt_pk_fp8_f32 v32, v33, v34
	v_med3_f32 v38, v46, s49, v25
	v_med3_f32 v39, v47, s49, v25
	v_mov_b32_e32 v33, v1
	v_cvt_pk_fp8_f32 v33, v38, v39
	s_waitcnt lgkmcnt(0)
	v_mul_f32_e32 v36, 0x41800000, v36
	v_mul_f32_e32 v37, 0x41800000, v37
	v_med3_f32 v34, v43, s49, v25
	v_med3_f32 v35, v45, s49, v25
	v_med3_f32 v40, v42, s49, v25
	v_med3_f32 v41, v44, s49, v25
	v_cvt_pk_fp8_f32 v32, v34, v35 op_sel:[0,0,1]
	v_med3_f32 v34, v36, s49, v25
	v_med3_f32 v35, v37, s49, v25
	v_cvt_pk_fp8_f32 v30, v40, v41 op_sel:[0,0,1]
	v_cvt_pk_fp8_f32 v33, v34, v35 op_sel:[0,0,1]
	v_or_b32_e32 v34, s18, v10
	v_lshlrev_b32_e32 v34, 10, v34
	v_mov_b32_e32 v35, v1
	v_lshl_add_u64 v[34:35], v[4:5], 0, v[34:35]
	global_store_dwordx4 v[34:35], v[30:33], off sc1
	ds_read2_b32 v[30:31], v13 offset0:64 offset1:96
	ds_read2_b32 v[36:37], v13 offset1:32
	ds_read2_b32 v[32:33], v28 offset0:64 offset1:96
	ds_read2_b32 v[34:35], v13 offset0:128 offset1:160
	ds_read2_b32 v[38:39], v28 offset1:32
	s_waitcnt lgkmcnt(4)
	v_mul_f32_e32 v42, 0x41800000, v30
	v_mul_f32_e32 v44, 0x41800000, v31
	ds_read2_b32 v[30:31], v28 offset0:128 offset1:160
	s_waitcnt lgkmcnt(4)
	v_mul_f32_e32 v40, 0x41800000, v36
	v_mul_f32_e32 v41, 0x41800000, v37
	s_waitcnt lgkmcnt(3)
	v_mul_f32_e32 v43, 0x41800000, v32
	v_mul_f32_e32 v45, 0x41800000, v33
	s_waitcnt lgkmcnt(2)
	v_mul_f32_e32 v34, 0x41800000, v34
	ds_read2_b32 v[32:33], v13 offset0:192 offset1:224
	ds_read2_b32 v[36:37], v28 offset0:192 offset1:224
	s_waitcnt lgkmcnt(2)
	v_mul_f32_e32 v46, 0x41800000, v30
	v_mul_f32_e32 v35, 0x41800000, v35
	v_mul_f32_e32 v47, 0x41800000, v31
	v_med3_f32 v31, v40, s49, v25
	v_med3_f32 v40, v41, s49, v25
	v_mov_b32_e32 v30, v1
	v_cvt_pk_fp8_f32 v30, v31, v40
	v_med3_f32 v34, v34, s49, v25
	v_med3_f32 v35, v35, s49, v25
	v_mov_b32_e32 v31, v1
	v_cvt_pk_fp8_f32 v31, v34, v35
	s_waitcnt lgkmcnt(1)
	v_mul_f32_e32 v32, 0x41800000, v32
	v_mul_f32_e32 v33, 0x41800000, v33
	v_mul_f32_e32 v38, 0x41800000, v38
	v_mul_f32_e32 v39, 0x41800000, v39
	v_med3_f32 v32, v32, s49, v25
	v_med3_f32 v33, v33, s49, v25
	v_cvt_pk_fp8_f32 v31, v32, v33 op_sel:[0,0,1]
	v_med3_f32 v33, v38, s49, v25
	v_med3_f32 v34, v39, s49, v25
	v_mov_b32_e32 v32, v1
	v_cvt_pk_fp8_f32 v32, v33, v34
	v_med3_f32 v38, v46, s49, v25
	v_med3_f32 v39, v47, s49, v25
	v_mov_b32_e32 v33, v1
	v_cvt_pk_fp8_f32 v33, v38, v39
	s_waitcnt lgkmcnt(0)
	v_mul_f32_e32 v36, 0x41800000, v36
	v_mul_f32_e32 v37, 0x41800000, v37
	v_med3_f32 v34, v43, s49, v25
	v_med3_f32 v35, v45, s49, v25
	v_med3_f32 v40, v42, s49, v25
	v_med3_f32 v41, v44, s49, v25
	v_cvt_pk_fp8_f32 v32, v34, v35 op_sel:[0,0,1]
	v_med3_f32 v34, v36, s49, v25
	v_med3_f32 v35, v37, s49, v25
	v_cvt_pk_fp8_f32 v30, v40, v41 op_sel:[0,0,1]
	v_cvt_pk_fp8_f32 v33, v34, v35 op_sel:[0,0,1]
	v_or_b32_e32 v34, s18, v12
	v_lshlrev_b32_e32 v34, 10, v34
	v_mov_b32_e32 v35, v1
	v_lshl_add_u64 v[4:5], v[4:5], 0, v[34:35]
	global_store_dwordx4 v[4:5], v[30:33], off sc1
	s_waitcnt lgkmcnt(0)
	s_mov_b64 s[18:19], 0
.LBB0_181:
	s_andn2_b64 vcc, exec, s[18:19]
	s_cbranch_vccnz .LBB0_183
	s_waitcnt lgkmcnt(0)
	s_add_u32 s16, s6, s16
	s_addc_u32 s17, s7, s17
	s_lshl_b64 s[18:19], s[14:15], 22
	s_add_u32 s15, s20, s18
	s_addc_u32 s18, s21, s19
	s_and_b32 s19, s27, 0x780
	v_or_b32_e32 v4, s19, v24
	s_and_b32 s10, s25, 0x3e0
	v_lshlrev_b32_e32 v4, 12, v4
	v_mov_b32_e32 v5, v1
	v_lshl_add_u64 v[4:5], s[16:17], 0, v[4:5]
	s_lshl_b32 s10, s10, 2
	v_lshl_add_u64 v[4:5], v[4:5], 0, s[10:11]
	v_lshl_add_u64 v[4:5], v[4:5], 0, v[0:1]
	v_add_co_u32_e32 v34, vcc, s50, v4
	s_mul_i32 s10, s14, 0xfffe8000
	s_nop 0
	v_addc_co_u32_e32 v35, vcc, 0, v5, vcc
	v_add_co_u32_e32 v38, vcc, s31, v4
	global_load_dwordx4 v[30:33], v[4:5], off
	s_nop 0
	global_load_dwordx4 v[34:37], v[34:35], off
	v_addc_co_u32_e32 v39, vcc, 0, v5, vcc
	v_add_co_u32_e32 v42, vcc, s51, v4
	s_add_u32 s16, s15, s19
	s_nop 0
	v_addc_co_u32_e32 v43, vcc, 0, v5, vcc
	v_add_co_u32_e32 v46, vcc, s35, v4
	global_load_dwordx4 v[38:41], v[38:39], off
	s_nop 0
	global_load_dwordx4 v[42:45], v[42:43], off
	v_addc_co_u32_e32 v47, vcc, 0, v5, vcc
	v_add_co_u32_e32 v50, vcc, s52, v4
	s_addc_u32 s17, s18, 0
	s_nop 0
	v_addc_co_u32_e32 v51, vcc, 0, v5, vcc
	v_add_co_u32_e32 v54, vcc, s36, v4
	global_load_dwordx4 v[46:49], v[46:47], off
	s_nop 0
	global_load_dwordx4 v[50:53], v[50:51], off
	v_addc_co_u32_e32 v55, vcc, 0, v5, vcc
	v_add_co_u32_e32 v58, vcc, s53, v4
	s_nop 1
	v_addc_co_u32_e32 v59, vcc, 0, v5, vcc
	v_add_co_u32_e32 v62, vcc, s37, v4
	global_load_dwordx4 v[54:57], v[54:55], off
	s_nop 0
	global_load_dwordx4 v[58:61], v[58:59], off
	v_addc_co_u32_e32 v63, vcc, 0, v5, vcc
	v_add_co_u32_e32 v66, vcc, s54, v4
	s_nop 1
	v_addc_co_u32_e32 v67, vcc, 0, v5, vcc
	v_add_co_u32_e32 v70, vcc, s38, v4
	global_load_dwordx4 v[62:65], v[62:63], off
	s_nop 0
	global_load_dwordx4 v[66:69], v[66:67], off
	v_addc_co_u32_e32 v71, vcc, 0, v5, vcc
	v_add_co_u32_e32 v74, vcc, s55, v4
	s_nop 1
	v_addc_co_u32_e32 v75, vcc, 0, v5, vcc
	v_add_co_u32_e32 v78, vcc, s39, v4
	global_load_dwordx4 v[70:73], v[70:71], off
	s_nop 0
	global_load_dwordx4 v[74:77], v[74:75], off
	v_addc_co_u32_e32 v79, vcc, 0, v5, vcc
	v_add_co_u32_e32 v82, vcc, s56, v4
	s_nop 1
	v_addc_co_u32_e32 v83, vcc, 0, v5, vcc
	v_add_co_u32_e32 v86, vcc, s40, v4
	global_load_dwordx4 v[78:81], v[78:79], off
	s_nop 0
	global_load_dwordx4 v[82:85], v[82:83], off
	v_addc_co_u32_e32 v87, vcc, 0, v5, vcc
	v_add_co_u32_e32 v4, vcc, s57, v4
	s_nop 1
	v_addc_co_u32_e32 v5, vcc, 0, v5, vcc
	global_load_dwordx4 v[86:89], v[86:87], off
	s_nop 0
	global_load_dwordx4 v[90:93], v[4:5], off
	v_lshl_add_u64 v[4:5], s[16:17], 0, v[2:3]
	s_waitcnt vmcnt(15)
	ds_write_b128 v22, v[30:33]
	s_waitcnt vmcnt(14)
	ds_write_b128 v22, v[34:37] offset:1024
	s_waitcnt vmcnt(13)
	ds_write_b128 v15, v[38:41] offset:2048
	s_waitcnt vmcnt(12)
	ds_write_b128 v15, v[42:45] offset:3072
	s_waitcnt vmcnt(11)
	ds_write_b128 v16, v[46:49] offset:4096
	s_waitcnt vmcnt(10)
	ds_write_b128 v16, v[50:53] offset:5120
	s_waitcnt vmcnt(9)
	ds_write_b128 v17, v[54:57] offset:6144
	s_waitcnt vmcnt(8)
	ds_write_b128 v17, v[58:61] offset:7168
	s_waitcnt vmcnt(7)
	ds_write_b128 v18, v[62:65] offset:8192
	s_waitcnt vmcnt(6)
	ds_write_b128 v18, v[66:69] offset:9216
	s_waitcnt vmcnt(5)
	ds_write_b128 v19, v[70:73] offset:10240
	s_waitcnt vmcnt(4)
	ds_write_b128 v19, v[74:77] offset:11264
	s_waitcnt vmcnt(3)
	ds_write_b128 v20, v[78:81] offset:12288
	s_waitcnt vmcnt(2)
	ds_write_b128 v20, v[82:85] offset:13312
	s_waitcnt vmcnt(1)
	ds_write_b128 v21, v[86:89] offset:14336
	s_waitcnt vmcnt(0)
	ds_write_b128 v21, v[90:93] offset:15360
	s_waitcnt lgkmcnt(0)
	ds_read2_b32 v[30:31], v7 offset1:32
	ds_read2_b32 v[32:33], v23 offset1:32
	ds_read2_b32 v[34:35], v7 offset0:64 offset1:96
	ds_read2_b32 v[36:37], v23 offset0:64 offset1:96
	s_waitcnt lgkmcnt(3)
	v_mul_f32_e32 v38, 0x42000000, v30
	s_waitcnt lgkmcnt(2)
	v_mul_f32_e32 v39, 0x42000000, v32
	v_mul_f32_e32 v40, 0x42000000, v31
	v_mul_f32_e32 v41, 0x42000000, v33
	s_waitcnt lgkmcnt(1)
	v_mul_f32_e32 v42, 0x42000000, v34
	ds_read2_b32 v[30:31], v7 offset0:128 offset1:160
	s_waitcnt lgkmcnt(1)
	v_mul_f32_e32 v43, 0x42000000, v36
	v_mul_f32_e32 v44, 0x42000000, v35
	ds_read2_b32 v[32:33], v23 offset0:128 offset1:160
	v_mul_f32_e32 v45, 0x42000000, v37
	ds_read2_b32 v[34:35], v7 offset0:192 offset1:224
	ds_read2_b32 v[36:37], v23 offset0:192 offset1:224
	s_waitcnt lgkmcnt(3)
	v_mul_f32_e32 v46, 0x42000000, v30
	v_mul_f32_e32 v31, 0x42000000, v31
	s_waitcnt lgkmcnt(2)
	v_mul_f32_e32 v47, 0x42000000, v32
	s_waitcnt lgkmcnt(1)
	v_mul_f32_e32 v32, 0x42000000, v34
	s_waitcnt lgkmcnt(0)
	v_mul_f32_e32 v34, 0x42000000, v36
	v_mul_f32_e32 v36, 0x42000000, v37
	v_med3_f32 v37, v38, s49, v25
	v_med3_f32 v38, v40, s49, v25
	v_mov_b32_e32 v30, v1
	v_cvt_pk_fp8_f32 v30, v37, v38
	v_med3_f32 v37, v42, s49, v25
	v_med3_f32 v40, v46, s49, v25
	v_med3_f32 v42, v31, s49, v25
	v_mov_b32_e32 v31, v1
	v_cvt_pk_fp8_f32 v31, v40, v42
	v_mul_f32_e32 v35, 0x42000000, v35
	v_med3_f32 v38, v44, s49, v25
	v_med3_f32 v32, v32, s49, v25
	v_med3_f32 v35, v35, s49, v25
	v_mul_f32_e32 v33, 0x42000000, v33
	v_cvt_pk_fp8_f32 v30, v37, v38 op_sel:[0,0,1]
	v_cvt_pk_fp8_f32 v31, v32, v35 op_sel:[0,0,1]
	v_med3_f32 v35, v39, s49, v25
	v_med3_f32 v37, v41, s49, v25
	v_mov_b32_e32 v32, v1
	v_cvt_pk_fp8_f32 v32, v35, v37
	v_med3_f32 v38, v47, s49, v25
	v_med3_f32 v39, v33, s49, v25
	v_mov_b32_e32 v33, v1
	v_cvt_pk_fp8_f32 v33, v38, v39
	v_med3_f32 v35, v43, s49, v25
	v_med3_f32 v37, v45, s49, v25
	v_cvt_pk_fp8_f32 v32, v35, v37 op_sel:[0,0,1]
	v_med3_f32 v34, v34, s49, v25
	v_med3_f32 v35, v36, s49, v25
	v_add_u32_e32 v40, s10, v14
	v_cvt_pk_fp8_f32 v33, v34, v35 op_sel:[0,0,1]
	v_add_u32_e32 v34, 0xffff8000, v40
	v_and_or_b32 v34, v34, s58, v24
	v_lshl_or_b32 v34, v34, 11, v29
	v_mov_b32_e32 v35, v1
	v_lshl_add_u64 v[34:35], v[4:5], 0, v[34:35]
	global_store_dwordx4 v[34:35], v[30:33], off sc1
	ds_read2_b32 v[30:31], v9 offset0:64 offset1:96
	ds_read2_b32 v[36:37], v9 offset1:32
	ds_read2_b32 v[32:33], v26 offset0:64 offset1:96
	ds_read2_b32 v[34:35], v9 offset0:128 offset1:160
	ds_read2_b32 v[38:39], v26 offset1:32
	s_waitcnt lgkmcnt(4)
	v_mul_f32_e32 v43, 0x42000000, v30
	v_mul_f32_e32 v45, 0x42000000, v31
	ds_read2_b32 v[30:31], v26 offset0:128 offset1:160
	s_waitcnt lgkmcnt(4)
	v_mul_f32_e32 v41, 0x42000000, v36
	v_mul_f32_e32 v42, 0x42000000, v37
	s_waitcnt lgkmcnt(3)
	v_mul_f32_e32 v44, 0x42000000, v32
	v_mul_f32_e32 v46, 0x42000000, v33
	s_waitcnt lgkmcnt(2)
	v_mul_f32_e32 v34, 0x42000000, v34
	ds_read2_b32 v[32:33], v9 offset0:192 offset1:224
	ds_read2_b32 v[36:37], v26 offset0:192 offset1:224
	s_waitcnt lgkmcnt(2)
	v_mul_f32_e32 v47, 0x42000000, v30
	v_mul_f32_e32 v35, 0x42000000, v35
	v_mul_f32_e32 v48, 0x42000000, v31
	v_med3_f32 v31, v41, s49, v25
	v_med3_f32 v41, v42, s49, v25
	v_mov_b32_e32 v30, v1
	v_cvt_pk_fp8_f32 v30, v31, v41
	v_med3_f32 v34, v34, s49, v25
	v_med3_f32 v35, v35, s49, v25
	v_mov_b32_e32 v31, v1
	v_cvt_pk_fp8_f32 v31, v34, v35
	s_waitcnt lgkmcnt(1)
	v_mul_f32_e32 v32, 0x42000000, v32
	v_mul_f32_e32 v33, 0x42000000, v33
	v_mul_f32_e32 v38, 0x42000000, v38
	v_mul_f32_e32 v39, 0x42000000, v39
	v_med3_f32 v32, v32, s49, v25
	v_med3_f32 v33, v33, s49, v25
	v_cvt_pk_fp8_f32 v31, v32, v33 op_sel:[0,0,1]
	v_med3_f32 v33, v38, s49, v25
	v_med3_f32 v34, v39, s49, v25
	v_mov_b32_e32 v32, v1
	v_cvt_pk_fp8_f32 v32, v33, v34
	v_med3_f32 v38, v47, s49, v25
	v_med3_f32 v39, v48, s49, v25
	v_mov_b32_e32 v33, v1
	v_cvt_pk_fp8_f32 v33, v38, v39
	s_waitcnt lgkmcnt(0)
	v_mul_f32_e32 v36, 0x42000000, v36
	v_mul_f32_e32 v37, 0x42000000, v37
	v_med3_f32 v34, v44, s49, v25
	v_med3_f32 v35, v46, s49, v25
	v_med3_f32 v41, v43, s49, v25
	v_med3_f32 v42, v45, s49, v25
	v_cvt_pk_fp8_f32 v32, v34, v35 op_sel:[0,0,1]
	v_med3_f32 v34, v36, s49, v25
	v_med3_f32 v35, v37, s49, v25
	v_cvt_pk_fp8_f32 v30, v41, v42 op_sel:[0,0,1]
	v_cvt_pk_fp8_f32 v33, v34, v35 op_sel:[0,0,1]
	v_add_u32_e32 v34, 0xffff8010, v40
	v_and_or_b32 v34, v34, s59, v24
	v_lshl_or_b32 v34, v34, 11, v29
	v_mov_b32_e32 v35, v1
	v_lshl_add_u64 v[34:35], v[4:5], 0, v[34:35]
	global_store_dwordx4 v[34:35], v[30:33], off sc1
	ds_read2_b32 v[30:31], v11 offset0:64 offset1:96
	ds_read2_b32 v[36:37], v11 offset1:32
	ds_read2_b32 v[32:33], v27 offset0:64 offset1:96
	ds_read2_b32 v[34:35], v11 offset0:128 offset1:160
	ds_read2_b32 v[38:39], v27 offset1:32
	s_waitcnt lgkmcnt(4)
	v_mul_f32_e32 v43, 0x42000000, v30
	v_mul_f32_e32 v45, 0x42000000, v31
	ds_read2_b32 v[30:31], v27 offset0:128 offset1:160
	s_waitcnt lgkmcnt(4)
	v_mul_f32_e32 v41, 0x42000000, v36
	v_mul_f32_e32 v42, 0x42000000, v37
	s_waitcnt lgkmcnt(3)
	v_mul_f32_e32 v44, 0x42000000, v32
	v_mul_f32_e32 v46, 0x42000000, v33
	s_waitcnt lgkmcnt(2)
	v_mul_f32_e32 v34, 0x42000000, v34
	ds_read2_b32 v[32:33], v11 offset0:192 offset1:224
	ds_read2_b32 v[36:37], v27 offset0:192 offset1:224
	s_waitcnt lgkmcnt(2)
	v_mul_f32_e32 v47, 0x42000000, v30
	v_mul_f32_e32 v35, 0x42000000, v35
	v_mul_f32_e32 v48, 0x42000000, v31
	v_med3_f32 v31, v41, s49, v25
	v_med3_f32 v41, v42, s49, v25
	v_mov_b32_e32 v30, v1
	v_cvt_pk_fp8_f32 v30, v31, v41
	v_med3_f32 v34, v34, s49, v25
	v_med3_f32 v35, v35, s49, v25
	v_mov_b32_e32 v31, v1
	v_cvt_pk_fp8_f32 v31, v34, v35
	s_waitcnt lgkmcnt(1)
	v_mul_f32_e32 v32, 0x42000000, v32
	v_mul_f32_e32 v33, 0x42000000, v33
	v_mul_f32_e32 v38, 0x42000000, v38
	v_mul_f32_e32 v39, 0x42000000, v39
	v_med3_f32 v32, v32, s49, v25
	v_med3_f32 v33, v33, s49, v25
	v_cvt_pk_fp8_f32 v31, v32, v33 op_sel:[0,0,1]
	v_med3_f32 v33, v38, s49, v25
	v_med3_f32 v34, v39, s49, v25
	v_mov_b32_e32 v32, v1
	v_cvt_pk_fp8_f32 v32, v33, v34
	v_med3_f32 v38, v47, s49, v25
	v_med3_f32 v39, v48, s49, v25
	v_mov_b32_e32 v33, v1
	v_cvt_pk_fp8_f32 v33, v38, v39
	s_waitcnt lgkmcnt(0)
	v_mul_f32_e32 v36, 0x42000000, v36
	v_mul_f32_e32 v37, 0x42000000, v37
	v_med3_f32 v34, v44, s49, v25
	v_med3_f32 v35, v46, s49, v25
	v_med3_f32 v41, v43, s49, v25
	v_med3_f32 v42, v45, s49, v25
	v_cvt_pk_fp8_f32 v32, v34, v35 op_sel:[0,0,1]
	v_med3_f32 v34, v36, s49, v25
	v_med3_f32 v35, v37, s49, v25
	v_cvt_pk_fp8_f32 v30, v41, v42 op_sel:[0,0,1]
	v_cvt_pk_fp8_f32 v33, v34, v35 op_sel:[0,0,1]
	v_add_u32_e32 v34, 0xffff8020, v40
	v_and_or_b32 v34, v34, s60, v24
	v_lshl_or_b32 v34, v34, 11, v29
	v_mov_b32_e32 v35, v1
	v_lshl_add_u64 v[34:35], v[4:5], 0, v[34:35]
	global_store_dwordx4 v[34:35], v[30:33], off sc1
	ds_read2_b32 v[30:31], v13 offset0:64 offset1:96
	ds_read2_b32 v[36:37], v13 offset1:32
	ds_read2_b32 v[32:33], v28 offset0:64 offset1:96
	ds_read2_b32 v[34:35], v13 offset0:128 offset1:160
	ds_read2_b32 v[38:39], v28 offset1:32
	s_waitcnt lgkmcnt(4)
	v_mul_f32_e32 v43, 0x42000000, v30
	v_mul_f32_e32 v45, 0x42000000, v31
	ds_read2_b32 v[30:31], v28 offset0:128 offset1:160
	s_waitcnt lgkmcnt(4)
	v_mul_f32_e32 v41, 0x42000000, v36
	v_mul_f32_e32 v42, 0x42000000, v37
	s_waitcnt lgkmcnt(3)
	v_mul_f32_e32 v44, 0x42000000, v32
	v_mul_f32_e32 v46, 0x42000000, v33
	s_waitcnt lgkmcnt(2)
	v_mul_f32_e32 v34, 0x42000000, v34
	ds_read2_b32 v[32:33], v13 offset0:192 offset1:224
	ds_read2_b32 v[36:37], v28 offset0:192 offset1:224
	s_waitcnt lgkmcnt(2)
	v_mul_f32_e32 v47, 0x42000000, v30
	v_mul_f32_e32 v35, 0x42000000, v35
	v_mul_f32_e32 v48, 0x42000000, v31
	v_med3_f32 v31, v41, s49, v25
	v_med3_f32 v41, v42, s49, v25
	v_mov_b32_e32 v30, v1
	v_cvt_pk_fp8_f32 v30, v31, v41
	v_med3_f32 v34, v34, s49, v25
	v_med3_f32 v35, v35, s49, v25
	v_mov_b32_e32 v31, v1
	v_cvt_pk_fp8_f32 v31, v34, v35
	s_waitcnt lgkmcnt(1)
	v_mul_f32_e32 v32, 0x42000000, v32
	v_mul_f32_e32 v33, 0x42000000, v33
	v_mul_f32_e32 v38, 0x42000000, v38
	v_mul_f32_e32 v39, 0x42000000, v39
	v_med3_f32 v32, v32, s49, v25
	v_med3_f32 v33, v33, s49, v25
	v_cvt_pk_fp8_f32 v31, v32, v33 op_sel:[0,0,1]
	v_med3_f32 v33, v38, s49, v25
	v_med3_f32 v34, v39, s49, v25
	v_mov_b32_e32 v32, v1
	v_cvt_pk_fp8_f32 v32, v33, v34
	v_med3_f32 v38, v47, s49, v25
	v_med3_f32 v39, v48, s49, v25
	v_mov_b32_e32 v33, v1
	v_cvt_pk_fp8_f32 v33, v38, v39
	s_waitcnt lgkmcnt(0)
	v_mul_f32_e32 v36, 0x42000000, v36
	v_mul_f32_e32 v37, 0x42000000, v37
	v_med3_f32 v34, v44, s49, v25
	v_med3_f32 v35, v46, s49, v25
	v_med3_f32 v41, v43, s49, v25
	v_med3_f32 v42, v45, s49, v25
	v_cvt_pk_fp8_f32 v32, v34, v35 op_sel:[0,0,1]
	v_med3_f32 v34, v36, s49, v25
	v_med3_f32 v35, v37, s49, v25
	v_cvt_pk_fp8_f32 v30, v41, v42 op_sel:[0,0,1]
	v_cvt_pk_fp8_f32 v33, v34, v35 op_sel:[0,0,1]
	v_add_u32_e32 v34, 0xffff8030, v40
	v_and_or_b32 v34, v34, s61, v24
	v_lshl_or_b32 v34, v34, 11, v29
	v_mov_b32_e32 v35, v1
	v_lshl_add_u64 v[4:5], v[4:5], 0, v[34:35]
	global_store_dwordx4 v[4:5], v[30:33], off sc1
	s_waitcnt lgkmcnt(0)

.LBB0_184:
	s_andn2_b64 vcc, exec, s[16:17]
	s_cbranch_vccnz .LBB0_177
	s_ashr_i32 s15, s14, 31
	s_lshl_b64 s[16:17], s[14:15], 23
	s_waitcnt lgkmcnt(0)
	s_add_u32 s16, s4, s16
	s_addc_u32 s17, s5, s17
	s_lshl_b64 s[14:15], s[14:15], 22
	s_add_u32 s10, s20, s14
	s_addc_u32 s18, s21, s15
	s_bfe_u32 s14, s65, 0x5001a
	s_add_i32 s14, s65, s14
	s_sext_i32_i16 s15, s14
	s_lshl_b32 s15, s15, 2
	s_and_b32 s14, s14, 0xffe0
	s_and_b32 s19, s15, 0xffffff80
	s_sub_i32 s14, s65, s14
	v_or_b32_e32 v4, s19, v24
	s_sext_i32_i16 s14, s14
	v_ashrrev_i32_e32 v5, 31, v4
	s_lshl_b32 s14, s14, 5
	v_lshlrev_b64 v[4:5], 12, v[4:5]
	v_lshl_add_u64 v[4:5], s[16:17], 0, v[4:5]
	s_ashr_i32 s15, s14, 31
	v_lshl_add_u64 v[4:5], s[14:15], 2, v[4:5]
	v_lshl_add_u64 v[4:5], v[4:5], 0, v[0:1]
	v_add_co_u32_e32 v34, vcc, s50, v4
	s_ashr_i32 s15, s19, 31
	s_nop 0
	v_addc_co_u32_e32 v35, vcc, 0, v5, vcc
	v_add_co_u32_e32 v38, vcc, s31, v4
	global_load_dwordx4 v[30:33], v[4:5], off
	s_nop 0
	global_load_dwordx4 v[34:37], v[34:35], off
	v_addc_co_u32_e32 v39, vcc, 0, v5, vcc
	v_add_co_u32_e32 v42, vcc, s51, v4
	s_add_u32 s16, s10, s19
	s_nop 0
	v_addc_co_u32_e32 v43, vcc, 0, v5, vcc
	v_add_co_u32_e32 v46, vcc, s35, v4
	global_load_dwordx4 v[38:41], v[38:39], off
	s_nop 0
	global_load_dwordx4 v[42:45], v[42:43], off
	v_addc_co_u32_e32 v47, vcc, 0, v5, vcc
	v_add_co_u32_e32 v50, vcc, s52, v4
	s_addc_u32 s17, s18, s15
	s_nop 0
	v_addc_co_u32_e32 v51, vcc, 0, v5, vcc
	v_add_co_u32_e32 v54, vcc, s36, v4
	global_load_dwordx4 v[46:49], v[46:47], off
	s_nop 0
	global_load_dwordx4 v[50:53], v[50:51], off
	v_addc_co_u32_e32 v55, vcc, 0, v5, vcc
	v_add_co_u32_e32 v58, vcc, s53, v4
	s_nop 1
	v_addc_co_u32_e32 v59, vcc, 0, v5, vcc
	v_add_co_u32_e32 v62, vcc, s37, v4
	global_load_dwordx4 v[54:57], v[54:55], off
	s_nop 0
	global_load_dwordx4 v[58:61], v[58:59], off
	v_addc_co_u32_e32 v63, vcc, 0, v5, vcc
	v_add_co_u32_e32 v66, vcc, s54, v4
	s_nop 1
	v_addc_co_u32_e32 v67, vcc, 0, v5, vcc
	v_add_co_u32_e32 v70, vcc, s38, v4
	global_load_dwordx4 v[62:65], v[62:63], off
	s_nop 0
	global_load_dwordx4 v[66:69], v[66:67], off
	v_addc_co_u32_e32 v71, vcc, 0, v5, vcc
	v_add_co_u32_e32 v74, vcc, s55, v4
	s_nop 1
	v_addc_co_u32_e32 v75, vcc, 0, v5, vcc
	v_add_co_u32_e32 v78, vcc, s39, v4
	global_load_dwordx4 v[70:73], v[70:71], off
	s_nop 0
	global_load_dwordx4 v[74:77], v[74:75], off
	v_addc_co_u32_e32 v79, vcc, 0, v5, vcc
	v_add_co_u32_e32 v82, vcc, s56, v4
	s_nop 1
	v_addc_co_u32_e32 v83, vcc, 0, v5, vcc
	v_add_co_u32_e32 v86, vcc, s40, v4
	global_load_dwordx4 v[78:81], v[78:79], off
	s_nop 0
	global_load_dwordx4 v[82:85], v[82:83], off
	v_addc_co_u32_e32 v87, vcc, 0, v5, vcc
	v_add_co_u32_e32 v4, vcc, s57, v4
	s_nop 1
	v_addc_co_u32_e32 v5, vcc, 0, v5, vcc
	global_load_dwordx4 v[86:89], v[86:87], off
	s_nop 0
	global_load_dwordx4 v[90:93], v[4:5], off
	v_lshl_add_u64 v[4:5], s[16:17], 0, v[2:3]
	s_waitcnt vmcnt(15)
	ds_write_b128 v22, v[30:33]
	s_waitcnt vmcnt(14)
	ds_write_b128 v22, v[34:37] offset:1024
	s_waitcnt vmcnt(13)
	ds_write_b128 v15, v[38:41] offset:2048
	s_waitcnt vmcnt(12)
	ds_write_b128 v15, v[42:45] offset:3072
	s_waitcnt vmcnt(11)
	ds_write_b128 v16, v[46:49] offset:4096
	s_waitcnt vmcnt(10)
	ds_write_b128 v16, v[50:53] offset:5120
	s_waitcnt vmcnt(9)
	ds_write_b128 v17, v[54:57] offset:6144
	s_waitcnt vmcnt(8)
	ds_write_b128 v17, v[58:61] offset:7168
	s_waitcnt vmcnt(7)
	ds_write_b128 v18, v[62:65] offset:8192
	s_waitcnt vmcnt(6)
	ds_write_b128 v18, v[66:69] offset:9216
	s_waitcnt vmcnt(5)
	ds_write_b128 v19, v[70:73] offset:10240
	s_waitcnt vmcnt(4)
	ds_write_b128 v19, v[74:77] offset:11264
	s_waitcnt vmcnt(3)
	ds_write_b128 v20, v[78:81] offset:12288
	s_waitcnt vmcnt(2)
	ds_write_b128 v20, v[82:85] offset:13312
	s_waitcnt vmcnt(1)
	ds_write_b128 v21, v[86:89] offset:14336
	s_waitcnt vmcnt(0)
	ds_write_b128 v21, v[90:93] offset:15360
	s_waitcnt lgkmcnt(0)
	ds_read2_b32 v[30:31], v7 offset1:32
	ds_read2_b32 v[32:33], v23 offset1:32
	ds_read2_b32 v[34:35], v7 offset0:64 offset1:96
	ds_read2_b32 v[36:37], v23 offset0:64 offset1:96
	s_waitcnt lgkmcnt(3)
	v_mul_f32_e32 v38, 0x42000000, v30
	s_waitcnt lgkmcnt(2)
	v_mul_f32_e32 v39, 0x42000000, v32
	v_mul_f32_e32 v40, 0x42000000, v31
	v_mul_f32_e32 v41, 0x42000000, v33
	s_waitcnt lgkmcnt(1)
	v_mul_f32_e32 v42, 0x42000000, v34
	ds_read2_b32 v[30:31], v7 offset0:128 offset1:160
	s_waitcnt lgkmcnt(1)
	v_mul_f32_e32 v43, 0x42000000, v36
	v_mul_f32_e32 v44, 0x42000000, v35
	ds_read2_b32 v[32:33], v23 offset0:128 offset1:160
	v_mul_f32_e32 v45, 0x42000000, v37
	ds_read2_b32 v[34:35], v7 offset0:192 offset1:224
	ds_read2_b32 v[36:37], v23 offset0:192 offset1:224
	s_waitcnt lgkmcnt(3)
	v_mul_f32_e32 v46, 0x42000000, v30
	v_mul_f32_e32 v31, 0x42000000, v31
	s_waitcnt lgkmcnt(2)
	v_mul_f32_e32 v47, 0x42000000, v32
	s_waitcnt lgkmcnt(1)
	v_mul_f32_e32 v32, 0x42000000, v34
	s_waitcnt lgkmcnt(0)
	v_mul_f32_e32 v34, 0x42000000, v36
	v_mul_f32_e32 v36, 0x42000000, v37
	v_med3_f32 v37, v38, s49, v25
	v_med3_f32 v38, v40, s49, v25
	v_mov_b32_e32 v30, v1
	v_cvt_pk_fp8_f32 v30, v37, v38
	v_med3_f32 v37, v42, s49, v25
	v_med3_f32 v40, v46, s49, v25
	v_med3_f32 v42, v31, s49, v25
	v_mov_b32_e32 v31, v1
	v_cvt_pk_fp8_f32 v31, v40, v42
	v_mul_f32_e32 v35, 0x42000000, v35
	v_med3_f32 v38, v44, s49, v25
	v_med3_f32 v32, v32, s49, v25
	v_med3_f32 v35, v35, s49, v25
	v_mul_f32_e32 v33, 0x42000000, v33
	v_cvt_pk_fp8_f32 v30, v37, v38 op_sel:[0,0,1]
	v_cvt_pk_fp8_f32 v31, v32, v35 op_sel:[0,0,1]
	v_med3_f32 v35, v39, s49, v25
	v_med3_f32 v37, v41, s49, v25
	v_mov_b32_e32 v32, v1
	v_cvt_pk_fp8_f32 v32, v35, v37
	v_med3_f32 v38, v47, s49, v25
	v_med3_f32 v39, v33, s49, v25
	v_mov_b32_e32 v33, v1
	v_cvt_pk_fp8_f32 v33, v38, v39
	v_med3_f32 v35, v43, s49, v25
	v_med3_f32 v37, v45, s49, v25
	v_cvt_pk_fp8_f32 v32, v35, v37 op_sel:[0,0,1]
	v_med3_f32 v34, v34, s49, v25
	v_med3_f32 v35, v36, s49, v25
	v_cvt_pk_fp8_f32 v33, v34, v35 op_sel:[0,0,1]
	v_or_b32_e32 v34, s14, v24
	v_lshlrev_b32_e32 v34, 1, v34
	v_and_or_b32 v34, v34, s62, v6
	v_ashrrev_i32_e32 v35, 31, v34
	v_lshlrev_b64 v[34:35], 11, v[34:35]
	v_lshl_add_u64 v[34:35], v[4:5], 0, v[34:35]
	global_store_dwordx4 v[34:35], v[30:33], off sc1
	ds_read2_b32 v[30:31], v9 offset0:64 offset1:96
	ds_read2_b32 v[36:37], v9 offset1:32
	ds_read2_b32 v[32:33], v26 offset0:64 offset1:96
	ds_read2_b32 v[34:35], v9 offset0:128 offset1:160
	ds_read2_b32 v[38:39], v26 offset1:32
	s_waitcnt lgkmcnt(4)
	v_mul_f32_e32 v42, 0x42000000, v30
	v_mul_f32_e32 v44, 0x42000000, v31
	ds_read2_b32 v[30:31], v26 offset0:128 offset1:160
	s_waitcnt lgkmcnt(4)
	v_mul_f32_e32 v40, 0x42000000, v36
	v_mul_f32_e32 v41, 0x42000000, v37
	s_waitcnt lgkmcnt(3)
	v_mul_f32_e32 v43, 0x42000000, v32
	v_mul_f32_e32 v45, 0x42000000, v33
	s_waitcnt lgkmcnt(2)
	v_mul_f32_e32 v34, 0x42000000, v34
	ds_read2_b32 v[32:33], v9 offset0:192 offset1:224
	ds_read2_b32 v[36:37], v26 offset0:192 offset1:224
	s_waitcnt lgkmcnt(2)
	v_mul_f32_e32 v46, 0x42000000, v30
	v_mul_f32_e32 v35, 0x42000000, v35
	v_mul_f32_e32 v47, 0x42000000, v31
	v_med3_f32 v31, v40, s49, v25
	v_med3_f32 v40, v41, s49, v25
	v_mov_b32_e32 v30, v1
	v_cvt_pk_fp8_f32 v30, v31, v40
	v_med3_f32 v34, v34, s49, v25
	v_med3_f32 v35, v35, s49, v25
	v_mov_b32_e32 v31, v1
	v_cvt_pk_fp8_f32 v31, v34, v35
	s_waitcnt lgkmcnt(1)
	v_mul_f32_e32 v32, 0x42000000, v32
	v_mul_f32_e32 v33, 0x42000000, v33
	v_mul_f32_e32 v38, 0x42000000, v38
	v_mul_f32_e32 v39, 0x42000000, v39
	v_med3_f32 v32, v32, s49, v25
	v_med3_f32 v33, v33, s49, v25
	v_cvt_pk_fp8_f32 v31, v32, v33 op_sel:[0,0,1]
	v_med3_f32 v33, v38, s49, v25
	v_med3_f32 v34, v39, s49, v25
	v_mov_b32_e32 v32, v1
	v_cvt_pk_fp8_f32 v32, v33, v34
	v_med3_f32 v38, v46, s49, v25
	v_med3_f32 v39, v47, s49, v25
	v_mov_b32_e32 v33, v1
	v_cvt_pk_fp8_f32 v33, v38, v39
	s_waitcnt lgkmcnt(0)
	v_mul_f32_e32 v36, 0x42000000, v36
	v_mul_f32_e32 v37, 0x42000000, v37
	v_med3_f32 v34, v43, s49, v25
	v_med3_f32 v35, v45, s49, v25
	v_cvt_pk_fp8_f32 v32, v34, v35 op_sel:[0,0,1]
	v_med3_f32 v34, v36, s49, v25
	v_med3_f32 v35, v37, s49, v25
	v_cvt_pk_fp8_f32 v33, v34, v35 op_sel:[0,0,1]
	v_or_b32_e32 v34, s14, v8
	v_med3_f32 v40, v42, s49, v25
	v_med3_f32 v41, v44, s49, v25
	v_lshlrev_b32_e32 v34, 1, v34
	v_cvt_pk_fp8_f32 v30, v40, v41 op_sel:[0,0,1]
	v_and_or_b32 v34, v34, s63, v6
	v_ashrrev_i32_e32 v35, 31, v34
	v_lshlrev_b64 v[34:35], 11, v[34:35]
	v_lshl_add_u64 v[34:35], v[4:5], 0, v[34:35]
	global_store_dwordx4 v[34:35], v[30:33], off sc1
	ds_read2_b32 v[30:31], v11 offset0:64 offset1:96
	ds_read2_b32 v[36:37], v11 offset1:32
	ds_read2_b32 v[32:33], v27 offset0:64 offset1:96
	ds_read2_b32 v[34:35], v11 offset0:128 offset1:160
	ds_read2_b32 v[38:39], v27 offset1:32
	s_waitcnt lgkmcnt(4)
	v_mul_f32_e32 v42, 0x42000000, v30
	v_mul_f32_e32 v44, 0x42000000, v31
	ds_read2_b32 v[30:31], v27 offset0:128 offset1:160
	s_waitcnt lgkmcnt(4)
	v_mul_f32_e32 v40, 0x42000000, v36
	v_mul_f32_e32 v41, 0x42000000, v37
	s_waitcnt lgkmcnt(3)
	v_mul_f32_e32 v43, 0x42000000, v32
	v_mul_f32_e32 v45, 0x42000000, v33
	s_waitcnt lgkmcnt(2)
	v_mul_f32_e32 v34, 0x42000000, v34
	ds_read2_b32 v[32:33], v11 offset0:192 offset1:224
	ds_read2_b32 v[36:37], v27 offset0:192 offset1:224
	s_waitcnt lgkmcnt(2)
	v_mul_f32_e32 v46, 0x42000000, v30
	v_mul_f32_e32 v35, 0x42000000, v35
	v_mul_f32_e32 v47, 0x42000000, v31
	v_med3_f32 v31, v40, s49, v25
	v_med3_f32 v40, v41, s49, v25
	v_mov_b32_e32 v30, v1
	v_cvt_pk_fp8_f32 v30, v31, v40
	v_med3_f32 v34, v34, s49, v25
	v_med3_f32 v35, v35, s49, v25
	v_mov_b32_e32 v31, v1
	v_cvt_pk_fp8_f32 v31, v34, v35
	s_waitcnt lgkmcnt(1)
	v_mul_f32_e32 v32, 0x42000000, v32
	v_mul_f32_e32 v33, 0x42000000, v33
	v_mul_f32_e32 v38, 0x42000000, v38
	v_mul_f32_e32 v39, 0x42000000, v39
	v_med3_f32 v32, v32, s49, v25
	v_med3_f32 v33, v33, s49, v25
	v_cvt_pk_fp8_f32 v31, v32, v33 op_sel:[0,0,1]
	v_med3_f32 v33, v38, s49, v25
	v_med3_f32 v34, v39, s49, v25
	v_mov_b32_e32 v32, v1
	v_cvt_pk_fp8_f32 v32, v33, v34
	v_med3_f32 v38, v46, s49, v25
	v_med3_f32 v39, v47, s49, v25
	v_mov_b32_e32 v33, v1
	v_cvt_pk_fp8_f32 v33, v38, v39
	s_waitcnt lgkmcnt(0)
	v_mul_f32_e32 v36, 0x42000000, v36
	v_mul_f32_e32 v37, 0x42000000, v37
	v_med3_f32 v34, v43, s49, v25
	v_med3_f32 v35, v45, s49, v25
	v_cvt_pk_fp8_f32 v32, v34, v35 op_sel:[0,0,1]
	v_med3_f32 v34, v36, s49, v25
	v_med3_f32 v35, v37, s49, v25
	v_cvt_pk_fp8_f32 v33, v34, v35 op_sel:[0,0,1]
	v_or_b32_e32 v34, s14, v10
	v_med3_f32 v40, v42, s49, v25
	v_med3_f32 v41, v44, s49, v25
	v_lshlrev_b32_e32 v34, 1, v34
	v_cvt_pk_fp8_f32 v30, v40, v41 op_sel:[0,0,1]
	v_and_or_b32 v34, v34, s64, v6
	v_ashrrev_i32_e32 v35, 31, v34
	v_lshlrev_b64 v[34:35], 11, v[34:35]
	v_lshl_add_u64 v[34:35], v[4:5], 0, v[34:35]
	global_store_dwordx4 v[34:35], v[30:33], off sc1
	ds_read2_b32 v[30:31], v13 offset0:64 offset1:96
	ds_read2_b32 v[36:37], v13 offset1:32
	ds_read2_b32 v[32:33], v28 offset0:64 offset1:96
	ds_read2_b32 v[34:35], v13 offset0:128 offset1:160
	ds_read2_b32 v[38:39], v28 offset1:32
	s_waitcnt lgkmcnt(4)
	v_mul_f32_e32 v42, 0x42000000, v30
	v_mul_f32_e32 v44, 0x42000000, v31
	ds_read2_b32 v[30:31], v28 offset0:128 offset1:160
	s_waitcnt lgkmcnt(4)
	v_mul_f32_e32 v40, 0x42000000, v36
	v_mul_f32_e32 v41, 0x42000000, v37
	s_waitcnt lgkmcnt(3)
	v_mul_f32_e32 v43, 0x42000000, v32
	v_mul_f32_e32 v45, 0x42000000, v33
	s_waitcnt lgkmcnt(2)
	v_mul_f32_e32 v34, 0x42000000, v34
	ds_read2_b32 v[32:33], v13 offset0:192 offset1:224
	ds_read2_b32 v[36:37], v28 offset0:192 offset1:224
	s_waitcnt lgkmcnt(2)
	v_mul_f32_e32 v46, 0x42000000, v30
	v_mul_f32_e32 v35, 0x42000000, v35
	v_mul_f32_e32 v47, 0x42000000, v31
	v_med3_f32 v31, v40, s49, v25
	v_med3_f32 v40, v41, s49, v25
	v_mov_b32_e32 v30, v1
	v_cvt_pk_fp8_f32 v30, v31, v40
	v_med3_f32 v34, v34, s49, v25
	v_med3_f32 v35, v35, s49, v25
	v_mov_b32_e32 v31, v1
	v_cvt_pk_fp8_f32 v31, v34, v35
	s_waitcnt lgkmcnt(1)
	v_mul_f32_e32 v32, 0x42000000, v32
	v_mul_f32_e32 v33, 0x42000000, v33
	v_mul_f32_e32 v38, 0x42000000, v38
	v_mul_f32_e32 v39, 0x42000000, v39
	v_med3_f32 v32, v32, s49, v25
	v_med3_f32 v33, v33, s49, v25
	v_cvt_pk_fp8_f32 v31, v32, v33 op_sel:[0,0,1]
	v_med3_f32 v33, v38, s49, v25
	v_med3_f32 v34, v39, s49, v25
	v_mov_b32_e32 v32, v1
	v_cvt_pk_fp8_f32 v32, v33, v34
	v_med3_f32 v38, v46, s49, v25
	v_med3_f32 v39, v47, s49, v25
	v_mov_b32_e32 v33, v1
	v_cvt_pk_fp8_f32 v33, v38, v39
	s_waitcnt lgkmcnt(0)
	v_mul_f32_e32 v36, 0x42000000, v36
	v_mul_f32_e32 v37, 0x42000000, v37
	v_med3_f32 v34, v43, s49, v25
	v_med3_f32 v35, v45, s49, v25
	v_cvt_pk_fp8_f32 v32, v34, v35 op_sel:[0,0,1]
	v_med3_f32 v34, v36, s49, v25
	v_med3_f32 v35, v37, s49, v25
	v_cvt_pk_fp8_f32 v33, v34, v35 op_sel:[0,0,1]
	v_or_b32_e32 v34, s14, v12
	v_med3_f32 v40, v42, s49, v25
	v_med3_f32 v41, v44, s49, v25
	v_lshlrev_b32_e32 v34, 1, v34
	v_cvt_pk_fp8_f32 v30, v40, v41 op_sel:[0,0,1]
	v_and_or_b32 v34, v34, -8, v6
	v_ashrrev_i32_e32 v35, 31, v34
	v_lshlrev_b64 v[34:35], 11, v[34:35]
	v_lshl_add_u64 v[4:5], v[4:5], 0, v[34:35]
	global_store_dwordx4 v[4:5], v[30:33], off sc1
	s_waitcnt lgkmcnt(0)
	s_branch .LBB0_177

.LBB0_260:
	s_mul_hi_i32 s4, s13, 0x2aaaaaab
	s_lshr_b32 s5, s4, 31
	s_ashr_i32 s4, s4, 8
	s_add_i32 s4, s4, s5
	s_mul_i32 s5, s4, 0xfffffa00
	s_add_i32 s55, s13, s5
	s_cmpk_gt_i32 s55, 0x1ff
	s_mov_b64 s[6:7], -1
	s_cbranch_scc0 .LBB0_266
	s_ashr_i32 s5, s4, 31
	s_lshl_b64 s[6:7], s[4:5], 23
	s_cmpk_gt_u32 s55, 0x3ff
	s_mov_b64 s[8:9], -1
	s_cbranch_scc0 .LBB0_263
	s_add_u32 s56, s42, s6
	s_addc_u32 s57, s43, s7
	s_lshl_b64 s[8:9], s[4:5], 21
	s_add_u32 s58, s28, s8
	s_addc_u32 s9, s29, s9
	s_lshl_b32 s8, s4, 10
	s_sub_i32 s8, s53, s8
	s_and_b32 s59, s8, 0x780
	s_add_i32 s8, s49, 0xffffc000
	v_or_b32_e32 v0, s59, v3
	s_and_b32 s8, s8, 0x7e0
	v_lshlrev_b32_e32 v0, 13, v0
	v_lshl_add_u64 v[6:7], s[56:57], 0, v[0:1]
	s_lshl_b32 s20, s8, 2
	v_lshl_add_u64 v[6:7], v[6:7], 0, s[20:21]
	v_lshlrev_b32_e32 v0, 2, v2
	v_lshl_add_u64 v[6:7], v[6:7], 0, v[0:1]
	s_mov_b32 s20, 0x10000
	v_add_co_u32_e32 v30, vcc, s20, v6
	s_mov_b32 s20, 0x20000
	s_nop 0
	v_addc_co_u32_e32 v31, vcc, 0, v7, vcc
	v_add_co_u32_e32 v34, vcc, s20, v6
	s_mov_b32 s20, 0x30000
	s_nop 0
	v_addc_co_u32_e32 v35, vcc, 0, v7, vcc
	v_add_co_u32_e32 v38, vcc, s20, v6
	s_mov_b32 s20, 0x40000
	s_nop 0
	v_addc_co_u32_e32 v39, vcc, 0, v7, vcc
	v_add_co_u32_e32 v42, vcc, s20, v6
	s_mov_b32 s20, 0x50000
	s_nop 0
	v_addc_co_u32_e32 v43, vcc, 0, v7, vcc
	v_add_co_u32_e32 v46, vcc, s20, v6
	s_mov_b32 s20, 0x60000
	s_nop 0
	v_addc_co_u32_e32 v47, vcc, 0, v7, vcc
	v_add_co_u32_e32 v50, vcc, s20, v6
	s_mov_b32 s20, 0x70000
	s_nop 0
	v_addc_co_u32_e32 v51, vcc, 0, v7, vcc
	v_add_co_u32_e32 v54, vcc, s20, v6
	s_mov_b32 s20, 0x80000
	s_nop 0
	v_addc_co_u32_e32 v55, vcc, 0, v7, vcc
	v_add_co_u32_e32 v58, vcc, s20, v6
	s_mov_b32 s20, 0x90000
	s_nop 0
	v_addc_co_u32_e32 v59, vcc, 0, v7, vcc
	v_add_co_u32_e32 v62, vcc, s20, v6
	s_mov_b32 s20, 0xa0000
	s_nop 0
	v_addc_co_u32_e32 v63, vcc, 0, v7, vcc
	v_add_co_u32_e32 v68, vcc, s20, v6
	s_mov_b32 s20, 0xb0000
	s_nop 0
	v_addc_co_u32_e32 v69, vcc, 0, v7, vcc
	v_add_co_u32_e32 v72, vcc, s20, v6
	s_mov_b32 s20, 0xc0000
	s_nop 0
	v_addc_co_u32_e32 v73, vcc, 0, v7, vcc
	global_load_dwordx4 v[26:29], v[6:7], off
	s_nop 0
	global_load_dwordx4 v[30:33], v[30:31], off
	v_add_co_u32_e32 v76, vcc, s20, v6
	global_load_dwordx4 v[34:37], v[34:35], off
	s_nop 0
	global_load_dwordx4 v[38:41], v[38:39], off
	v_addc_co_u32_e32 v77, vcc, 0, v7, vcc
	s_mov_b32 s20, 0xd0000
	global_load_dwordx4 v[42:45], v[42:43], off
	s_nop 0
	global_load_dwordx4 v[46:49], v[46:47], off
	v_add_co_u32_e32 v80, vcc, s20, v6
	global_load_dwordx4 v[50:53], v[50:51], off
	s_nop 0
	global_load_dwordx4 v[54:57], v[54:55], off
	v_addc_co_u32_e32 v81, vcc, 0, v7, vcc
	s_mov_b32 s20, 0xe0000
	global_load_dwordx4 v[58:61], v[58:59], off
	s_nop 0
	global_load_dwordx4 v[62:65], v[62:63], off
	v_add_co_u32_e32 v84, vcc, s20, v6
	global_load_dwordx4 v[68:71], v[68:69], off
	s_nop 0
	global_load_dwordx4 v[72:75], v[72:73], off
	v_addc_co_u32_e32 v85, vcc, 0, v7, vcc
	s_mov_b32 s20, 0xf0000
	global_load_dwordx4 v[76:79], v[76:77], off
	s_nop 0
	global_load_dwordx4 v[80:83], v[80:81], off
	v_add_co_u32_e32 v6, vcc, s20, v6
	v_add_u32_e32 v0, v8, v4
	s_nop 0
	v_addc_co_u32_e32 v7, vcc, 0, v7, vcc
	global_load_dwordx4 v[84:87], v[84:85], off
	s_nop 0
	global_load_dwordx4 v[88:91], v[6:7], off
	s_waitcnt vmcnt(0)
	ds_write_b128 v0, v[26:29]
	s_waitcnt vmcnt(14)
	ds_write_b128 v0, v[30:33] offset:1024
	v_add_u32_e32 v0, v8, v9
	s_waitcnt vmcnt(13)
	ds_write_b128 v0, v[34:37] offset:2048
	s_waitcnt vmcnt(12)
	ds_write_b128 v0, v[38:41] offset:3072
	v_add_u32_e32 v0, v8, v10
	s_waitcnt vmcnt(11)
	ds_write_b128 v0, v[42:45] offset:4096
	s_waitcnt vmcnt(10)
	ds_write_b128 v0, v[46:49] offset:5120
	v_add_u32_e32 v0, v8, v11
	s_waitcnt vmcnt(9)
	ds_write_b128 v0, v[50:53] offset:6144
	s_waitcnt vmcnt(8)
	ds_write_b128 v0, v[54:57] offset:7168
	v_add_u32_e32 v0, v8, v12
	s_waitcnt vmcnt(7)
	ds_write_b128 v0, v[58:61] offset:8192
	s_waitcnt vmcnt(6)
	ds_write_b128 v0, v[62:65] offset:9216
	v_add_u32_e32 v0, v8, v13
	s_waitcnt vmcnt(5)
	ds_write_b128 v0, v[68:71] offset:10240
	s_waitcnt vmcnt(4)
	ds_write_b128 v0, v[72:75] offset:11264
	v_add_u32_e32 v0, v8, v14
	s_waitcnt vmcnt(3)
	ds_write_b128 v0, v[76:79] offset:12288
	s_waitcnt vmcnt(2)
	ds_write_b128 v0, v[80:83] offset:13312
	v_add_u32_e32 v0, v8, v15
	s_waitcnt vmcnt(1)
	ds_write_b128 v0, v[84:87] offset:14336
	s_waitcnt vmcnt(0)
	ds_write_b128 v0, v[88:91] offset:15360
	s_waitcnt lgkmcnt(0)
	v_add_u32_e32 v0, 0x400, v17
	ds_read2_b32 v[26:27], v17 offset1:32
	ds_read2_b32 v[28:29], v0 offset1:32
	ds_read2_b32 v[30:31], v17 offset0:64 offset1:96
	ds_read2_b32 v[32:33], v0 offset0:64 offset1:96
	s_add_u32 s56, s58, s59
	s_waitcnt lgkmcnt(3)
	v_mul_f32_e32 v25, 0x41800000, v26
	s_waitcnt lgkmcnt(2)
	v_mul_f32_e32 v34, 0x41800000, v28
	v_mul_f32_e32 v35, 0x41800000, v27
	v_mul_f32_e32 v36, 0x41800000, v29
	s_waitcnt lgkmcnt(1)
	v_mul_f32_e32 v37, 0x41800000, v30
	ds_read2_b32 v[26:27], v17 offset0:128 offset1:160
	s_waitcnt lgkmcnt(1)
	v_mul_f32_e32 v38, 0x41800000, v32
	v_mul_f32_e32 v39, 0x41800000, v31
	ds_read2_b32 v[28:29], v0 offset0:128 offset1:160
	v_mul_f32_e32 v40, 0x41800000, v33
	ds_read2_b32 v[30:31], v17 offset0:192 offset1:224
	ds_read2_b32 v[32:33], v0 offset0:192 offset1:224
	s_waitcnt lgkmcnt(3)
	v_mul_f32_e32 v41, 0x41800000, v26
	v_mul_f32_e32 v27, 0x41800000, v27
	s_waitcnt lgkmcnt(2)
	v_mul_f32_e32 v0, 0x41800000, v28
	s_waitcnt lgkmcnt(1)
	v_mul_f32_e32 v28, 0x41800000, v30
	s_waitcnt lgkmcnt(0)
	v_mul_f32_e32 v30, 0x41800000, v32
	v_mul_f32_e32 v32, 0x41800000, v33
	v_med3_f32 v25, v25, s33, v233
	v_med3_f32 v33, v35, s33, v233
	v_mov_b32_e32 v26, v1
	v_cvt_pk_fp8_f32 v26, v25, v33
	v_med3_f32 v25, v37, s33, v233
	v_med3_f32 v35, v41, s33, v233
	v_med3_f32 v37, v27, s33, v233
	v_mov_b32_e32 v27, v1
	v_cvt_pk_fp8_f32 v27, v35, v37
	v_mul_f32_e32 v31, 0x41800000, v31
	v_med3_f32 v33, v39, s33, v233
	v_cvt_pk_fp8_f32 v26, v25, v33 op_sel:[0,0,1]
	v_med3_f32 v25, v28, s33, v233
	v_med3_f32 v28, v31, s33, v233
	v_mul_f32_e32 v29, 0x41800000, v29
	v_cvt_pk_fp8_f32 v27, v25, v28 op_sel:[0,0,1]
	v_med3_f32 v25, v34, s33, v233
	v_med3_f32 v31, v36, s33, v233
	v_mov_b32_e32 v28, v1
	v_cvt_pk_fp8_f32 v28, v25, v31
	v_med3_f32 v0, v0, s33, v233
	v_med3_f32 v33, v29, s33, v233
	v_mov_b32_e32 v29, v1
	v_cvt_pk_fp8_f32 v29, v0, v33
	v_med3_f32 v25, v38, s33, v233
	v_med3_f32 v31, v40, s33, v233
	v_cvt_pk_fp8_f32 v28, v25, v31 op_sel:[0,0,1]
	v_med3_f32 v0, v30, s33, v233
	v_med3_f32 v25, v32, s33, v233
	v_cvt_pk_fp8_f32 v29, v0, v25 op_sel:[0,0,1]
	s_addc_u32 s57, s9, 0
	v_or_b32_e32 v0, s8, v3
	v_lshl_add_u64 v[6:7], s[56:57], 0, v[4:5]
	v_lshlrev_b32_e32 v0, 10, v0
	v_lshl_add_u64 v[34:35], v[6:7], 0, v[0:1]
	ds_read2_b32 v[30:31], v19 offset1:32
	global_store_dwordx4 v[34:35], v[26:29], off sc1
	ds_read2_b32 v[26:27], v19 offset0:64 offset1:96
	v_add_u32_e32 v25, 0x400, v19
	ds_read2_b32 v[32:33], v25 offset1:32
	s_waitcnt lgkmcnt(2)
	v_mul_f32_e32 v0, 0x41800000, v30
	ds_read2_b32 v[28:29], v25 offset0:64 offset1:96
	v_mul_f32_e32 v35, 0x41800000, v31
	s_waitcnt lgkmcnt(2)
	v_mul_f32_e32 v37, 0x41800000, v26
	ds_read2_b32 v[30:31], v19 offset0:128 offset1:160
	v_mul_f32_e32 v39, 0x41800000, v27
	ds_read2_b32 v[26:27], v25 offset0:128 offset1:160
	s_waitcnt lgkmcnt(3)
	v_mul_f32_e32 v34, 0x41800000, v32
	v_mul_f32_e32 v36, 0x41800000, v33
	s_waitcnt lgkmcnt(2)
	v_mul_f32_e32 v38, 0x41800000, v28
	v_mul_f32_e32 v40, 0x41800000, v29
	s_waitcnt lgkmcnt(1)
	v_mul_f32_e32 v30, 0x41800000, v30
	ds_read2_b32 v[28:29], v19 offset0:192 offset1:224
	ds_read2_b32 v[32:33], v25 offset0:192 offset1:224
	s_waitcnt lgkmcnt(2)
	v_mul_f32_e32 v25, 0x41800000, v26
	v_mul_f32_e32 v31, 0x41800000, v31
	v_mul_f32_e32 v41, 0x41800000, v27
	v_med3_f32 v0, v0, s33, v233
	v_med3_f32 v27, v35, s33, v233
	v_mov_b32_e32 v26, v1
	v_cvt_pk_fp8_f32 v26, v0, v27
	v_med3_f32 v30, v30, s33, v233
	v_med3_f32 v31, v31, s33, v233
	v_mov_b32_e32 v27, v1
	v_cvt_pk_fp8_f32 v27, v30, v31
	s_waitcnt lgkmcnt(1)
	v_mul_f32_e32 v28, 0x41800000, v28
	v_mul_f32_e32 v29, 0x41800000, v29
	v_med3_f32 v0, v37, s33, v233
	v_med3_f32 v35, v39, s33, v233
	v_cvt_pk_fp8_f32 v26, v0, v35 op_sel:[0,0,1]
	v_med3_f32 v0, v28, s33, v233
	v_med3_f32 v28, v29, s33, v233
	v_cvt_pk_fp8_f32 v27, v0, v28 op_sel:[0,0,1]
	v_med3_f32 v0, v34, s33, v233
	v_med3_f32 v29, v36, s33, v233
	v_mov_b32_e32 v28, v1
	v_cvt_pk_fp8_f32 v28, v0, v29
	v_med3_f32 v25, v25, s33, v233
	v_med3_f32 v31, v41, s33, v233
	v_mov_b32_e32 v29, v1
	v_cvt_pk_fp8_f32 v29, v25, v31
	s_waitcnt lgkmcnt(0)
	v_mul_f32_e32 v32, 0x41800000, v32
	v_mul_f32_e32 v33, 0x41800000, v33
	v_med3_f32 v0, v38, s33, v233
	v_med3_f32 v30, v40, s33, v233
	v_cvt_pk_fp8_f32 v28, v0, v30 op_sel:[0,0,1]
	v_med3_f32 v0, v32, s33, v233
	v_med3_f32 v25, v33, s33, v233
	v_cvt_pk_fp8_f32 v29, v0, v25 op_sel:[0,0,1]
	v_or_b32_e32 v0, s8, v18
	v_lshlrev_b32_e32 v0, 10, v0
	v_lshl_add_u64 v[34:35], v[6:7], 0, v[0:1]
	ds_read2_b32 v[30:31], v21 offset1:32
	global_store_dwordx4 v[34:35], v[26:29], off sc1
	ds_read2_b32 v[26:27], v21 offset0:64 offset1:96
	v_add_u32_e32 v25, 0x400, v21
	ds_read2_b32 v[32:33], v25 offset1:32
	s_waitcnt lgkmcnt(2)
	v_mul_f32_e32 v0, 0x41800000, v30
	ds_read2_b32 v[28:29], v25 offset0:64 offset1:96
	v_mul_f32_e32 v35, 0x41800000, v31
	s_waitcnt lgkmcnt(2)
	v_mul_f32_e32 v37, 0x41800000, v26
	ds_read2_b32 v[30:31], v21 offset0:128 offset1:160
	v_mul_f32_e32 v39, 0x41800000, v27
	ds_read2_b32 v[26:27], v25 offset0:128 offset1:160
	s_waitcnt lgkmcnt(3)
	v_mul_f32_e32 v34, 0x41800000, v32
	v_mul_f32_e32 v36, 0x41800000, v33
	s_waitcnt lgkmcnt(2)
	v_mul_f32_e32 v38, 0x41800000, v28
	v_mul_f32_e32 v40, 0x41800000, v29
	s_waitcnt lgkmcnt(1)
	v_mul_f32_e32 v30, 0x41800000, v30
	ds_read2_b32 v[28:29], v21 offset0:192 offset1:224
	ds_read2_b32 v[32:33], v25 offset0:192 offset1:224
	s_waitcnt lgkmcnt(2)
	v_mul_f32_e32 v25, 0x41800000, v26
	v_mul_f32_e32 v31, 0x41800000, v31
	v_mul_f32_e32 v41, 0x41800000, v27
	v_med3_f32 v0, v0, s33, v233
	v_med3_f32 v27, v35, s33, v233
	v_mov_b32_e32 v26, v1
	v_cvt_pk_fp8_f32 v26, v0, v27
	v_med3_f32 v30, v30, s33, v233
	v_med3_f32 v31, v31, s33, v233
	v_mov_b32_e32 v27, v1
	v_cvt_pk_fp8_f32 v27, v30, v31
	s_waitcnt lgkmcnt(1)
	v_mul_f32_e32 v28, 0x41800000, v28
	v_mul_f32_e32 v29, 0x41800000, v29
	v_med3_f32 v0, v37, s33, v233
	v_med3_f32 v35, v39, s33, v233
	v_cvt_pk_fp8_f32 v26, v0, v35 op_sel:[0,0,1]
	v_med3_f32 v0, v28, s33, v233
	v_med3_f32 v28, v29, s33, v233
	v_cvt_pk_fp8_f32 v27, v0, v28 op_sel:[0,0,1]
	v_med3_f32 v0, v34, s33, v233
	v_med3_f32 v29, v36, s33, v233
	v_mov_b32_e32 v28, v1
	v_cvt_pk_fp8_f32 v28, v0, v29
	v_med3_f32 v25, v25, s33, v233
	v_med3_f32 v31, v41, s33, v233
	v_mov_b32_e32 v29, v1
	v_cvt_pk_fp8_f32 v29, v25, v31
	s_waitcnt lgkmcnt(0)
	v_mul_f32_e32 v32, 0x41800000, v32
	v_mul_f32_e32 v33, 0x41800000, v33
	v_med3_f32 v0, v38, s33, v233
	v_med3_f32 v30, v40, s33, v233
	v_cvt_pk_fp8_f32 v28, v0, v30 op_sel:[0,0,1]
	v_med3_f32 v0, v32, s33, v233
	v_med3_f32 v25, v33, s33, v233
	v_cvt_pk_fp8_f32 v29, v0, v25 op_sel:[0,0,1]
	v_or_b32_e32 v0, s8, v20
	v_lshlrev_b32_e32 v0, 10, v0
	v_lshl_add_u64 v[34:35], v[6:7], 0, v[0:1]
	ds_read2_b32 v[30:31], v23 offset1:32
	global_store_dwordx4 v[34:35], v[26:29], off sc1
	ds_read2_b32 v[26:27], v23 offset0:64 offset1:96
	v_add_u32_e32 v25, 0x400, v23
	ds_read2_b32 v[32:33], v25 offset1:32
	s_waitcnt lgkmcnt(2)
	v_mul_f32_e32 v0, 0x41800000, v30
	ds_read2_b32 v[28:29], v25 offset0:64 offset1:96
	v_mul_f32_e32 v35, 0x41800000, v31
	s_waitcnt lgkmcnt(2)
	v_mul_f32_e32 v37, 0x41800000, v26
	ds_read2_b32 v[30:31], v23 offset0:128 offset1:160
	v_mul_f32_e32 v39, 0x41800000, v27
	ds_read2_b32 v[26:27], v25 offset0:128 offset1:160
	s_waitcnt lgkmcnt(3)
	v_mul_f32_e32 v34, 0x41800000, v32
	v_mul_f32_e32 v36, 0x41800000, v33
	s_waitcnt lgkmcnt(2)
	v_mul_f32_e32 v38, 0x41800000, v28
	v_mul_f32_e32 v40, 0x41800000, v29
	s_waitcnt lgkmcnt(1)
	v_mul_f32_e32 v30, 0x41800000, v30
	ds_read2_b32 v[28:29], v23 offset0:192 offset1:224
	ds_read2_b32 v[32:33], v25 offset0:192 offset1:224
	s_waitcnt lgkmcnt(2)
	v_mul_f32_e32 v25, 0x41800000, v26
	v_mul_f32_e32 v31, 0x41800000, v31
	v_mul_f32_e32 v41, 0x41800000, v27
	v_med3_f32 v0, v0, s33, v233
	v_med3_f32 v27, v35, s33, v233
	v_mov_b32_e32 v26, v1
	v_cvt_pk_fp8_f32 v26, v0, v27
	v_med3_f32 v30, v30, s33, v233
	v_med3_f32 v31, v31, s33, v233
	v_mov_b32_e32 v27, v1
	v_cvt_pk_fp8_f32 v27, v30, v31
	s_waitcnt lgkmcnt(1)
	v_mul_f32_e32 v28, 0x41800000, v28
	v_mul_f32_e32 v29, 0x41800000, v29
	v_med3_f32 v0, v37, s33, v233
	v_med3_f32 v35, v39, s33, v233
	v_cvt_pk_fp8_f32 v26, v0, v35 op_sel:[0,0,1]
	v_med3_f32 v0, v28, s33, v233
	v_med3_f32 v28, v29, s33, v233
	v_cvt_pk_fp8_f32 v27, v0, v28 op_sel:[0,0,1]
	v_med3_f32 v0, v34, s33, v233
	v_med3_f32 v29, v36, s33, v233
	v_mov_b32_e32 v28, v1
	v_cvt_pk_fp8_f32 v28, v0, v29
	v_med3_f32 v25, v25, s33, v233
	v_med3_f32 v31, v41, s33, v233
	v_mov_b32_e32 v29, v1
	v_cvt_pk_fp8_f32 v29, v25, v31
	s_waitcnt lgkmcnt(0)
	v_mul_f32_e32 v32, 0x41800000, v32
	v_mul_f32_e32 v33, 0x41800000, v33
	v_med3_f32 v0, v38, s33, v233
	v_med3_f32 v30, v40, s33, v233
	v_cvt_pk_fp8_f32 v28, v0, v30 op_sel:[0,0,1]
	v_med3_f32 v0, v32, s33, v233
	v_med3_f32 v25, v33, s33, v233
	v_cvt_pk_fp8_f32 v29, v0, v25 op_sel:[0,0,1]
	v_or_b32_e32 v0, s8, v22
	v_lshlrev_b32_e32 v0, 10, v0
	v_lshl_add_u64 v[6:7], v[6:7], 0, v[0:1]
	global_store_dwordx4 v[6:7], v[26:29], off sc1
	s_waitcnt lgkmcnt(0)
	s_mov_b64 s[8:9], 0
.LBB0_263:
	s_andn2_b64 vcc, exec, s[8:9]
	s_cbranch_vccnz .LBB0_265
	s_add_u32 s6, s40, s6
	s_addc_u32 s7, s41, s7
	s_lshl_b64 s[8:9], s[4:5], 22
	s_add_u32 s5, s24, s8
	s_addc_u32 s8, s25, s9
	s_and_b32 s9, s51, 0x780
	v_or_b32_e32 v0, s9, v3
	s_and_b32 s20, s49, 0x3e0
	v_lshlrev_b32_e32 v0, 12, v0
	v_lshl_add_u64 v[6:7], s[6:7], 0, v[0:1]
	s_lshl_b32 s20, s20, 2
	v_lshl_add_u64 v[6:7], v[6:7], 0, s[20:21]
	v_lshlrev_b32_e32 v0, 2, v2
	v_lshl_add_u64 v[6:7], v[6:7], 0, v[0:1]
	s_mov_b32 s6, 0x8000
	v_add_co_u32_e32 v30, vcc, s6, v6
	s_mov_b32 s6, 0x10000
	s_nop 0
	v_addc_co_u32_e32 v31, vcc, 0, v7, vcc
	v_add_co_u32_e32 v34, vcc, s6, v6
	s_mov_b32 s6, 0x18000
	s_nop 0
	v_addc_co_u32_e32 v35, vcc, 0, v7, vcc
	v_add_co_u32_e32 v38, vcc, s6, v6
	s_mov_b32 s6, 0x20000
	s_nop 0
	v_addc_co_u32_e32 v39, vcc, 0, v7, vcc
	v_add_co_u32_e32 v42, vcc, s6, v6
	s_mov_b32 s6, 0x28000
	s_nop 0
	v_addc_co_u32_e32 v43, vcc, 0, v7, vcc
	v_add_co_u32_e32 v46, vcc, s6, v6
	s_mov_b32 s6, 0x30000
	s_nop 0
	v_addc_co_u32_e32 v47, vcc, 0, v7, vcc
	v_add_co_u32_e32 v50, vcc, s6, v6
	s_mov_b32 s6, 0x38000
	s_nop 0
	v_addc_co_u32_e32 v51, vcc, 0, v7, vcc
	v_add_co_u32_e32 v54, vcc, s6, v6
	s_mov_b32 s6, 0x40000
	s_nop 0
	v_addc_co_u32_e32 v55, vcc, 0, v7, vcc
	v_add_co_u32_e32 v58, vcc, s6, v6
	s_mov_b32 s6, 0x48000
	s_nop 0
	v_addc_co_u32_e32 v59, vcc, 0, v7, vcc
	v_add_co_u32_e32 v62, vcc, s6, v6
	s_mov_b32 s6, 0x50000
	s_nop 0
	v_addc_co_u32_e32 v63, vcc, 0, v7, vcc
	v_add_co_u32_e32 v68, vcc, s6, v6
	s_mov_b32 s6, 0x58000
	s_nop 0
	v_addc_co_u32_e32 v69, vcc, 0, v7, vcc
	v_add_co_u32_e32 v72, vcc, s6, v6
	s_mov_b32 s6, 0x60000
	s_nop 0
	v_addc_co_u32_e32 v73, vcc, 0, v7, vcc
	global_load_dwordx4 v[26:29], v[6:7], off
	s_nop 0
	global_load_dwordx4 v[30:33], v[30:31], off
	v_add_co_u32_e32 v76, vcc, s6, v6
	global_load_dwordx4 v[34:37], v[34:35], off
	s_nop 0
	global_load_dwordx4 v[38:41], v[38:39], off
	v_addc_co_u32_e32 v77, vcc, 0, v7, vcc
	s_mov_b32 s6, 0x68000
	global_load_dwordx4 v[42:45], v[42:43], off
	s_nop 0
	global_load_dwordx4 v[46:49], v[46:47], off
	v_add_co_u32_e32 v80, vcc, s6, v6
	global_load_dwordx4 v[50:53], v[50:51], off
	s_nop 0
	global_load_dwordx4 v[54:57], v[54:55], off
	v_addc_co_u32_e32 v81, vcc, 0, v7, vcc
	s_mov_b32 s6, 0x70000
	global_load_dwordx4 v[58:61], v[58:59], off
	s_nop 0
	global_load_dwordx4 v[62:65], v[62:63], off
	v_add_co_u32_e32 v84, vcc, s6, v6
	global_load_dwordx4 v[68:71], v[68:69], off
	s_nop 0
	global_load_dwordx4 v[72:75], v[72:73], off
	v_addc_co_u32_e32 v85, vcc, 0, v7, vcc
	s_mov_b32 s6, 0x78000
	global_load_dwordx4 v[76:79], v[76:77], off
	s_nop 0
	global_load_dwordx4 v[80:83], v[80:81], off
	v_add_co_u32_e32 v6, vcc, s6, v6
	v_add_u32_e32 v0, v8, v4
	s_nop 0
	v_addc_co_u32_e32 v7, vcc, 0, v7, vcc
	global_load_dwordx4 v[84:87], v[84:85], off
	s_nop 0
	global_load_dwordx4 v[88:91], v[6:7], off
	s_waitcnt vmcnt(0)
	ds_write_b128 v0, v[26:29]
	s_waitcnt vmcnt(14)
	ds_write_b128 v0, v[30:33] offset:1024
	v_add_u32_e32 v0, v8, v9
	s_waitcnt vmcnt(13)
	ds_write_b128 v0, v[34:37] offset:2048
	s_waitcnt vmcnt(12)
	ds_write_b128 v0, v[38:41] offset:3072
	v_add_u32_e32 v0, v8, v10
	s_waitcnt vmcnt(11)
	ds_write_b128 v0, v[42:45] offset:4096
	s_waitcnt vmcnt(10)
	ds_write_b128 v0, v[46:49] offset:5120
	v_add_u32_e32 v0, v8, v11
	s_waitcnt vmcnt(9)
	ds_write_b128 v0, v[50:53] offset:6144
	s_waitcnt vmcnt(8)
	ds_write_b128 v0, v[54:57] offset:7168
	v_add_u32_e32 v0, v8, v12
	s_waitcnt vmcnt(7)
	ds_write_b128 v0, v[58:61] offset:8192
	s_waitcnt vmcnt(6)
	ds_write_b128 v0, v[62:65] offset:9216
	v_add_u32_e32 v0, v8, v13
	s_waitcnt vmcnt(5)
	ds_write_b128 v0, v[68:71] offset:10240
	s_waitcnt vmcnt(4)
	ds_write_b128 v0, v[72:75] offset:11264
	v_add_u32_e32 v0, v8, v14
	s_waitcnt vmcnt(3)
	ds_write_b128 v0, v[76:79] offset:12288
	s_waitcnt vmcnt(2)
	ds_write_b128 v0, v[80:83] offset:13312
	v_add_u32_e32 v0, v8, v15
	s_waitcnt vmcnt(1)
	ds_write_b128 v0, v[84:87] offset:14336
	s_waitcnt vmcnt(0)
	ds_write_b128 v0, v[88:91] offset:15360
	s_waitcnt lgkmcnt(0)
	v_add_u32_e32 v0, 0x400, v17
	ds_read2_b32 v[26:27], v17 offset1:32
	ds_read2_b32 v[28:29], v0 offset1:32
	ds_read2_b32 v[30:31], v17 offset0:64 offset1:96
	ds_read2_b32 v[32:33], v0 offset0:64 offset1:96
	s_add_u32 s6, s5, s9
	s_waitcnt lgkmcnt(3)
	v_mul_f32_e32 v25, 0x42000000, v26
	s_waitcnt lgkmcnt(2)
	v_mul_f32_e32 v34, 0x42000000, v28
	v_mul_f32_e32 v35, 0x42000000, v27
	v_mul_f32_e32 v36, 0x42000000, v29
	s_waitcnt lgkmcnt(1)
	v_mul_f32_e32 v37, 0x42000000, v30
	ds_read2_b32 v[26:27], v17 offset0:128 offset1:160
	s_waitcnt lgkmcnt(1)
	v_mul_f32_e32 v38, 0x42000000, v32
	v_mul_f32_e32 v39, 0x42000000, v31
	ds_read2_b32 v[28:29], v0 offset0:128 offset1:160
	v_mul_f32_e32 v40, 0x42000000, v33
	ds_read2_b32 v[30:31], v17 offset0:192 offset1:224
	ds_read2_b32 v[32:33], v0 offset0:192 offset1:224
	s_waitcnt lgkmcnt(3)
	v_mul_f32_e32 v41, 0x42000000, v26
	v_mul_f32_e32 v27, 0x42000000, v27
	s_waitcnt lgkmcnt(2)
	v_mul_f32_e32 v0, 0x42000000, v28
	s_waitcnt lgkmcnt(1)
	v_mul_f32_e32 v28, 0x42000000, v30
	s_waitcnt lgkmcnt(0)
	v_mul_f32_e32 v30, 0x42000000, v32
	v_mul_f32_e32 v32, 0x42000000, v33
	v_med3_f32 v25, v25, s33, v233
	v_med3_f32 v33, v35, s33, v233
	v_mov_b32_e32 v26, v1
	v_cvt_pk_fp8_f32 v26, v25, v33
	v_med3_f32 v25, v37, s33, v233
	v_med3_f32 v35, v41, s33, v233
	v_med3_f32 v37, v27, s33, v233
	v_mov_b32_e32 v27, v1
	v_cvt_pk_fp8_f32 v27, v35, v37
	v_mul_f32_e32 v31, 0x42000000, v31
	v_med3_f32 v33, v39, s33, v233
	v_cvt_pk_fp8_f32 v26, v25, v33 op_sel:[0,0,1]
	v_med3_f32 v25, v28, s33, v233
	v_med3_f32 v28, v31, s33, v233
	v_mul_f32_e32 v29, 0x42000000, v29
	v_cvt_pk_fp8_f32 v27, v25, v28 op_sel:[0,0,1]
	v_med3_f32 v25, v34, s33, v233
	v_med3_f32 v31, v36, s33, v233
	v_mov_b32_e32 v28, v1
	v_cvt_pk_fp8_f32 v28, v25, v31
	v_med3_f32 v0, v0, s33, v233
	v_med3_f32 v33, v29, s33, v233
	v_mov_b32_e32 v29, v1
	v_cvt_pk_fp8_f32 v29, v0, v33
	v_med3_f32 v25, v38, s33, v233
	v_med3_f32 v31, v40, s33, v233
	v_cvt_pk_fp8_f32 v28, v25, v31 op_sel:[0,0,1]
	v_med3_f32 v0, v30, s33, v233
	v_med3_f32 v25, v32, s33, v233
	s_mul_i32 s5, s4, 0xfffe8000
	v_cvt_pk_fp8_f32 v29, v0, v25 op_sel:[0,0,1]
	v_add_u32_e32 v25, s5, v24
	v_add_u32_e32 v0, 0xffff8000, v25
	s_movk_i32 s5, 0x7c8
	s_addc_u32 s7, s8, 0
	v_and_or_b32 v0, v0, s5, v3
	v_mov_b32_e32 v43, 0x2000
	v_lshl_add_u64 v[6:7], s[6:7], 0, v[4:5]
	v_lshl_or_b32 v0, v0, 11, v43
	v_lshl_add_u64 v[34:35], v[6:7], 0, v[0:1]
	ds_read2_b32 v[30:31], v19 offset1:32
	global_store_dwordx4 v[34:35], v[26:29], off sc1
	ds_read2_b32 v[26:27], v19 offset0:64 offset1:96
	v_add_u32_e32 v36, 0x400, v19
	ds_read2_b32 v[32:33], v36 offset1:32
	s_waitcnt lgkmcnt(2)
	v_mul_f32_e32 v0, 0x42000000, v30
	ds_read2_b32 v[28:29], v36 offset0:64 offset1:96
	v_mul_f32_e32 v35, 0x42000000, v31
	s_waitcnt lgkmcnt(2)
	v_mul_f32_e32 v38, 0x42000000, v26
	ds_read2_b32 v[30:31], v19 offset0:128 offset1:160
	v_mul_f32_e32 v40, 0x42000000, v27
	ds_read2_b32 v[26:27], v36 offset0:128 offset1:160
	s_waitcnt lgkmcnt(3)
	v_mul_f32_e32 v34, 0x42000000, v32
	v_mul_f32_e32 v37, 0x42000000, v33
	s_waitcnt lgkmcnt(2)
	v_mul_f32_e32 v39, 0x42000000, v28
	v_mul_f32_e32 v41, 0x42000000, v29
	s_waitcnt lgkmcnt(1)
	v_mul_f32_e32 v30, 0x42000000, v30
	ds_read2_b32 v[28:29], v19 offset0:192 offset1:224
	ds_read2_b32 v[32:33], v36 offset0:192 offset1:224
	s_waitcnt lgkmcnt(2)
	v_mul_f32_e32 v36, 0x42000000, v26
	v_mul_f32_e32 v31, 0x42000000, v31
	v_mul_f32_e32 v42, 0x42000000, v27
	v_med3_f32 v0, v0, s33, v233
	v_med3_f32 v27, v35, s33, v233
	v_mov_b32_e32 v26, v1
	v_cvt_pk_fp8_f32 v26, v0, v27
	v_med3_f32 v30, v30, s33, v233
	v_med3_f32 v31, v31, s33, v233
	v_mov_b32_e32 v27, v1
	v_cvt_pk_fp8_f32 v27, v30, v31
	s_waitcnt lgkmcnt(1)
	v_mul_f32_e32 v28, 0x42000000, v28
	v_mul_f32_e32 v29, 0x42000000, v29
	v_med3_f32 v0, v38, s33, v233
	v_med3_f32 v35, v40, s33, v233
	v_cvt_pk_fp8_f32 v26, v0, v35 op_sel:[0,0,1]
	v_med3_f32 v0, v28, s33, v233
	v_med3_f32 v28, v29, s33, v233
	v_cvt_pk_fp8_f32 v27, v0, v28 op_sel:[0,0,1]
	v_med3_f32 v0, v34, s33, v233
	v_med3_f32 v29, v37, s33, v233
	v_mov_b32_e32 v28, v1
	v_cvt_pk_fp8_f32 v28, v0, v29
	v_med3_f32 v31, v36, s33, v233
	v_med3_f32 v34, v42, s33, v233
	v_mov_b32_e32 v29, v1
	v_cvt_pk_fp8_f32 v29, v31, v34
	s_waitcnt lgkmcnt(0)
	v_mul_f32_e32 v32, 0x42000000, v32
	v_mul_f32_e32 v33, 0x42000000, v33
	v_med3_f32 v0, v39, s33, v233
	v_med3_f32 v30, v41, s33, v233
	v_cvt_pk_fp8_f32 v28, v0, v30 op_sel:[0,0,1]
	v_med3_f32 v0, v32, s33, v233
	v_med3_f32 v30, v33, s33, v233
	v_cvt_pk_fp8_f32 v29, v0, v30 op_sel:[0,0,1]
	v_add_u32_e32 v0, 0xffff8010, v25
	s_movk_i32 s5, 0x7d8
	v_and_or_b32 v0, v0, s5, v3
	v_lshl_or_b32 v0, v0, 11, v43
	v_lshl_add_u64 v[34:35], v[6:7], 0, v[0:1]
	ds_read2_b32 v[30:31], v21 offset1:32
	global_store_dwordx4 v[34:35], v[26:29], off sc1
	ds_read2_b32 v[26:27], v21 offset0:64 offset1:96
	v_add_u32_e32 v36, 0x400, v21
	ds_read2_b32 v[32:33], v36 offset1:32
	s_waitcnt lgkmcnt(2)
	v_mul_f32_e32 v0, 0x42000000, v30
	ds_read2_b32 v[28:29], v36 offset0:64 offset1:96
	v_mul_f32_e32 v35, 0x42000000, v31
	s_waitcnt lgkmcnt(2)
	v_mul_f32_e32 v38, 0x42000000, v26
	ds_read2_b32 v[30:31], v21 offset0:128 offset1:160
	v_mul_f32_e32 v40, 0x42000000, v27
	ds_read2_b32 v[26:27], v36 offset0:128 offset1:160
	s_waitcnt lgkmcnt(3)
	v_mul_f32_e32 v34, 0x42000000, v32
	v_mul_f32_e32 v37, 0x42000000, v33
	s_waitcnt lgkmcnt(2)
	v_mul_f32_e32 v39, 0x42000000, v28
	v_mul_f32_e32 v41, 0x42000000, v29
	s_waitcnt lgkmcnt(1)
	v_mul_f32_e32 v30, 0x42000000, v30
	ds_read2_b32 v[28:29], v21 offset0:192 offset1:224
	ds_read2_b32 v[32:33], v36 offset0:192 offset1:224
	s_waitcnt lgkmcnt(2)
	v_mul_f32_e32 v36, 0x42000000, v26
	v_mul_f32_e32 v31, 0x42000000, v31
	v_mul_f32_e32 v42, 0x42000000, v27
	v_med3_f32 v0, v0, s33, v233
	v_med3_f32 v27, v35, s33, v233
	v_mov_b32_e32 v26, v1
	v_cvt_pk_fp8_f32 v26, v0, v27
	v_med3_f32 v30, v30, s33, v233
	v_med3_f32 v31, v31, s33, v233
	v_mov_b32_e32 v27, v1
	v_cvt_pk_fp8_f32 v27, v30, v31
	s_waitcnt lgkmcnt(1)
	v_mul_f32_e32 v28, 0x42000000, v28
	v_mul_f32_e32 v29, 0x42000000, v29
	v_med3_f32 v0, v38, s33, v233
	v_med3_f32 v35, v40, s33, v233
	v_cvt_pk_fp8_f32 v26, v0, v35 op_sel:[0,0,1]
	v_med3_f32 v0, v28, s33, v233
	v_med3_f32 v28, v29, s33, v233
	v_cvt_pk_fp8_f32 v27, v0, v28 op_sel:[0,0,1]
	v_med3_f32 v0, v34, s33, v233
	v_med3_f32 v29, v37, s33, v233
	v_mov_b32_e32 v28, v1
	v_cvt_pk_fp8_f32 v28, v0, v29
	v_med3_f32 v31, v36, s33, v233
	v_med3_f32 v34, v42, s33, v233
	v_mov_b32_e32 v29, v1
	v_cvt_pk_fp8_f32 v29, v31, v34
	s_waitcnt lgkmcnt(0)
	v_mul_f32_e32 v32, 0x42000000, v32
	v_mul_f32_e32 v33, 0x42000000, v33
	v_med3_f32 v0, v39, s33, v233
	v_med3_f32 v30, v41, s33, v233
	v_cvt_pk_fp8_f32 v28, v0, v30 op_sel:[0,0,1]
	v_med3_f32 v0, v32, s33, v233
	v_med3_f32 v30, v33, s33, v233
	v_cvt_pk_fp8_f32 v29, v0, v30 op_sel:[0,0,1]
	v_add_u32_e32 v0, 0xffff8020, v25
	s_movk_i32 s5, 0x7e8
	v_and_or_b32 v0, v0, s5, v3
	v_lshl_or_b32 v0, v0, 11, v43
	v_lshl_add_u64 v[34:35], v[6:7], 0, v[0:1]
	ds_read2_b32 v[30:31], v23 offset1:32
	global_store_dwordx4 v[34:35], v[26:29], off sc1
	ds_read2_b32 v[26:27], v23 offset0:64 offset1:96
	v_add_u32_e32 v36, 0x400, v23
	ds_read2_b32 v[32:33], v36 offset1:32
	s_waitcnt lgkmcnt(2)
	v_mul_f32_e32 v0, 0x42000000, v30
	ds_read2_b32 v[28:29], v36 offset0:64 offset1:96
	v_mul_f32_e32 v35, 0x42000000, v31
	s_waitcnt lgkmcnt(2)
	v_mul_f32_e32 v38, 0x42000000, v26
	ds_read2_b32 v[30:31], v23 offset0:128 offset1:160
	v_mul_f32_e32 v40, 0x42000000, v27
	ds_read2_b32 v[26:27], v36 offset0:128 offset1:160
	s_waitcnt lgkmcnt(3)
	v_mul_f32_e32 v34, 0x42000000, v32
	v_mul_f32_e32 v37, 0x42000000, v33
	s_waitcnt lgkmcnt(2)
	v_mul_f32_e32 v39, 0x42000000, v28
	v_mul_f32_e32 v41, 0x42000000, v29
	s_waitcnt lgkmcnt(1)
	v_mul_f32_e32 v30, 0x42000000, v30
	ds_read2_b32 v[28:29], v23 offset0:192 offset1:224
	ds_read2_b32 v[32:33], v36 offset0:192 offset1:224
	s_waitcnt lgkmcnt(2)
	v_mul_f32_e32 v36, 0x42000000, v26
	v_mul_f32_e32 v31, 0x42000000, v31
	v_mul_f32_e32 v42, 0x42000000, v27
	v_med3_f32 v0, v0, s33, v233
	v_med3_f32 v27, v35, s33, v233
	v_mov_b32_e32 v26, v1
	v_cvt_pk_fp8_f32 v26, v0, v27
	v_med3_f32 v30, v30, s33, v233
	v_med3_f32 v31, v31, s33, v233
	v_mov_b32_e32 v27, v1
	v_cvt_pk_fp8_f32 v27, v30, v31
	s_waitcnt lgkmcnt(1)
	v_mul_f32_e32 v28, 0x42000000, v28
	v_mul_f32_e32 v29, 0x42000000, v29
	v_med3_f32 v0, v38, s33, v233
	v_med3_f32 v35, v40, s33, v233
	v_cvt_pk_fp8_f32 v26, v0, v35 op_sel:[0,0,1]
	v_med3_f32 v0, v28, s33, v233
	v_med3_f32 v28, v29, s33, v233
	v_cvt_pk_fp8_f32 v27, v0, v28 op_sel:[0,0,1]
	v_med3_f32 v0, v34, s33, v233
	v_med3_f32 v29, v37, s33, v233
	v_mov_b32_e32 v28, v1
	v_cvt_pk_fp8_f32 v28, v0, v29
	v_med3_f32 v31, v36, s33, v233
	v_med3_f32 v34, v42, s33, v233
	v_mov_b32_e32 v29, v1
	v_cvt_pk_fp8_f32 v29, v31, v34
	s_waitcnt lgkmcnt(0)
	v_mul_f32_e32 v32, 0x42000000, v32
	v_mul_f32_e32 v33, 0x42000000, v33
	v_med3_f32 v0, v39, s33, v233
	v_med3_f32 v30, v41, s33, v233
	v_cvt_pk_fp8_f32 v28, v0, v30 op_sel:[0,0,1]
	v_med3_f32 v0, v32, s33, v233
	v_med3_f32 v30, v33, s33, v233
	v_cvt_pk_fp8_f32 v29, v0, v30 op_sel:[0,0,1]
	v_add_u32_e32 v0, 0xffff8030, v25
	s_movk_i32 s5, 0x7f8
	v_and_or_b32 v0, v0, s5, v3
	v_lshl_or_b32 v0, v0, 11, v43
	v_lshl_add_u64 v[6:7], v[6:7], 0, v[0:1]
	global_store_dwordx4 v[6:7], v[26:29], off sc1
	s_waitcnt lgkmcnt(0)

.LBB0_266:
	s_andn2_b64 vcc, exec, s[6:7]
	s_cbranch_vccnz .LBB0_259
	s_ashr_i32 s5, s4, 31
	s_lshl_b64 s[6:7], s[4:5], 23
	s_add_u32 s6, s38, s6
	s_addc_u32 s7, s39, s7
	s_lshl_b64 s[4:5], s[4:5], 22
	s_add_u32 s8, s24, s4
	s_addc_u32 s9, s25, s5
	s_bfe_u32 s4, s55, 0x5001a
	s_add_i32 s4, s55, s4
	s_sext_i32_i16 s5, s4
	s_lshl_b32 s5, s5, 2
	s_and_b32 s4, s4, 0xffe0
	s_and_b32 s20, s5, 0xffffff80
	s_sub_i32 s4, s55, s4
	v_or_b32_e32 v6, s20, v3
	s_sext_i32_i16 s4, s4
	v_ashrrev_i32_e32 v7, 31, v6
	s_lshl_b32 s4, s4, 5
	v_lshlrev_b64 v[6:7], 12, v[6:7]
	v_lshl_add_u64 v[6:7], s[6:7], 0, v[6:7]
	s_ashr_i32 s5, s4, 31
	v_lshl_add_u64 v[6:7], s[4:5], 2, v[6:7]
	v_lshlrev_b32_e32 v0, 2, v2
	v_lshl_add_u64 v[6:7], v[6:7], 0, v[0:1]
	s_mov_b32 s5, 0x8000
	v_add_co_u32_e32 v30, vcc, s5, v6
	s_mov_b32 s5, 0x10000
	s_nop 0
	v_addc_co_u32_e32 v31, vcc, 0, v7, vcc
	v_add_co_u32_e32 v34, vcc, s5, v6
	s_mov_b32 s5, 0x18000
	s_nop 0
	v_addc_co_u32_e32 v35, vcc, 0, v7, vcc
	v_add_co_u32_e32 v38, vcc, s5, v6
	s_mov_b32 s5, 0x20000
	s_nop 0
	v_addc_co_u32_e32 v39, vcc, 0, v7, vcc
	v_add_co_u32_e32 v42, vcc, s5, v6
	s_mov_b32 s5, 0x28000
	s_nop 0
	v_addc_co_u32_e32 v43, vcc, 0, v7, vcc
	v_add_co_u32_e32 v46, vcc, s5, v6
	s_mov_b32 s5, 0x30000
	s_nop 0
	v_addc_co_u32_e32 v47, vcc, 0, v7, vcc
	v_add_co_u32_e32 v50, vcc, s5, v6
	s_mov_b32 s5, 0x38000
	s_nop 0
	v_addc_co_u32_e32 v51, vcc, 0, v7, vcc
	v_add_co_u32_e32 v54, vcc, s5, v6
	s_mov_b32 s5, 0x40000
	s_nop 0
	v_addc_co_u32_e32 v55, vcc, 0, v7, vcc
	v_add_co_u32_e32 v58, vcc, s5, v6
	s_mov_b32 s5, 0x48000
	s_nop 0
	v_addc_co_u32_e32 v59, vcc, 0, v7, vcc
	v_add_co_u32_e32 v62, vcc, s5, v6
	s_mov_b32 s5, 0x50000
	s_nop 0
	v_addc_co_u32_e32 v63, vcc, 0, v7, vcc
	v_add_co_u32_e32 v68, vcc, s5, v6
	s_mov_b32 s5, 0x58000
	s_nop 0
	v_addc_co_u32_e32 v69, vcc, 0, v7, vcc
	v_add_co_u32_e32 v72, vcc, s5, v6
	s_mov_b32 s5, 0x60000
	s_nop 0
	v_addc_co_u32_e32 v73, vcc, 0, v7, vcc
	global_load_dwordx4 v[26:29], v[6:7], off
	s_nop 0
	global_load_dwordx4 v[30:33], v[30:31], off
	v_add_co_u32_e32 v76, vcc, s5, v6
	global_load_dwordx4 v[34:37], v[34:35], off
	s_nop 0
	global_load_dwordx4 v[38:41], v[38:39], off
	v_addc_co_u32_e32 v77, vcc, 0, v7, vcc
	s_mov_b32 s5, 0x68000
	global_load_dwordx4 v[42:45], v[42:43], off
	s_nop 0
	global_load_dwordx4 v[46:49], v[46:47], off
	v_add_co_u32_e32 v80, vcc, s5, v6
	global_load_dwordx4 v[50:53], v[50:51], off
	s_nop 0
	global_load_dwordx4 v[54:57], v[54:55], off
	v_addc_co_u32_e32 v81, vcc, 0, v7, vcc
	s_mov_b32 s5, 0x70000
	global_load_dwordx4 v[58:61], v[58:59], off
	s_nop 0
	global_load_dwordx4 v[62:65], v[62:63], off
	v_add_co_u32_e32 v84, vcc, s5, v6
	global_load_dwordx4 v[68:71], v[68:69], off
	s_nop 0
	global_load_dwordx4 v[72:75], v[72:73], off
	v_addc_co_u32_e32 v85, vcc, 0, v7, vcc
	s_mov_b32 s5, 0x78000
	global_load_dwordx4 v[76:79], v[76:77], off
	s_nop 0
	global_load_dwordx4 v[80:83], v[80:81], off
	v_add_co_u32_e32 v6, vcc, s5, v6
	v_add_u32_e32 v0, v8, v4
	s_nop 0
	v_addc_co_u32_e32 v7, vcc, 0, v7, vcc
	global_load_dwordx4 v[84:87], v[84:85], off
	s_nop 0
	global_load_dwordx4 v[88:91], v[6:7], off
	s_waitcnt vmcnt(0)
	ds_write_b128 v0, v[26:29]
	s_waitcnt vmcnt(14)
	ds_write_b128 v0, v[30:33] offset:1024
	v_add_u32_e32 v0, v8, v9
	s_waitcnt vmcnt(13)
	ds_write_b128 v0, v[34:37] offset:2048
	s_waitcnt vmcnt(12)
	ds_write_b128 v0, v[38:41] offset:3072
	v_add_u32_e32 v0, v8, v10
	s_waitcnt vmcnt(11)
	ds_write_b128 v0, v[42:45] offset:4096
	s_waitcnt vmcnt(10)
	ds_write_b128 v0, v[46:49] offset:5120
	v_add_u32_e32 v0, v8, v11
	s_waitcnt vmcnt(9)
	ds_write_b128 v0, v[50:53] offset:6144
	s_waitcnt vmcnt(8)
	ds_write_b128 v0, v[54:57] offset:7168
	v_add_u32_e32 v0, v8, v12
	s_waitcnt vmcnt(7)
	ds_write_b128 v0, v[58:61] offset:8192
	s_waitcnt vmcnt(6)
	ds_write_b128 v0, v[62:65] offset:9216
	v_add_u32_e32 v0, v8, v13
	s_waitcnt vmcnt(5)
	ds_write_b128 v0, v[68:71] offset:10240
	s_waitcnt vmcnt(4)
	ds_write_b128 v0, v[72:75] offset:11264
	v_add_u32_e32 v0, v8, v14
	s_waitcnt vmcnt(3)
	ds_write_b128 v0, v[76:79] offset:12288
	s_waitcnt vmcnt(2)
	ds_write_b128 v0, v[80:83] offset:13312
	v_add_u32_e32 v0, v8, v15
	s_waitcnt vmcnt(1)
	ds_write_b128 v0, v[84:87] offset:14336
	s_waitcnt vmcnt(0)
	ds_write_b128 v0, v[88:91] offset:15360
	s_waitcnt lgkmcnt(0)
	v_add_u32_e32 v0, 0x400, v17
	ds_read2_b32 v[26:27], v17 offset1:32
	ds_read2_b32 v[28:29], v0 offset1:32
	ds_read2_b32 v[30:31], v17 offset0:64 offset1:96
	ds_read2_b32 v[32:33], v0 offset0:64 offset1:96
	s_ashr_i32 s5, s20, 31
	s_waitcnt lgkmcnt(3)
	v_mul_f32_e32 v25, 0x42000000, v26
	s_waitcnt lgkmcnt(2)
	v_mul_f32_e32 v34, 0x42000000, v28
	v_mul_f32_e32 v35, 0x42000000, v27
	v_mul_f32_e32 v36, 0x42000000, v29
	s_waitcnt lgkmcnt(1)
	v_mul_f32_e32 v37, 0x42000000, v30
	ds_read2_b32 v[26:27], v17 offset0:128 offset1:160
	s_waitcnt lgkmcnt(1)
	v_mul_f32_e32 v38, 0x42000000, v32
	v_mul_f32_e32 v39, 0x42000000, v31
	ds_read2_b32 v[28:29], v0 offset0:128 offset1:160
	v_mul_f32_e32 v40, 0x42000000, v33
	ds_read2_b32 v[30:31], v17 offset0:192 offset1:224
	ds_read2_b32 v[32:33], v0 offset0:192 offset1:224
	s_waitcnt lgkmcnt(3)
	v_mul_f32_e32 v41, 0x42000000, v26
	v_mul_f32_e32 v27, 0x42000000, v27
	s_waitcnt lgkmcnt(2)
	v_mul_f32_e32 v0, 0x42000000, v28
	s_waitcnt lgkmcnt(1)
	v_mul_f32_e32 v28, 0x42000000, v30
	s_waitcnt lgkmcnt(0)
	v_mul_f32_e32 v30, 0x42000000, v32
	v_mul_f32_e32 v32, 0x42000000, v33
	v_med3_f32 v25, v25, s33, v233
	v_med3_f32 v33, v35, s33, v233
	v_mov_b32_e32 v26, v1
	v_cvt_pk_fp8_f32 v26, v25, v33
	v_med3_f32 v25, v37, s33, v233
	v_med3_f32 v35, v41, s33, v233
	v_med3_f32 v37, v27, s33, v233
	v_mov_b32_e32 v27, v1
	v_cvt_pk_fp8_f32 v27, v35, v37
	v_mul_f32_e32 v31, 0x42000000, v31
	v_med3_f32 v33, v39, s33, v233
	v_cvt_pk_fp8_f32 v26, v25, v33 op_sel:[0,0,1]
	v_med3_f32 v25, v28, s33, v233
	v_med3_f32 v28, v31, s33, v233
	v_mul_f32_e32 v29, 0x42000000, v29
	v_cvt_pk_fp8_f32 v27, v25, v28 op_sel:[0,0,1]
	v_med3_f32 v25, v34, s33, v233
	v_med3_f32 v31, v36, s33, v233
	v_mov_b32_e32 v28, v1
	v_cvt_pk_fp8_f32 v28, v25, v31
	v_med3_f32 v0, v0, s33, v233
	v_med3_f32 v33, v29, s33, v233
	v_mov_b32_e32 v29, v1
	v_cvt_pk_fp8_f32 v29, v0, v33
	v_med3_f32 v25, v38, s33, v233
	v_med3_f32 v31, v40, s33, v233
	v_cvt_pk_fp8_f32 v28, v25, v31 op_sel:[0,0,1]
	v_med3_f32 v0, v30, s33, v233
	v_med3_f32 v25, v32, s33, v233
	s_add_u32 s6, s8, s20
	v_cvt_pk_fp8_f32 v29, v0, v25 op_sel:[0,0,1]
	v_or_b32_e32 v0, s4, v3
	s_addc_u32 s7, s9, s5
	v_lshlrev_b32_e32 v0, 1, v0
	s_movk_i32 s5, 0xffc8
	v_and_or_b32 v30, v0, s5, v16
	v_ashrrev_i32_e32 v31, 31, v30
	v_lshl_add_u64 v[6:7], s[6:7], 0, v[4:5]
	v_lshlrev_b64 v[30:31], 11, v[30:31]
	v_lshl_add_u64 v[30:31], v[6:7], 0, v[30:31]
	global_store_dwordx4 v[30:31], v[26:29], off sc1
	ds_read2_b32 v[26:27], v19 offset0:64 offset1:96
	ds_read2_b32 v[32:33], v19 offset1:32
	v_add_u32_e32 v0, 0x400, v19
	ds_read2_b32 v[28:29], v0 offset0:64 offset1:96
	ds_read2_b32 v[30:31], v19 offset0:128 offset1:160
	s_waitcnt lgkmcnt(3)
	v_mul_f32_e32 v37, 0x42000000, v26
	v_mul_f32_e32 v39, 0x42000000, v27
	ds_read2_b32 v[26:27], v0 offset0:128 offset1:160
	s_waitcnt lgkmcnt(3)
	v_mul_f32_e32 v25, 0x42000000, v32
	v_mul_f32_e32 v36, 0x42000000, v33
	ds_read2_b32 v[34:35], v0 offset1:32
	s_waitcnt lgkmcnt(3)
	v_mul_f32_e32 v38, 0x42000000, v28
	v_mul_f32_e32 v40, 0x42000000, v29
	s_waitcnt lgkmcnt(2)
	v_mul_f32_e32 v30, 0x42000000, v30
	ds_read2_b32 v[28:29], v19 offset0:192 offset1:224
	ds_read2_b32 v[32:33], v0 offset0:192 offset1:224
	s_waitcnt lgkmcnt(3)
	v_mul_f32_e32 v0, 0x42000000, v26
	v_mul_f32_e32 v31, 0x42000000, v31
	v_mul_f32_e32 v41, 0x42000000, v27
	v_med3_f32 v25, v25, s33, v233
	v_med3_f32 v27, v36, s33, v233
	v_mov_b32_e32 v26, v1
	v_cvt_pk_fp8_f32 v26, v25, v27
	v_med3_f32 v30, v30, s33, v233
	v_med3_f32 v31, v31, s33, v233
	v_mov_b32_e32 v27, v1
	v_cvt_pk_fp8_f32 v27, v30, v31
	s_waitcnt lgkmcnt(1)
	v_mul_f32_e32 v28, 0x42000000, v28
	v_mul_f32_e32 v29, 0x42000000, v29
	v_med3_f32 v25, v37, s33, v233
	v_med3_f32 v36, v39, s33, v233
	v_mul_f32_e32 v34, 0x42000000, v34
	v_mul_f32_e32 v35, 0x42000000, v35
	v_cvt_pk_fp8_f32 v26, v25, v36 op_sel:[0,0,1]
	v_med3_f32 v25, v28, s33, v233
	v_med3_f32 v28, v29, s33, v233
	v_cvt_pk_fp8_f32 v27, v25, v28 op_sel:[0,0,1]
	v_med3_f32 v25, v34, s33, v233
	v_med3_f32 v29, v35, s33, v233
	v_mov_b32_e32 v28, v1
	v_cvt_pk_fp8_f32 v28, v25, v29
	v_med3_f32 v0, v0, s33, v233
	v_med3_f32 v31, v41, s33, v233
	v_mov_b32_e32 v29, v1
	v_cvt_pk_fp8_f32 v29, v0, v31
	s_waitcnt lgkmcnt(0)
	v_mul_f32_e32 v32, 0x42000000, v32
	v_mul_f32_e32 v33, 0x42000000, v33
	v_med3_f32 v25, v38, s33, v233
	v_med3_f32 v30, v40, s33, v233
	v_cvt_pk_fp8_f32 v28, v25, v30 op_sel:[0,0,1]
	v_med3_f32 v0, v32, s33, v233
	v_med3_f32 v25, v33, s33, v233
	v_cvt_pk_fp8_f32 v29, v0, v25 op_sel:[0,0,1]
	v_or_b32_e32 v0, s4, v18
	v_lshlrev_b32_e32 v0, 1, v0
	s_movk_i32 s5, 0xffd8
	v_and_or_b32 v30, v0, s5, v16
	v_ashrrev_i32_e32 v31, 31, v30
	v_lshlrev_b64 v[30:31], 11, v[30:31]
	v_lshl_add_u64 v[30:31], v[6:7], 0, v[30:31]
	global_store_dwordx4 v[30:31], v[26:29], off sc1
	ds_read2_b32 v[26:27], v21 offset0:64 offset1:96
	ds_read2_b32 v[32:33], v21 offset1:32
	v_add_u32_e32 v0, 0x400, v21
	ds_read2_b32 v[28:29], v0 offset0:64 offset1:96
	ds_read2_b32 v[30:31], v21 offset0:128 offset1:160
	s_waitcnt lgkmcnt(3)
	v_mul_f32_e32 v37, 0x42000000, v26
	v_mul_f32_e32 v39, 0x42000000, v27
	ds_read2_b32 v[26:27], v0 offset0:128 offset1:160
	s_waitcnt lgkmcnt(3)
	v_mul_f32_e32 v25, 0x42000000, v32
	v_mul_f32_e32 v36, 0x42000000, v33
	ds_read2_b32 v[34:35], v0 offset1:32
	s_waitcnt lgkmcnt(3)
	v_mul_f32_e32 v38, 0x42000000, v28
	v_mul_f32_e32 v40, 0x42000000, v29
	s_waitcnt lgkmcnt(2)
	v_mul_f32_e32 v30, 0x42000000, v30
	ds_read2_b32 v[28:29], v21 offset0:192 offset1:224
	ds_read2_b32 v[32:33], v0 offset0:192 offset1:224
	s_waitcnt lgkmcnt(3)
	v_mul_f32_e32 v0, 0x42000000, v26
	v_mul_f32_e32 v31, 0x42000000, v31
	v_mul_f32_e32 v41, 0x42000000, v27
	v_med3_f32 v25, v25, s33, v233
	v_med3_f32 v27, v36, s33, v233
	v_mov_b32_e32 v26, v1
	v_cvt_pk_fp8_f32 v26, v25, v27
	v_med3_f32 v30, v30, s33, v233
	v_med3_f32 v31, v31, s33, v233
	v_mov_b32_e32 v27, v1
	v_cvt_pk_fp8_f32 v27, v30, v31
	s_waitcnt lgkmcnt(1)
	v_mul_f32_e32 v28, 0x42000000, v28
	v_mul_f32_e32 v29, 0x42000000, v29
	v_med3_f32 v25, v37, s33, v233
	v_med3_f32 v36, v39, s33, v233
	v_mul_f32_e32 v34, 0x42000000, v34
	v_mul_f32_e32 v35, 0x42000000, v35
	v_cvt_pk_fp8_f32 v26, v25, v36 op_sel:[0,0,1]
	v_med3_f32 v25, v28, s33, v233
	v_med3_f32 v28, v29, s33, v233
	v_cvt_pk_fp8_f32 v27, v25, v28 op_sel:[0,0,1]
	v_med3_f32 v25, v34, s33, v233
	v_med3_f32 v29, v35, s33, v233
	v_mov_b32_e32 v28, v1
	v_cvt_pk_fp8_f32 v28, v25, v29
	v_med3_f32 v0, v0, s33, v233
	v_med3_f32 v31, v41, s33, v233
	v_mov_b32_e32 v29, v1
	v_cvt_pk_fp8_f32 v29, v0, v31
	s_waitcnt lgkmcnt(0)
	v_mul_f32_e32 v32, 0x42000000, v32
	v_mul_f32_e32 v33, 0x42000000, v33
	v_med3_f32 v25, v38, s33, v233
	v_med3_f32 v30, v40, s33, v233
	v_cvt_pk_fp8_f32 v28, v25, v30 op_sel:[0,0,1]
	v_med3_f32 v0, v32, s33, v233
	v_med3_f32 v25, v33, s33, v233
	v_cvt_pk_fp8_f32 v29, v0, v25 op_sel:[0,0,1]
	v_or_b32_e32 v0, s4, v20
	v_lshlrev_b32_e32 v0, 1, v0
	s_movk_i32 s5, 0xffe8
	v_and_or_b32 v30, v0, s5, v16
	v_ashrrev_i32_e32 v31, 31, v30
	v_lshlrev_b64 v[30:31], 11, v[30:31]
	v_lshl_add_u64 v[30:31], v[6:7], 0, v[30:31]
	global_store_dwordx4 v[30:31], v[26:29], off sc1
	ds_read2_b32 v[26:27], v23 offset0:64 offset1:96
	ds_read2_b32 v[32:33], v23 offset1:32
	v_add_u32_e32 v0, 0x400, v23
	ds_read2_b32 v[28:29], v0 offset0:64 offset1:96
	ds_read2_b32 v[30:31], v23 offset0:128 offset1:160
	s_waitcnt lgkmcnt(3)
	v_mul_f32_e32 v37, 0x42000000, v26
	v_mul_f32_e32 v39, 0x42000000, v27
	ds_read2_b32 v[26:27], v0 offset0:128 offset1:160
	s_waitcnt lgkmcnt(3)
	v_mul_f32_e32 v25, 0x42000000, v32
	v_mul_f32_e32 v36, 0x42000000, v33
	ds_read2_b32 v[34:35], v0 offset1:32
	s_waitcnt lgkmcnt(3)
	v_mul_f32_e32 v38, 0x42000000, v28
	v_mul_f32_e32 v40, 0x42000000, v29
	s_waitcnt lgkmcnt(2)
	v_mul_f32_e32 v30, 0x42000000, v30
	ds_read2_b32 v[28:29], v23 offset0:192 offset1:224
	ds_read2_b32 v[32:33], v0 offset0:192 offset1:224
	s_waitcnt lgkmcnt(3)
	v_mul_f32_e32 v0, 0x42000000, v26
	v_mul_f32_e32 v31, 0x42000000, v31
	v_mul_f32_e32 v41, 0x42000000, v27
	v_med3_f32 v25, v25, s33, v233
	v_med3_f32 v27, v36, s33, v233
	v_mov_b32_e32 v26, v1
	v_cvt_pk_fp8_f32 v26, v25, v27
	v_med3_f32 v30, v30, s33, v233
	v_med3_f32 v31, v31, s33, v233
	v_mov_b32_e32 v27, v1
	v_cvt_pk_fp8_f32 v27, v30, v31
	s_waitcnt lgkmcnt(1)
	v_mul_f32_e32 v28, 0x42000000, v28
	v_mul_f32_e32 v29, 0x42000000, v29
	v_med3_f32 v25, v37, s33, v233
	v_med3_f32 v36, v39, s33, v233
	v_mul_f32_e32 v34, 0x42000000, v34
	v_mul_f32_e32 v35, 0x42000000, v35
	v_cvt_pk_fp8_f32 v26, v25, v36 op_sel:[0,0,1]
	v_med3_f32 v25, v28, s33, v233
	v_med3_f32 v28, v29, s33, v233
	v_cvt_pk_fp8_f32 v27, v25, v28 op_sel:[0,0,1]
	v_med3_f32 v25, v34, s33, v233
	v_med3_f32 v29, v35, s33, v233
	v_mov_b32_e32 v28, v1
	v_cvt_pk_fp8_f32 v28, v25, v29
	v_med3_f32 v0, v0, s33, v233
	v_med3_f32 v31, v41, s33, v233
	v_mov_b32_e32 v29, v1
	v_cvt_pk_fp8_f32 v29, v0, v31
	s_waitcnt lgkmcnt(0)
	v_mul_f32_e32 v32, 0x42000000, v32
	v_mul_f32_e32 v33, 0x42000000, v33
	v_med3_f32 v25, v38, s33, v233
	v_med3_f32 v30, v40, s33, v233
	v_cvt_pk_fp8_f32 v28, v25, v30 op_sel:[0,0,1]
	v_med3_f32 v0, v32, s33, v233
	v_med3_f32 v25, v33, s33, v233
	v_cvt_pk_fp8_f32 v29, v0, v25 op_sel:[0,0,1]
	v_or_b32_e32 v0, s4, v22
	v_lshlrev_b32_e32 v0, 1, v0
	v_and_or_b32 v30, v0, -8, v16
	v_ashrrev_i32_e32 v31, 31, v30
	v_lshlrev_b64 v[30:31], 11, v[30:31]
	v_lshl_add_u64 v[6:7], v[6:7], 0, v[30:31]
	global_store_dwordx4 v[6:7], v[26:29], off sc1
	s_waitcnt lgkmcnt(0)
	s_branch .LBB0_259

.LBB0_353:
	s_or_b64 exec, exec, s[6:7]
	s_lshl_b32 s6, s88, 8
	s_or_b32 s6, s6, s67
	s_cmp_lt_i32 s88, 4
	v_lshl_add_u32 v22, v3, 3, s6
	s_cselect_b64 vcc, -1, 0
	v_mov_b32_e32 v3, 0x3d000000
	v_mov_b32_e32 v4, 0x3bb8aa3b
	v_pk_mul_f32 v[24:25], v[160:161], v[10:11]
	v_pk_mul_f32 v[26:27], v[158:159], v[8:9]
	v_cndmask_b32_e32 v16, v3, v4, vcc
	v_pk_fma_f32 v[26:27], v[154:155], v[12:13], v[26:27] neg_lo:[0,0,1] neg_hi:[0,0,1]
	v_pk_fma_f32 v[24:25], v[156:157], v[14:15], v[24:25] neg_lo:[0,0,1] neg_hi:[0,0,1]
	v_pk_mul_f32 v[30:31], v[158:159], v[12:13]
	v_pk_mul_f32 v[28:29], v[16:17], v[24:25] op_sel_hi:[0,1]
	v_pk_mul_f32 v[24:25], v[16:17], v[26:27] op_sel_hi:[0,1]
	v_pk_mul_f32 v[26:27], v[160:161], v[14:15]
	v_mov_b64_e32 v[4:5], s[48:49]
	v_pk_fma_f32 v[30:31], v[154:155], v[8:9], v[30:31]
	v_pk_fma_f32 v[26:27], v[156:157], v[10:11], v[26:27]
	v_ashrrev_i32_e32 v23, 31, v22
	v_mad_i64_i32 v[4:5], s[6:7], v20, s83, v[4:5]
	v_pk_mul_f32 v[32:33], v[16:17], v[26:27] op_sel_hi:[0,1]
	v_pk_mul_f32 v[26:27], v[16:17], v[30:31] op_sel_hi:[0,1]
	v_lshl_add_u64 v[4:5], v[22:23], 1, v[4:5]
	v_cvt_pk_bf16_f32 v24, v24, v25
	v_cvt_pk_bf16_f32 v25, v28, v29
	v_cvt_pk_bf16_f32 v26, v26, v27
	v_cvt_pk_bf16_f32 v27, v32, v33
	global_store_dwordx4 v[4:5], v[24:27], off sc1
	v_mov_b32_e32 v7, 0
	v_mov_b32_e32 v3, 1.0
	v_pk_mul_f32 v[24:25], v[152:153], v[10:11]
	v_pk_mul_f32 v[26:27], v[150:151], v[8:9]
	v_pk_fma_f32 v[24:25], v[148:149], v[14:15], v[24:25] neg_lo:[0,0,1] neg_hi:[0,0,1]
	v_pk_fma_f32 v[26:27], v[146:147], v[12:13], v[26:27] neg_lo:[0,0,1] neg_hi:[0,0,1]
	v_pk_mul_f32 v[14:15], v[152:153], v[14:15]
	v_pk_mul_f32 v[12:13], v[150:151], v[12:13]
	v_pk_fma_f32 v[10:11], v[148:149], v[10:11], v[14:15]
	v_pk_fma_f32 v[8:9], v[146:147], v[8:9], v[12:13]
	v_pk_mul_f32 v[12:13], v[16:17], v[10:11] op_sel_hi:[0,1]
	v_pk_mul_f32 v[10:11], v[16:17], v[8:9] op_sel_hi:[0,1]
	v_pk_mul_f32 v[24:25], v[16:17], v[24:25] op_sel_hi:[0,1]
	v_pk_mul_f32 v[26:27], v[16:17], v[26:27] op_sel_hi:[0,1]
	v_cvt_pk_bf16_f32 v8, v26, v27
	v_cvt_pk_bf16_f32 v9, v24, v25
	v_cvt_pk_bf16_f32 v10, v10, v11
	v_cvt_pk_bf16_f32 v11, v12, v13
	global_store_dwordx4 v[4:5], v[8:11], off offset:256 sc1
	v_mov_b32_e32 v4, 1.0
	v_mov_b32_e32 v5, 1.0
	v_or_b32_e32 v10, 16, v20
	v_ashrrev_i32_e32 v11, 31, v10
	v_mov_b32_e32 v8, 0
	v_mov_b32_e32 v9, 0
	s_and_saveexec_b64 s[6:7], s[4:5]
	s_cbranch_execz .LBB0_355
	v_lshlrev_b64 v[2:3], 6, v[10:11]
	v_lshl_add_u64 v[2:3], s[50:51], 0, v[2:3]
	v_lshl_add_u64 v[6:7], v[18:19], 2, v[2:3]
	global_load_dwordx4 v[2:5], v[6:7], off
	s_nop 0
	global_load_dwordx4 v[6:9], v[6:7], off offset:32
	s_waitcnt vmcnt(0)
.LBB0_355:
	s_or_b64 exec, exec, s[6:7]
	v_mov_b64_e32 v[12:13], s[48:49]
	v_mad_i64_i32 v[10:11], s[6:7], v10, s83, v[12:13]
	v_lshl_add_u64 v[14:15], v[22:23], 1, v[10:11]
	v_pk_mul_f32 v[10:11], v[144:145], v[8:9]
	v_pk_mul_f32 v[12:13], v[142:143], v[6:7]
	v_mov_b32_e32 v17, v16
	v_pk_fma_f32 v[12:13], v[138:139], v[2:3], v[12:13] neg_lo:[0,0,1] neg_hi:[0,0,1]
	v_pk_fma_f32 v[10:11], v[140:141], v[4:5], v[10:11] neg_lo:[0,0,1] neg_hi:[0,0,1]
	v_mov_b32_e32 v24, v16
	v_mov_b32_e32 v25, v16
	v_pk_mul_f32 v[26:27], v[24:25], v[10:11]
	v_pk_mul_f32 v[10:11], v[16:17], v[12:13]
	v_pk_mul_f32 v[12:13], v[144:145], v[4:5]
	v_pk_mul_f32 v[28:29], v[142:143], v[2:3]
	v_pk_fma_f32 v[12:13], v[140:141], v[8:9], v[12:13]
	v_pk_fma_f32 v[28:29], v[138:139], v[6:7], v[28:29]
	v_pk_mul_f32 v[30:31], v[24:25], v[12:13]
	v_pk_mul_f32 v[12:13], v[16:17], v[28:29]
	v_cvt_pk_bf16_f32 v10, v10, v11
	v_cvt_pk_bf16_f32 v11, v26, v27
	s_nop 0
	v_cvt_pk_bf16_f32 v12, v12, v13
	v_cvt_pk_bf16_f32 v13, v30, v31
	global_store_dwordx4 v[14:15], v[10:13], off sc1
	s_nop 1
	v_pk_mul_f32 v[10:11], v[136:137], v[8:9]
	v_pk_mul_f32 v[12:13], v[134:135], v[6:7]
	v_pk_fma_f32 v[10:11], v[132:133], v[4:5], v[10:11] neg_lo:[0,0,1] neg_hi:[0,0,1]
	v_pk_fma_f32 v[12:13], v[130:131], v[2:3], v[12:13] neg_lo:[0,0,1] neg_hi:[0,0,1]
	v_pk_mul_f32 v[4:5], v[136:137], v[4:5]
	v_pk_mul_f32 v[2:3], v[134:135], v[2:3]
	v_pk_fma_f32 v[4:5], v[132:133], v[8:9], v[4:5]
	v_pk_fma_f32 v[2:3], v[130:131], v[6:7], v[2:3]
	v_pk_mul_f32 v[6:7], v[24:25], v[4:5]
	v_pk_mul_f32 v[4:5], v[16:17], v[2:3]
	v_pk_mul_f32 v[10:11], v[24:25], v[10:11]
	v_pk_mul_f32 v[12:13], v[16:17], v[12:13]
	v_mov_b32_e32 v8, 0
	v_cvt_pk_bf16_f32 v2, v12, v13
	v_cvt_pk_bf16_f32 v3, v10, v11
	v_cvt_pk_bf16_f32 v4, v4, v5
	v_cvt_pk_bf16_f32 v5, v6, v7
	global_store_dwordx4 v[14:15], v[2:5], off offset:256 sc1
	v_mov_b32_e32 v6, 0
	v_mov_b32_e32 v9, 0
	v_or_b32_e32 v4, 32, v20
	v_ashrrev_i32_e32 v5, 31, v4
	v_mov_b32_e32 v2, 1.0
	v_mov_b32_e32 v10, 0
	v_mov_b32_e32 v11, 0
	v_mov_b32_e32 v12, 1.0
	v_mov_b32_e32 v13, 1.0
	v_mov_b32_e32 v14, 1.0
	v_mov_b32_e32 v15, 1.0
	s_and_saveexec_b64 s[6:7], s[4:5]
	s_cbranch_execz .LBB0_357
	v_lshlrev_b64 v[8:9], 6, v[4:5]
	v_lshl_add_u64 v[8:9], s[50:51], 0, v[8:9]
	v_lshl_add_u64 v[8:9], v[18:19], 2, v[8:9]
	global_load_dwordx4 v[12:15], v[8:9], off
	s_nop 0
	global_load_dwordx4 v[8:11], v[8:9], off offset:32
	s_waitcnt vmcnt(0)
.LBB0_357:
	s_or_b64 exec, exec, s[6:7]
	v_mov_b64_e32 v[26:27], s[48:49]
	v_mad_i64_i32 v[4:5], s[6:7], v4, s83, v[26:27]
	v_pk_mul_f32 v[26:27], v[128:129], v[10:11]
	v_pk_mul_f32 v[28:29], v[126:127], v[8:9]
	v_pk_fma_f32 v[26:27], v[124:125], v[14:15], v[26:27] neg_lo:[0,0,1] neg_hi:[0,0,1]
	v_pk_fma_f32 v[28:29], v[122:123], v[12:13], v[28:29] neg_lo:[0,0,1] neg_hi:[0,0,1]
	v_pk_mul_f32 v[30:31], v[24:25], v[26:27]
	v_pk_mul_f32 v[26:27], v[16:17], v[28:29]
	v_pk_mul_f32 v[28:29], v[128:129], v[14:15]
	v_pk_mul_f32 v[32:33], v[126:127], v[12:13]
	v_pk_fma_f32 v[28:29], v[124:125], v[10:11], v[28:29]
	v_pk_fma_f32 v[32:33], v[122:123], v[8:9], v[32:33]
	v_pk_mul_f32 v[122:123], v[24:25], v[28:29]
	v_pk_mul_f32 v[28:29], v[16:17], v[32:33]
	v_lshl_add_u64 v[4:5], v[22:23], 1, v[4:5]
	v_cvt_pk_bf16_f32 v26, v26, v27
	v_cvt_pk_bf16_f32 v27, v30, v31
	v_cvt_pk_bf16_f32 v28, v28, v29
	v_cvt_pk_bf16_f32 v29, v122, v123
	global_store_dwordx4 v[4:5], v[26:29], off sc1
	v_mov_b32_e32 v7, 0
	v_mov_b32_e32 v3, 1.0
	v_pk_mul_f32 v[26:27], v[120:121], v[10:11]
	v_pk_mul_f32 v[28:29], v[118:119], v[8:9]
	v_pk_fma_f32 v[26:27], v[116:117], v[14:15], v[26:27] neg_lo:[0,0,1] neg_hi:[0,0,1]
	v_pk_fma_f32 v[28:29], v[114:115], v[12:13], v[28:29] neg_lo:[0,0,1] neg_hi:[0,0,1]
	v_pk_mul_f32 v[14:15], v[120:121], v[14:15]
	v_pk_mul_f32 v[12:13], v[118:119], v[12:13]
	v_pk_fma_f32 v[10:11], v[116:117], v[10:11], v[14:15]
	v_pk_fma_f32 v[8:9], v[114:115], v[8:9], v[12:13]
	v_pk_mul_f32 v[12:13], v[24:25], v[10:11]
	v_pk_mul_f32 v[10:11], v[16:17], v[8:9]
	v_pk_mul_f32 v[26:27], v[24:25], v[26:27]
	v_pk_mul_f32 v[28:29], v[16:17], v[28:29]
	s_nop 0
	v_cvt_pk_bf16_f32 v8, v28, v29
	v_cvt_pk_bf16_f32 v9, v26, v27
	v_cvt_pk_bf16_f32 v10, v10, v11
	v_cvt_pk_bf16_f32 v11, v12, v13
	global_store_dwordx4 v[4:5], v[8:11], off offset:256 sc1
	v_mov_b32_e32 v4, 1.0
	v_mov_b32_e32 v5, 1.0
	v_or_b32_e32 v10, 48, v20
	v_ashrrev_i32_e32 v11, 31, v10
	v_mov_b32_e32 v8, 0
	v_mov_b32_e32 v9, 0
	s_and_saveexec_b64 s[6:7], s[4:5]
	s_cbranch_execz .LBB0_359
	v_lshlrev_b64 v[2:3], 6, v[10:11]
	v_lshl_add_u64 v[2:3], s[50:51], 0, v[2:3]
	v_lshl_add_u64 v[6:7], v[18:19], 2, v[2:3]
	global_load_dwordx4 v[2:5], v[6:7], off
	s_nop 0
	global_load_dwordx4 v[6:9], v[6:7], off offset:32
	s_waitcnt vmcnt(0)
.LBB0_359:
	s_or_b64 exec, exec, s[6:7]
	v_mov_b64_e32 v[12:13], s[48:49]
	v_mad_i64_i32 v[10:11], s[6:7], v10, s83, v[12:13]
	v_lshl_add_u64 v[14:15], v[22:23], 1, v[10:11]
	v_pk_mul_f32 v[10:11], v[112:113], v[8:9]
	v_pk_mul_f32 v[12:13], v[110:111], v[6:7]
	v_pk_fma_f32 v[10:11], v[108:109], v[4:5], v[10:11] neg_lo:[0,0,1] neg_hi:[0,0,1]
	v_pk_fma_f32 v[12:13], v[106:107], v[2:3], v[12:13] neg_lo:[0,0,1] neg_hi:[0,0,1]
	v_mov_b32_e32 v24, v16
	v_mov_b32_e32 v25, v16
	v_pk_mul_f32 v[26:27], v[24:25], v[10:11]
	v_pk_mul_f32 v[10:11], v[16:17], v[12:13]
	v_pk_mul_f32 v[12:13], v[112:113], v[4:5]
	v_pk_mul_f32 v[28:29], v[110:111], v[2:3]
	v_pk_fma_f32 v[12:13], v[108:109], v[8:9], v[12:13]
	v_pk_fma_f32 v[28:29], v[106:107], v[6:7], v[28:29]
	v_pk_mul_f32 v[30:31], v[24:25], v[12:13]
	v_pk_mul_f32 v[12:13], v[16:17], v[28:29]
	v_cvt_pk_bf16_f32 v10, v10, v11
	v_cvt_pk_bf16_f32 v11, v26, v27
	s_nop 0
	v_cvt_pk_bf16_f32 v12, v12, v13
	v_cvt_pk_bf16_f32 v13, v30, v31
	global_store_dwordx4 v[14:15], v[10:13], off sc1
	s_nop 1
	v_pk_mul_f32 v[10:11], v[104:105], v[8:9]
	v_pk_mul_f32 v[12:13], v[102:103], v[6:7]
	v_pk_fma_f32 v[10:11], v[100:101], v[4:5], v[10:11] neg_lo:[0,0,1] neg_hi:[0,0,1]
	v_pk_fma_f32 v[12:13], v[98:99], v[2:3], v[12:13] neg_lo:[0,0,1] neg_hi:[0,0,1]
	v_pk_mul_f32 v[4:5], v[104:105], v[4:5]
	v_pk_mul_f32 v[2:3], v[102:103], v[2:3]
	v_pk_fma_f32 v[4:5], v[100:101], v[8:9], v[4:5]
	v_pk_fma_f32 v[2:3], v[98:99], v[6:7], v[2:3]
	v_pk_mul_f32 v[6:7], v[24:25], v[4:5]
	v_pk_mul_f32 v[4:5], v[16:17], v[2:3]
	v_pk_mul_f32 v[10:11], v[24:25], v[10:11]
	v_pk_mul_f32 v[12:13], v[16:17], v[12:13]
	v_mov_b32_e32 v8, 0
	v_cvt_pk_bf16_f32 v2, v12, v13
	v_cvt_pk_bf16_f32 v3, v10, v11
	v_cvt_pk_bf16_f32 v4, v4, v5
	v_cvt_pk_bf16_f32 v5, v6, v7
	global_store_dwordx4 v[14:15], v[2:5], off offset:256 sc1
	v_mov_b32_e32 v6, 0
	v_mov_b32_e32 v9, 0
	v_add_u32_e32 v4, 0x80, v20
	v_ashrrev_i32_e32 v5, 31, v4
	v_mov_b32_e32 v2, 1.0
	v_mov_b32_e32 v10, 0
	v_mov_b32_e32 v11, 0
	v_mov_b32_e32 v12, 1.0
	v_mov_b32_e32 v13, 1.0
	v_mov_b32_e32 v14, 1.0
	v_mov_b32_e32 v15, 1.0
	s_and_saveexec_b64 s[6:7], s[4:5]
	s_cbranch_execz .LBB0_361
	v_lshlrev_b64 v[8:9], 6, v[4:5]
	v_lshl_add_u64 v[8:9], s[50:51], 0, v[8:9]
	v_lshl_add_u64 v[8:9], v[18:19], 2, v[8:9]
	global_load_dwordx4 v[12:15], v[8:9], off
	s_nop 0
	global_load_dwordx4 v[8:11], v[8:9], off offset:32
	s_waitcnt vmcnt(0)
.LBB0_361:
	s_or_b64 exec, exec, s[6:7]
	v_mov_b64_e32 v[26:27], s[48:49]
	v_mad_i64_i32 v[4:5], s[6:7], v4, s83, v[26:27]
	v_pk_mul_f32 v[26:27], v[96:97], v[10:11]
	v_pk_mul_f32 v[28:29], v[94:95], v[8:9]
	v_pk_fma_f32 v[26:27], v[92:93], v[14:15], v[26:27] neg_lo:[0,0,1] neg_hi:[0,0,1]
	v_pk_fma_f32 v[28:29], v[90:91], v[12:13], v[28:29] neg_lo:[0,0,1] neg_hi:[0,0,1]
	v_pk_mul_f32 v[30:31], v[24:25], v[26:27]
	v_pk_mul_f32 v[26:27], v[16:17], v[28:29]
	v_pk_mul_f32 v[28:29], v[96:97], v[14:15]
	v_pk_mul_f32 v[32:33], v[94:95], v[12:13]
	v_pk_fma_f32 v[28:29], v[92:93], v[10:11], v[28:29]
	v_pk_fma_f32 v[32:33], v[90:91], v[8:9], v[32:33]
	v_pk_mul_f32 v[90:91], v[24:25], v[28:29]
	v_pk_mul_f32 v[28:29], v[16:17], v[32:33]
	v_lshl_add_u64 v[4:5], v[22:23], 1, v[4:5]
	v_cvt_pk_bf16_f32 v26, v26, v27
	v_cvt_pk_bf16_f32 v27, v30, v31
	v_cvt_pk_bf16_f32 v28, v28, v29
	v_cvt_pk_bf16_f32 v29, v90, v91
	global_store_dwordx4 v[4:5], v[26:29], off sc1
	v_mov_b32_e32 v7, 0
	v_mov_b32_e32 v3, 1.0
	v_pk_mul_f32 v[26:27], v[88:89], v[10:11]
	v_pk_mul_f32 v[28:29], v[86:87], v[8:9]
	v_pk_fma_f32 v[26:27], v[84:85], v[14:15], v[26:27] neg_lo:[0,0,1] neg_hi:[0,0,1]
	v_pk_fma_f32 v[28:29], v[82:83], v[12:13], v[28:29] neg_lo:[0,0,1] neg_hi:[0,0,1]
	v_pk_mul_f32 v[14:15], v[88:89], v[14:15]
	v_pk_mul_f32 v[12:13], v[86:87], v[12:13]
	v_pk_fma_f32 v[10:11], v[84:85], v[10:11], v[14:15]
	v_pk_fma_f32 v[8:9], v[82:83], v[8:9], v[12:13]
	v_pk_mul_f32 v[12:13], v[24:25], v[10:11]
	v_pk_mul_f32 v[10:11], v[16:17], v[8:9]
	v_pk_mul_f32 v[26:27], v[24:25], v[26:27]
	v_pk_mul_f32 v[28:29], v[16:17], v[28:29]
	s_nop 0
	v_cvt_pk_bf16_f32 v8, v28, v29
	v_cvt_pk_bf16_f32 v9, v26, v27
	v_cvt_pk_bf16_f32 v10, v10, v11
	v_cvt_pk_bf16_f32 v11, v12, v13
	global_store_dwordx4 v[4:5], v[8:11], off offset:256 sc1
	v_mov_b32_e32 v4, 1.0
	v_mov_b32_e32 v5, 1.0
	v_add_u32_e32 v10, 0x90, v20
	v_ashrrev_i32_e32 v11, 31, v10
	v_mov_b32_e32 v8, 0
	v_mov_b32_e32 v9, 0
	s_and_saveexec_b64 s[6:7], s[4:5]
	s_cbranch_execz .LBB0_363
	v_lshlrev_b64 v[2:3], 6, v[10:11]
	v_lshl_add_u64 v[2:3], s[50:51], 0, v[2:3]
	v_lshl_add_u64 v[6:7], v[18:19], 2, v[2:3]
	global_load_dwordx4 v[2:5], v[6:7], off
	s_nop 0
	global_load_dwordx4 v[6:9], v[6:7], off offset:32
	s_waitcnt vmcnt(0)
.LBB0_363:
	s_or_b64 exec, exec, s[6:7]
	v_mov_b64_e32 v[12:13], s[48:49]
	v_mad_i64_i32 v[10:11], s[6:7], v10, s83, v[12:13]
	v_lshl_add_u64 v[14:15], v[22:23], 1, v[10:11]
	v_pk_mul_f32 v[10:11], v[80:81], v[8:9]
	v_pk_mul_f32 v[12:13], v[78:79], v[6:7]
	v_pk_fma_f32 v[10:11], v[76:77], v[4:5], v[10:11] neg_lo:[0,0,1] neg_hi:[0,0,1]
	v_pk_fma_f32 v[12:13], v[74:75], v[2:3], v[12:13] neg_lo:[0,0,1] neg_hi:[0,0,1]
	v_mov_b32_e32 v24, v16
	v_mov_b32_e32 v25, v16
	v_pk_mul_f32 v[26:27], v[24:25], v[10:11]
	v_pk_mul_f32 v[10:11], v[16:17], v[12:13]
	v_pk_mul_f32 v[12:13], v[80:81], v[4:5]
	v_pk_mul_f32 v[28:29], v[78:79], v[2:3]
	v_pk_fma_f32 v[12:13], v[76:77], v[8:9], v[12:13]
	v_pk_fma_f32 v[28:29], v[74:75], v[6:7], v[28:29]
	v_pk_mul_f32 v[30:31], v[24:25], v[12:13]
	v_pk_mul_f32 v[12:13], v[16:17], v[28:29]
	v_cvt_pk_bf16_f32 v10, v10, v11
	v_cvt_pk_bf16_f32 v11, v26, v27
	s_nop 0
	v_cvt_pk_bf16_f32 v12, v12, v13
	v_cvt_pk_bf16_f32 v13, v30, v31
	global_store_dwordx4 v[14:15], v[10:13], off sc1
	s_nop 1
	v_pk_mul_f32 v[10:11], v[72:73], v[8:9]
	v_pk_mul_f32 v[12:13], v[70:71], v[6:7]
	v_pk_fma_f32 v[10:11], v[68:69], v[4:5], v[10:11] neg_lo:[0,0,1] neg_hi:[0,0,1]
	v_pk_fma_f32 v[12:13], v[66:67], v[2:3], v[12:13] neg_lo:[0,0,1] neg_hi:[0,0,1]
	v_pk_mul_f32 v[4:5], v[72:73], v[4:5]
	v_pk_mul_f32 v[2:3], v[70:71], v[2:3]
	v_pk_fma_f32 v[4:5], v[68:69], v[8:9], v[4:5]
	v_pk_fma_f32 v[2:3], v[66:67], v[6:7], v[2:3]
	v_pk_mul_f32 v[6:7], v[24:25], v[4:5]
	v_pk_mul_f32 v[4:5], v[16:17], v[2:3]
	v_pk_mul_f32 v[10:11], v[24:25], v[10:11]
	v_pk_mul_f32 v[12:13], v[16:17], v[12:13]
	v_mov_b32_e32 v8, 0
	v_cvt_pk_bf16_f32 v2, v12, v13
	v_cvt_pk_bf16_f32 v3, v10, v11
	v_cvt_pk_bf16_f32 v4, v4, v5
	v_cvt_pk_bf16_f32 v5, v6, v7
	global_store_dwordx4 v[14:15], v[2:5], off offset:256 sc1
	v_mov_b32_e32 v6, 0
	v_mov_b32_e32 v9, 0
	v_add_u32_e32 v4, 0xa0, v20
	v_ashrrev_i32_e32 v5, 31, v4
	v_mov_b32_e32 v2, 1.0
	v_mov_b32_e32 v10, 0
	v_mov_b32_e32 v11, 0
	v_mov_b32_e32 v12, 1.0
	v_mov_b32_e32 v13, 1.0
	v_mov_b32_e32 v14, 1.0
	v_mov_b32_e32 v15, 1.0
	s_and_saveexec_b64 s[6:7], s[4:5]
	s_cbranch_execz .LBB0_365
	v_lshlrev_b64 v[8:9], 6, v[4:5]
	v_lshl_add_u64 v[8:9], s[50:51], 0, v[8:9]
	v_lshl_add_u64 v[8:9], v[18:19], 2, v[8:9]
	global_load_dwordx4 v[12:15], v[8:9], off
	s_nop 0
	global_load_dwordx4 v[8:11], v[8:9], off offset:32
	s_waitcnt vmcnt(0)
.LBB0_365:
	s_or_b64 exec, exec, s[6:7]
	v_mov_b64_e32 v[26:27], s[48:49]
	v_mad_i64_i32 v[4:5], s[6:7], v4, s83, v[26:27]
	v_pk_mul_f32 v[26:27], v[64:65], v[10:11]
	v_pk_mul_f32 v[28:29], v[62:63], v[8:9]
	v_pk_fma_f32 v[26:27], v[60:61], v[14:15], v[26:27] neg_lo:[0,0,1] neg_hi:[0,0,1]
	v_pk_fma_f32 v[28:29], v[58:59], v[12:13], v[28:29] neg_lo:[0,0,1] neg_hi:[0,0,1]
	v_pk_mul_f32 v[30:31], v[24:25], v[26:27]
	v_pk_mul_f32 v[26:27], v[16:17], v[28:29]
	v_pk_mul_f32 v[28:29], v[64:65], v[14:15]
	v_pk_mul_f32 v[32:33], v[62:63], v[12:13]
	v_pk_fma_f32 v[28:29], v[60:61], v[10:11], v[28:29]
	v_pk_fma_f32 v[32:33], v[58:59], v[8:9], v[32:33]
	v_pk_mul_f32 v[58:59], v[24:25], v[28:29]
	v_pk_mul_f32 v[28:29], v[16:17], v[32:33]
	v_lshl_add_u64 v[4:5], v[22:23], 1, v[4:5]
	v_cvt_pk_bf16_f32 v26, v26, v27
	v_cvt_pk_bf16_f32 v27, v30, v31
	v_cvt_pk_bf16_f32 v28, v28, v29
	v_cvt_pk_bf16_f32 v29, v58, v59
	global_store_dwordx4 v[4:5], v[26:29], off sc1
	v_mov_b32_e32 v7, 0
	v_mov_b32_e32 v3, 1.0
	v_pk_mul_f32 v[26:27], v[56:57], v[10:11]
	v_pk_mul_f32 v[28:29], v[54:55], v[8:9]
	v_pk_fma_f32 v[26:27], v[52:53], v[14:15], v[26:27] neg_lo:[0,0,1] neg_hi:[0,0,1]
	v_pk_fma_f32 v[28:29], v[50:51], v[12:13], v[28:29] neg_lo:[0,0,1] neg_hi:[0,0,1]
	v_pk_mul_f32 v[14:15], v[56:57], v[14:15]
	v_pk_mul_f32 v[12:13], v[54:55], v[12:13]
	v_pk_fma_f32 v[10:11], v[52:53], v[10:11], v[14:15]
	v_pk_fma_f32 v[8:9], v[50:51], v[8:9], v[12:13]
	v_pk_mul_f32 v[12:13], v[24:25], v[10:11]
	v_pk_mul_f32 v[10:11], v[16:17], v[8:9]
	v_pk_mul_f32 v[26:27], v[24:25], v[26:27]
	v_pk_mul_f32 v[28:29], v[16:17], v[28:29]
	s_nop 0
	v_cvt_pk_bf16_f32 v8, v28, v29
	v_cvt_pk_bf16_f32 v9, v26, v27
	v_cvt_pk_bf16_f32 v10, v10, v11
	v_cvt_pk_bf16_f32 v11, v12, v13
	global_store_dwordx4 v[4:5], v[8:11], off offset:256 sc1
	v_mov_b32_e32 v4, 1.0
	v_mov_b32_e32 v5, 1.0
	v_add_u32_e32 v10, 0xb0, v20
	v_ashrrev_i32_e32 v11, 31, v10
	v_mov_b32_e32 v8, 0
	v_mov_b32_e32 v9, 0
	s_and_saveexec_b64 s[6:7], s[4:5]
	s_cbranch_execz .LBB0_367
	v_lshlrev_b64 v[2:3], 6, v[10:11]
	v_lshl_add_u64 v[2:3], s[50:51], 0, v[2:3]
	v_lshl_add_u64 v[6:7], v[18:19], 2, v[2:3]
	global_load_dwordx4 v[2:5], v[6:7], off
	s_nop 0
	global_load_dwordx4 v[6:9], v[6:7], off offset:32
	s_waitcnt vmcnt(0)
.LBB0_367:
	s_or_b64 exec, exec, s[6:7]
	v_mov_b64_e32 v[12:13], s[48:49]
	v_mad_i64_i32 v[10:11], s[4:5], v10, s83, v[12:13]
	v_lshl_add_u64 v[14:15], v[22:23], 1, v[10:11]
	v_pk_mul_f32 v[10:11], v[48:49], v[8:9]
	v_pk_mul_f32 v[12:13], v[46:47], v[6:7]
	v_pk_fma_f32 v[10:11], v[44:45], v[4:5], v[10:11] neg_lo:[0,0,1] neg_hi:[0,0,1]
	v_pk_fma_f32 v[12:13], v[42:43], v[2:3], v[12:13] neg_lo:[0,0,1] neg_hi:[0,0,1]
	v_mov_b32_e32 v18, v16
	v_mov_b32_e32 v19, v16
	v_pk_mul_f32 v[20:21], v[18:19], v[10:11]
	v_pk_mul_f32 v[10:11], v[16:17], v[12:13]
	v_pk_mul_f32 v[12:13], v[48:49], v[4:5]
	v_pk_mul_f32 v[22:23], v[46:47], v[2:3]
	v_pk_fma_f32 v[12:13], v[44:45], v[8:9], v[12:13]
	v_pk_fma_f32 v[22:23], v[42:43], v[6:7], v[22:23]
	v_pk_mul_f32 v[24:25], v[18:19], v[12:13]
	v_pk_mul_f32 v[12:13], v[16:17], v[22:23]
	v_cvt_pk_bf16_f32 v10, v10, v11
	v_cvt_pk_bf16_f32 v11, v20, v21
	s_and_b64 vcc, exec, s[38:39]
	v_cvt_pk_bf16_f32 v12, v12, v13
	v_cvt_pk_bf16_f32 v13, v24, v25
	global_store_dwordx4 v[14:15], v[10:13], off sc1
	s_mov_b64 s[4:5], -1
	s_nop 0
	v_pk_mul_f32 v[10:11], v[36:37], v[8:9]
	v_pk_mul_f32 v[12:13], v[34:35], v[6:7]
	v_pk_fma_f32 v[10:11], v[40:41], v[4:5], v[10:11] neg_lo:[0,0,1] neg_hi:[0,0,1]
	v_pk_fma_f32 v[12:13], v[38:39], v[2:3], v[12:13] neg_lo:[0,0,1] neg_hi:[0,0,1]
	v_pk_mul_f32 v[4:5], v[36:37], v[4:5]
	v_pk_mul_f32 v[2:3], v[34:35], v[2:3]
	v_pk_fma_f32 v[4:5], v[40:41], v[8:9], v[4:5]
	v_pk_fma_f32 v[2:3], v[38:39], v[6:7], v[2:3]
	v_pk_mul_f32 v[6:7], v[18:19], v[4:5]
	v_pk_mul_f32 v[4:5], v[16:17], v[2:3]
	v_pk_mul_f32 v[10:11], v[18:19], v[10:11]
	v_pk_mul_f32 v[12:13], v[16:17], v[12:13]
	s_nop 0
	v_cvt_pk_bf16_f32 v2, v12, v13
	v_cvt_pk_bf16_f32 v3, v10, v11
	v_cvt_pk_bf16_f32 v4, v4, v5
	v_cvt_pk_bf16_f32 v5, v6, v7
	global_store_dwordx4 v[14:15], v[2:5], off offset:256 sc1
	s_cbranch_vccnz .LBB0_338
	s_andn2_b64 vcc, exec, s[46:47]
	s_cbranch_vccnz .LBB0_337
	s_barrier
	s_branch .LBB0_337

.LBB0_457:
	v_lshlrev_b32_e32 v119, 16, v62
	v_and_b32_e32 v118, 0xffff0000, v62
	v_sub_f32_e32 v62, v99, v115
	v_fma_f32 v120, v101, v62, v115
	v_sub_f32_e32 v62, v119, v115
	v_fmac_f32_e32 v120, v102, v62
	v_sub_f32_e32 v62, v98, v114
	v_fma_f32 v121, v105, v62, v114
	v_sub_f32_e32 v62, v118, v114
	v_lshlrev_b32_e32 v117, 16, v63
	v_fmac_f32_e32 v121, v106, v62
	v_sub_f32_e32 v62, v97, v113
	v_fma_f32 v122, v107, v62, v113
	v_sub_f32_e32 v62, v117, v113
	v_and_b32_e32 v116, 0xffff0000, v63
	v_fmac_f32_e32 v122, v108, v62
	v_sub_f32_e32 v62, v96, v0
	v_fma_f32 v123, v111, v62, v0
	v_sub_f32_e32 v62, v116, v0
	v_fmac_f32_e32 v123, v112, v62
	v_and_b32_e32 v97, 0xffff0000, v64
	v_lshlrev_b32_e32 v96, 16, v64
	v_pk_add_f32 v[62:63], v[88:89], v[94:95] neg_lo:[0,1] neg_hi:[0,1]
	v_pk_add_f32 v[88:89], v[96:97], v[94:95] neg_lo:[0,1] neg_hi:[0,1]
	v_pk_fma_f32 v[62:63], v[68:69], v[62:63], v[94:95]
	s_andn2_b64 vcc, exec, s[56:57]
	v_pk_fma_f32 v[98:99], v[70:71], v[88:89], v[62:63]
	v_and_b32_e32 v89, 0xffff0000, v65
	v_lshlrev_b32_e32 v88, 16, v65
	v_pk_add_f32 v[62:63], v[90:91], v[92:93] neg_lo:[0,1] neg_hi:[0,1]
	v_pk_add_f32 v[64:65], v[88:89], v[92:93] neg_lo:[0,1] neg_hi:[0,1]
	v_pk_fma_f32 v[62:63], v[74:75], v[62:63], v[92:93]
	s_mov_b64 s[4:5], -1
	v_pk_fma_f32 v[64:65], v[76:77], v[64:65], v[62:63]
	v_cndmask_b32_e64 v62, 0, 1, s[56:57]
	v_cmp_ne_u32_e64 s[44:45], 1, v62
	s_cbranch_vccnz .LBB0_491
	v_mov_b32_e32 v128, 0xbfb8aa3b
	v_mov_b32_e32 v131, 0xc038aa3b
	v_cndmask_b32_e64 v128, v131, v128, s[38:39]
	v_cndmask_b32_e64 v129, 2.0, 1.0, s[38:39]
	v_cndmask_b32_e64 v130, -1.0, 0, s[38:39]
	v_mul_f32_e32 v62, v128, v120
	v_mul_f32_e32 v63, v128, v121
	v_mul_f32_e32 v90, v128, v122
	v_mul_f32_e32 v91, v128, v123
	v_mul_f32_e32 v124, v128, v98
	v_mul_f32_e32 v125, v128, v99
	v_mul_f32_e32 v126, v128, v64
	v_mul_f32_e32 v127, v128, v65
	v_exp_f32_e32 v62, v62
	v_exp_f32_e32 v63, v63
	v_exp_f32_e32 v90, v90
	v_exp_f32_e32 v91, v91
	v_exp_f32_e32 v124, v124
	v_exp_f32_e32 v125, v125
	v_exp_f32_e32 v126, v126
	v_exp_f32_e32 v127, v127
	v_add_f32_e32 v62, 1.0, v62
	v_add_f32_e32 v63, 1.0, v63
	v_add_f32_e32 v90, 1.0, v90
	v_add_f32_e32 v91, 1.0, v91
	v_add_f32_e32 v124, 1.0, v124
	v_add_f32_e32 v125, 1.0, v125
	v_add_f32_e32 v126, 1.0, v126
	v_add_f32_e32 v127, 1.0, v127
	v_rcp_f32_e32 v62, v62
	v_rcp_f32_e32 v63, v63
	v_rcp_f32_e32 v90, v90
	v_rcp_f32_e32 v91, v91
	v_rcp_f32_e32 v124, v124
	v_rcp_f32_e32 v125, v125
	v_rcp_f32_e32 v126, v126
	v_rcp_f32_e32 v127, v127
	v_fma_f32 v62, v62, v129, v130
	v_fma_f32 v63, v63, v129, v130
	v_fma_f32 v90, v90, v129, v130
	v_fma_f32 v91, v91, v129, v130
	v_fma_f32 v124, v124, v129, v130
	v_fma_f32 v125, v125, v129, v130
	v_fma_f32 v126, v126, v129, v130
	v_fma_f32 v127, v127, v129, v130
	v_cndmask_b32_e64 v62, v62, v120, s[40:41]
	v_cndmask_b32_e64 v63, v63, v121, s[40:41]
	v_cndmask_b32_e64 v90, v90, v122, s[40:41]
	v_cndmask_b32_e64 v91, v91, v123, s[40:41]
	v_cndmask_b32_e64 v124, v124, v98, s[40:41]
	v_cndmask_b32_e64 v125, v125, v99, s[40:41]
	v_cndmask_b32_e64 v126, v126, v64, s[40:41]
	v_cndmask_b32_e64 v127, v127, v65, s[40:41]
	v_cvt_pk_bf16_f32 v128, v62, v63
	v_lshl_add_u64 v[62:63], s[50:51], 0, v[82:83]
	v_add_co_u32_e32 v62, vcc, 0x36200000, v62
	s_mov_b64 s[4:5], 0
	s_nop 0
	v_addc_co_u32_e32 v63, vcc, 0, v63, vcc
	v_cvt_pk_bf16_f32 v129, v90, v91
	v_cvt_pk_bf16_f32 v130, v124, v125
	v_cvt_pk_bf16_f32 v131, v126, v127
	global_store_dwordx4 v[62:63], v[128:131], off sc1
.LBB0_491:
	v_cndmask_b32_e64 v90, 0, 1, s[58:59]
	s_and_b64 vcc, exec, s[4:5]
	v_lshl_add_u64 v[62:63], s[50:51], 0, v[86:87]
	v_cmp_ne_u32_e64 s[42:43], 1, v90
	s_cbranch_vccz .LBB0_494
	v_add_co_u32_e32 v90, vcc, 0x2e200000, v62
	v_cvt_pk_bf16_f32 v124, v120, v121
	v_cvt_pk_bf16_f32 v125, v122, v123
	v_cvt_pk_bf16_f32 v126, v98, v99
	v_cvt_pk_bf16_f32 v127, v64, v65
	s_nop 1
	v_addc_co_u32_e32 v91, vcc, 0, v63, vcc
	s_and_b64 vcc, exec, s[42:43]
	global_store_dwordx4 v[90:91], v[124:127], off sc1
	s_cbranch_vccnz .LBB0_494
	v_mul_f32_e32 v121, v103, v121
	v_mul_f32_e32 v120, v104, v120
	v_mul_f32_e32 v124, v121, v121
	v_fmac_f32_e32 v124, v120, v120
	v_mul_f32_e32 v122, v110, v122
	v_fmac_f32_e32 v124, v122, v122
	v_mul_f32_e32 v123, v109, v123
	v_pk_mul_f32 v[90:91], v[72:73], v[98:99]
	v_fmac_f32_e32 v124, v123, v123
	v_pk_mul_f32 v[98:99], v[90:91], v[90:91]
	v_pk_mul_f32 v[64:65], v[78:79], v[64:65]
	v_add_f32_e32 v98, v98, v124
	v_add_f32_e32 v124, v99, v98
	v_pk_mul_f32 v[98:99], v[64:65], v[64:65]
	s_nop 0
	v_add_f32_e32 v98, v98, v124
	v_and_b32_e32 v124, 64, v226
	v_add_f32_e32 v98, v99, v98
	v_xor_b32_e32 v99, 1, v226
	v_add_u32_e32 v124, 64, v124
	v_cmp_lt_i32_e32 vcc, v99, v124
	s_nop 1
	v_cndmask_b32_e32 v99, v226, v99, vcc
	v_lshlrev_b32_e32 v99, 2, v99
	ds_bpermute_b32 v99, v99, v98
	s_waitcnt lgkmcnt(0)
	v_add_f32_e32 v98, v98, v99
	v_xor_b32_e32 v99, 2, v226
	v_cmp_lt_i32_e32 vcc, v99, v124
	s_nop 1
	v_cndmask_b32_e32 v99, v226, v99, vcc
	v_lshlrev_b32_e32 v99, 2, v99
	ds_bpermute_b32 v99, v99, v98
	s_waitcnt lgkmcnt(0)
	v_add_f32_e32 v98, v98, v99
	v_xor_b32_e32 v99, 4, v226
	v_cmp_lt_i32_e32 vcc, v99, v124
	s_nop 1
	v_cndmask_b32_e32 v99, v226, v99, vcc
	v_lshlrev_b32_e32 v99, 2, v99
	ds_bpermute_b32 v99, v99, v98
	s_waitcnt lgkmcnt(0)
	v_add_f32_e32 v98, v98, v99
	v_mul_f32_e32 v99, 0x4f800000, v98
	v_cmp_gt_f32_e32 vcc, s82, v98
	s_nop 1
	v_cndmask_b32_e32 v98, v98, v99, vcc
	v_sqrt_f32_e32 v99, v98
	s_nop 0
	v_add_u32_e32 v124, -1, v99
	v_fma_f32 v125, -v124, v99, v98
	v_cmp_ge_f32_e64 s[46:47], 0, v125
	v_add_u32_e32 v125, 1, v99
	s_nop 0
	v_cndmask_b32_e64 v124, v99, v124, s[46:47]
	v_fma_f32 v99, -v125, v99, v98
	v_cmp_lt_f32_e64 s[46:47], 0, v99
	s_nop 1
	v_cndmask_b32_e64 v99, v124, v125, s[46:47]
	v_mul_f32_e32 v124, 0x37800000, v99
	v_cndmask_b32_e32 v99, v99, v124, vcc
	v_cmp_class_f32_e32 vcc, v98, v229
	s_nop 1
	v_cndmask_b32_e32 v98, v99, v98, vcc
	v_max_f32_e32 v98, 0x2b8cbccc, v98
	v_div_scale_f32 v99, s[4:5], v98, v98, 1.0
	v_rcp_f32_e32 v124, v99
	s_nop 0
	v_fma_f32 v125, -v99, v124, 1.0
	v_fmac_f32_e32 v124, v125, v124
	v_div_scale_f32 v125, vcc, 1.0, v98, 1.0
	v_mul_f32_e32 v126, v125, v124
	v_fma_f32 v127, -v99, v126, v125
	v_fmac_f32_e32 v126, v127, v124
	v_fma_f32 v99, -v99, v126, v125
	v_div_fmas_f32 v99, v99, v124, v126
	v_div_fixup_f32 v98, v99, v98, 1.0
	v_mul_f32_e32 v99, v120, v98
	v_mul_f32_e32 v120, v121, v98
	v_mul_f32_e32 v121, v122, v98
	v_mul_f32_e32 v122, v123, v98
	v_mul_f32_e32 v64, v64, v98
	v_mul_f32_e32 v65, v65, v98
	v_mul_f32_e32 v90, v90, v98
	v_mul_f32_e32 v91, v91, v98
	v_cvt_pk_bf16_f32 v120, v99, v120
	v_cvt_pk_bf16_f32 v121, v121, v122
	v_cvt_pk_bf16_f32 v122, v90, v91
	v_cvt_pk_bf16_f32 v123, v64, v65
	v_lshl_add_u64 v[64:65], s[50:51], 0, v[84:85]
	v_add_co_u32_e32 v64, vcc, 0x2e201000, v64
	s_nop 1
	v_addc_co_u32_e32 v65, vcc, 0, v65, vcc
	global_store_dwordx4 v[64:65], v[120:123], off offset:2048 sc1
.LBB0_494:
	s_nop 1
	v_lshlrev_b32_e32 v121, 16, v58
	v_and_b32_e32 v120, 0xffff0000, v58
	v_sub_f32_e32 v58, v115, v119
	v_fma_f32 v115, v101, v58, v119
	v_sub_f32_e32 v58, v121, v119
	v_fmac_f32_e32 v115, v102, v58
	v_sub_f32_e32 v58, v114, v118
	v_fma_f32 v114, v105, v58, v118
	v_sub_f32_e32 v58, v120, v118
	v_lshlrev_b32_e32 v99, 16, v59
	v_fmac_f32_e32 v114, v106, v58
	v_sub_f32_e32 v58, v113, v117
	v_and_b32_e32 v98, 0xffff0000, v59
	v_fma_f32 v113, v107, v58, v117
	v_sub_f32_e32 v58, v99, v117
	v_sub_f32_e32 v0, v0, v116
	v_fmac_f32_e32 v113, v108, v58
	v_fma_f32 v0, v111, v0, v116
	v_sub_f32_e32 v58, v98, v116
	v_fmac_f32_e32 v0, v112, v58
	v_and_b32_e32 v91, 0xffff0000, v60
	v_lshlrev_b32_e32 v90, 16, v60
	v_pk_add_f32 v[58:59], v[94:95], v[96:97] neg_lo:[0,1] neg_hi:[0,1]
	v_pk_add_f32 v[64:65], v[90:91], v[96:97] neg_lo:[0,1] neg_hi:[0,1]
	v_pk_fma_f32 v[58:59], v[68:69], v[58:59], v[96:97]
	s_and_b64 vcc, exec, s[44:45]
	v_pk_fma_f32 v[58:59], v[70:71], v[64:65], v[58:59]
	v_and_b32_e32 v65, 0xffff0000, v61
	v_lshlrev_b32_e32 v64, 16, v61
	v_pk_add_f32 v[60:61], v[92:93], v[88:89] neg_lo:[0,1] neg_hi:[0,1]
	v_pk_add_f32 v[92:93], v[64:65], v[88:89] neg_lo:[0,1] neg_hi:[0,1]
	v_pk_fma_f32 v[60:61], v[74:75], v[60:61], v[88:89]
	s_mov_b64 s[4:5], -1
	v_pk_fma_f32 v[60:61], v[76:77], v[92:93], v[60:61]
	s_cbranch_vccnz .LBB0_528
	v_mov_b32_e32 v126, 0xbfb8aa3b
	v_mov_b32_e32 v129, 0xc038aa3b
	v_cndmask_b32_e64 v126, v129, v126, s[38:39]
	v_cndmask_b32_e64 v127, 2.0, 1.0, s[38:39]
	v_cndmask_b32_e64 v128, -1.0, 0, s[38:39]
	v_mul_f32_e32 v92, v126, v115
	v_mul_f32_e32 v93, v126, v114
	v_mul_f32_e32 v94, v126, v113
	v_mul_f32_e32 v95, v126, v0
	v_mul_f32_e32 v122, v126, v58
	v_mul_f32_e32 v123, v126, v59
	v_mul_f32_e32 v124, v126, v60
	v_mul_f32_e32 v125, v126, v61
	v_exp_f32_e32 v92, v92
	v_exp_f32_e32 v93, v93
	v_exp_f32_e32 v94, v94
	v_exp_f32_e32 v95, v95
	v_exp_f32_e32 v122, v122
	v_exp_f32_e32 v123, v123
	v_exp_f32_e32 v124, v124
	v_exp_f32_e32 v125, v125
	v_add_f32_e32 v92, 1.0, v92
	v_add_f32_e32 v93, 1.0, v93
	v_add_f32_e32 v94, 1.0, v94
	v_add_f32_e32 v95, 1.0, v95
	v_add_f32_e32 v122, 1.0, v122
	v_add_f32_e32 v123, 1.0, v123
	v_add_f32_e32 v124, 1.0, v124
	v_add_f32_e32 v125, 1.0, v125
	v_rcp_f32_e32 v92, v92
	v_rcp_f32_e32 v93, v93
	v_rcp_f32_e32 v94, v94
	v_rcp_f32_e32 v95, v95
	v_rcp_f32_e32 v122, v122
	v_rcp_f32_e32 v123, v123
	v_rcp_f32_e32 v124, v124
	v_rcp_f32_e32 v125, v125
	v_fma_f32 v92, v92, v127, v128
	v_fma_f32 v93, v93, v127, v128
	v_fma_f32 v94, v94, v127, v128
	v_fma_f32 v95, v95, v127, v128
	v_fma_f32 v122, v122, v127, v128
	v_fma_f32 v123, v123, v127, v128
	v_fma_f32 v124, v124, v127, v128
	v_fma_f32 v125, v125, v127, v128
	v_cndmask_b32_e64 v92, v92, v115, s[40:41]
	v_cndmask_b32_e64 v93, v93, v114, s[40:41]
	v_cndmask_b32_e64 v94, v94, v113, s[40:41]
	v_cndmask_b32_e64 v95, v95, v0, s[40:41]
	v_cndmask_b32_e64 v122, v122, v58, s[40:41]
	v_cndmask_b32_e64 v123, v123, v59, s[40:41]
	v_cndmask_b32_e64 v124, v124, v60, s[40:41]
	v_cndmask_b32_e64 v125, v125, v61, s[40:41]
	v_cvt_pk_bf16_f32 v92, v92, v93
	v_cvt_pk_bf16_f32 v93, v94, v95
	v_cvt_pk_bf16_f32 v94, v122, v123
	v_lshl_add_u64 v[122:123], s[50:51], 0, v[82:83]
	v_add_co_u32_e32 v122, vcc, 0x36200000, v122
	s_mov_b64 s[4:5], 0
	s_nop 0
	v_addc_co_u32_e32 v123, vcc, 0, v123, vcc
	v_cvt_pk_bf16_f32 v95, v124, v125
	global_store_dwordx4 v[122:123], v[92:95], off offset:768 sc1
.LBB0_528:
	s_and_b64 vcc, exec, s[4:5]
	s_cbranch_vccz .LBB0_531
	v_add_co_u32_e32 v122, vcc, 0x2e202000, v62
	v_cvt_pk_bf16_f32 v92, v115, v114
	v_cvt_pk_bf16_f32 v93, v113, v0
	v_cvt_pk_bf16_f32 v94, v58, v59
	v_cvt_pk_bf16_f32 v95, v60, v61
	s_nop 1
	v_addc_co_u32_e32 v123, vcc, 0, v63, vcc
	s_and_b64 vcc, exec, s[42:43]
	global_store_dwordx4 v[122:123], v[92:95], off sc1
	s_cbranch_vccnz .LBB0_531
	s_nop 0
	v_mul_f32_e32 v95, v103, v114
	v_mul_f32_e32 v94, v104, v115
	v_mul_f32_e32 v114, v95, v95
	v_fmac_f32_e32 v114, v94, v94
	v_mul_f32_e32 v113, v110, v113
	v_fmac_f32_e32 v114, v113, v113
	v_mul_f32_e32 v0, v109, v0
	v_pk_mul_f32 v[58:59], v[72:73], v[58:59]
	v_fmac_f32_e32 v114, v0, v0
	v_pk_mul_f32 v[92:93], v[58:59], v[58:59]
	v_pk_mul_f32 v[60:61], v[78:79], v[60:61]
	v_add_f32_e32 v92, v92, v114
	v_add_f32_e32 v114, v93, v92
	v_pk_mul_f32 v[92:93], v[60:61], v[60:61]
	s_nop 0
	v_add_f32_e32 v92, v92, v114
	v_and_b32_e32 v114, 64, v226
	v_add_f32_e32 v92, v93, v92
	v_xor_b32_e32 v93, 1, v226
	v_add_u32_e32 v114, 64, v114
	v_cmp_lt_i32_e32 vcc, v93, v114
	s_nop 1
	v_cndmask_b32_e32 v93, v226, v93, vcc
	v_lshlrev_b32_e32 v93, 2, v93
	ds_bpermute_b32 v93, v93, v92
	s_waitcnt lgkmcnt(0)
	v_add_f32_e32 v92, v92, v93
	v_xor_b32_e32 v93, 2, v226
	v_cmp_lt_i32_e32 vcc, v93, v114
	s_nop 1
	v_cndmask_b32_e32 v93, v226, v93, vcc
	v_lshlrev_b32_e32 v93, 2, v93
	ds_bpermute_b32 v93, v93, v92
	s_waitcnt lgkmcnt(0)
	v_add_f32_e32 v92, v92, v93
	v_xor_b32_e32 v93, 4, v226
	v_cmp_lt_i32_e32 vcc, v93, v114
	s_nop 1
	v_cndmask_b32_e32 v93, v226, v93, vcc
	v_lshlrev_b32_e32 v93, 2, v93
	ds_bpermute_b32 v93, v93, v92
	s_waitcnt lgkmcnt(0)
	v_add_f32_e32 v92, v92, v93
	v_mul_f32_e32 v93, 0x4f800000, v92
	v_cmp_gt_f32_e32 vcc, s82, v92
	s_nop 1
	v_cndmask_b32_e32 v92, v92, v93, vcc
	v_sqrt_f32_e32 v93, v92
	s_nop 0
	v_add_u32_e32 v114, -1, v93
	v_fma_f32 v115, -v114, v93, v92
	v_cmp_ge_f32_e64 s[46:47], 0, v115
	v_add_u32_e32 v115, 1, v93
	s_nop 0
	v_cndmask_b32_e64 v114, v93, v114, s[46:47]
	v_fma_f32 v93, -v115, v93, v92
	v_cmp_lt_f32_e64 s[46:47], 0, v93
	s_nop 1
	v_cndmask_b32_e64 v93, v114, v115, s[46:47]
	v_mul_f32_e32 v114, 0x37800000, v93
	v_cndmask_b32_e32 v93, v93, v114, vcc
	v_cmp_class_f32_e32 vcc, v92, v229
	s_nop 1
	v_cndmask_b32_e32 v92, v93, v92, vcc
	v_max_f32_e32 v92, 0x2b8cbccc, v92
	v_div_scale_f32 v93, s[4:5], v92, v92, 1.0
	v_rcp_f32_e32 v114, v93
	s_nop 0
	v_fma_f32 v115, -v93, v114, 1.0
	v_fmac_f32_e32 v114, v115, v114
	v_div_scale_f32 v115, vcc, 1.0, v92, 1.0
	v_mul_f32_e32 v122, v115, v114
	v_fma_f32 v123, -v93, v122, v115
	v_fmac_f32_e32 v122, v123, v114
	v_fma_f32 v93, -v93, v122, v115
	v_div_fmas_f32 v93, v93, v114, v122
	v_div_fixup_f32 v92, v93, v92, 1.0
	v_mul_f32_e32 v93, v94, v92
	v_mul_f32_e32 v94, v95, v92
	v_mul_f32_e32 v95, v113, v92
	v_mul_f32_e32 v0, v0, v92
	v_mul_f32_e32 v113, v58, v92
	v_mul_f32_e32 v114, v59, v92
	v_mul_f32_e32 v115, v60, v92
	v_mul_f32_e32 v61, v61, v92
	v_cvt_pk_bf16_f32 v58, v93, v94
	v_lshl_add_u64 v[92:93], s[50:51], 0, v[84:85]
	v_add_co_u32_e32 v92, vcc, 0x2e203000, v92
	v_cvt_pk_bf16_f32 v59, v95, v0
	v_cvt_pk_bf16_f32 v60, v113, v114
	v_cvt_pk_bf16_f32 v61, v115, v61
	s_nop 1
	v_addc_co_u32_e32 v93, vcc, 0, v93, vcc
	global_store_dwordx4 v[92:93], v[58:61], off offset:2048 sc1
.LBB0_531:
	s_nop 0
	v_lshlrev_b32_e32 v95, 16, v54
	v_and_b32_e32 v93, 0xffff0000, v54
	v_sub_f32_e32 v54, v119, v121
	v_fma_f32 v94, v101, v54, v121
	v_sub_f32_e32 v54, v95, v121
	v_fmac_f32_e32 v94, v102, v54
	v_sub_f32_e32 v54, v118, v120
	v_fma_f32 v113, v105, v54, v120
	v_sub_f32_e32 v54, v93, v120
	v_lshlrev_b32_e32 v92, 16, v55
	v_fmac_f32_e32 v113, v106, v54
	v_sub_f32_e32 v54, v117, v99
	v_fma_f32 v114, v107, v54, v99
	v_sub_f32_e32 v54, v92, v99
	v_and_b32_e32 v0, 0xffff0000, v55
	v_fmac_f32_e32 v114, v108, v54
	v_sub_f32_e32 v54, v116, v98
	v_fma_f32 v115, v111, v54, v98
	v_sub_f32_e32 v54, v0, v98
	v_fmac_f32_e32 v115, v112, v54
	v_and_b32_e32 v61, 0xffff0000, v56
	v_lshlrev_b32_e32 v60, 16, v56
	v_pk_add_f32 v[54:55], v[96:97], v[90:91] neg_lo:[0,1] neg_hi:[0,1]
	v_pk_add_f32 v[58:59], v[60:61], v[90:91] neg_lo:[0,1] neg_hi:[0,1]
	v_pk_fma_f32 v[54:55], v[68:69], v[54:55], v[90:91]
	s_and_b64 vcc, exec, s[44:45]
	v_pk_fma_f32 v[54:55], v[70:71], v[58:59], v[54:55]
	v_and_b32_e32 v59, 0xffff0000, v57
	v_lshlrev_b32_e32 v58, 16, v57
	v_pk_add_f32 v[56:57], v[88:89], v[64:65] neg_lo:[0,1] neg_hi:[0,1]
	v_pk_add_f32 v[88:89], v[58:59], v[64:65] neg_lo:[0,1] neg_hi:[0,1]
	v_pk_fma_f32 v[56:57], v[74:75], v[56:57], v[64:65]
	s_mov_b64 s[4:5], -1
	v_pk_fma_f32 v[56:57], v[76:77], v[88:89], v[56:57]
	s_cbranch_vccnz .LBB0_565
	v_mov_b32_e32 v122, 0xbfb8aa3b
	v_mov_b32_e32 v125, 0xc038aa3b
	v_cndmask_b32_e64 v122, v125, v122, s[38:39]
	v_cndmask_b32_e64 v123, 2.0, 1.0, s[38:39]
	v_cndmask_b32_e64 v124, -1.0, 0, s[38:39]
	v_mul_f32_e32 v88, v122, v94
	v_mul_f32_e32 v89, v122, v113
	v_mul_f32_e32 v96, v122, v114
	v_mul_f32_e32 v97, v122, v115
	v_mul_f32_e32 v116, v122, v54
	v_mul_f32_e32 v117, v122, v55
	v_mul_f32_e32 v118, v122, v56
	v_mul_f32_e32 v119, v122, v57
	v_exp_f32_e32 v88, v88
	v_exp_f32_e32 v89, v89
	v_exp_f32_e32 v96, v96
	v_exp_f32_e32 v97, v97
	v_exp_f32_e32 v116, v116
	v_exp_f32_e32 v117, v117
	v_exp_f32_e32 v118, v118
	v_exp_f32_e32 v119, v119
	v_add_f32_e32 v88, 1.0, v88
	v_add_f32_e32 v89, 1.0, v89
	v_add_f32_e32 v96, 1.0, v96
	v_add_f32_e32 v97, 1.0, v97
	v_add_f32_e32 v116, 1.0, v116
	v_add_f32_e32 v117, 1.0, v117
	v_add_f32_e32 v118, 1.0, v118
	v_add_f32_e32 v119, 1.0, v119
	v_rcp_f32_e32 v88, v88
	v_rcp_f32_e32 v89, v89
	v_rcp_f32_e32 v96, v96
	v_rcp_f32_e32 v97, v97
	v_rcp_f32_e32 v116, v116
	v_rcp_f32_e32 v117, v117
	v_rcp_f32_e32 v118, v118
	v_rcp_f32_e32 v119, v119
	v_fma_f32 v88, v88, v123, v124
	v_fma_f32 v89, v89, v123, v124
	v_fma_f32 v96, v96, v123, v124
	v_fma_f32 v97, v97, v123, v124
	v_fma_f32 v116, v116, v123, v124
	v_fma_f32 v117, v117, v123, v124
	v_fma_f32 v118, v118, v123, v124
	v_fma_f32 v119, v119, v123, v124
	v_cndmask_b32_e64 v88, v88, v94, s[40:41]
	v_cndmask_b32_e64 v89, v89, v113, s[40:41]
	v_cndmask_b32_e64 v96, v96, v114, s[40:41]
	v_cndmask_b32_e64 v97, v97, v115, s[40:41]
	v_cndmask_b32_e64 v116, v116, v54, s[40:41]
	v_cndmask_b32_e64 v117, v117, v55, s[40:41]
	v_cndmask_b32_e64 v118, v118, v56, s[40:41]
	v_cndmask_b32_e64 v119, v119, v57, s[40:41]
	v_cvt_pk_bf16_f32 v122, v88, v89
	v_lshl_add_u64 v[88:89], s[50:51], 0, v[82:83]
	v_add_co_u32_e32 v88, vcc, 0x36200000, v88
	s_mov_b64 s[4:5], 0
	s_nop 0
	v_addc_co_u32_e32 v89, vcc, 0, v89, vcc
	v_cvt_pk_bf16_f32 v123, v96, v97
	v_cvt_pk_bf16_f32 v124, v116, v117
	v_cvt_pk_bf16_f32 v125, v118, v119
	global_store_dwordx4 v[88:89], v[122:125], off offset:1536 sc1
.LBB0_565:
	s_and_b64 vcc, exec, s[4:5]
	s_cbranch_vccz .LBB0_568
	v_add_co_u32_e32 v88, vcc, 0x2e204000, v62
	v_cvt_pk_bf16_f32 v116, v94, v113
	v_cvt_pk_bf16_f32 v117, v114, v115
	v_cvt_pk_bf16_f32 v118, v54, v55
	v_cvt_pk_bf16_f32 v119, v56, v57
	s_nop 1
	v_addc_co_u32_e32 v89, vcc, 0, v63, vcc
	s_and_b64 vcc, exec, s[42:43]
	global_store_dwordx4 v[88:89], v[116:119], off sc1
	s_cbranch_vccnz .LBB0_568
	v_mul_f32_e32 v96, v103, v113
	v_mul_f32_e32 v94, v104, v94
	v_mul_f32_e32 v97, v96, v96
	v_fmac_f32_e32 v97, v94, v94
	v_mul_f32_e32 v113, v110, v114
	v_fmac_f32_e32 v97, v113, v113
	v_mul_f32_e32 v114, v109, v115
	v_pk_mul_f32 v[54:55], v[72:73], v[54:55]
	v_fmac_f32_e32 v97, v114, v114
	v_pk_mul_f32 v[88:89], v[54:55], v[54:55]
	v_pk_mul_f32 v[56:57], v[78:79], v[56:57]
	v_add_f32_e32 v88, v88, v97
	v_add_f32_e32 v97, v89, v88
	v_pk_mul_f32 v[88:89], v[56:57], v[56:57]
	s_nop 0
	v_add_f32_e32 v88, v88, v97
	v_and_b32_e32 v97, 64, v226
	v_add_f32_e32 v88, v89, v88
	v_xor_b32_e32 v89, 1, v226
	v_add_u32_e32 v97, 64, v97
	v_cmp_lt_i32_e32 vcc, v89, v97
	s_nop 1
	v_cndmask_b32_e32 v89, v226, v89, vcc
	v_lshlrev_b32_e32 v89, 2, v89
	ds_bpermute_b32 v89, v89, v88
	s_waitcnt lgkmcnt(0)
	v_add_f32_e32 v88, v88, v89
	v_xor_b32_e32 v89, 2, v226
	v_cmp_lt_i32_e32 vcc, v89, v97
	s_nop 1
	v_cndmask_b32_e32 v89, v226, v89, vcc
	v_lshlrev_b32_e32 v89, 2, v89
	ds_bpermute_b32 v89, v89, v88
	s_waitcnt lgkmcnt(0)
	v_add_f32_e32 v88, v88, v89
	v_xor_b32_e32 v89, 4, v226
	v_cmp_lt_i32_e32 vcc, v89, v97
	s_nop 1
	v_cndmask_b32_e32 v89, v226, v89, vcc
	v_lshlrev_b32_e32 v89, 2, v89
	ds_bpermute_b32 v89, v89, v88
	s_waitcnt lgkmcnt(0)
	v_add_f32_e32 v88, v88, v89
	v_mul_f32_e32 v89, 0x4f800000, v88
	v_cmp_gt_f32_e32 vcc, s82, v88
	s_nop 1
	v_cndmask_b32_e32 v88, v88, v89, vcc
	v_sqrt_f32_e32 v89, v88
	s_nop 0
	v_add_u32_e32 v97, -1, v89
	v_fma_f32 v115, -v97, v89, v88
	v_cmp_ge_f32_e64 s[46:47], 0, v115
	v_add_u32_e32 v115, 1, v89
	s_nop 0
	v_cndmask_b32_e64 v97, v89, v97, s[46:47]
	v_fma_f32 v89, -v115, v89, v88
	v_cmp_lt_f32_e64 s[46:47], 0, v89
	s_nop 1
	v_cndmask_b32_e64 v89, v97, v115, s[46:47]
	v_mul_f32_e32 v97, 0x37800000, v89
	v_cndmask_b32_e32 v89, v89, v97, vcc
	v_cmp_class_f32_e32 vcc, v88, v229
	s_nop 1
	v_cndmask_b32_e32 v88, v89, v88, vcc
	v_max_f32_e32 v88, 0x2b8cbccc, v88
	v_div_scale_f32 v89, s[4:5], v88, v88, 1.0
	v_rcp_f32_e32 v97, v89
	s_nop 0
	v_fma_f32 v115, -v89, v97, 1.0
	v_fmac_f32_e32 v97, v115, v97
	v_div_scale_f32 v115, vcc, 1.0, v88, 1.0
	v_mul_f32_e32 v116, v115, v97
	v_fma_f32 v117, -v89, v116, v115
	v_fmac_f32_e32 v116, v117, v97
	v_fma_f32 v89, -v89, v116, v115
	v_div_fmas_f32 v89, v89, v97, v116
	v_div_fixup_f32 v88, v89, v88, 1.0
	v_mul_f32_e32 v89, v94, v88
	v_mul_f32_e32 v94, v96, v88
	v_mul_f32_e32 v96, v113, v88
	v_mul_f32_e32 v97, v114, v88
	v_mul_f32_e32 v113, v54, v88
	v_mul_f32_e32 v114, v55, v88
	v_mul_f32_e32 v115, v56, v88
	v_mul_f32_e32 v57, v57, v88
	v_cvt_pk_bf16_f32 v54, v89, v94
	v_lshl_add_u64 v[88:89], s[50:51], 0, v[84:85]
	v_add_co_u32_e32 v88, vcc, 0x2e205000, v88
	v_cvt_pk_bf16_f32 v55, v96, v97
	v_cvt_pk_bf16_f32 v56, v113, v114
	v_cvt_pk_bf16_f32 v57, v115, v57
	s_nop 1
	v_addc_co_u32_e32 v89, vcc, 0, v89, vcc
	global_store_dwordx4 v[88:89], v[54:57], off offset:2048 sc1
.LBB0_568:
	v_lshlrev_b32_e32 v96, 16, v50
	v_and_b32_e32 v94, 0xffff0000, v50
	v_sub_f32_e32 v50, v121, v95
	v_fma_f32 v97, v101, v50, v95
	v_sub_f32_e32 v50, v96, v95
	v_fmac_f32_e32 v97, v102, v50
	v_sub_f32_e32 v50, v120, v93
	v_fma_f32 v113, v105, v50, v93
	v_sub_f32_e32 v50, v94, v93
	v_lshlrev_b32_e32 v89, 16, v51
	v_fmac_f32_e32 v113, v106, v50
	v_sub_f32_e32 v50, v99, v92
	v_fma_f32 v99, v107, v50, v92
	v_sub_f32_e32 v50, v89, v92
	v_and_b32_e32 v88, 0xffff0000, v51
	v_fmac_f32_e32 v99, v108, v50
	v_sub_f32_e32 v50, v98, v0
	v_fma_f32 v98, v111, v50, v0
	v_sub_f32_e32 v50, v88, v0
	v_fmac_f32_e32 v98, v112, v50
	v_and_b32_e32 v57, 0xffff0000, v52
	v_lshlrev_b32_e32 v56, 16, v52
	v_pk_add_f32 v[50:51], v[90:91], v[60:61] neg_lo:[0,1] neg_hi:[0,1]
	v_pk_add_f32 v[54:55], v[56:57], v[60:61] neg_lo:[0,1] neg_hi:[0,1]
	v_pk_fma_f32 v[50:51], v[68:69], v[50:51], v[60:61]
	s_and_b64 vcc, exec, s[44:45]
	v_pk_fma_f32 v[50:51], v[70:71], v[54:55], v[50:51]
	v_and_b32_e32 v55, 0xffff0000, v53
	v_lshlrev_b32_e32 v54, 16, v53
	v_pk_add_f32 v[52:53], v[64:65], v[58:59] neg_lo:[0,1] neg_hi:[0,1]
	v_pk_add_f32 v[64:65], v[54:55], v[58:59] neg_lo:[0,1] neg_hi:[0,1]
	v_pk_fma_f32 v[52:53], v[74:75], v[52:53], v[58:59]
	s_mov_b64 s[4:5], -1
	v_pk_fma_f32 v[52:53], v[76:77], v[64:65], v[52:53]
	s_cbranch_vccnz .LBB0_602
	v_mov_b32_e32 v118, 0xbfb8aa3b
	v_mov_b32_e32 v121, 0xc038aa3b
	v_cndmask_b32_e64 v118, v121, v118, s[38:39]
	v_cndmask_b32_e64 v119, 2.0, 1.0, s[38:39]
	v_cndmask_b32_e64 v120, -1.0, 0, s[38:39]
	v_mul_f32_e32 v64, v118, v97
	v_mul_f32_e32 v65, v118, v113
	v_mul_f32_e32 v90, v118, v99
	v_mul_f32_e32 v91, v118, v98
	v_mul_f32_e32 v114, v118, v50
	v_mul_f32_e32 v115, v118, v51
	v_mul_f32_e32 v116, v118, v52
	v_mul_f32_e32 v117, v118, v53
	v_exp_f32_e32 v64, v64
	v_exp_f32_e32 v65, v65
	v_exp_f32_e32 v90, v90
	v_exp_f32_e32 v91, v91
	v_exp_f32_e32 v114, v114
	v_exp_f32_e32 v115, v115
	v_exp_f32_e32 v116, v116
	v_exp_f32_e32 v117, v117
	v_add_f32_e32 v64, 1.0, v64
	v_add_f32_e32 v65, 1.0, v65
	v_add_f32_e32 v90, 1.0, v90
	v_add_f32_e32 v91, 1.0, v91
	v_add_f32_e32 v114, 1.0, v114
	v_add_f32_e32 v115, 1.0, v115
	v_add_f32_e32 v116, 1.0, v116
	v_add_f32_e32 v117, 1.0, v117
	v_rcp_f32_e32 v64, v64
	v_rcp_f32_e32 v65, v65
	v_rcp_f32_e32 v90, v90
	v_rcp_f32_e32 v91, v91
	v_rcp_f32_e32 v114, v114
	v_rcp_f32_e32 v115, v115
	v_rcp_f32_e32 v116, v116
	v_rcp_f32_e32 v117, v117
	v_fma_f32 v64, v64, v119, v120
	v_fma_f32 v65, v65, v119, v120
	v_fma_f32 v90, v90, v119, v120
	v_fma_f32 v91, v91, v119, v120
	v_fma_f32 v114, v114, v119, v120
	v_fma_f32 v115, v115, v119, v120
	v_fma_f32 v116, v116, v119, v120
	v_fma_f32 v117, v117, v119, v120
	v_cndmask_b32_e64 v64, v64, v97, s[40:41]
	v_cndmask_b32_e64 v65, v65, v113, s[40:41]
	v_cndmask_b32_e64 v90, v90, v99, s[40:41]
	v_cndmask_b32_e64 v91, v91, v98, s[40:41]
	v_cndmask_b32_e64 v114, v114, v50, s[40:41]
	v_cndmask_b32_e64 v115, v115, v51, s[40:41]
	v_cndmask_b32_e64 v116, v116, v52, s[40:41]
	v_cndmask_b32_e64 v117, v117, v53, s[40:41]
	v_cvt_pk_bf16_f32 v118, v64, v65
	v_lshl_add_u64 v[64:65], s[50:51], 0, v[82:83]
	v_add_co_u32_e32 v64, vcc, 0x36200000, v64
	s_mov_b64 s[4:5], 0
	s_nop 0
	v_addc_co_u32_e32 v65, vcc, 0, v65, vcc
	v_cvt_pk_bf16_f32 v119, v90, v91
	v_cvt_pk_bf16_f32 v120, v114, v115
	v_cvt_pk_bf16_f32 v121, v116, v117
	global_store_dwordx4 v[64:65], v[118:121], off offset:2304 sc1
.LBB0_602:
	s_and_b64 vcc, exec, s[4:5]
	s_cbranch_vccz .LBB0_605
	v_add_co_u32_e32 v64, vcc, 0x2e206000, v62
	v_cvt_pk_bf16_f32 v114, v97, v113
	v_cvt_pk_bf16_f32 v115, v99, v98
	v_cvt_pk_bf16_f32 v116, v50, v51
	v_cvt_pk_bf16_f32 v117, v52, v53
	s_nop 1
	v_addc_co_u32_e32 v65, vcc, 0, v63, vcc
	s_and_b64 vcc, exec, s[42:43]
	global_store_dwordx4 v[64:65], v[114:117], off sc1
	s_cbranch_vccnz .LBB0_605
	v_mul_f32_e32 v91, v103, v113
	v_mul_f32_e32 v90, v104, v97
	v_mul_f32_e32 v97, v91, v91
	v_fmac_f32_e32 v97, v90, v90
	v_mul_f32_e32 v99, v110, v99
	v_fmac_f32_e32 v97, v99, v99
	v_mul_f32_e32 v98, v109, v98
	v_pk_mul_f32 v[50:51], v[72:73], v[50:51]
	v_fmac_f32_e32 v97, v98, v98
	v_pk_mul_f32 v[64:65], v[50:51], v[50:51]
	v_pk_mul_f32 v[52:53], v[78:79], v[52:53]
	v_add_f32_e32 v64, v64, v97
	v_add_f32_e32 v97, v65, v64
	v_pk_mul_f32 v[64:65], v[52:53], v[52:53]
	s_nop 0
	v_add_f32_e32 v64, v64, v97
	v_and_b32_e32 v97, 64, v226
	v_add_f32_e32 v64, v65, v64
	v_xor_b32_e32 v65, 1, v226
	v_add_u32_e32 v97, 64, v97
	v_cmp_lt_i32_e32 vcc, v65, v97
	s_nop 1
	v_cndmask_b32_e32 v65, v226, v65, vcc
	v_lshlrev_b32_e32 v65, 2, v65
	ds_bpermute_b32 v65, v65, v64
	s_waitcnt lgkmcnt(0)
	v_add_f32_e32 v64, v64, v65
	v_xor_b32_e32 v65, 2, v226
	v_cmp_lt_i32_e32 vcc, v65, v97
	s_nop 1
	v_cndmask_b32_e32 v65, v226, v65, vcc
	v_lshlrev_b32_e32 v65, 2, v65
	ds_bpermute_b32 v65, v65, v64
	s_waitcnt lgkmcnt(0)
	v_add_f32_e32 v64, v64, v65
	v_xor_b32_e32 v65, 4, v226
	v_cmp_lt_i32_e32 vcc, v65, v97
	s_nop 1
	v_cndmask_b32_e32 v65, v226, v65, vcc
	v_lshlrev_b32_e32 v65, 2, v65
	ds_bpermute_b32 v65, v65, v64
	s_waitcnt lgkmcnt(0)
	v_add_f32_e32 v64, v64, v65
	v_mul_f32_e32 v65, 0x4f800000, v64
	v_cmp_gt_f32_e32 vcc, s82, v64
	s_nop 1
	v_cndmask_b32_e32 v64, v64, v65, vcc
	v_sqrt_f32_e32 v65, v64
	s_nop 0
	v_add_u32_e32 v97, -1, v65
	v_fma_f32 v113, -v97, v65, v64
	v_cmp_ge_f32_e64 s[46:47], 0, v113
	v_add_u32_e32 v113, 1, v65
	s_nop 0
	v_cndmask_b32_e64 v97, v65, v97, s[46:47]
	v_fma_f32 v65, -v113, v65, v64
	v_cmp_lt_f32_e64 s[46:47], 0, v65
	s_nop 1
	v_cndmask_b32_e64 v65, v97, v113, s[46:47]
	v_mul_f32_e32 v97, 0x37800000, v65
	v_cndmask_b32_e32 v65, v65, v97, vcc
	v_cmp_class_f32_e32 vcc, v64, v229
	s_nop 1
	v_cndmask_b32_e32 v64, v65, v64, vcc
	v_max_f32_e32 v64, 0x2b8cbccc, v64
	v_div_scale_f32 v65, s[4:5], v64, v64, 1.0
	v_rcp_f32_e32 v97, v65
	s_nop 0
	v_fma_f32 v113, -v65, v97, 1.0
	v_fmac_f32_e32 v97, v113, v97
	v_div_scale_f32 v113, vcc, 1.0, v64, 1.0
	v_mul_f32_e32 v114, v113, v97
	v_fma_f32 v115, -v65, v114, v113
	v_fmac_f32_e32 v114, v115, v97
	v_fma_f32 v65, -v65, v114, v113
	v_div_fmas_f32 v65, v65, v97, v114
	v_div_fixup_f32 v64, v65, v64, 1.0
	v_mul_f32_e32 v65, v90, v64
	v_mul_f32_e32 v90, v91, v64
	v_mul_f32_e32 v91, v99, v64
	v_mul_f32_e32 v97, v98, v64
	v_mul_f32_e32 v98, v50, v64
	v_mul_f32_e32 v99, v51, v64
	v_mul_f32_e32 v113, v52, v64
	v_mul_f32_e32 v53, v53, v64
	v_cvt_pk_bf16_f32 v50, v65, v90
	v_lshl_add_u64 v[64:65], s[50:51], 0, v[84:85]
	v_add_co_u32_e32 v64, vcc, 0x2e207000, v64
	v_cvt_pk_bf16_f32 v51, v91, v97
	v_cvt_pk_bf16_f32 v52, v98, v99
	v_cvt_pk_bf16_f32 v53, v113, v53
	s_nop 1
	v_addc_co_u32_e32 v65, vcc, 0, v65, vcc
	global_store_dwordx4 v[64:65], v[50:53], off offset:2048 sc1
.LBB0_605:
	v_lshlrev_b32_e32 v91, 16, v46
	v_and_b32_e32 v90, 0xffff0000, v46
	v_sub_f32_e32 v46, v95, v96
	v_fma_f32 v95, v101, v46, v96
	v_sub_f32_e32 v46, v91, v96
	v_fmac_f32_e32 v95, v102, v46
	v_sub_f32_e32 v46, v93, v94
	v_fma_f32 v93, v105, v46, v94
	v_sub_f32_e32 v46, v90, v94
	v_lshlrev_b32_e32 v65, 16, v47
	v_fmac_f32_e32 v93, v106, v46
	v_sub_f32_e32 v46, v92, v89
	v_and_b32_e32 v64, 0xffff0000, v47
	v_fma_f32 v92, v107, v46, v89
	v_sub_f32_e32 v46, v65, v89
	v_sub_f32_e32 v0, v0, v88
	v_fmac_f32_e32 v92, v108, v46
	v_fma_f32 v0, v111, v0, v88
	v_sub_f32_e32 v46, v64, v88
	v_fmac_f32_e32 v0, v112, v46
	v_and_b32_e32 v53, 0xffff0000, v48
	v_lshlrev_b32_e32 v52, 16, v48
	v_pk_add_f32 v[46:47], v[60:61], v[56:57] neg_lo:[0,1] neg_hi:[0,1]
	v_pk_add_f32 v[50:51], v[52:53], v[56:57] neg_lo:[0,1] neg_hi:[0,1]
	v_pk_fma_f32 v[46:47], v[68:69], v[46:47], v[56:57]
	s_and_b64 vcc, exec, s[44:45]
	v_pk_fma_f32 v[46:47], v[70:71], v[50:51], v[46:47]
	v_and_b32_e32 v51, 0xffff0000, v49
	v_lshlrev_b32_e32 v50, 16, v49
	v_pk_add_f32 v[48:49], v[58:59], v[54:55] neg_lo:[0,1] neg_hi:[0,1]
	v_pk_add_f32 v[58:59], v[50:51], v[54:55] neg_lo:[0,1] neg_hi:[0,1]
	v_pk_fma_f32 v[48:49], v[74:75], v[48:49], v[54:55]
	s_mov_b64 s[4:5], -1
	v_pk_fma_f32 v[48:49], v[76:77], v[58:59], v[48:49]
	s_cbranch_vccnz .LBB0_639
	v_mov_b32_e32 v114, 0xbfb8aa3b
	v_mov_b32_e32 v117, 0xc038aa3b
	v_cndmask_b32_e64 v114, v117, v114, s[38:39]
	v_cndmask_b32_e64 v115, 2.0, 1.0, s[38:39]
	v_cndmask_b32_e64 v116, -1.0, 0, s[38:39]
	v_mul_f32_e32 v58, v114, v95
	v_mul_f32_e32 v59, v114, v93
	v_mul_f32_e32 v60, v114, v92
	v_mul_f32_e32 v61, v114, v0
	v_mul_f32_e32 v97, v114, v46
	v_mul_f32_e32 v98, v114, v47
	v_mul_f32_e32 v99, v114, v48
	v_mul_f32_e32 v113, v114, v49
	v_exp_f32_e32 v58, v58
	v_exp_f32_e32 v59, v59
	v_exp_f32_e32 v60, v60
	v_exp_f32_e32 v61, v61
	v_exp_f32_e32 v97, v97
	v_exp_f32_e32 v98, v98
	v_exp_f32_e32 v99, v99
	v_exp_f32_e32 v113, v113
	v_add_f32_e32 v58, 1.0, v58
	v_add_f32_e32 v59, 1.0, v59
	v_add_f32_e32 v60, 1.0, v60
	v_add_f32_e32 v61, 1.0, v61
	v_add_f32_e32 v97, 1.0, v97
	v_add_f32_e32 v98, 1.0, v98
	v_add_f32_e32 v99, 1.0, v99
	v_add_f32_e32 v113, 1.0, v113
	v_rcp_f32_e32 v58, v58
	v_rcp_f32_e32 v59, v59
	v_rcp_f32_e32 v60, v60
	v_rcp_f32_e32 v61, v61
	v_rcp_f32_e32 v97, v97
	v_rcp_f32_e32 v98, v98
	v_rcp_f32_e32 v99, v99
	v_rcp_f32_e32 v113, v113
	v_fma_f32 v58, v58, v115, v116
	v_fma_f32 v59, v59, v115, v116
	v_fma_f32 v60, v60, v115, v116
	v_fma_f32 v61, v61, v115, v116
	v_fma_f32 v97, v97, v115, v116
	v_fma_f32 v98, v98, v115, v116
	v_fma_f32 v99, v99, v115, v116
	v_fma_f32 v113, v113, v115, v116
	v_cndmask_b32_e64 v58, v58, v95, s[40:41]
	v_cndmask_b32_e64 v59, v59, v93, s[40:41]
	v_cndmask_b32_e64 v60, v60, v92, s[40:41]
	v_cndmask_b32_e64 v61, v61, v0, s[40:41]
	v_cndmask_b32_e64 v97, v97, v46, s[40:41]
	v_cndmask_b32_e64 v98, v98, v47, s[40:41]
	v_cndmask_b32_e64 v99, v99, v48, s[40:41]
	v_cndmask_b32_e64 v113, v113, v49, s[40:41]
	v_cvt_pk_bf16_f32 v58, v58, v59
	v_cvt_pk_bf16_f32 v59, v60, v61
	v_cvt_pk_bf16_f32 v60, v97, v98
	v_cvt_pk_bf16_f32 v61, v99, v113
	v_lshl_add_u64 v[98:99], s[50:51], 0, v[82:83]
	v_add_co_u32_e32 v98, vcc, 0x36200000, v98
	s_mov_b64 s[4:5], 0
	s_nop 0
	v_addc_co_u32_e32 v99, vcc, 0, v99, vcc
	global_store_dwordx4 v[98:99], v[58:61], off offset:3072 sc1
.LBB0_639:
	s_and_b64 vcc, exec, s[4:5]
	s_cbranch_vccz .LBB0_642
	v_add_co_u32_e32 v98, vcc, 0x2e208000, v62
	v_cvt_pk_bf16_f32 v58, v95, v93
	v_cvt_pk_bf16_f32 v59, v92, v0
	v_cvt_pk_bf16_f32 v60, v46, v47
	v_cvt_pk_bf16_f32 v61, v48, v49
	s_nop 1
	v_addc_co_u32_e32 v99, vcc, 0, v63, vcc
	s_and_b64 vcc, exec, s[42:43]
	global_store_dwordx4 v[98:99], v[58:61], off sc1
	s_cbranch_vccnz .LBB0_642
	s_nop 0
	v_mul_f32_e32 v61, v103, v93
	v_mul_f32_e32 v60, v104, v95
	v_mul_f32_e32 v93, v61, v61
	v_fmac_f32_e32 v93, v60, v60
	v_mul_f32_e32 v92, v110, v92
	v_fmac_f32_e32 v93, v92, v92
	v_mul_f32_e32 v0, v109, v0
	v_pk_mul_f32 v[46:47], v[72:73], v[46:47]
	v_fmac_f32_e32 v93, v0, v0
	v_pk_mul_f32 v[58:59], v[46:47], v[46:47]
	v_pk_mul_f32 v[48:49], v[78:79], v[48:49]
	v_add_f32_e32 v58, v58, v93
	v_add_f32_e32 v93, v59, v58
	v_pk_mul_f32 v[58:59], v[48:49], v[48:49]
	s_nop 0
	v_add_f32_e32 v58, v58, v93
	v_and_b32_e32 v93, 64, v226
	v_add_f32_e32 v58, v59, v58
	v_xor_b32_e32 v59, 1, v226
	v_add_u32_e32 v93, 64, v93
	v_cmp_lt_i32_e32 vcc, v59, v93
	s_nop 1
	v_cndmask_b32_e32 v59, v226, v59, vcc
	v_lshlrev_b32_e32 v59, 2, v59
	ds_bpermute_b32 v59, v59, v58
	s_waitcnt lgkmcnt(0)
	v_add_f32_e32 v58, v58, v59
	v_xor_b32_e32 v59, 2, v226
	v_cmp_lt_i32_e32 vcc, v59, v93
	s_nop 1
	v_cndmask_b32_e32 v59, v226, v59, vcc
	v_lshlrev_b32_e32 v59, 2, v59
	ds_bpermute_b32 v59, v59, v58
	s_waitcnt lgkmcnt(0)
	v_add_f32_e32 v58, v58, v59
	v_xor_b32_e32 v59, 4, v226
	v_cmp_lt_i32_e32 vcc, v59, v93
	s_nop 1
	v_cndmask_b32_e32 v59, v226, v59, vcc
	v_lshlrev_b32_e32 v59, 2, v59
	ds_bpermute_b32 v59, v59, v58
	s_waitcnt lgkmcnt(0)
	v_add_f32_e32 v58, v58, v59
	v_mul_f32_e32 v59, 0x4f800000, v58
	v_cmp_gt_f32_e32 vcc, s82, v58
	s_nop 1
	v_cndmask_b32_e32 v58, v58, v59, vcc
	v_sqrt_f32_e32 v59, v58
	s_nop 0
	v_add_u32_e32 v93, -1, v59
	v_fma_f32 v95, -v93, v59, v58
	v_cmp_ge_f32_e64 s[46:47], 0, v95
	v_add_u32_e32 v95, 1, v59
	s_nop 0
	v_cndmask_b32_e64 v93, v59, v93, s[46:47]
	v_fma_f32 v59, -v95, v59, v58
	v_cmp_lt_f32_e64 s[46:47], 0, v59
	s_nop 1
	v_cndmask_b32_e64 v59, v93, v95, s[46:47]
	v_mul_f32_e32 v93, 0x37800000, v59
	v_cndmask_b32_e32 v59, v59, v93, vcc
	v_cmp_class_f32_e32 vcc, v58, v229
	s_nop 1
	v_cndmask_b32_e32 v58, v59, v58, vcc
	v_max_f32_e32 v58, 0x2b8cbccc, v58
	v_div_scale_f32 v59, s[4:5], v58, v58, 1.0
	v_rcp_f32_e32 v93, v59
	s_nop 0
	v_fma_f32 v95, -v59, v93, 1.0
	v_fmac_f32_e32 v93, v95, v93
	v_div_scale_f32 v95, vcc, 1.0, v58, 1.0
	v_mul_f32_e32 v97, v95, v93
	v_fma_f32 v98, -v59, v97, v95
	v_fmac_f32_e32 v97, v98, v93
	v_fma_f32 v59, -v59, v97, v95
	v_div_fmas_f32 v59, v59, v93, v97
	v_div_fixup_f32 v58, v59, v58, 1.0
	v_mul_f32_e32 v59, v60, v58
	v_mul_f32_e32 v60, v61, v58
	v_mul_f32_e32 v61, v92, v58
	v_mul_f32_e32 v0, v0, v58
	v_mul_f32_e32 v92, v46, v58
	v_mul_f32_e32 v93, v47, v58
	v_mul_f32_e32 v95, v48, v58
	v_mul_f32_e32 v49, v49, v58
	v_cvt_pk_bf16_f32 v46, v59, v60
	v_lshl_add_u64 v[58:59], s[50:51], 0, v[84:85]
	v_add_co_u32_e32 v58, vcc, 0x2e209000, v58
	v_cvt_pk_bf16_f32 v47, v61, v0
	v_cvt_pk_bf16_f32 v48, v92, v93
	v_cvt_pk_bf16_f32 v49, v95, v49
	s_nop 1
	v_addc_co_u32_e32 v59, vcc, 0, v59, vcc
	global_store_dwordx4 v[58:59], v[46:49], off offset:2048 sc1
.LBB0_642:
	s_nop 0
	v_lshlrev_b32_e32 v61, 16, v42
	v_sub_f32_e32 v0, v96, v91
	v_and_b32_e32 v60, 0xffff0000, v42
	v_fma_f32 v0, v101, v0, v91
	v_sub_f32_e32 v42, v61, v91
	v_fmac_f32_e32 v0, v102, v42
	v_sub_f32_e32 v42, v94, v90
	v_fma_f32 v92, v105, v42, v90
	v_sub_f32_e32 v42, v60, v90
	v_lshlrev_b32_e32 v59, 16, v43
	v_fmac_f32_e32 v92, v106, v42
	v_sub_f32_e32 v42, v89, v65
	v_fma_f32 v89, v107, v42, v65
	v_sub_f32_e32 v42, v59, v65
	v_and_b32_e32 v58, 0xffff0000, v43
	v_fmac_f32_e32 v89, v108, v42
	v_sub_f32_e32 v42, v88, v64
	v_fma_f32 v88, v111, v42, v64
	v_sub_f32_e32 v42, v58, v64
	v_fmac_f32_e32 v88, v112, v42
	v_and_b32_e32 v43, 0xffff0000, v44
	v_lshlrev_b32_e32 v42, 16, v44
	v_pk_add_f32 v[46:47], v[56:57], v[52:53] neg_lo:[0,1] neg_hi:[0,1]
	v_pk_add_f32 v[48:49], v[42:43], v[52:53] neg_lo:[0,1] neg_hi:[0,1]
	v_pk_fma_f32 v[46:47], v[68:69], v[46:47], v[52:53]
	s_and_b64 vcc, exec, s[44:45]
	v_pk_fma_f32 v[48:49], v[70:71], v[48:49], v[46:47]
	v_and_b32_e32 v47, 0xffff0000, v45
	v_lshlrev_b32_e32 v46, 16, v45
	v_pk_add_f32 v[44:45], v[54:55], v[50:51] neg_lo:[0,1] neg_hi:[0,1]
	v_pk_add_f32 v[54:55], v[46:47], v[50:51] neg_lo:[0,1] neg_hi:[0,1]
	v_pk_fma_f32 v[44:45], v[74:75], v[44:45], v[50:51]
	s_mov_b64 s[4:5], -1
	v_pk_fma_f32 v[44:45], v[76:77], v[54:55], v[44:45]
	s_cbranch_vccnz .LBB0_676
	v_mov_b32_e32 v97, 0xbfb8aa3b
	v_mov_b32_e32 v113, 0xc038aa3b
	v_cndmask_b32_e64 v97, v113, v97, s[38:39]
	v_cndmask_b32_e64 v98, 2.0, 1.0, s[38:39]
	v_cndmask_b32_e64 v99, -1.0, 0, s[38:39]
	v_mul_f32_e32 v54, v97, v0
	v_mul_f32_e32 v55, v97, v92
	v_mul_f32_e32 v56, v97, v89
	v_mul_f32_e32 v57, v97, v88
	v_mul_f32_e32 v93, v97, v48
	v_mul_f32_e32 v94, v97, v49
	v_mul_f32_e32 v95, v97, v44
	v_mul_f32_e32 v96, v97, v45
	v_exp_f32_e32 v54, v54
	v_exp_f32_e32 v55, v55
	v_exp_f32_e32 v56, v56
	v_exp_f32_e32 v57, v57
	v_exp_f32_e32 v93, v93
	v_exp_f32_e32 v94, v94
	v_exp_f32_e32 v95, v95
	v_exp_f32_e32 v96, v96
	v_add_f32_e32 v54, 1.0, v54
	v_add_f32_e32 v55, 1.0, v55
	v_add_f32_e32 v56, 1.0, v56
	v_add_f32_e32 v57, 1.0, v57
	v_add_f32_e32 v93, 1.0, v93
	v_add_f32_e32 v94, 1.0, v94
	v_add_f32_e32 v95, 1.0, v95
	v_add_f32_e32 v96, 1.0, v96
	v_rcp_f32_e32 v54, v54
	v_rcp_f32_e32 v55, v55
	v_rcp_f32_e32 v56, v56
	v_rcp_f32_e32 v57, v57
	v_rcp_f32_e32 v93, v93
	v_rcp_f32_e32 v94, v94
	v_rcp_f32_e32 v95, v95
	v_rcp_f32_e32 v96, v96
	v_fma_f32 v54, v54, v98, v99
	v_fma_f32 v55, v55, v98, v99
	v_fma_f32 v56, v56, v98, v99
	v_fma_f32 v57, v57, v98, v99
	v_fma_f32 v93, v93, v98, v99
	v_fma_f32 v94, v94, v98, v99
	v_fma_f32 v95, v95, v98, v99
	v_fma_f32 v96, v96, v98, v99
	v_cndmask_b32_e64 v54, v54, v0, s[40:41]
	v_cndmask_b32_e64 v55, v55, v92, s[40:41]
	v_cndmask_b32_e64 v56, v56, v89, s[40:41]
	v_cndmask_b32_e64 v57, v57, v88, s[40:41]
	v_cndmask_b32_e64 v93, v93, v48, s[40:41]
	v_cndmask_b32_e64 v94, v94, v49, s[40:41]
	v_cndmask_b32_e64 v95, v95, v44, s[40:41]
	v_cndmask_b32_e64 v96, v96, v45, s[40:41]
	v_cvt_pk_bf16_f32 v54, v54, v55
	v_cvt_pk_bf16_f32 v55, v56, v57
	v_cvt_pk_bf16_f32 v56, v93, v94
	v_cvt_pk_bf16_f32 v57, v95, v96
	v_lshl_add_u64 v[94:95], s[50:51], 0, v[82:83]
	v_add_co_u32_e32 v94, vcc, 0x36200000, v94
	s_mov_b64 s[4:5], 0
	s_nop 0
	v_addc_co_u32_e32 v95, vcc, 0, v95, vcc
	global_store_dwordx4 v[94:95], v[54:57], off offset:3840 sc1
.LBB0_676:
	s_and_b64 vcc, exec, s[4:5]
	s_cbranch_vccz .LBB0_679
	v_add_co_u32_e32 v94, vcc, 0x2e20a000, v62
	v_cvt_pk_bf16_f32 v54, v0, v92
	v_cvt_pk_bf16_f32 v55, v89, v88
	v_cvt_pk_bf16_f32 v56, v48, v49
	v_cvt_pk_bf16_f32 v57, v44, v45
	s_nop 1
	v_addc_co_u32_e32 v95, vcc, 0, v63, vcc
	s_and_b64 vcc, exec, s[42:43]
	global_store_dwordx4 v[94:95], v[54:57], off sc1
	s_cbranch_vccnz .LBB0_679
	s_nop 0
	v_mul_f32_e32 v56, v103, v92
	v_mul_f32_e32 v0, v104, v0
	v_mul_f32_e32 v57, v56, v56
	v_fmac_f32_e32 v57, v0, v0
	v_mul_f32_e32 v89, v110, v89
	v_fmac_f32_e32 v57, v89, v89
	v_mul_f32_e32 v88, v109, v88
	v_pk_mul_f32 v[48:49], v[72:73], v[48:49]
	v_fmac_f32_e32 v57, v88, v88
	v_pk_mul_f32 v[54:55], v[48:49], v[48:49]
	v_pk_mul_f32 v[44:45], v[78:79], v[44:45]
	v_add_f32_e32 v54, v54, v57
	v_add_f32_e32 v57, v55, v54
	v_pk_mul_f32 v[54:55], v[44:45], v[44:45]
	s_nop 0
	v_add_f32_e32 v54, v54, v57
	v_and_b32_e32 v57, 64, v226
	v_add_f32_e32 v54, v55, v54
	v_xor_b32_e32 v55, 1, v226
	v_add_u32_e32 v57, 64, v57
	v_cmp_lt_i32_e32 vcc, v55, v57
	s_nop 1
	v_cndmask_b32_e32 v55, v226, v55, vcc
	v_lshlrev_b32_e32 v55, 2, v55
	ds_bpermute_b32 v55, v55, v54
	s_waitcnt lgkmcnt(0)
	v_add_f32_e32 v54, v54, v55
	v_xor_b32_e32 v55, 2, v226
	v_cmp_lt_i32_e32 vcc, v55, v57
	s_nop 1
	v_cndmask_b32_e32 v55, v226, v55, vcc
	v_lshlrev_b32_e32 v55, 2, v55
	ds_bpermute_b32 v55, v55, v54
	s_waitcnt lgkmcnt(0)
	v_add_f32_e32 v54, v54, v55
	v_xor_b32_e32 v55, 4, v226
	v_cmp_lt_i32_e32 vcc, v55, v57
	s_nop 1
	v_cndmask_b32_e32 v55, v226, v55, vcc
	v_lshlrev_b32_e32 v55, 2, v55
	ds_bpermute_b32 v55, v55, v54
	s_waitcnt lgkmcnt(0)
	v_add_f32_e32 v54, v54, v55
	v_mul_f32_e32 v55, 0x4f800000, v54
	v_cmp_gt_f32_e32 vcc, s82, v54
	s_nop 1
	v_cndmask_b32_e32 v54, v54, v55, vcc
	v_sqrt_f32_e32 v55, v54
	s_nop 0
	v_add_u32_e32 v57, -1, v55
	v_fma_f32 v92, -v57, v55, v54
	v_cmp_ge_f32_e64 s[46:47], 0, v92
	v_add_u32_e32 v92, 1, v55
	s_nop 0
	v_cndmask_b32_e64 v57, v55, v57, s[46:47]
	v_fma_f32 v55, -v92, v55, v54
	v_cmp_lt_f32_e64 s[46:47], 0, v55
	s_nop 1
	v_cndmask_b32_e64 v55, v57, v92, s[46:47]
	v_mul_f32_e32 v57, 0x37800000, v55
	v_cndmask_b32_e32 v55, v55, v57, vcc
	v_cmp_class_f32_e32 vcc, v54, v229
	s_nop 1
	v_cndmask_b32_e32 v54, v55, v54, vcc
	v_max_f32_e32 v54, 0x2b8cbccc, v54
	v_div_scale_f32 v55, s[4:5], v54, v54, 1.0
	v_rcp_f32_e32 v57, v55
	s_nop 0
	v_fma_f32 v92, -v55, v57, 1.0
	v_fmac_f32_e32 v57, v92, v57
	v_div_scale_f32 v92, vcc, 1.0, v54, 1.0
	v_mul_f32_e32 v93, v92, v57
	v_fma_f32 v94, -v55, v93, v92
	v_fmac_f32_e32 v93, v94, v57
	v_fma_f32 v55, -v55, v93, v92
	v_div_fmas_f32 v55, v55, v57, v93
	v_div_fixup_f32 v54, v55, v54, 1.0
	v_mul_f32_e32 v55, v56, v54
	v_mul_f32_e32 v56, v89, v54
	v_mul_f32_e32 v57, v88, v54
	v_mul_f32_e32 v44, v44, v54
	v_mul_f32_e32 v45, v45, v54
	v_mul_f32_e32 v0, v0, v54
	v_mul_f32_e32 v48, v48, v54
	v_mul_f32_e32 v49, v49, v54
	v_cvt_pk_bf16_f32 v54, v0, v55
	v_cvt_pk_bf16_f32 v55, v56, v57
	v_cvt_pk_bf16_f32 v56, v48, v49
	v_cvt_pk_bf16_f32 v57, v44, v45
	v_lshl_add_u64 v[44:45], s[50:51], 0, v[84:85]
	v_add_co_u32_e32 v44, vcc, 0x2e20b000, v44
	s_nop 1
	v_addc_co_u32_e32 v45, vcc, 0, v45, vcc
	global_store_dwordx4 v[44:45], v[54:57], off offset:2048 sc1
.LBB0_679:
	v_lshlrev_b32_e32 v99, 16, v38
	v_sub_f32_e32 v0, v91, v61
	v_and_b32_e32 v98, 0xffff0000, v38
	v_fma_f32 v0, v101, v0, v61
	v_sub_f32_e32 v38, v99, v61
	v_fmac_f32_e32 v0, v102, v38
	v_sub_f32_e32 v38, v90, v60
	v_fma_f32 v44, v105, v38, v60
	v_sub_f32_e32 v38, v98, v60
	v_lshlrev_b32_e32 v97, 16, v39
	v_fmac_f32_e32 v44, v106, v38
	v_sub_f32_e32 v38, v65, v59
	v_fma_f32 v45, v107, v38, v59
	v_sub_f32_e32 v38, v97, v59
	v_and_b32_e32 v96, 0xffff0000, v39
	v_fmac_f32_e32 v45, v108, v38
	v_sub_f32_e32 v38, v64, v58
	v_fma_f32 v48, v111, v38, v58
	v_sub_f32_e32 v38, v96, v58
	v_fmac_f32_e32 v48, v112, v38
	v_and_b32_e32 v89, 0xffff0000, v40
	v_lshlrev_b32_e32 v88, 16, v40
	v_pk_add_f32 v[38:39], v[52:53], v[42:43] neg_lo:[0,1] neg_hi:[0,1]
	v_and_b32_e32 v91, 0xffff0000, v41
	v_lshlrev_b32_e32 v90, 16, v41
	v_pk_add_f32 v[40:41], v[50:51], v[46:47] neg_lo:[0,1] neg_hi:[0,1]
	v_pk_fma_f32 v[38:39], v[68:69], v[38:39], v[42:43]
	v_pk_add_f32 v[52:53], v[88:89], v[42:43] neg_lo:[0,1] neg_hi:[0,1]
	v_pk_fma_f32 v[40:41], v[74:75], v[40:41], v[46:47]
	v_pk_add_f32 v[50:51], v[90:91], v[46:47] neg_lo:[0,1] neg_hi:[0,1]
	v_pk_fma_f32 v[38:39], v[70:71], v[52:53], v[38:39]
	v_pk_fma_f32 v[40:41], v[76:77], v[50:51], v[40:41]
	s_and_b64 vcc, exec, s[44:45]
	s_mov_b64 s[4:5], -1
	s_cbranch_vccnz .LBB0_713
	v_mov_b32_e32 v57, 0xbfb8aa3b
	v_mov_b32_e32 v92, 0xc038aa3b
	v_cndmask_b32_e64 v57, v92, v57, s[38:39]
	v_cndmask_b32_e64 v64, 2.0, 1.0, s[38:39]
	v_cndmask_b32_e64 v65, -1.0, 0, s[38:39]
	v_mul_f32_e32 v49, v57, v0
	v_mul_f32_e32 v50, v57, v44
	v_mul_f32_e32 v51, v57, v45
	v_mul_f32_e32 v52, v57, v48
	v_mul_f32_e32 v53, v57, v38
	v_mul_f32_e32 v54, v57, v39
	v_mul_f32_e32 v55, v57, v40
	v_mul_f32_e32 v56, v57, v41
	v_exp_f32_e32 v49, v49
	v_exp_f32_e32 v50, v50
	v_exp_f32_e32 v51, v51
	v_exp_f32_e32 v52, v52
	v_exp_f32_e32 v53, v53
	v_exp_f32_e32 v54, v54
	v_exp_f32_e32 v55, v55
	v_exp_f32_e32 v56, v56
	v_add_f32_e32 v49, 1.0, v49
	v_add_f32_e32 v50, 1.0, v50
	v_add_f32_e32 v51, 1.0, v51
	v_add_f32_e32 v52, 1.0, v52
	v_add_f32_e32 v53, 1.0, v53
	v_add_f32_e32 v54, 1.0, v54
	v_add_f32_e32 v55, 1.0, v55
	v_add_f32_e32 v56, 1.0, v56
	v_rcp_f32_e32 v49, v49
	v_rcp_f32_e32 v50, v50
	v_rcp_f32_e32 v51, v51
	v_rcp_f32_e32 v52, v52
	v_rcp_f32_e32 v53, v53
	v_rcp_f32_e32 v54, v54
	v_rcp_f32_e32 v55, v55
	v_rcp_f32_e32 v56, v56
	v_fma_f32 v49, v49, v64, v65
	v_fma_f32 v50, v50, v64, v65
	v_fma_f32 v51, v51, v64, v65
	v_fma_f32 v52, v52, v64, v65
	v_fma_f32 v53, v53, v64, v65
	v_fma_f32 v54, v54, v64, v65
	v_fma_f32 v55, v55, v64, v65
	v_fma_f32 v56, v56, v64, v65
	v_cndmask_b32_e64 v49, v49, v0, s[40:41]
	v_cndmask_b32_e64 v50, v50, v44, s[40:41]
	v_cndmask_b32_e64 v51, v51, v45, s[40:41]
	v_cndmask_b32_e64 v52, v52, v48, s[40:41]
	v_cndmask_b32_e64 v53, v53, v38, s[40:41]
	v_cndmask_b32_e64 v54, v54, v39, s[40:41]
	v_cndmask_b32_e64 v55, v55, v40, s[40:41]
	v_cndmask_b32_e64 v56, v56, v41, s[40:41]
	v_cvt_pk_bf16_f32 v50, v49, v50
	v_cvt_pk_bf16_f32 v51, v51, v52
	v_cvt_pk_bf16_f32 v52, v53, v54
	v_cvt_pk_bf16_f32 v53, v55, v56
	v_lshl_add_u64 v[54:55], s[50:51], 0, v[82:83]
	v_add_co_u32_e32 v54, vcc, 0x36201000, v54
	s_mov_b64 s[4:5], 0
	s_nop 0
	v_addc_co_u32_e32 v55, vcc, 0, v55, vcc
	global_store_dwordx4 v[54:55], v[50:53], off offset:512 sc1
.LBB0_713:
	s_and_b64 vcc, exec, s[4:5]
	s_cbranch_vccz .LBB0_716
	v_add_co_u32_e32 v54, vcc, 0x2e20c000, v62
	v_cvt_pk_bf16_f32 v50, v0, v44
	v_cvt_pk_bf16_f32 v51, v45, v48
	v_cvt_pk_bf16_f32 v52, v38, v39
	v_cvt_pk_bf16_f32 v53, v40, v41
	s_nop 1
	v_addc_co_u32_e32 v55, vcc, 0, v63, vcc
	s_and_b64 vcc, exec, s[42:43]
	global_store_dwordx4 v[54:55], v[50:53], off sc1
	s_cbranch_vccnz .LBB0_716
	v_mul_f32_e32 v49, v103, v44
	v_mul_f32_e32 v0, v104, v0
	v_mul_f32_e32 v50, v49, v49
	v_fmac_f32_e32 v50, v0, v0
	v_mul_f32_e32 v51, v110, v45
	v_fmac_f32_e32 v50, v51, v51
	v_mul_f32_e32 v48, v109, v48
	v_pk_mul_f32 v[38:39], v[72:73], v[38:39]
	v_fmac_f32_e32 v50, v48, v48
	v_pk_mul_f32 v[44:45], v[38:39], v[38:39]
	v_pk_mul_f32 v[40:41], v[78:79], v[40:41]
	v_add_f32_e32 v44, v44, v50
	v_add_f32_e32 v50, v45, v44
	v_pk_mul_f32 v[44:45], v[40:41], v[40:41]
	s_nop 0
	v_add_f32_e32 v44, v44, v50
	v_and_b32_e32 v50, 64, v226
	v_add_f32_e32 v44, v45, v44
	v_xor_b32_e32 v45, 1, v226
	v_add_u32_e32 v50, 64, v50
	v_cmp_lt_i32_e32 vcc, v45, v50
	s_nop 1
	v_cndmask_b32_e32 v45, v226, v45, vcc
	v_lshlrev_b32_e32 v45, 2, v45
	ds_bpermute_b32 v45, v45, v44
	s_waitcnt lgkmcnt(0)
	v_add_f32_e32 v44, v44, v45
	v_xor_b32_e32 v45, 2, v226
	v_cmp_lt_i32_e32 vcc, v45, v50
	s_nop 1
	v_cndmask_b32_e32 v45, v226, v45, vcc
	v_lshlrev_b32_e32 v45, 2, v45
	ds_bpermute_b32 v45, v45, v44
	s_waitcnt lgkmcnt(0)
	v_add_f32_e32 v44, v44, v45
	v_xor_b32_e32 v45, 4, v226
	v_cmp_lt_i32_e32 vcc, v45, v50
	s_nop 1
	v_cndmask_b32_e32 v45, v226, v45, vcc
	v_lshlrev_b32_e32 v45, 2, v45
	ds_bpermute_b32 v45, v45, v44
	s_waitcnt lgkmcnt(0)
	v_add_f32_e32 v44, v44, v45
	v_mul_f32_e32 v45, 0x4f800000, v44
	v_cmp_gt_f32_e32 vcc, s82, v44
	s_nop 1
	v_cndmask_b32_e32 v44, v44, v45, vcc
	v_sqrt_f32_e32 v45, v44
	s_nop 0
	v_add_u32_e32 v50, -1, v45
	v_fma_f32 v52, -v50, v45, v44
	v_cmp_ge_f32_e64 s[46:47], 0, v52
	v_add_u32_e32 v52, 1, v45
	s_nop 0
	v_cndmask_b32_e64 v50, v45, v50, s[46:47]
	v_fma_f32 v45, -v52, v45, v44
	v_cmp_lt_f32_e64 s[46:47], 0, v45
	s_nop 1
	v_cndmask_b32_e64 v45, v50, v52, s[46:47]
	v_mul_f32_e32 v50, 0x37800000, v45
	v_cndmask_b32_e32 v45, v45, v50, vcc
	v_cmp_class_f32_e32 vcc, v44, v229
	s_nop 1
	v_cndmask_b32_e32 v44, v45, v44, vcc
	v_max_f32_e32 v44, 0x2b8cbccc, v44
	v_div_scale_f32 v45, s[4:5], v44, v44, 1.0
	v_rcp_f32_e32 v50, v45
	s_nop 0
	v_fma_f32 v52, -v45, v50, 1.0
	v_fmac_f32_e32 v50, v52, v50
	v_div_scale_f32 v52, vcc, 1.0, v44, 1.0
	v_mul_f32_e32 v53, v52, v50
	v_fma_f32 v54, -v45, v53, v52
	v_fmac_f32_e32 v53, v54, v50
	v_fma_f32 v45, -v45, v53, v52
	v_div_fmas_f32 v45, v45, v50, v53
	v_div_fixup_f32 v44, v45, v44, 1.0
	v_mul_f32_e32 v45, v49, v44
	v_mul_f32_e32 v0, v0, v44
	v_mul_f32_e32 v49, v51, v44
	v_mul_f32_e32 v48, v48, v44
	v_mul_f32_e32 v50, v38, v44
	v_mul_f32_e32 v51, v39, v44
	v_mul_f32_e32 v52, v40, v44
	v_mul_f32_e32 v41, v41, v44
	v_cvt_pk_bf16_f32 v38, v0, v45
	v_lshl_add_u64 v[44:45], s[50:51], 0, v[84:85]
	v_add_co_u32_e32 v44, vcc, 0x2e20d000, v44
	v_cvt_pk_bf16_f32 v39, v49, v48
	v_cvt_pk_bf16_f32 v40, v50, v51
	v_cvt_pk_bf16_f32 v41, v52, v41
	s_nop 1
	v_addc_co_u32_e32 v45, vcc, 0, v45, vcc
	global_store_dwordx4 v[44:45], v[38:41], off offset:2048 sc1
.LBB0_716:
	s_or_b32 s4, s6, s10
	s_cmpk_lg_i32 s4, 0xfff
	v_lshlrev_b32_e32 v38, 16, v34
	v_and_b32_e32 v34, 0xffff0000, v34
	s_cselect_b64 vcc, -1, 0
	v_cndmask_b32_e32 v114, 0, v34, vcc
	v_cndmask_b32_e32 v115, 0, v38, vcc
	v_sub_f32_e32 v34, v61, v99
	v_fma_f32 v38, v101, v34, v99
	v_sub_f32_e32 v34, v115, v99
	v_lshlrev_b32_e32 v39, 16, v35
	v_fmac_f32_e32 v38, v102, v34
	v_sub_f32_e32 v34, v60, v98
	v_cndmask_b32_e32 v113, 0, v39, vcc
	v_fma_f32 v39, v105, v34, v98
	v_sub_f32_e32 v34, v114, v98
	v_lshlrev_b32_e32 v40, 16, v37
	v_fmac_f32_e32 v39, v106, v34
	v_sub_f32_e32 v34, v59, v97
	v_and_b32_e32 v0, 0xffff0000, v35
	v_cndmask_b32_e32 v92, 0, v40, vcc
	v_fma_f32 v40, v107, v34, v97
	v_sub_f32_e32 v34, v113, v97
	v_cndmask_b32_e32 v0, 0, v0, vcc
	v_fmac_f32_e32 v40, v108, v34
	v_sub_f32_e32 v34, v58, v96
	v_lshlrev_b32_e32 v35, 16, v36
	v_and_b32_e32 v36, 0xffff0000, v36
	v_fma_f32 v41, v111, v34, v96
	v_sub_f32_e32 v34, v0, v96
	v_and_b32_e32 v37, 0xffff0000, v37
	v_cndmask_b32_e32 v95, 0, v36, vcc
	v_cndmask_b32_e32 v94, 0, v35, vcc
	v_fmac_f32_e32 v41, v112, v34
	v_pk_add_f32 v[34:35], v[42:43], v[88:89] neg_lo:[0,1] neg_hi:[0,1]
	v_cndmask_b32_e32 v93, 0, v37, vcc
	v_pk_fma_f32 v[34:35], v[68:69], v[34:35], v[88:89]
	v_pk_add_f32 v[36:37], v[94:95], v[88:89] neg_lo:[0,1] neg_hi:[0,1]
	v_pk_add_f32 v[42:43], v[92:93], v[90:91] neg_lo:[0,1] neg_hi:[0,1]
	v_pk_fma_f32 v[34:35], v[70:71], v[36:37], v[34:35]
	v_pk_add_f32 v[36:37], v[46:47], v[90:91] neg_lo:[0,1] neg_hi:[0,1]
	s_and_b64 vcc, exec, s[44:45]
	v_pk_fma_f32 v[36:37], v[74:75], v[36:37], v[90:91]
	s_mov_b64 s[4:5], -1
	v_pk_fma_f32 v[36:37], v[76:77], v[42:43], v[36:37]
	s_cbranch_vccnz .LBB0_750
	v_mov_b32_e32 v50, 0xbfb8aa3b
	v_mov_b32_e32 v53, 0xc038aa3b
	v_cndmask_b32_e64 v50, v53, v50, s[38:39]
	v_cndmask_b32_e64 v51, 2.0, 1.0, s[38:39]
	v_cndmask_b32_e64 v52, -1.0, 0, s[38:39]
	v_mul_f32_e32 v42, v50, v38
	v_mul_f32_e32 v43, v50, v39
	v_mul_f32_e32 v44, v50, v40
	v_mul_f32_e32 v45, v50, v41
	v_mul_f32_e32 v46, v50, v34
	v_mul_f32_e32 v47, v50, v35
	v_mul_f32_e32 v48, v50, v36
	v_mul_f32_e32 v49, v50, v37
	v_exp_f32_e32 v42, v42
	v_exp_f32_e32 v43, v43
	v_exp_f32_e32 v44, v44
	v_exp_f32_e32 v45, v45
	v_exp_f32_e32 v46, v46
	v_exp_f32_e32 v47, v47
	v_exp_f32_e32 v48, v48
	v_exp_f32_e32 v49, v49
	v_add_f32_e32 v42, 1.0, v42
	v_add_f32_e32 v43, 1.0, v43
	v_add_f32_e32 v44, 1.0, v44
	v_add_f32_e32 v45, 1.0, v45
	v_add_f32_e32 v46, 1.0, v46
	v_add_f32_e32 v47, 1.0, v47
	v_add_f32_e32 v48, 1.0, v48
	v_add_f32_e32 v49, 1.0, v49
	v_rcp_f32_e32 v42, v42
	v_rcp_f32_e32 v43, v43
	v_rcp_f32_e32 v44, v44
	v_rcp_f32_e32 v45, v45
	v_rcp_f32_e32 v46, v46
	v_rcp_f32_e32 v47, v47
	v_rcp_f32_e32 v48, v48
	v_rcp_f32_e32 v49, v49
	v_fma_f32 v42, v42, v51, v52
	v_fma_f32 v43, v43, v51, v52
	v_fma_f32 v44, v44, v51, v52
	v_fma_f32 v45, v45, v51, v52
	v_fma_f32 v46, v46, v51, v52
	v_fma_f32 v47, v47, v51, v52
	v_fma_f32 v48, v48, v51, v52
	v_fma_f32 v49, v49, v51, v52
	v_cndmask_b32_e64 v42, v42, v38, s[40:41]
	v_cndmask_b32_e64 v43, v43, v39, s[40:41]
	v_cndmask_b32_e64 v44, v44, v40, s[40:41]
	v_cndmask_b32_e64 v45, v45, v41, s[40:41]
	v_cndmask_b32_e64 v46, v46, v34, s[40:41]
	v_cndmask_b32_e64 v47, v47, v35, s[40:41]
	v_cndmask_b32_e64 v48, v48, v36, s[40:41]
	v_cndmask_b32_e64 v49, v49, v37, s[40:41]
	v_cvt_pk_bf16_f32 v42, v42, v43
	v_cvt_pk_bf16_f32 v43, v44, v45
	v_cvt_pk_bf16_f32 v44, v46, v47
	v_lshl_add_u64 v[46:47], s[50:51], 0, v[82:83]
	v_add_co_u32_e32 v46, vcc, 0x36201000, v46
	s_mov_b64 s[4:5], 0
	s_nop 0
	v_addc_co_u32_e32 v47, vcc, 0, v47, vcc
	v_cvt_pk_bf16_f32 v45, v48, v49
	global_store_dwordx4 v[46:47], v[42:45], off offset:1280 sc1
.LBB0_750:
	s_and_b64 vcc, exec, s[4:5]
	s_cbranch_vccz .LBB0_454
	v_add_co_u32_e32 v46, vcc, 0x2e20e000, v62
	v_cvt_pk_bf16_f32 v42, v38, v39
	v_cvt_pk_bf16_f32 v43, v40, v41
	v_cvt_pk_bf16_f32 v44, v34, v35
	v_cvt_pk_bf16_f32 v45, v36, v37
	s_nop 1
	v_addc_co_u32_e32 v47, vcc, 0, v63, vcc
	s_and_b64 vcc, exec, s[42:43]
	global_store_dwordx4 v[46:47], v[42:45], off sc1
	s_cbranch_vccnz .LBB0_454
	s_nop 0
	v_mul_f32_e32 v43, v103, v39
	v_mul_f32_e32 v42, v104, v38
	v_mul_f32_e32 v44, v43, v43
	v_fmac_f32_e32 v44, v42, v42
	v_mul_f32_e32 v40, v110, v40
	v_fmac_f32_e32 v44, v40, v40
	v_mul_f32_e32 v41, v109, v41
	v_pk_mul_f32 v[34:35], v[72:73], v[34:35]
	v_fmac_f32_e32 v44, v41, v41
	v_pk_mul_f32 v[38:39], v[34:35], v[34:35]
	v_pk_mul_f32 v[36:37], v[78:79], v[36:37]
	v_add_f32_e32 v38, v38, v44
	v_add_f32_e32 v44, v39, v38
	v_pk_mul_f32 v[38:39], v[36:37], v[36:37]
	s_nop 0
	v_add_f32_e32 v38, v38, v44
	v_and_b32_e32 v44, 64, v226
	v_add_f32_e32 v38, v39, v38
	v_xor_b32_e32 v39, 1, v226
	v_add_u32_e32 v44, 64, v44
	v_cmp_lt_i32_e32 vcc, v39, v44
	s_nop 1
	v_cndmask_b32_e32 v39, v226, v39, vcc
	v_lshlrev_b32_e32 v39, 2, v39
	ds_bpermute_b32 v39, v39, v38
	s_waitcnt lgkmcnt(0)
	v_add_f32_e32 v38, v38, v39
	v_xor_b32_e32 v39, 2, v226
	v_cmp_lt_i32_e32 vcc, v39, v44
	s_nop 1
	v_cndmask_b32_e32 v39, v226, v39, vcc
	v_lshlrev_b32_e32 v39, 2, v39
	ds_bpermute_b32 v39, v39, v38
	s_waitcnt lgkmcnt(0)
	v_add_f32_e32 v38, v38, v39
	v_xor_b32_e32 v39, 4, v226
	v_cmp_lt_i32_e32 vcc, v39, v44
	s_nop 1
	v_cndmask_b32_e32 v39, v226, v39, vcc
	v_lshlrev_b32_e32 v39, 2, v39
	ds_bpermute_b32 v39, v39, v38
	s_waitcnt lgkmcnt(0)
	v_add_f32_e32 v38, v38, v39
	v_mul_f32_e32 v39, 0x4f800000, v38
	v_cmp_gt_f32_e32 vcc, s82, v38
	s_nop 1
	v_cndmask_b32_e32 v38, v38, v39, vcc
	v_sqrt_f32_e32 v39, v38
	s_nop 0
	v_add_u32_e32 v44, -1, v39
	v_fma_f32 v45, -v44, v39, v38
	v_cmp_ge_f32_e64 s[42:43], 0, v45
	v_add_u32_e32 v45, 1, v39
	s_nop 0
	v_cndmask_b32_e64 v44, v39, v44, s[42:43]
	v_fma_f32 v39, -v45, v39, v38
	v_cmp_lt_f32_e64 s[42:43], 0, v39
	s_nop 1
	v_cndmask_b32_e64 v39, v44, v45, s[42:43]
	v_mul_f32_e32 v44, 0x37800000, v39
	v_cndmask_b32_e32 v39, v39, v44, vcc
	v_cmp_class_f32_e32 vcc, v38, v229
	s_nop 1
	v_cndmask_b32_e32 v38, v39, v38, vcc
	v_max_f32_e32 v38, 0x2b8cbccc, v38
	v_div_scale_f32 v39, s[4:5], v38, v38, 1.0
	v_rcp_f32_e32 v44, v39
	s_nop 0
	v_fma_f32 v45, -v39, v44, 1.0
	v_fmac_f32_e32 v44, v45, v44
	v_div_scale_f32 v45, vcc, 1.0, v38, 1.0
	v_mul_f32_e32 v46, v45, v44
	v_fma_f32 v47, -v39, v46, v45
	v_fmac_f32_e32 v46, v47, v44
	v_fma_f32 v39, -v39, v46, v45
	v_div_fmas_f32 v39, v39, v44, v46
	v_div_fixup_f32 v38, v39, v38, 1.0
	v_mul_f32_e32 v39, v42, v38
	v_mul_f32_e32 v42, v43, v38
	v_mul_f32_e32 v40, v40, v38
	v_mul_f32_e32 v41, v41, v38
	v_mul_f32_e32 v43, v34, v38
	v_mul_f32_e32 v44, v35, v38
	v_mul_f32_e32 v45, v36, v38
	v_mul_f32_e32 v37, v37, v38
	v_cvt_pk_bf16_f32 v34, v39, v42
	v_lshl_add_u64 v[38:39], s[50:51], 0, v[84:85]
	v_add_co_u32_e32 v38, vcc, 0x2e20f000, v38
	v_cvt_pk_bf16_f32 v35, v40, v41
	v_cvt_pk_bf16_f32 v36, v43, v44
	v_cvt_pk_bf16_f32 v37, v45, v37
	s_nop 1
	v_addc_co_u32_e32 v39, vcc, 0, v39, vcc
	global_store_dwordx4 v[38:39], v[34:37], off offset:2048 sc1
	s_branch .LBB0_454

.LBB0_830:
	s_lshl_b32 s4, s70, 8
	s_add_i32 s4, s4, s20
	v_and_or_b32 v155, v155, 15, s4
	v_cvt_pk_bf16_f32 v134, v134, v135
	v_cvt_pk_bf16_f32 v135, v136, v137
	v_cvt_pk_bf16_f32 v136, v130, v131
	v_mov_b64_e32 v[130:131], s[50:51]
	v_mad_i64_i32 v[130:131], s[4:5], v155, s95, v[130:131]
	v_lshl_add_u64 v[130:131], v[150:151], 1, v[130:131]
	v_cvt_pk_bf16_f32 v137, v132, v133
	global_store_dwordx4 v[130:131], v[134:137], off sc1
	v_pk_add_f32 v[128:129], v[128:129], v[112:113]
	v_pk_add_f32 v[126:127], v[126:127], v[110:111]
	v_pk_add_f32 v[124:125], v[124:125], v[108:109]
	s_and_b64 vcc, exec, s[42:43]
	v_pk_add_f32 v[122:123], v[122:123], v[106:107]
	s_cbranch_vccnz .LBB0_832
	v_mul_f32_e32 v126, 0xbfb8aa3b, v126
	v_mul_f32_e32 v122, 0xbfb8aa3b, v122
	v_exp_f32_e32 v126, v126
	v_exp_f32_e32 v122, v122
	v_mul_f32_e32 v127, 0xbfb8aa3b, v127
	v_mul_f32_e32 v123, 0xbfb8aa3b, v123
	v_add_f32_e32 v126, 1.0, v126
	v_add_f32_e32 v122, 1.0, v122
	v_rcp_f32_e32 v126, v126
	v_rcp_f32_e32 v122, v122
	v_exp_f32_e32 v127, v127
	v_exp_f32_e32 v123, v123
	v_mul_f32_e32 v132, 0xbf60028e, v126
	v_mul_f32_e32 v133, 0xbf60028e, v122
	v_add_f32_e32 v127, 1.0, v127
	v_add_f32_e32 v123, 1.0, v123
	v_mul_f32_e32 v128, 0xbfb8aa3b, v128
	v_mul_f32_e32 v124, 0xbfb8aa3b, v124
	v_exp_f32_e32 v132, v132
	v_exp_f32_e32 v133, v133
	v_rcp_f32_e32 v127, v127
	v_rcp_f32_e32 v123, v123
	v_exp_f32_e32 v128, v128
	v_exp_f32_e32 v124, v124
	v_cndmask_b32_e64 v126, v126, v132, s[40:41]
	v_cndmask_b32_e64 v122, v122, v133, s[40:41]
	v_mul_f32_e32 v132, 0xbf60028e, v127
	v_mul_f32_e32 v133, 0xbf60028e, v123
	v_add_f32_e32 v128, 1.0, v128
	v_add_f32_e32 v124, 1.0, v124
	v_mul_f32_e32 v129, 0xbfb8aa3b, v129
	v_mul_f32_e32 v125, 0xbfb8aa3b, v125
	v_exp_f32_e32 v132, v132
	v_exp_f32_e32 v133, v133
	v_rcp_f32_e32 v128, v128
	v_rcp_f32_e32 v124, v124
	v_exp_f32_e32 v129, v129
	v_exp_f32_e32 v125, v125
	v_cndmask_b32_e64 v127, v127, v132, s[40:41]
	v_cndmask_b32_e64 v123, v123, v133, s[40:41]
	v_mul_f32_e32 v132, 0xbf60028e, v128
	v_mul_f32_e32 v133, 0xbf60028e, v124
	v_add_f32_e32 v129, 1.0, v129
	v_add_f32_e32 v125, 1.0, v125
	v_exp_f32_e32 v132, v132
	v_exp_f32_e32 v133, v133
	v_rcp_f32_e32 v129, v129
	v_rcp_f32_e32 v125, v125
	v_cndmask_b32_e64 v128, v128, v132, s[40:41]
	v_cndmask_b32_e64 v124, v124, v133, s[40:41]
	v_mul_f32_e32 v132, 0xbf60028e, v129
	v_mul_f32_e32 v133, 0xbf60028e, v125
	v_exp_f32_e32 v132, v132
	v_exp_f32_e32 v133, v133
	v_cndmask_b32_e64 v129, v129, v132, s[40:41]
	v_cndmask_b32_e64 v125, v125, v133, s[40:41]
.LBB0_832:
	v_cvt_pk_bf16_f32 v126, v126, v127
	v_cvt_pk_bf16_f32 v127, v128, v129
	v_cvt_pk_bf16_f32 v128, v122, v123
	v_cvt_pk_bf16_f32 v129, v124, v125
	v_or_b32_e32 v124, 16, v155
	v_mov_b64_e32 v[122:123], s[50:51]
	v_mad_i64_i32 v[122:123], s[4:5], v124, s95, v[122:123]
	v_lshl_add_u64 v[122:123], v[150:151], 1, v[122:123]
	global_store_dwordx4 v[122:123], v[126:129], off sc1
	v_pk_add_f32 v[120:121], v[120:121], v[112:113]
	v_pk_add_f32 v[118:119], v[118:119], v[110:111]
	v_pk_add_f32 v[116:117], v[116:117], v[108:109]
	s_and_b64 vcc, exec, s[42:43]
	v_pk_add_f32 v[114:115], v[114:115], v[106:107]
	s_cbranch_vccnz .LBB0_834
	v_mul_f32_e32 v118, 0xbfb8aa3b, v118
	v_mul_f32_e32 v114, 0xbfb8aa3b, v114
	v_exp_f32_e32 v118, v118
	v_exp_f32_e32 v114, v114
	v_mul_f32_e32 v119, 0xbfb8aa3b, v119
	v_mul_f32_e32 v115, 0xbfb8aa3b, v115
	v_add_f32_e32 v118, 1.0, v118
	v_add_f32_e32 v114, 1.0, v114
	v_rcp_f32_e32 v118, v118
	v_rcp_f32_e32 v114, v114
	v_exp_f32_e32 v119, v119
	v_exp_f32_e32 v115, v115
	v_mul_f32_e32 v124, 0xbf60028e, v118
	v_mul_f32_e32 v125, 0xbf60028e, v114
	v_add_f32_e32 v119, 1.0, v119
	v_add_f32_e32 v115, 1.0, v115
	v_mul_f32_e32 v120, 0xbfb8aa3b, v120
	v_mul_f32_e32 v116, 0xbfb8aa3b, v116
	v_exp_f32_e32 v124, v124
	v_exp_f32_e32 v125, v125
	v_rcp_f32_e32 v119, v119
	v_rcp_f32_e32 v115, v115
	v_exp_f32_e32 v120, v120
	v_exp_f32_e32 v116, v116
	v_cndmask_b32_e64 v118, v118, v124, s[40:41]
	v_cndmask_b32_e64 v114, v114, v125, s[40:41]
	v_mul_f32_e32 v124, 0xbf60028e, v119
	v_mul_f32_e32 v125, 0xbf60028e, v115
	v_add_f32_e32 v120, 1.0, v120
	v_add_f32_e32 v116, 1.0, v116
	v_mul_f32_e32 v121, 0xbfb8aa3b, v121
	v_mul_f32_e32 v117, 0xbfb8aa3b, v117
	v_exp_f32_e32 v124, v124
	v_exp_f32_e32 v125, v125
	v_rcp_f32_e32 v120, v120
	v_rcp_f32_e32 v116, v116
	v_exp_f32_e32 v121, v121
	v_exp_f32_e32 v117, v117
	v_cndmask_b32_e64 v119, v119, v124, s[40:41]
	v_cndmask_b32_e64 v115, v115, v125, s[40:41]
	v_mul_f32_e32 v124, 0xbf60028e, v120
	v_mul_f32_e32 v125, 0xbf60028e, v116
	v_add_f32_e32 v121, 1.0, v121
	v_add_f32_e32 v117, 1.0, v117
	v_exp_f32_e32 v124, v124
	v_exp_f32_e32 v125, v125
	v_rcp_f32_e32 v121, v121
	v_rcp_f32_e32 v117, v117
	v_cndmask_b32_e64 v120, v120, v124, s[40:41]
	v_cndmask_b32_e64 v116, v116, v125, s[40:41]
	v_mul_f32_e32 v124, 0xbf60028e, v121
	v_mul_f32_e32 v125, 0xbf60028e, v117
	v_exp_f32_e32 v124, v124
	v_exp_f32_e32 v125, v125
	v_cndmask_b32_e64 v121, v121, v124, s[40:41]
	v_cndmask_b32_e64 v117, v117, v125, s[40:41]
.LBB0_834:
	v_cvt_pk_bf16_f32 v118, v118, v119
	v_cvt_pk_bf16_f32 v119, v120, v121
	v_cvt_pk_bf16_f32 v120, v114, v115
	v_cvt_pk_bf16_f32 v121, v116, v117
	v_or_b32_e32 v116, 32, v155
	v_mov_b64_e32 v[114:115], s[50:51]
	v_mad_i64_i32 v[114:115], s[4:5], v116, s95, v[114:115]
	v_lshl_add_u64 v[114:115], v[150:151], 1, v[114:115]
	global_store_dwordx4 v[114:115], v[118:121], off sc1
	v_pk_add_f32 v[104:105], v[104:105], v[112:113]
	v_pk_add_f32 v[102:103], v[102:103], v[110:111]
	v_pk_add_f32 v[100:101], v[100:101], v[108:109]
	s_and_b64 vcc, exec, s[42:43]
	v_pk_add_f32 v[98:99], v[98:99], v[106:107]
	s_cbranch_vccnz .LBB0_836
	v_mul_f32_e32 v102, 0xbfb8aa3b, v102
	v_mul_f32_e32 v98, 0xbfb8aa3b, v98
	v_exp_f32_e32 v102, v102
	v_exp_f32_e32 v98, v98
	v_mul_f32_e32 v103, 0xbfb8aa3b, v103
	v_mul_f32_e32 v99, 0xbfb8aa3b, v99
	v_add_f32_e32 v102, 1.0, v102
	v_add_f32_e32 v98, 1.0, v98
	v_rcp_f32_e32 v102, v102
	v_rcp_f32_e32 v98, v98
	v_exp_f32_e32 v103, v103
	v_exp_f32_e32 v99, v99
	v_mul_f32_e32 v116, 0xbf60028e, v102
	v_mul_f32_e32 v117, 0xbf60028e, v98
	v_add_f32_e32 v103, 1.0, v103
	v_add_f32_e32 v99, 1.0, v99
	v_mul_f32_e32 v104, 0xbfb8aa3b, v104
	v_mul_f32_e32 v100, 0xbfb8aa3b, v100
	v_exp_f32_e32 v116, v116
	v_exp_f32_e32 v117, v117
	v_rcp_f32_e32 v103, v103
	v_rcp_f32_e32 v99, v99
	v_exp_f32_e32 v104, v104
	v_exp_f32_e32 v100, v100
	v_cndmask_b32_e64 v102, v102, v116, s[40:41]
	v_cndmask_b32_e64 v98, v98, v117, s[40:41]
	v_mul_f32_e32 v116, 0xbf60028e, v103
	v_mul_f32_e32 v117, 0xbf60028e, v99
	v_add_f32_e32 v104, 1.0, v104
	v_add_f32_e32 v100, 1.0, v100
	v_mul_f32_e32 v105, 0xbfb8aa3b, v105
	v_mul_f32_e32 v101, 0xbfb8aa3b, v101
	v_exp_f32_e32 v116, v116
	v_exp_f32_e32 v117, v117
	v_rcp_f32_e32 v104, v104
	v_rcp_f32_e32 v100, v100
	v_exp_f32_e32 v105, v105
	v_exp_f32_e32 v101, v101
	v_cndmask_b32_e64 v103, v103, v116, s[40:41]
	v_cndmask_b32_e64 v99, v99, v117, s[40:41]
	v_mul_f32_e32 v116, 0xbf60028e, v104
	v_mul_f32_e32 v117, 0xbf60028e, v100
	v_add_f32_e32 v105, 1.0, v105
	v_add_f32_e32 v101, 1.0, v101
	v_exp_f32_e32 v116, v116
	v_exp_f32_e32 v117, v117
	v_rcp_f32_e32 v105, v105
	v_rcp_f32_e32 v101, v101
	v_cndmask_b32_e64 v104, v104, v116, s[40:41]
	v_cndmask_b32_e64 v100, v100, v117, s[40:41]
	v_mul_f32_e32 v116, 0xbf60028e, v105
	v_mul_f32_e32 v117, 0xbf60028e, v101
	v_exp_f32_e32 v116, v116
	v_exp_f32_e32 v117, v117
	v_cndmask_b32_e64 v105, v105, v116, s[40:41]
	v_cndmask_b32_e64 v101, v101, v117, s[40:41]
.LBB0_836:
	v_cvt_pk_bf16_f32 v102, v102, v103
	v_cvt_pk_bf16_f32 v103, v104, v105
	v_cvt_pk_bf16_f32 v104, v98, v99
	v_cvt_pk_bf16_f32 v105, v100, v101
	v_or_b32_e32 v100, 48, v155
	v_mov_b64_e32 v[98:99], s[50:51]
	v_mad_i64_i32 v[98:99], s[4:5], v100, s95, v[98:99]
	v_lshl_add_u64 v[98:99], v[150:151], 1, v[98:99]
	global_store_dwordx4 v[98:99], v[102:105], off sc1
	v_pk_add_f32 v[96:97], v[96:97], v[112:113]
	v_pk_add_f32 v[94:95], v[94:95], v[110:111]
	v_pk_add_f32 v[92:93], v[92:93], v[108:109]
	s_and_b64 vcc, exec, s[42:43]
	v_pk_add_f32 v[90:91], v[90:91], v[106:107]
	s_cbranch_vccnz .LBB0_838
	v_mul_f32_e32 v94, 0xbfb8aa3b, v94
	v_mul_f32_e32 v90, 0xbfb8aa3b, v90
	v_exp_f32_e32 v94, v94
	v_exp_f32_e32 v90, v90
	v_mul_f32_e32 v95, 0xbfb8aa3b, v95
	v_mul_f32_e32 v91, 0xbfb8aa3b, v91
	v_add_f32_e32 v94, 1.0, v94
	v_add_f32_e32 v90, 1.0, v90
	v_rcp_f32_e32 v94, v94
	v_rcp_f32_e32 v90, v90
	v_exp_f32_e32 v95, v95
	v_exp_f32_e32 v91, v91
	v_mul_f32_e32 v100, 0xbf60028e, v94
	v_mul_f32_e32 v101, 0xbf60028e, v90
	v_add_f32_e32 v95, 1.0, v95
	v_add_f32_e32 v91, 1.0, v91
	v_mul_f32_e32 v96, 0xbfb8aa3b, v96
	v_mul_f32_e32 v92, 0xbfb8aa3b, v92
	v_exp_f32_e32 v100, v100
	v_exp_f32_e32 v101, v101
	v_rcp_f32_e32 v95, v95
	v_rcp_f32_e32 v91, v91
	v_exp_f32_e32 v96, v96
	v_exp_f32_e32 v92, v92
	v_cndmask_b32_e64 v94, v94, v100, s[40:41]
	v_cndmask_b32_e64 v90, v90, v101, s[40:41]
	v_mul_f32_e32 v100, 0xbf60028e, v95
	v_mul_f32_e32 v101, 0xbf60028e, v91
	v_add_f32_e32 v96, 1.0, v96
	v_add_f32_e32 v92, 1.0, v92
	v_mul_f32_e32 v97, 0xbfb8aa3b, v97
	v_mul_f32_e32 v93, 0xbfb8aa3b, v93
	v_exp_f32_e32 v100, v100
	v_exp_f32_e32 v101, v101
	v_rcp_f32_e32 v96, v96
	v_rcp_f32_e32 v92, v92
	v_exp_f32_e32 v97, v97
	v_exp_f32_e32 v93, v93
	v_cndmask_b32_e64 v95, v95, v100, s[40:41]
	v_cndmask_b32_e64 v91, v91, v101, s[40:41]
	v_mul_f32_e32 v100, 0xbf60028e, v96
	v_mul_f32_e32 v101, 0xbf60028e, v92
	v_add_f32_e32 v97, 1.0, v97
	v_add_f32_e32 v93, 1.0, v93
	v_exp_f32_e32 v100, v100
	v_exp_f32_e32 v101, v101
	v_rcp_f32_e32 v97, v97
	v_rcp_f32_e32 v93, v93
	v_cndmask_b32_e64 v96, v96, v100, s[40:41]
	v_cndmask_b32_e64 v92, v92, v101, s[40:41]
	v_mul_f32_e32 v100, 0xbf60028e, v97
	v_mul_f32_e32 v101, 0xbf60028e, v93
	v_exp_f32_e32 v100, v100
	v_exp_f32_e32 v101, v101
	v_cndmask_b32_e64 v97, v97, v100, s[40:41]
	v_cndmask_b32_e64 v93, v93, v101, s[40:41]
.LBB0_838:
	v_add_u32_e32 v100, 0x80, v155
	v_cvt_pk_bf16_f32 v94, v94, v95
	v_cvt_pk_bf16_f32 v95, v96, v97
	v_cvt_pk_bf16_f32 v96, v90, v91
	v_mov_b64_e32 v[90:91], s[50:51]
	v_mad_i64_i32 v[90:91], s[4:5], v100, s95, v[90:91]
	v_lshl_add_u64 v[90:91], v[150:151], 1, v[90:91]
	v_cvt_pk_bf16_f32 v97, v92, v93
	global_store_dwordx4 v[90:91], v[94:97], off sc1
	v_pk_add_f32 v[88:89], v[88:89], v[112:113]
	v_pk_add_f32 v[86:87], v[86:87], v[110:111]
	v_pk_add_f32 v[84:85], v[84:85], v[108:109]
	s_and_b64 vcc, exec, s[42:43]
	v_pk_add_f32 v[82:83], v[82:83], v[106:107]
	s_cbranch_vccnz .LBB0_840
	v_mul_f32_e32 v86, 0xbfb8aa3b, v86
	v_mul_f32_e32 v82, 0xbfb8aa3b, v82
	v_exp_f32_e32 v86, v86
	v_exp_f32_e32 v82, v82
	v_mul_f32_e32 v87, 0xbfb8aa3b, v87
	v_mul_f32_e32 v83, 0xbfb8aa3b, v83
	v_add_f32_e32 v86, 1.0, v86
	v_add_f32_e32 v82, 1.0, v82
	v_rcp_f32_e32 v86, v86
	v_rcp_f32_e32 v82, v82
	v_exp_f32_e32 v87, v87
	v_exp_f32_e32 v83, v83
	v_mul_f32_e32 v92, 0xbf60028e, v86
	v_mul_f32_e32 v93, 0xbf60028e, v82
	v_add_f32_e32 v87, 1.0, v87
	v_add_f32_e32 v83, 1.0, v83
	v_mul_f32_e32 v88, 0xbfb8aa3b, v88
	v_mul_f32_e32 v84, 0xbfb8aa3b, v84
	v_exp_f32_e32 v92, v92
	v_exp_f32_e32 v93, v93
	v_rcp_f32_e32 v87, v87
	v_rcp_f32_e32 v83, v83
	v_exp_f32_e32 v88, v88
	v_exp_f32_e32 v84, v84
	v_cndmask_b32_e64 v86, v86, v92, s[40:41]
	v_cndmask_b32_e64 v82, v82, v93, s[40:41]
	v_mul_f32_e32 v92, 0xbf60028e, v87
	v_mul_f32_e32 v93, 0xbf60028e, v83
	v_add_f32_e32 v88, 1.0, v88
	v_add_f32_e32 v84, 1.0, v84
	v_mul_f32_e32 v89, 0xbfb8aa3b, v89
	v_mul_f32_e32 v85, 0xbfb8aa3b, v85
	v_exp_f32_e32 v92, v92
	v_exp_f32_e32 v93, v93
	v_rcp_f32_e32 v88, v88
	v_rcp_f32_e32 v84, v84
	v_exp_f32_e32 v89, v89
	v_exp_f32_e32 v85, v85
	v_cndmask_b32_e64 v87, v87, v92, s[40:41]
	v_cndmask_b32_e64 v83, v83, v93, s[40:41]
	v_mul_f32_e32 v92, 0xbf60028e, v88
	v_mul_f32_e32 v93, 0xbf60028e, v84
	v_add_f32_e32 v89, 1.0, v89
	v_add_f32_e32 v85, 1.0, v85
	v_exp_f32_e32 v92, v92
	v_exp_f32_e32 v93, v93
	v_rcp_f32_e32 v89, v89
	v_rcp_f32_e32 v85, v85
	v_cndmask_b32_e64 v88, v88, v92, s[40:41]
	v_cndmask_b32_e64 v84, v84, v93, s[40:41]
	v_mul_f32_e32 v92, 0xbf60028e, v89
	v_mul_f32_e32 v93, 0xbf60028e, v85
	v_exp_f32_e32 v92, v92
	v_exp_f32_e32 v93, v93
	v_cndmask_b32_e64 v89, v89, v92, s[40:41]
	v_cndmask_b32_e64 v85, v85, v93, s[40:41]
.LBB0_840:
	v_cvt_pk_bf16_f32 v86, v86, v87
	v_cvt_pk_bf16_f32 v87, v88, v89
	v_cvt_pk_bf16_f32 v88, v82, v83
	v_cvt_pk_bf16_f32 v89, v84, v85
	v_add_u32_e32 v84, 0x90, v155
	v_mov_b64_e32 v[82:83], s[50:51]
	v_mad_i64_i32 v[82:83], s[4:5], v84, s95, v[82:83]
	v_lshl_add_u64 v[82:83], v[150:151], 1, v[82:83]
	global_store_dwordx4 v[82:83], v[86:89], off sc1
	v_pk_add_f32 v[80:81], v[80:81], v[112:113]
	v_pk_add_f32 v[78:79], v[78:79], v[110:111]
	v_pk_add_f32 v[76:77], v[76:77], v[108:109]
	s_and_b64 vcc, exec, s[42:43]
	v_pk_add_f32 v[74:75], v[74:75], v[106:107]
	s_cbranch_vccnz .LBB0_842
	v_mul_f32_e32 v78, 0xbfb8aa3b, v78
	v_mul_f32_e32 v74, 0xbfb8aa3b, v74
	v_exp_f32_e32 v78, v78
	v_exp_f32_e32 v74, v74
	v_mul_f32_e32 v79, 0xbfb8aa3b, v79
	v_mul_f32_e32 v75, 0xbfb8aa3b, v75
	v_add_f32_e32 v78, 1.0, v78
	v_add_f32_e32 v74, 1.0, v74
	v_rcp_f32_e32 v78, v78
	v_rcp_f32_e32 v74, v74
	v_exp_f32_e32 v79, v79
	v_exp_f32_e32 v75, v75
	v_mul_f32_e32 v84, 0xbf60028e, v78
	v_mul_f32_e32 v85, 0xbf60028e, v74
	v_add_f32_e32 v79, 1.0, v79
	v_add_f32_e32 v75, 1.0, v75
	v_mul_f32_e32 v80, 0xbfb8aa3b, v80
	v_mul_f32_e32 v76, 0xbfb8aa3b, v76
	v_exp_f32_e32 v84, v84
	v_exp_f32_e32 v85, v85
	v_rcp_f32_e32 v79, v79
	v_rcp_f32_e32 v75, v75
	v_exp_f32_e32 v80, v80
	v_exp_f32_e32 v76, v76
	v_cndmask_b32_e64 v78, v78, v84, s[40:41]
	v_cndmask_b32_e64 v74, v74, v85, s[40:41]
	v_mul_f32_e32 v84, 0xbf60028e, v79
	v_mul_f32_e32 v85, 0xbf60028e, v75
	v_add_f32_e32 v80, 1.0, v80
	v_add_f32_e32 v76, 1.0, v76
	v_mul_f32_e32 v81, 0xbfb8aa3b, v81
	v_mul_f32_e32 v77, 0xbfb8aa3b, v77
	v_exp_f32_e32 v84, v84
	v_exp_f32_e32 v85, v85
	v_rcp_f32_e32 v80, v80
	v_rcp_f32_e32 v76, v76
	v_exp_f32_e32 v81, v81
	v_exp_f32_e32 v77, v77
	v_cndmask_b32_e64 v79, v79, v84, s[40:41]
	v_cndmask_b32_e64 v75, v75, v85, s[40:41]
	v_mul_f32_e32 v84, 0xbf60028e, v80
	v_mul_f32_e32 v85, 0xbf60028e, v76
	v_add_f32_e32 v81, 1.0, v81
	v_add_f32_e32 v77, 1.0, v77
	v_exp_f32_e32 v84, v84
	v_exp_f32_e32 v85, v85
	v_rcp_f32_e32 v81, v81
	v_rcp_f32_e32 v77, v77
	v_cndmask_b32_e64 v80, v80, v84, s[40:41]
	v_cndmask_b32_e64 v76, v76, v85, s[40:41]
	v_mul_f32_e32 v84, 0xbf60028e, v81
	v_mul_f32_e32 v85, 0xbf60028e, v77
	v_exp_f32_e32 v84, v84
	v_exp_f32_e32 v85, v85
	v_cndmask_b32_e64 v81, v81, v84, s[40:41]
	v_cndmask_b32_e64 v77, v77, v85, s[40:41]
.LBB0_842:
	v_cvt_pk_bf16_f32 v78, v78, v79
	v_cvt_pk_bf16_f32 v79, v80, v81
	v_cvt_pk_bf16_f32 v80, v74, v75
	v_cvt_pk_bf16_f32 v81, v76, v77
	v_add_u32_e32 v76, 0xa0, v155
	v_mov_b64_e32 v[74:75], s[50:51]
	v_mad_i64_i32 v[74:75], s[4:5], v76, s95, v[74:75]
	v_lshl_add_u64 v[74:75], v[150:151], 1, v[74:75]
	global_store_dwordx4 v[74:75], v[78:81], off sc1
	v_pk_add_f32 v[72:73], v[72:73], v[112:113]
	v_pk_add_f32 v[70:71], v[70:71], v[110:111]
	v_pk_add_f32 v[68:69], v[68:69], v[108:109]
	s_and_b64 vcc, exec, s[42:43]
	v_pk_add_f32 v[66:67], v[66:67], v[106:107]
	s_cbranch_vccnz .LBB0_844
	v_mul_f32_e32 v70, 0xbfb8aa3b, v70
	v_mul_f32_e32 v66, 0xbfb8aa3b, v66
	v_exp_f32_e32 v70, v70
	v_exp_f32_e32 v66, v66
	v_mul_f32_e32 v71, 0xbfb8aa3b, v71
	v_mul_f32_e32 v67, 0xbfb8aa3b, v67
	v_add_f32_e32 v70, 1.0, v70
	v_add_f32_e32 v66, 1.0, v66
	v_rcp_f32_e32 v70, v70
	v_rcp_f32_e32 v66, v66
	v_exp_f32_e32 v71, v71
	v_exp_f32_e32 v67, v67
	v_mul_f32_e32 v76, 0xbf60028e, v70
	v_mul_f32_e32 v77, 0xbf60028e, v66
	v_add_f32_e32 v71, 1.0, v71
	v_add_f32_e32 v67, 1.0, v67
	v_mul_f32_e32 v72, 0xbfb8aa3b, v72
	v_mul_f32_e32 v68, 0xbfb8aa3b, v68
	v_exp_f32_e32 v76, v76
	v_exp_f32_e32 v77, v77
	v_rcp_f32_e32 v71, v71
	v_rcp_f32_e32 v67, v67
	v_exp_f32_e32 v72, v72
	v_exp_f32_e32 v68, v68
	v_cndmask_b32_e64 v70, v70, v76, s[40:41]
	v_cndmask_b32_e64 v66, v66, v77, s[40:41]
	v_mul_f32_e32 v76, 0xbf60028e, v71
	v_mul_f32_e32 v77, 0xbf60028e, v67
	v_add_f32_e32 v72, 1.0, v72
	v_add_f32_e32 v68, 1.0, v68
	v_mul_f32_e32 v73, 0xbfb8aa3b, v73
	v_mul_f32_e32 v69, 0xbfb8aa3b, v69
	v_exp_f32_e32 v76, v76
	v_exp_f32_e32 v77, v77
	v_rcp_f32_e32 v72, v72
	v_rcp_f32_e32 v68, v68
	v_exp_f32_e32 v73, v73
	v_exp_f32_e32 v69, v69
	v_cndmask_b32_e64 v71, v71, v76, s[40:41]
	v_cndmask_b32_e64 v67, v67, v77, s[40:41]
	v_mul_f32_e32 v76, 0xbf60028e, v72
	v_mul_f32_e32 v77, 0xbf60028e, v68
	v_add_f32_e32 v73, 1.0, v73
	v_add_f32_e32 v69, 1.0, v69
	v_exp_f32_e32 v76, v76
	v_exp_f32_e32 v77, v77
	v_rcp_f32_e32 v73, v73
	v_rcp_f32_e32 v69, v69
	v_cndmask_b32_e64 v72, v72, v76, s[40:41]
	v_cndmask_b32_e64 v68, v68, v77, s[40:41]
	v_mul_f32_e32 v76, 0xbf60028e, v73
	v_mul_f32_e32 v77, 0xbf60028e, v69
	v_exp_f32_e32 v76, v76
	v_exp_f32_e32 v77, v77
	v_cndmask_b32_e64 v73, v73, v76, s[40:41]
	v_cndmask_b32_e64 v69, v69, v77, s[40:41]
.LBB0_844:
	v_cvt_pk_bf16_f32 v70, v70, v71
	v_cvt_pk_bf16_f32 v71, v72, v73
	v_cvt_pk_bf16_f32 v72, v66, v67
	v_cvt_pk_bf16_f32 v73, v68, v69
	v_add_u32_e32 v68, 0xb0, v155
	v_mov_b64_e32 v[66:67], s[50:51]
	v_mad_i64_i32 v[66:67], s[4:5], v68, s95, v[66:67]
	v_lshl_add_u64 v[76:77], v[150:151], 1, v[66:67]
	global_store_dwordx4 v[76:77], v[70:73], off sc1
	s_nop 1
	v_mov_b32_e32 v70, 0
	s_and_b64 vcc, exec, s[42:43]
	v_mov_b32_e32 v71, v70
	v_mov_b32_e32 v72, v70
	v_mov_b32_e32 v73, v70
	v_mov_b32_e32 v66, v70
	v_mov_b32_e32 v67, v70
	v_mov_b32_e32 v68, v70
	v_mov_b32_e32 v69, v70
	s_cbranch_vccnz .LBB0_846
	global_load_dwordx4 v[70:73], v[148:149], off offset:512
	global_load_dwordx4 v[66:69], v[148:149], off offset:528

.LBB0_848:
	v_cvt_pk_bf16_f32 v62, v62, v63
	v_cvt_pk_bf16_f32 v63, v64, v65
	v_cvt_pk_bf16_f32 v64, v58, v59
	v_cvt_pk_bf16_f32 v65, v60, v61
	global_store_dwordx4 v[130:131], v[62:65], off offset:256 sc1
	v_pk_add_f32 v[56:57], v[56:57], v[72:73]
	v_pk_add_f32 v[54:55], v[54:55], v[70:71]
	v_pk_add_f32 v[52:53], v[52:53], v[68:69]
	s_and_b64 vcc, exec, s[42:43]
	v_pk_add_f32 v[50:51], v[50:51], v[66:67]
	s_cbranch_vccnz .LBB0_850
	v_mul_f32_e32 v54, 0xbfb8aa3b, v54
	v_mul_f32_e32 v50, 0xbfb8aa3b, v50
	v_exp_f32_e32 v54, v54
	v_exp_f32_e32 v50, v50
	v_mul_f32_e32 v55, 0xbfb8aa3b, v55
	v_mul_f32_e32 v51, 0xbfb8aa3b, v51
	v_add_f32_e32 v54, 1.0, v54
	v_add_f32_e32 v50, 1.0, v50
	v_rcp_f32_e32 v54, v54
	v_rcp_f32_e32 v50, v50
	v_exp_f32_e32 v55, v55
	v_exp_f32_e32 v51, v51
	v_mul_f32_e32 v58, 0xbf60028e, v54
	v_mul_f32_e32 v59, 0xbf60028e, v50
	v_add_f32_e32 v55, 1.0, v55
	v_add_f32_e32 v51, 1.0, v51
	v_mul_f32_e32 v56, 0xbfb8aa3b, v56
	v_mul_f32_e32 v52, 0xbfb8aa3b, v52
	v_exp_f32_e32 v58, v58
	v_exp_f32_e32 v59, v59
	v_rcp_f32_e32 v55, v55
	v_rcp_f32_e32 v51, v51
	v_exp_f32_e32 v56, v56
	v_exp_f32_e32 v52, v52
	v_cndmask_b32_e64 v54, v54, v58, s[40:41]
	v_cndmask_b32_e64 v50, v50, v59, s[40:41]
	v_mul_f32_e32 v58, 0xbf60028e, v55
	v_mul_f32_e32 v59, 0xbf60028e, v51
	v_add_f32_e32 v56, 1.0, v56
	v_add_f32_e32 v52, 1.0, v52
	v_mul_f32_e32 v57, 0xbfb8aa3b, v57
	v_mul_f32_e32 v53, 0xbfb8aa3b, v53
	v_exp_f32_e32 v58, v58
	v_exp_f32_e32 v59, v59
	v_rcp_f32_e32 v56, v56
	v_rcp_f32_e32 v52, v52
	v_exp_f32_e32 v57, v57
	v_exp_f32_e32 v53, v53
	v_cndmask_b32_e64 v55, v55, v58, s[40:41]
	v_cndmask_b32_e64 v51, v51, v59, s[40:41]
	v_mul_f32_e32 v58, 0xbf60028e, v56
	v_mul_f32_e32 v59, 0xbf60028e, v52
	v_add_f32_e32 v57, 1.0, v57
	v_add_f32_e32 v53, 1.0, v53
	v_exp_f32_e32 v58, v58
	v_exp_f32_e32 v59, v59
	v_rcp_f32_e32 v57, v57
	v_rcp_f32_e32 v53, v53
	v_cndmask_b32_e64 v56, v56, v58, s[40:41]
	v_cndmask_b32_e64 v52, v52, v59, s[40:41]
	v_mul_f32_e32 v58, 0xbf60028e, v57
	v_mul_f32_e32 v59, 0xbf60028e, v53
	v_exp_f32_e32 v58, v58
	v_exp_f32_e32 v59, v59
	v_cndmask_b32_e64 v57, v57, v58, s[40:41]
	v_cndmask_b32_e64 v53, v53, v59, s[40:41]
.LBB0_850:
	v_cvt_pk_bf16_f32 v54, v54, v55
	v_cvt_pk_bf16_f32 v55, v56, v57
	v_cvt_pk_bf16_f32 v56, v50, v51
	v_cvt_pk_bf16_f32 v57, v52, v53
	global_store_dwordx4 v[122:123], v[54:57], off offset:256 sc1
	v_pk_add_f32 v[48:49], v[48:49], v[72:73]
	v_pk_add_f32 v[46:47], v[46:47], v[70:71]
	v_pk_add_f32 v[44:45], v[44:45], v[68:69]
	s_and_b64 vcc, exec, s[42:43]
	v_pk_add_f32 v[42:43], v[42:43], v[66:67]
	s_cbranch_vccnz .LBB0_852
	v_mul_f32_e32 v46, 0xbfb8aa3b, v46
	v_mul_f32_e32 v42, 0xbfb8aa3b, v42
	v_exp_f32_e32 v46, v46
	v_exp_f32_e32 v42, v42
	v_mul_f32_e32 v47, 0xbfb8aa3b, v47
	v_mul_f32_e32 v43, 0xbfb8aa3b, v43
	v_add_f32_e32 v46, 1.0, v46
	v_add_f32_e32 v42, 1.0, v42
	v_rcp_f32_e32 v46, v46
	v_rcp_f32_e32 v42, v42
	v_exp_f32_e32 v47, v47
	v_exp_f32_e32 v43, v43
	v_mul_f32_e32 v50, 0xbf60028e, v46
	v_mul_f32_e32 v51, 0xbf60028e, v42
	v_add_f32_e32 v47, 1.0, v47
	v_add_f32_e32 v43, 1.0, v43
	v_mul_f32_e32 v48, 0xbfb8aa3b, v48
	v_mul_f32_e32 v44, 0xbfb8aa3b, v44
	v_exp_f32_e32 v50, v50
	v_exp_f32_e32 v51, v51
	v_rcp_f32_e32 v47, v47
	v_rcp_f32_e32 v43, v43
	v_exp_f32_e32 v48, v48
	v_exp_f32_e32 v44, v44
	v_cndmask_b32_e64 v46, v46, v50, s[40:41]
	v_cndmask_b32_e64 v42, v42, v51, s[40:41]
	v_mul_f32_e32 v50, 0xbf60028e, v47
	v_mul_f32_e32 v51, 0xbf60028e, v43
	v_add_f32_e32 v48, 1.0, v48
	v_add_f32_e32 v44, 1.0, v44
	v_mul_f32_e32 v49, 0xbfb8aa3b, v49
	v_mul_f32_e32 v45, 0xbfb8aa3b, v45
	v_exp_f32_e32 v50, v50
	v_exp_f32_e32 v51, v51
	v_rcp_f32_e32 v48, v48
	v_rcp_f32_e32 v44, v44
	v_exp_f32_e32 v49, v49
	v_exp_f32_e32 v45, v45
	v_cndmask_b32_e64 v47, v47, v50, s[40:41]
	v_cndmask_b32_e64 v43, v43, v51, s[40:41]
	v_mul_f32_e32 v50, 0xbf60028e, v48
	v_mul_f32_e32 v51, 0xbf60028e, v44
	v_add_f32_e32 v49, 1.0, v49
	v_add_f32_e32 v45, 1.0, v45
	v_exp_f32_e32 v50, v50
	v_exp_f32_e32 v51, v51
	v_rcp_f32_e32 v49, v49
	v_rcp_f32_e32 v45, v45
	v_cndmask_b32_e64 v48, v48, v50, s[40:41]
	v_cndmask_b32_e64 v44, v44, v51, s[40:41]
	v_mul_f32_e32 v50, 0xbf60028e, v49
	v_mul_f32_e32 v51, 0xbf60028e, v45
	v_exp_f32_e32 v50, v50
	v_exp_f32_e32 v51, v51
	v_cndmask_b32_e64 v49, v49, v50, s[40:41]
	v_cndmask_b32_e64 v45, v45, v51, s[40:41]
.LBB0_852:
	v_cvt_pk_bf16_f32 v46, v46, v47
	v_cvt_pk_bf16_f32 v47, v48, v49
	v_cvt_pk_bf16_f32 v48, v42, v43
	v_cvt_pk_bf16_f32 v49, v44, v45
	global_store_dwordx4 v[114:115], v[46:49], off offset:256 sc1
	v_pk_add_f32 v[40:41], v[40:41], v[72:73]
	v_pk_add_f32 v[38:39], v[38:39], v[70:71]
	v_pk_add_f32 v[36:37], v[36:37], v[68:69]
	s_and_b64 vcc, exec, s[42:43]
	v_pk_add_f32 v[34:35], v[34:35], v[66:67]
	s_cbranch_vccnz .LBB0_854
	v_mul_f32_e32 v38, 0xbfb8aa3b, v38
	v_mul_f32_e32 v34, 0xbfb8aa3b, v34
	v_exp_f32_e32 v38, v38
	v_exp_f32_e32 v34, v34
	v_mul_f32_e32 v39, 0xbfb8aa3b, v39
	v_mul_f32_e32 v35, 0xbfb8aa3b, v35
	v_add_f32_e32 v38, 1.0, v38
	v_add_f32_e32 v34, 1.0, v34
	v_rcp_f32_e32 v38, v38
	v_rcp_f32_e32 v34, v34
	v_exp_f32_e32 v39, v39
	v_exp_f32_e32 v35, v35
	v_mul_f32_e32 v42, 0xbf60028e, v38
	v_mul_f32_e32 v43, 0xbf60028e, v34
	v_add_f32_e32 v39, 1.0, v39
	v_add_f32_e32 v35, 1.0, v35
	v_mul_f32_e32 v40, 0xbfb8aa3b, v40
	v_mul_f32_e32 v36, 0xbfb8aa3b, v36
	v_exp_f32_e32 v42, v42
	v_exp_f32_e32 v43, v43
	v_rcp_f32_e32 v39, v39
	v_rcp_f32_e32 v35, v35
	v_exp_f32_e32 v40, v40
	v_exp_f32_e32 v36, v36
	v_cndmask_b32_e64 v38, v38, v42, s[40:41]
	v_cndmask_b32_e64 v34, v34, v43, s[40:41]
	v_mul_f32_e32 v42, 0xbf60028e, v39
	v_mul_f32_e32 v43, 0xbf60028e, v35
	v_add_f32_e32 v40, 1.0, v40
	v_add_f32_e32 v36, 1.0, v36
	v_mul_f32_e32 v41, 0xbfb8aa3b, v41
	v_mul_f32_e32 v37, 0xbfb8aa3b, v37
	v_exp_f32_e32 v42, v42
	v_exp_f32_e32 v43, v43
	v_rcp_f32_e32 v40, v40
	v_rcp_f32_e32 v36, v36
	v_exp_f32_e32 v41, v41
	v_exp_f32_e32 v37, v37
	v_cndmask_b32_e64 v39, v39, v42, s[40:41]
	v_cndmask_b32_e64 v35, v35, v43, s[40:41]
	v_mul_f32_e32 v42, 0xbf60028e, v40
	v_mul_f32_e32 v43, 0xbf60028e, v36
	v_add_f32_e32 v41, 1.0, v41
	v_add_f32_e32 v37, 1.0, v37
	v_exp_f32_e32 v42, v42
	v_exp_f32_e32 v43, v43
	v_rcp_f32_e32 v41, v41
	v_rcp_f32_e32 v37, v37
	v_cndmask_b32_e64 v40, v40, v42, s[40:41]
	v_cndmask_b32_e64 v36, v36, v43, s[40:41]
	v_mul_f32_e32 v42, 0xbf60028e, v41
	v_mul_f32_e32 v43, 0xbf60028e, v37
	v_exp_f32_e32 v42, v42
	v_exp_f32_e32 v43, v43
	v_cndmask_b32_e64 v41, v41, v42, s[40:41]
	v_cndmask_b32_e64 v37, v37, v43, s[40:41]
.LBB0_854:
	v_cvt_pk_bf16_f32 v38, v38, v39
	v_cvt_pk_bf16_f32 v39, v40, v41
	v_cvt_pk_bf16_f32 v40, v34, v35
	v_cvt_pk_bf16_f32 v41, v36, v37
	global_store_dwordx4 v[98:99], v[38:41], off offset:256 sc1
	v_pk_add_f32 v[32:33], v[32:33], v[72:73]
	v_pk_add_f32 v[30:31], v[30:31], v[70:71]
	v_pk_add_f32 v[28:29], v[28:29], v[68:69]
	s_and_b64 vcc, exec, s[42:43]
	v_pk_add_f32 v[26:27], v[26:27], v[66:67]
	s_cbranch_vccnz .LBB0_856
	v_mul_f32_e32 v30, 0xbfb8aa3b, v30
	v_mul_f32_e32 v26, 0xbfb8aa3b, v26
	v_exp_f32_e32 v30, v30
	v_exp_f32_e32 v26, v26
	v_mul_f32_e32 v31, 0xbfb8aa3b, v31
	v_mul_f32_e32 v27, 0xbfb8aa3b, v27
	v_add_f32_e32 v30, 1.0, v30
	v_add_f32_e32 v26, 1.0, v26
	v_rcp_f32_e32 v30, v30
	v_rcp_f32_e32 v26, v26
	v_exp_f32_e32 v31, v31
	v_exp_f32_e32 v27, v27
	v_mul_f32_e32 v34, 0xbf60028e, v30
	v_mul_f32_e32 v35, 0xbf60028e, v26
	v_add_f32_e32 v31, 1.0, v31
	v_add_f32_e32 v27, 1.0, v27
	v_mul_f32_e32 v32, 0xbfb8aa3b, v32
	v_mul_f32_e32 v28, 0xbfb8aa3b, v28
	v_exp_f32_e32 v34, v34
	v_exp_f32_e32 v35, v35
	v_rcp_f32_e32 v31, v31
	v_rcp_f32_e32 v27, v27
	v_exp_f32_e32 v32, v32
	v_exp_f32_e32 v28, v28
	v_cndmask_b32_e64 v30, v30, v34, s[40:41]
	v_cndmask_b32_e64 v26, v26, v35, s[40:41]
	v_mul_f32_e32 v34, 0xbf60028e, v31
	v_mul_f32_e32 v35, 0xbf60028e, v27
	v_add_f32_e32 v32, 1.0, v32
	v_add_f32_e32 v28, 1.0, v28
	v_mul_f32_e32 v33, 0xbfb8aa3b, v33
	v_mul_f32_e32 v29, 0xbfb8aa3b, v29
	v_exp_f32_e32 v34, v34
	v_exp_f32_e32 v35, v35
	v_rcp_f32_e32 v32, v32
	v_rcp_f32_e32 v28, v28
	v_exp_f32_e32 v33, v33
	v_exp_f32_e32 v29, v29
	v_cndmask_b32_e64 v31, v31, v34, s[40:41]
	v_cndmask_b32_e64 v27, v27, v35, s[40:41]
	v_mul_f32_e32 v34, 0xbf60028e, v32
	v_mul_f32_e32 v35, 0xbf60028e, v28
	v_add_f32_e32 v33, 1.0, v33
	v_add_f32_e32 v29, 1.0, v29
	v_exp_f32_e32 v34, v34
	v_exp_f32_e32 v35, v35
	v_rcp_f32_e32 v33, v33
	v_rcp_f32_e32 v29, v29
	v_cndmask_b32_e64 v32, v32, v34, s[40:41]
	v_cndmask_b32_e64 v28, v28, v35, s[40:41]
	v_mul_f32_e32 v34, 0xbf60028e, v33
	v_mul_f32_e32 v35, 0xbf60028e, v29
	v_exp_f32_e32 v34, v34
	v_exp_f32_e32 v35, v35
	v_cndmask_b32_e64 v33, v33, v34, s[40:41]
	v_cndmask_b32_e64 v29, v29, v35, s[40:41]
.LBB0_856:
	v_cvt_pk_bf16_f32 v30, v30, v31
	v_cvt_pk_bf16_f32 v31, v32, v33
	v_cvt_pk_bf16_f32 v32, v26, v27
	v_cvt_pk_bf16_f32 v33, v28, v29
	global_store_dwordx4 v[90:91], v[30:33], off offset:256 sc1
	v_pk_add_f32 v[24:25], v[24:25], v[72:73]
	v_pk_add_f32 v[22:23], v[22:23], v[70:71]
	v_pk_add_f32 v[20:21], v[20:21], v[68:69]
	s_and_b64 vcc, exec, s[42:43]
	v_pk_add_f32 v[18:19], v[18:19], v[66:67]
	s_cbranch_vccnz .LBB0_858
	v_mul_f32_e32 v22, 0xbfb8aa3b, v22
	v_mul_f32_e32 v18, 0xbfb8aa3b, v18
	v_exp_f32_e32 v22, v22
	v_exp_f32_e32 v18, v18
	v_mul_f32_e32 v23, 0xbfb8aa3b, v23
	v_mul_f32_e32 v19, 0xbfb8aa3b, v19
	v_add_f32_e32 v22, 1.0, v22
	v_add_f32_e32 v18, 1.0, v18
	v_rcp_f32_e32 v22, v22
	v_rcp_f32_e32 v18, v18
	v_exp_f32_e32 v23, v23
	v_exp_f32_e32 v19, v19
	v_mul_f32_e32 v26, 0xbf60028e, v22
	v_mul_f32_e32 v27, 0xbf60028e, v18
	v_add_f32_e32 v23, 1.0, v23
	v_add_f32_e32 v19, 1.0, v19
	v_mul_f32_e32 v24, 0xbfb8aa3b, v24
	v_mul_f32_e32 v20, 0xbfb8aa3b, v20
	v_exp_f32_e32 v26, v26
	v_exp_f32_e32 v27, v27
	v_rcp_f32_e32 v23, v23
	v_rcp_f32_e32 v19, v19
	v_exp_f32_e32 v24, v24
	v_exp_f32_e32 v20, v20
	v_cndmask_b32_e64 v22, v22, v26, s[40:41]
	v_cndmask_b32_e64 v18, v18, v27, s[40:41]
	v_mul_f32_e32 v26, 0xbf60028e, v23
	v_mul_f32_e32 v27, 0xbf60028e, v19
	v_add_f32_e32 v24, 1.0, v24
	v_add_f32_e32 v20, 1.0, v20
	v_mul_f32_e32 v25, 0xbfb8aa3b, v25
	v_mul_f32_e32 v21, 0xbfb8aa3b, v21
	v_exp_f32_e32 v26, v26
	v_exp_f32_e32 v27, v27
	v_rcp_f32_e32 v24, v24
	v_rcp_f32_e32 v20, v20
	v_exp_f32_e32 v25, v25
	v_exp_f32_e32 v21, v21
	v_cndmask_b32_e64 v23, v23, v26, s[40:41]
	v_cndmask_b32_e64 v19, v19, v27, s[40:41]
	v_mul_f32_e32 v26, 0xbf60028e, v24
	v_mul_f32_e32 v27, 0xbf60028e, v20
	v_add_f32_e32 v25, 1.0, v25
	v_add_f32_e32 v21, 1.0, v21
	v_exp_f32_e32 v26, v26
	v_exp_f32_e32 v27, v27
	v_rcp_f32_e32 v25, v25
	v_rcp_f32_e32 v21, v21
	v_cndmask_b32_e64 v24, v24, v26, s[40:41]
	v_cndmask_b32_e64 v20, v20, v27, s[40:41]
	v_mul_f32_e32 v26, 0xbf60028e, v25
	v_mul_f32_e32 v27, 0xbf60028e, v21
	v_exp_f32_e32 v26, v26
	v_exp_f32_e32 v27, v27
	v_cndmask_b32_e64 v25, v25, v26, s[40:41]
	v_cndmask_b32_e64 v21, v21, v27, s[40:41]
.LBB0_858:
	v_cvt_pk_bf16_f32 v22, v22, v23
	v_cvt_pk_bf16_f32 v23, v24, v25
	v_cvt_pk_bf16_f32 v24, v18, v19
	v_cvt_pk_bf16_f32 v25, v20, v21
	global_store_dwordx4 v[82:83], v[22:25], off offset:256 sc1
	v_pk_add_f32 v[16:17], v[16:17], v[72:73]
	v_pk_add_f32 v[14:15], v[14:15], v[70:71]
	v_pk_add_f32 v[12:13], v[12:13], v[68:69]
	s_and_b64 vcc, exec, s[42:43]
	v_pk_add_f32 v[10:11], v[10:11], v[66:67]
	s_cbranch_vccnz .LBB0_860
	v_mul_f32_e32 v14, 0xbfb8aa3b, v14
	v_mul_f32_e32 v10, 0xbfb8aa3b, v10
	v_exp_f32_e32 v14, v14
	v_exp_f32_e32 v10, v10
	v_mul_f32_e32 v15, 0xbfb8aa3b, v15
	v_mul_f32_e32 v11, 0xbfb8aa3b, v11
	v_add_f32_e32 v14, 1.0, v14
	v_add_f32_e32 v10, 1.0, v10
	v_rcp_f32_e32 v14, v14
	v_rcp_f32_e32 v10, v10
	v_exp_f32_e32 v15, v15
	v_exp_f32_e32 v11, v11
	v_mul_f32_e32 v18, 0xbf60028e, v14
	v_mul_f32_e32 v19, 0xbf60028e, v10
	v_add_f32_e32 v15, 1.0, v15
	v_add_f32_e32 v11, 1.0, v11
	v_mul_f32_e32 v16, 0xbfb8aa3b, v16
	v_mul_f32_e32 v12, 0xbfb8aa3b, v12
	v_exp_f32_e32 v18, v18
	v_exp_f32_e32 v19, v19
	v_rcp_f32_e32 v15, v15
	v_rcp_f32_e32 v11, v11
	v_exp_f32_e32 v16, v16
	v_exp_f32_e32 v12, v12
	v_cndmask_b32_e64 v14, v14, v18, s[40:41]
	v_cndmask_b32_e64 v10, v10, v19, s[40:41]
	v_mul_f32_e32 v18, 0xbf60028e, v15
	v_mul_f32_e32 v19, 0xbf60028e, v11
	v_add_f32_e32 v16, 1.0, v16
	v_add_f32_e32 v12, 1.0, v12
	v_mul_f32_e32 v17, 0xbfb8aa3b, v17
	v_mul_f32_e32 v13, 0xbfb8aa3b, v13
	v_exp_f32_e32 v18, v18
	v_exp_f32_e32 v19, v19
	v_rcp_f32_e32 v16, v16
	v_rcp_f32_e32 v12, v12
	v_exp_f32_e32 v17, v17
	v_exp_f32_e32 v13, v13
	v_cndmask_b32_e64 v15, v15, v18, s[40:41]
	v_cndmask_b32_e64 v11, v11, v19, s[40:41]
	v_mul_f32_e32 v18, 0xbf60028e, v16
	v_mul_f32_e32 v19, 0xbf60028e, v12
	v_add_f32_e32 v17, 1.0, v17
	v_add_f32_e32 v13, 1.0, v13
	v_exp_f32_e32 v18, v18
	v_exp_f32_e32 v19, v19
	v_rcp_f32_e32 v17, v17
	v_rcp_f32_e32 v13, v13
	v_cndmask_b32_e64 v16, v16, v18, s[40:41]
	v_cndmask_b32_e64 v12, v12, v19, s[40:41]
	v_mul_f32_e32 v18, 0xbf60028e, v17
	v_mul_f32_e32 v19, 0xbf60028e, v13
	v_exp_f32_e32 v18, v18
	v_exp_f32_e32 v19, v19
	v_cndmask_b32_e64 v17, v17, v18, s[40:41]
	v_cndmask_b32_e64 v13, v13, v19, s[40:41]
.LBB0_860:
	v_cvt_pk_bf16_f32 v14, v14, v15
	v_cvt_pk_bf16_f32 v15, v16, v17
	v_cvt_pk_bf16_f32 v16, v10, v11
	v_cvt_pk_bf16_f32 v17, v12, v13
	global_store_dwordx4 v[74:75], v[14:17], off offset:256 sc1
	v_pk_add_f32 v[8:9], v[8:9], v[72:73]
	v_pk_add_f32 v[6:7], v[6:7], v[70:71]
	v_pk_add_f32 v[4:5], v[4:5], v[68:69]
	s_and_b64 vcc, exec, s[42:43]
	v_pk_add_f32 v[2:3], v[2:3], v[66:67]
	s_cbranch_vccnz .LBB0_862
	v_mul_f32_e32 v6, 0xbfb8aa3b, v6
	v_mul_f32_e32 v2, 0xbfb8aa3b, v2
	v_exp_f32_e32 v6, v6
	v_exp_f32_e32 v2, v2
	v_mul_f32_e32 v7, 0xbfb8aa3b, v7
	v_mul_f32_e32 v3, 0xbfb8aa3b, v3
	v_add_f32_e32 v6, 1.0, v6
	v_add_f32_e32 v2, 1.0, v2
	v_rcp_f32_e32 v6, v6
	v_rcp_f32_e32 v2, v2
	v_exp_f32_e32 v7, v7
	v_exp_f32_e32 v3, v3
	v_mul_f32_e32 v10, 0xbf60028e, v6
	v_mul_f32_e32 v11, 0xbf60028e, v2
	v_add_f32_e32 v7, 1.0, v7
	v_add_f32_e32 v3, 1.0, v3
	v_mul_f32_e32 v8, 0xbfb8aa3b, v8
	v_mul_f32_e32 v4, 0xbfb8aa3b, v4
	v_exp_f32_e32 v10, v10
	v_exp_f32_e32 v11, v11
	v_rcp_f32_e32 v7, v7
	v_rcp_f32_e32 v3, v3
	v_exp_f32_e32 v8, v8
	v_exp_f32_e32 v4, v4
	v_cndmask_b32_e64 v6, v6, v10, s[40:41]
	v_cndmask_b32_e64 v2, v2, v11, s[40:41]
	v_mul_f32_e32 v10, 0xbf60028e, v7
	v_mul_f32_e32 v11, 0xbf60028e, v3
	v_add_f32_e32 v8, 1.0, v8
	v_add_f32_e32 v4, 1.0, v4
	v_mul_f32_e32 v9, 0xbfb8aa3b, v9
	v_mul_f32_e32 v5, 0xbfb8aa3b, v5
	v_exp_f32_e32 v10, v10
	v_exp_f32_e32 v11, v11
	v_rcp_f32_e32 v8, v8
	v_rcp_f32_e32 v4, v4
	v_exp_f32_e32 v9, v9
	v_exp_f32_e32 v5, v5
	v_cndmask_b32_e64 v7, v7, v10, s[40:41]
	v_cndmask_b32_e64 v3, v3, v11, s[40:41]
	v_mul_f32_e32 v10, 0xbf60028e, v8
	v_mul_f32_e32 v11, 0xbf60028e, v4
	v_add_f32_e32 v9, 1.0, v9
	v_add_f32_e32 v5, 1.0, v5
	v_exp_f32_e32 v10, v10
	v_exp_f32_e32 v11, v11
	v_rcp_f32_e32 v9, v9
	v_rcp_f32_e32 v5, v5
	v_cndmask_b32_e64 v8, v8, v10, s[40:41]
	v_cndmask_b32_e64 v4, v4, v11, s[40:41]
	v_mul_f32_e32 v10, 0xbf60028e, v9
	v_mul_f32_e32 v11, 0xbf60028e, v5
	v_exp_f32_e32 v10, v10
	v_exp_f32_e32 v11, v11
	v_cndmask_b32_e64 v9, v9, v10, s[40:41]
	v_cndmask_b32_e64 v5, v5, v11, s[40:41]
.LBB0_862:
	v_cvt_pk_bf16_f32 v6, v6, v7
	v_cvt_pk_bf16_f32 v7, v8, v9
	v_cvt_pk_bf16_f32 v8, v2, v3
	v_cvt_pk_bf16_f32 v9, v4, v5
	global_store_dwordx4 v[76:77], v[6:9], off offset:256 sc1
	s_and_b64 vcc, exec, s[38:39]
	s_mov_b64 s[4:5], -1
	s_cbranch_vccnz .LBB0_816
	s_andn2_b64 vcc, exec, s[48:49]
	s_cbranch_vccnz .LBB0_815
	s_barrier
	s_branch .LBB0_815

.LBB0_997:
	s_cmp_gt_u32 s84, 2
	s_cselect_b64 s[4:5], -1, 0
	s_and_b64 s[4:5], s[96:97], s[4:5]
	s_andn2_b64 vcc, exec, s[4:5]
	s_cbranch_vccnz .LBB0_999
	s_and_b32 s4, s71, 0x1000
	v_add_u32_e32 v0, s4, v144
	ds_read_b128 v[2:5], v0 offset:63744
	ds_read_b128 v[6:9], v0 offset:63760
	ds_read_b128 v[10:13], v0 offset:63776
	ds_read_b128 v[48:51], v0 offset:63792
	v_add_u32_e32 v0, s70, v147
	s_waitcnt lgkmcnt(3)
	v_cvt_pk_bf16_f32 v2, v2, v3
	v_cvt_pk_bf16_f32 v3, v4, v5
	s_waitcnt lgkmcnt(2)
	v_cvt_pk_bf16_f32 v4, v6, v7
	v_cvt_pk_bf16_f32 v5, v8, v9
	s_waitcnt lgkmcnt(1)
	v_cvt_pk_bf16_f32 v6, v10, v11
	v_cndmask_b32_e64 v10, v153, v0, s[60:61]
	v_ashrrev_i32_e32 v11, 31, v10
	v_lshl_add_u64 v[10:11], v[10:11], 0, s[20:21]
	v_lshlrev_b64 v[10:11], 11, v[10:11]
	v_lshl_add_u64 v[10:11], v[122:123], 0, v[10:11]
	v_cvt_pk_bf16_f32 v7, v12, v13
	s_waitcnt lgkmcnt(0)
	v_cvt_pk_bf16_f32 v8, v48, v49
	v_cvt_pk_bf16_f32 v9, v50, v51
	global_store_dwordx4 v[10:11], v[2:5], off sc1
	global_store_dwordx4 v[10:11], v[6:9], off offset:16 sc1

.LBB0_1224:
	v_mov_b32_e32 v12, v192
	s_lshl_b32 s4, s70, 8
	s_add_i32 s6, s4, s84
	s_lshl_b32 s4, s71, 8
	v_ashrrev_i32_e32 v2, 1, v12
	s_or_b32 s4, s4, s85
	v_and_b32_e32 v2, -8, v2
	v_add_u32_e32 v22, s4, v2
	s_ashr_i32 s4, s70, 31
	s_lshr_b32 s4, s4, 28
	s_add_i32 s4, s70, s4
	s_ashr_i32 s4, s4, 4
	s_mul_hi_i32 s5, s4, 0xc000
	s_mul_i32 s4, s4, 0xc000
	s_add_u32 s4, s10, s4
	s_addc_u32 s5, s11, s5
	v_ashrrev_i32_e32 v23, 31, v22
	v_lshl_add_u64 v[10:11], v[22:23], 2, s[4:5]
	global_load_dwordx4 v[2:5], v[10:11], off offset:16
	global_load_dwordx4 v[6:9], v[10:11], off
	s_mov_b32 s4, 0x3b800000
	s_andn2_b64 vcc, exec, s[56:57]
	v_lshlrev_b64 v[178:179], 1, v[22:23]
	s_waitcnt vmcnt(0)
	v_pk_mul_f32 v[32:33], v[4:5], s[4:5] op_sel_hi:[1,0]
	v_pk_mul_f32 v[176:177], v[8:9], s[4:5] op_sel_hi:[1,0]
	v_pk_mul_f32 v[174:175], v[6:7], s[4:5] op_sel_hi:[1,0]
	v_pk_mul_f32 v[28:29], v[2:3], s[4:5] op_sel_hi:[1,0]
	global_load_dwordx4 v[2:5], v[10:11], off offset:528
	global_load_dwordx4 v[6:9], v[10:11], off offset:512
	s_waitcnt vmcnt(0)
	v_pk_mul_f32 v[24:25], v[2:3], s[4:5] op_sel_hi:[1,0]
	v_and_or_b32 v2, v12, 15, s6
	v_ashrrev_i32_e32 v3, 31, v2
	v_lshlrev_b64 v[180:181], 12, v[2:3]
	v_pk_mul_f32 v[172:173], v[8:9], s[4:5] op_sel_hi:[1,0]
	v_pk_mul_f32 v[30:31], v[6:7], s[4:5] op_sel_hi:[1,0]
	v_pk_mul_f32 v[26:27], v[4:5], s[4:5] op_sel_hi:[1,0]
	v_or_b32_e32 v12, 16, v2
	v_lshl_add_u64 v[182:183], s[50:51], 0, v[180:181]
	v_or_b32_e32 v10, 32, v2
	v_or_b32_e32 v184, 48, v2
	s_cbranch_vccnz .LBB0_1230
	v_lshl_add_u64 v[4:5], v[22:23], 2, s[42:43]
	v_lshlrev_b64 v[6:7], 13, v[2:3]
	v_lshl_add_u64 v[186:187], v[4:5], 0, v[6:7]
	global_load_dwordx4 v[6:9], v[186:187], off offset:16
	global_load_dwordx4 v[14:17], v[186:187], off
	global_load_dwordx4 v[18:21], v[186:187], off offset:528
	s_nop 0
	global_load_dwordx4 v[186:189], v[186:187], off offset:512
	v_ashrrev_i32_e32 v13, 31, v12
	v_lshlrev_b64 v[190:191], 13, v[12:13]
	v_lshl_add_u64 v[190:191], v[4:5], 0, v[190:191]
	global_load_dwordx4 v[196:199], v[190:191], off offset:16
	global_load_dwordx4 v[200:203], v[190:191], off
	global_load_dwordx4 v[204:207], v[190:191], off offset:528
	global_load_dwordx4 v[208:211], v[190:191], off offset:512
	v_ashrrev_i32_e32 v11, 31, v10
	v_ashrrev_i32_e32 v185, 31, v184
	s_waitcnt vmcnt(0)
	v_pk_fma_f32 v[190:191], v[160:161], v[32:33], v[8:9]
	v_pk_fma_f32 v[14:15], v[154:155], v[174:175], v[14:15]
	v_pk_fma_f32 v[8:9], v[158:159], v[28:29], v[6:7]
	v_pk_fma_f32 v[16:17], v[156:157], v[176:177], v[16:17]
	v_cvt_pk_bf16_f32 v6, v14, v15
	v_lshl_add_u64 v[14:15], v[182:183], 0, v[178:179]
	v_cvt_pk_bf16_f32 v7, v16, v17
	v_cvt_pk_bf16_f32 v8, v8, v9
	v_cvt_pk_bf16_f32 v9, v190, v191
	global_store_dwordx4 v[14:15], v[6:9], off sc1
	v_pk_fma_f32 v[16:17], v[148:149], v[26:27], v[20:21]
	v_pk_fma_f32 v[18:19], v[146:147], v[24:25], v[18:19]
	v_pk_fma_f32 v[8:9], v[152:153], v[172:173], v[188:189]
	v_pk_fma_f32 v[6:7], v[150:151], v[30:31], v[186:187]
	v_lshlrev_b64 v[190:191], 13, v[184:185]
	v_cvt_pk_bf16_f32 v6, v6, v7
	v_cvt_pk_bf16_f32 v7, v8, v9
	v_cvt_pk_bf16_f32 v8, v18, v19
	v_cvt_pk_bf16_f32 v9, v16, v17
	global_store_dwordx4 v[14:15], v[6:9], off offset:256 sc1
	v_lshlrev_b64 v[14:15], 12, v[12:13]
	v_lshl_add_u64 v[14:15], s[50:51], 0, v[14:15]
	v_pk_fma_f32 v[6:7], v[142:143], v[174:175], v[200:201]
	v_pk_fma_f32 v[8:9], v[144:145], v[176:177], v[202:203]
	v_cvt_pk_bf16_f32 v6, v6, v7
	v_lshl_add_u64 v[14:15], v[14:15], 0, v[178:179]
	v_cvt_pk_bf16_f32 v7, v8, v9
	v_pk_fma_f32 v[16:17], v[140:141], v[32:33], v[198:199]
	v_pk_fma_f32 v[18:19], v[138:139], v[28:29], v[196:197]
	v_lshl_add_u64 v[190:191], v[4:5], 0, v[190:191]
	v_cvt_pk_bf16_f32 v8, v18, v19
	v_cvt_pk_bf16_f32 v9, v16, v17
	global_store_dwordx4 v[14:15], v[6:9], off sc1
	v_pk_fma_f32 v[16:17], v[132:133], v[26:27], v[206:207]
	v_pk_fma_f32 v[18:19], v[130:131], v[24:25], v[204:205]
	v_pk_fma_f32 v[6:7], v[134:135], v[30:31], v[208:209]
	v_pk_fma_f32 v[8:9], v[136:137], v[172:173], v[210:211]
	v_cvt_pk_bf16_f32 v6, v6, v7
	s_nop 0
	v_cvt_pk_bf16_f32 v7, v8, v9
	v_cvt_pk_bf16_f32 v8, v18, v19
	v_cvt_pk_bf16_f32 v9, v16, v17
	global_store_dwordx4 v[14:15], v[6:9], off offset:256 sc1
	s_nop 1
	v_lshlrev_b64 v[6:7], 13, v[10:11]
	v_lshl_add_u64 v[186:187], v[4:5], 0, v[6:7]
	global_load_dwordx4 v[6:9], v[186:187], off offset:16
	global_load_dwordx4 v[14:17], v[186:187], off
	global_load_dwordx4 v[18:21], v[186:187], off offset:528
	s_nop 0
	global_load_dwordx4 v[186:189], v[186:187], off offset:512
	s_nop 0
	global_load_dwordx4 v[196:199], v[190:191], off offset:16
	global_load_dwordx4 v[200:203], v[190:191], off
	global_load_dwordx4 v[204:207], v[190:191], off offset:528
	global_load_dwordx4 v[208:211], v[190:191], off offset:512
	v_lshlrev_b64 v[190:191], 12, v[10:11]
	s_waitcnt vmcnt(0)
	v_pk_fma_f32 v[212:213], v[124:125], v[32:33], v[8:9]
	v_pk_fma_f32 v[14:15], v[126:127], v[174:175], v[14:15]
	v_pk_fma_f32 v[8:9], v[122:123], v[28:29], v[6:7]
	v_cvt_pk_bf16_f32 v6, v14, v15
	v_lshl_add_u64 v[14:15], s[50:51], 0, v[190:191]
	v_pk_fma_f32 v[16:17], v[128:129], v[176:177], v[16:17]
	v_lshl_add_u64 v[14:15], v[14:15], 0, v[178:179]
	v_cvt_pk_bf16_f32 v7, v16, v17
	v_cvt_pk_bf16_f32 v8, v8, v9
	v_cvt_pk_bf16_f32 v9, v212, v213
	global_store_dwordx4 v[14:15], v[6:9], off sc1
	v_pk_fma_f32 v[16:17], v[116:117], v[26:27], v[20:21]
	v_pk_fma_f32 v[18:19], v[114:115], v[24:25], v[18:19]
	v_pk_fma_f32 v[8:9], v[120:121], v[172:173], v[188:189]
	v_pk_fma_f32 v[6:7], v[118:119], v[30:31], v[186:187]
	v_add_u32_e32 v190, 0x80, v2
	v_cvt_pk_bf16_f32 v6, v6, v7
	v_cvt_pk_bf16_f32 v7, v8, v9
	v_cvt_pk_bf16_f32 v8, v18, v19
	v_cvt_pk_bf16_f32 v9, v16, v17
	global_store_dwordx4 v[14:15], v[6:9], off offset:256 sc1
	v_lshlrev_b64 v[14:15], 12, v[184:185]
	v_lshl_add_u64 v[14:15], s[50:51], 0, v[14:15]
	v_pk_fma_f32 v[6:7], v[110:111], v[174:175], v[200:201]
	v_pk_fma_f32 v[8:9], v[112:113], v[176:177], v[202:203]
	v_cvt_pk_bf16_f32 v6, v6, v7
	v_lshl_add_u64 v[14:15], v[14:15], 0, v[178:179]
	v_cvt_pk_bf16_f32 v7, v8, v9
	v_pk_fma_f32 v[16:17], v[108:109], v[32:33], v[198:199]
	v_pk_fma_f32 v[18:19], v[106:107], v[28:29], v[196:197]
	v_ashrrev_i32_e32 v191, 31, v190
	v_cvt_pk_bf16_f32 v8, v18, v19
	v_cvt_pk_bf16_f32 v9, v16, v17
	global_store_dwordx4 v[14:15], v[6:9], off sc1
	v_pk_fma_f32 v[16:17], v[100:101], v[26:27], v[206:207]
	v_pk_fma_f32 v[18:19], v[98:99], v[24:25], v[204:205]
	v_pk_fma_f32 v[6:7], v[102:103], v[30:31], v[208:209]
	v_pk_fma_f32 v[8:9], v[104:105], v[172:173], v[210:211]
	v_cvt_pk_bf16_f32 v6, v6, v7
	v_add_u32_e32 v212, 0x90, v2
	v_cvt_pk_bf16_f32 v7, v8, v9
	v_cvt_pk_bf16_f32 v8, v18, v19
	v_cvt_pk_bf16_f32 v9, v16, v17
	global_store_dwordx4 v[14:15], v[6:9], off offset:256 sc1
	v_ashrrev_i32_e32 v213, 31, v212
	v_lshlrev_b64 v[196:197], 13, v[212:213]
	v_lshlrev_b64 v[6:7], 13, v[190:191]
	v_lshl_add_u64 v[186:187], v[4:5], 0, v[6:7]
	global_load_dwordx4 v[6:9], v[186:187], off offset:16
	global_load_dwordx4 v[14:17], v[186:187], off
	global_load_dwordx4 v[18:21], v[186:187], off offset:528
	s_nop 0
	global_load_dwordx4 v[186:189], v[186:187], off offset:512
	v_lshl_add_u64 v[208:209], v[4:5], 0, v[196:197]
	global_load_dwordx4 v[196:199], v[208:209], off offset:16
	global_load_dwordx4 v[200:203], v[208:209], off
	global_load_dwordx4 v[204:207], v[208:209], off offset:528
	s_nop 0
	global_load_dwordx4 v[208:211], v[208:209], off offset:512
	v_lshlrev_b64 v[190:191], 12, v[190:191]
	s_waitcnt vmcnt(0)
	v_pk_fma_f32 v[214:215], v[92:93], v[32:33], v[8:9]
	v_pk_fma_f32 v[14:15], v[94:95], v[174:175], v[14:15]
	v_pk_fma_f32 v[8:9], v[90:91], v[28:29], v[6:7]
	v_cvt_pk_bf16_f32 v6, v14, v15
	v_lshl_add_u64 v[14:15], s[50:51], 0, v[190:191]
	v_pk_fma_f32 v[16:17], v[96:97], v[176:177], v[16:17]
	v_lshl_add_u64 v[14:15], v[14:15], 0, v[178:179]
	v_cvt_pk_bf16_f32 v7, v16, v17
	v_cvt_pk_bf16_f32 v8, v8, v9
	v_cvt_pk_bf16_f32 v9, v214, v215
	global_store_dwordx4 v[14:15], v[6:9], off sc1
	v_pk_fma_f32 v[16:17], v[84:85], v[26:27], v[20:21]
	v_pk_fma_f32 v[18:19], v[82:83], v[24:25], v[18:19]
	v_pk_fma_f32 v[8:9], v[88:89], v[172:173], v[188:189]
	v_pk_fma_f32 v[6:7], v[86:87], v[30:31], v[186:187]
	v_add_u32_e32 v190, 0xa0, v2
	v_cvt_pk_bf16_f32 v6, v6, v7
	v_cvt_pk_bf16_f32 v7, v8, v9
	v_cvt_pk_bf16_f32 v8, v18, v19
	v_cvt_pk_bf16_f32 v9, v16, v17
	global_store_dwordx4 v[14:15], v[6:9], off offset:256 sc1
	v_lshlrev_b64 v[14:15], 12, v[212:213]
	v_lshl_add_u64 v[14:15], s[50:51], 0, v[14:15]
	v_pk_fma_f32 v[6:7], v[78:79], v[174:175], v[200:201]
	v_pk_fma_f32 v[8:9], v[80:81], v[176:177], v[202:203]
	v_cvt_pk_bf16_f32 v6, v6, v7
	v_lshl_add_u64 v[14:15], v[14:15], 0, v[178:179]
	v_cvt_pk_bf16_f32 v7, v8, v9
	v_pk_fma_f32 v[16:17], v[76:77], v[32:33], v[198:199]
	v_pk_fma_f32 v[18:19], v[74:75], v[28:29], v[196:197]
	v_ashrrev_i32_e32 v191, 31, v190
	v_cvt_pk_bf16_f32 v8, v18, v19
	v_cvt_pk_bf16_f32 v9, v16, v17
	global_store_dwordx4 v[14:15], v[6:9], off sc1
	v_pk_fma_f32 v[16:17], v[68:69], v[26:27], v[206:207]
	v_pk_fma_f32 v[18:19], v[66:67], v[24:25], v[204:205]
	v_pk_fma_f32 v[6:7], v[70:71], v[30:31], v[208:209]
	v_pk_fma_f32 v[8:9], v[72:73], v[172:173], v[210:211]
	v_cvt_pk_bf16_f32 v6, v6, v7
	v_add_u32_e32 v208, 0xb0, v2
	v_cvt_pk_bf16_f32 v7, v8, v9
	v_cvt_pk_bf16_f32 v8, v18, v19
	v_cvt_pk_bf16_f32 v9, v16, v17
	global_store_dwordx4 v[14:15], v[6:9], off offset:256 sc1
	v_ashrrev_i32_e32 v209, 31, v208
	v_lshlrev_b64 v[2:3], 13, v[208:209]
	v_lshlrev_b64 v[6:7], 13, v[190:191]
	v_lshl_add_u64 v[6:7], v[4:5], 0, v[6:7]
	global_load_dwordx4 v[14:17], v[6:7], off offset:16
	global_load_dwordx4 v[18:21], v[6:7], off
	global_load_dwordx4 v[186:189], v[6:7], off offset:528
	global_load_dwordx4 v[196:199], v[6:7], off offset:512
	v_lshl_add_u64 v[6:7], v[4:5], 0, v[2:3]
	global_load_dwordx4 v[200:203], v[6:7], off offset:16
	global_load_dwordx4 v[204:207], v[6:7], off
	global_load_dwordx4 v[2:5], v[6:7], off offset:528
	s_nop 0
	global_load_dwordx4 v[6:9], v[6:7], off offset:512
	v_lshlrev_b64 v[190:191], 12, v[190:191]
	s_waitcnt vmcnt(0)
	v_pk_fma_f32 v[210:211], v[60:61], v[32:33], v[16:17]
	v_pk_fma_f32 v[18:19], v[62:63], v[174:175], v[18:19]
	v_pk_fma_f32 v[16:17], v[58:59], v[28:29], v[14:15]
	v_cvt_pk_bf16_f32 v14, v18, v19
	v_lshl_add_u64 v[18:19], s[50:51], 0, v[190:191]
	v_pk_fma_f32 v[20:21], v[64:65], v[176:177], v[20:21]
	v_lshl_add_u64 v[18:19], v[18:19], 0, v[178:179]
	v_cvt_pk_bf16_f32 v15, v20, v21
	v_cvt_pk_bf16_f32 v16, v16, v17
	v_cvt_pk_bf16_f32 v17, v210, v211
	global_store_dwordx4 v[18:19], v[14:17], off sc1
	v_pk_fma_f32 v[20:21], v[52:53], v[26:27], v[188:189]
	v_pk_fma_f32 v[186:187], v[50:51], v[24:25], v[186:187]
	v_pk_fma_f32 v[16:17], v[56:57], v[172:173], v[198:199]
	v_pk_fma_f32 v[14:15], v[54:55], v[30:31], v[196:197]
	v_pk_fma_f32 v[8:9], v[40:41], v[172:173], v[8:9]
	v_cvt_pk_bf16_f32 v14, v14, v15
	v_cvt_pk_bf16_f32 v15, v16, v17
	v_cvt_pk_bf16_f32 v16, v186, v187
	v_cvt_pk_bf16_f32 v17, v20, v21
	global_store_dwordx4 v[18:19], v[14:17], off offset:256 sc1
	v_pk_fma_f32 v[18:19], v[48:49], v[176:177], v[206:207]
	v_pk_fma_f32 v[20:21], v[44:45], v[32:33], v[202:203]
	v_lshlrev_b64 v[14:15], 12, v[208:209]
	v_pk_fma_f32 v[16:17], v[46:47], v[174:175], v[204:205]
	v_pk_fma_f32 v[186:187], v[42:43], v[28:29], v[200:201]
	v_cvt_pk_bf16_f32 v16, v16, v17
	v_cvt_pk_bf16_f32 v17, v18, v19
	v_pk_fma_f32 v[6:7], v[38:39], v[30:31], v[6:7]
	v_cvt_pk_bf16_f32 v18, v186, v187
	v_cvt_pk_bf16_f32 v19, v20, v21
	v_lshl_add_u64 v[20:21], s[50:51], 0, v[14:15]
	v_lshl_add_u64 v[20:21], v[20:21], 0, v[178:179]
	global_store_dwordx4 v[20:21], v[16:19], off sc1
	s_nop 1
	v_pk_fma_f32 v[16:17], v[36:37], v[26:27], v[4:5]
	v_pk_fma_f32 v[4:5], v[34:35], v[24:25], v[2:3]
	v_cvt_pk_bf16_f32 v2, v6, v7
	v_cvt_pk_bf16_f32 v3, v8, v9
	s_nop 0
	v_cvt_pk_bf16_f32 v4, v4, v5
	v_cvt_pk_bf16_f32 v5, v16, v17
	s_cbranch_execnz .LBB0_1227
.LBB0_1226:
	v_lshl_add_u64 v[186:187], s[50:51], 0, v[178:179]
	v_lshl_add_u64 v[2:3], v[186:187], 0, v[180:181]
	global_load_dwordx4 v[196:199], v[2:3], off
	global_load_dwordx4 v[200:203], v[2:3], off offset:256
	v_ashrrev_i32_e32 v13, 31, v12
	v_lshlrev_b64 v[190:191], 12, v[12:13]
	v_lshl_add_u64 v[2:3], v[186:187], 0, v[190:191]
	global_load_dwordx4 v[204:207], v[2:3], off
	global_load_dwordx4 v[18:21], v[2:3], off offset:256
	v_ashrrev_i32_e32 v11, 31, v10
	v_lshlrev_b64 v[188:189], 12, v[10:11]
	v_lshl_add_u64 v[2:3], v[186:187], 0, v[188:189]
	global_load_dwordx4 v[14:17], v[2:3], off
	global_load_dwordx4 v[10:13], v[2:3], off offset:256
	v_ashrrev_i32_e32 v185, 31, v184
	v_lshlrev_b64 v[184:185], 12, v[184:185]
	v_lshl_add_u64 v[2:3], v[186:187], 0, v[184:185]
	global_load_dwordx4 v[6:9], v[2:3], off
	s_nop 0
	global_load_dwordx4 v[2:5], v[2:3], off offset:256
	s_mov_b64 s[4:5], 0x80000
	s_waitcnt vmcnt(0)
	v_lshlrev_b32_e32 v208, 16, v196
	v_and_b32_e32 v209, 0xffff0000, v196
	v_lshlrev_b32_e32 v196, 16, v197
	v_and_b32_e32 v197, 0xffff0000, v197
	v_lshlrev_b32_e32 v210, 16, v198
	v_and_b32_e32 v211, 0xffff0000, v198
	v_lshlrev_b32_e32 v198, 16, v199
	v_and_b32_e32 v199, 0xffff0000, v199
	v_pk_fma_f32 v[156:157], v[156:157], v[176:177], v[196:197]
	v_pk_fma_f32 v[154:155], v[154:155], v[174:175], v[208:209]
	v_pk_fma_f32 v[158:159], v[158:159], v[28:29], v[210:211]
	v_pk_fma_f32 v[160:161], v[160:161], v[32:33], v[198:199]
	v_cvt_pk_bf16_f32 v154, v154, v155
	v_cvt_pk_bf16_f32 v155, v156, v157
	v_cvt_pk_bf16_f32 v156, v158, v159
	v_lshl_add_u64 v[158:159], v[182:183], 0, v[178:179]
	v_cvt_pk_bf16_f32 v157, v160, v161
	global_store_dwordx4 v[158:159], v[154:157], off sc1
	v_lshlrev_b32_e32 v160, 16, v202
	v_and_b32_e32 v161, 0xffff0000, v202
	v_lshlrev_b32_e32 v154, 16, v200
	v_and_b32_e32 v155, 0xffff0000, v200
	v_lshlrev_b32_e32 v156, 16, v201
	v_and_b32_e32 v157, 0xffff0000, v201
	v_lshlrev_b32_e32 v182, 16, v203
	v_and_b32_e32 v183, 0xffff0000, v203
	v_pk_fma_f32 v[152:153], v[152:153], v[172:173], v[156:157]
	v_pk_fma_f32 v[150:151], v[150:151], v[30:31], v[154:155]
	v_pk_fma_f32 v[154:155], v[148:149], v[26:27], v[182:183]
	v_pk_fma_f32 v[148:149], v[146:147], v[24:25], v[160:161]
	v_cvt_pk_bf16_f32 v146, v150, v151
	v_cvt_pk_bf16_f32 v147, v152, v153
	v_lshlrev_b32_e32 v150, 16, v206
	v_cvt_pk_bf16_f32 v148, v148, v149
	v_cvt_pk_bf16_f32 v149, v154, v155
	global_store_dwordx4 v[158:159], v[146:149], off offset:256 sc1
	v_and_b32_e32 v151, 0xffff0000, v206
	v_lshlrev_b32_e32 v152, 16, v207
	v_lshlrev_b32_e32 v146, 16, v204
	v_and_b32_e32 v147, 0xffff0000, v204
	v_and_b32_e32 v153, 0xffff0000, v207
	v_pk_fma_f32 v[142:143], v[142:143], v[174:175], v[146:147]
	v_lshlrev_b32_e32 v148, 16, v205
	v_and_b32_e32 v149, 0xffff0000, v205
	v_pk_fma_f32 v[146:147], v[140:141], v[32:33], v[152:153]
	v_pk_fma_f32 v[140:141], v[138:139], v[28:29], v[150:151]
	v_cvt_pk_bf16_f32 v138, v142, v143
	v_lshl_add_u64 v[142:143], s[50:51], 0, v[190:191]
	v_pk_fma_f32 v[144:145], v[144:145], v[176:177], v[148:149]
	v_lshl_add_u64 v[142:143], v[142:143], 0, v[178:179]
	v_cvt_pk_bf16_f32 v139, v144, v145
	v_cvt_pk_bf16_f32 v140, v140, v141
	v_cvt_pk_bf16_f32 v141, v146, v147
	global_store_dwordx4 v[142:143], v[138:141], off sc1
	s_nop 1
	v_lshlrev_b32_e32 v138, 16, v18
	v_and_b32_e32 v139, 0xffff0000, v18
	v_lshlrev_b32_e32 v18, 16, v19
	v_and_b32_e32 v19, 0xffff0000, v19
	v_lshlrev_b32_e32 v140, 16, v20
	v_and_b32_e32 v141, 0xffff0000, v20
	v_lshlrev_b32_e32 v20, 16, v21
	v_and_b32_e32 v21, 0xffff0000, v21
	v_pk_fma_f32 v[136:137], v[136:137], v[172:173], v[18:19]
	v_pk_fma_f32 v[18:19], v[134:135], v[30:31], v[138:139]
	v_pk_fma_f32 v[132:133], v[132:133], v[26:27], v[20:21]
	v_pk_fma_f32 v[20:21], v[130:131], v[24:25], v[140:141]
	v_cvt_pk_bf16_f32 v18, v18, v19
	v_cvt_pk_bf16_f32 v19, v136, v137
	s_nop 0
	v_cvt_pk_bf16_f32 v20, v20, v21
	v_cvt_pk_bf16_f32 v21, v132, v133
	global_store_dwordx4 v[142:143], v[18:21], off offset:256 sc1
	s_nop 1
	v_lshlrev_b32_e32 v18, 16, v14
	v_and_b32_e32 v19, 0xffff0000, v14
	v_lshlrev_b32_e32 v14, 16, v15
	v_and_b32_e32 v15, 0xffff0000, v15
	v_lshlrev_b32_e32 v20, 16, v16
	v_and_b32_e32 v21, 0xffff0000, v16
	v_lshlrev_b32_e32 v16, 16, v17
	v_and_b32_e32 v17, 0xffff0000, v17
	v_pk_fma_f32 v[128:129], v[128:129], v[176:177], v[14:15]
	v_pk_fma_f32 v[14:15], v[126:127], v[174:175], v[18:19]
	v_pk_fma_f32 v[18:19], v[124:125], v[32:33], v[16:17]
	v_pk_fma_f32 v[16:17], v[122:123], v[28:29], v[20:21]
	v_cvt_pk_bf16_f32 v14, v14, v15
	v_cvt_pk_bf16_f32 v15, v128, v129
	s_nop 0
	v_cvt_pk_bf16_f32 v16, v16, v17
	v_cvt_pk_bf16_f32 v17, v18, v19
	v_lshl_add_u64 v[18:19], s[50:51], 0, v[188:189]
	v_lshl_add_u64 v[18:19], v[18:19], 0, v[178:179]
	global_store_dwordx4 v[18:19], v[14:17], off sc1
	s_nop 1
	v_lshlrev_b32_e32 v14, 16, v10
	v_and_b32_e32 v15, 0xffff0000, v10
	v_lshlrev_b32_e32 v10, 16, v11
	v_and_b32_e32 v11, 0xffff0000, v11
	v_lshlrev_b32_e32 v16, 16, v12
	v_and_b32_e32 v17, 0xffff0000, v12
	v_lshlrev_b32_e32 v12, 16, v13
	v_and_b32_e32 v13, 0xffff0000, v13
	v_pk_fma_f32 v[20:21], v[120:121], v[172:173], v[10:11]
	v_pk_fma_f32 v[10:11], v[118:119], v[30:31], v[14:15]
	v_pk_fma_f32 v[14:15], v[116:117], v[26:27], v[12:13]
	v_pk_fma_f32 v[12:13], v[114:115], v[24:25], v[16:17]
	v_cvt_pk_bf16_f32 v10, v10, v11
	v_cvt_pk_bf16_f32 v11, v20, v21
	v_lshl_add_u64 v[20:21], v[180:181], 0, s[4:5]
	v_cvt_pk_bf16_f32 v12, v12, v13
	v_cvt_pk_bf16_f32 v13, v14, v15
	global_store_dwordx4 v[18:19], v[10:13], off offset:256 sc1
	s_mov_b64 s[4:5], 0x90000
	v_lshl_add_u64 v[114:115], v[180:181], 0, s[4:5]
	v_lshlrev_b32_e32 v10, 16, v6
	v_and_b32_e32 v11, 0xffff0000, v6
	v_lshlrev_b32_e32 v6, 16, v7
	v_and_b32_e32 v7, 0xffff0000, v7
	v_lshlrev_b32_e32 v12, 16, v8
	v_and_b32_e32 v13, 0xffff0000, v8
	v_lshlrev_b32_e32 v8, 16, v9
	v_and_b32_e32 v9, 0xffff0000, v9
	v_pk_fma_f32 v[14:15], v[112:113], v[176:177], v[6:7]
	v_pk_fma_f32 v[6:7], v[110:111], v[174:175], v[10:11]
	v_pk_fma_f32 v[10:11], v[108:109], v[32:33], v[8:9]
	v_pk_fma_f32 v[8:9], v[106:107], v[28:29], v[12:13]
	v_cvt_pk_bf16_f32 v6, v6, v7
	v_cvt_pk_bf16_f32 v7, v14, v15
	s_mov_b64 s[4:5], 0xa0000
	v_cvt_pk_bf16_f32 v8, v8, v9
	v_cvt_pk_bf16_f32 v9, v10, v11
	v_lshl_add_u64 v[10:11], s[50:51], 0, v[184:185]
	v_lshl_add_u64 v[10:11], v[10:11], 0, v[178:179]
	global_store_dwordx4 v[10:11], v[6:9], off sc1
	v_lshl_add_u64 v[116:117], v[180:181], 0, s[4:5]
	s_mov_b64 s[4:5], 0xb0000
	v_lshlrev_b32_e32 v6, 16, v2
	v_and_b32_e32 v7, 0xffff0000, v2
	v_lshlrev_b32_e32 v2, 16, v3
	v_and_b32_e32 v3, 0xffff0000, v3
	v_lshlrev_b32_e32 v8, 16, v4
	v_and_b32_e32 v9, 0xffff0000, v4
	v_lshlrev_b32_e32 v4, 16, v5
	v_and_b32_e32 v5, 0xffff0000, v5
	v_pk_fma_f32 v[12:13], v[104:105], v[172:173], v[2:3]
	v_pk_fma_f32 v[2:3], v[102:103], v[30:31], v[6:7]
	v_pk_fma_f32 v[6:7], v[100:101], v[26:27], v[4:5]
	v_pk_fma_f32 v[4:5], v[98:99], v[24:25], v[8:9]
	v_cvt_pk_bf16_f32 v2, v2, v3
	v_cvt_pk_bf16_f32 v3, v12, v13
	v_lshl_add_u64 v[14:15], v[180:181], 0, s[4:5]
	v_cvt_pk_bf16_f32 v4, v4, v5
	v_cvt_pk_bf16_f32 v5, v6, v7
	global_store_dwordx4 v[10:11], v[2:5], off offset:256 sc1
	s_nop 1
	v_lshl_add_u64 v[2:3], v[186:187], 0, v[20:21]
	global_load_dwordx4 v[10:13], v[2:3], off
	global_load_dwordx4 v[16:19], v[2:3], off offset:256
	v_lshl_add_u64 v[2:3], v[186:187], 0, v[114:115]
	global_load_dwordx4 v[98:101], v[2:3], off
	global_load_dwordx4 v[102:105], v[2:3], off offset:256
	v_lshl_add_u64 v[2:3], v[186:187], 0, v[116:117]
	global_load_dwordx4 v[106:109], v[2:3], off
	global_load_dwordx4 v[110:113], v[2:3], off offset:256
	v_lshl_add_u64 v[2:3], v[186:187], 0, v[14:15]
	global_load_dwordx4 v[6:9], v[2:3], off
	s_nop 0
	global_load_dwordx4 v[2:5], v[2:3], off offset:256
	v_lshl_add_u64 v[20:21], s[50:51], 0, v[20:21]
	v_lshl_add_u64 v[20:21], v[20:21], 0, v[178:179]
	s_waitcnt vmcnt(0)
	v_lshlrev_b32_e32 v118, 16, v10
	v_and_b32_e32 v119, 0xffff0000, v10
	v_lshlrev_b32_e32 v10, 16, v11
	v_and_b32_e32 v11, 0xffff0000, v11
	v_lshlrev_b32_e32 v120, 16, v12
	v_and_b32_e32 v121, 0xffff0000, v12
	v_lshlrev_b32_e32 v12, 16, v13
	v_and_b32_e32 v13, 0xffff0000, v13
	v_pk_fma_f32 v[96:97], v[96:97], v[176:177], v[10:11]
	v_pk_fma_f32 v[10:11], v[94:95], v[174:175], v[118:119]
	v_pk_fma_f32 v[92:93], v[92:93], v[32:33], v[12:13]
	v_pk_fma_f32 v[12:13], v[90:91], v[28:29], v[120:121]
	v_cvt_pk_bf16_f32 v10, v10, v11
	v_cvt_pk_bf16_f32 v11, v96, v97
	s_nop 0
	v_cvt_pk_bf16_f32 v12, v12, v13
	v_cvt_pk_bf16_f32 v13, v92, v93
	global_store_dwordx4 v[20:21], v[10:13], off sc1
	s_nop 1
	v_lshlrev_b32_e32 v10, 16, v16
	v_and_b32_e32 v11, 0xffff0000, v16
	v_lshlrev_b32_e32 v12, 16, v17
	v_and_b32_e32 v13, 0xffff0000, v17
	v_lshlrev_b32_e32 v16, 16, v18
	v_and_b32_e32 v17, 0xffff0000, v18
	v_lshlrev_b32_e32 v18, 16, v19
	v_and_b32_e32 v19, 0xffff0000, v19
	v_pk_fma_f32 v[12:13], v[88:89], v[172:173], v[12:13]
	v_pk_fma_f32 v[10:11], v[86:87], v[30:31], v[10:11]
	v_pk_fma_f32 v[18:19], v[84:85], v[26:27], v[18:19]
	v_pk_fma_f32 v[16:17], v[82:83], v[24:25], v[16:17]
	v_cvt_pk_bf16_f32 v10, v10, v11
	v_cvt_pk_bf16_f32 v11, v12, v13
	s_nop 0
	v_cvt_pk_bf16_f32 v12, v16, v17
	v_cvt_pk_bf16_f32 v13, v18, v19
	global_store_dwordx4 v[20:21], v[10:13], off offset:256 sc1
	v_lshlrev_b32_e32 v16, 16, v100
	v_and_b32_e32 v17, 0xffff0000, v100
	v_lshlrev_b32_e32 v10, 16, v98
	v_and_b32_e32 v11, 0xffff0000, v98
	v_lshlrev_b32_e32 v12, 16, v99
	v_and_b32_e32 v13, 0xffff0000, v99
	v_pk_fma_f32 v[12:13], v[80:81], v[176:177], v[12:13]
	v_pk_fma_f32 v[10:11], v[78:79], v[174:175], v[10:11]
	v_pk_fma_f32 v[16:17], v[74:75], v[28:29], v[16:17]
	v_lshlrev_b32_e32 v18, 16, v101
	v_and_b32_e32 v19, 0xffff0000, v101
	v_cvt_pk_bf16_f32 v10, v10, v11
	v_cvt_pk_bf16_f32 v11, v12, v13
	v_cvt_pk_bf16_f32 v12, v16, v17
	v_lshl_add_u64 v[16:17], s[50:51], 0, v[114:115]
	v_pk_fma_f32 v[18:19], v[76:77], v[32:33], v[18:19]
	v_lshl_add_u64 v[16:17], v[16:17], 0, v[178:179]
	v_cvt_pk_bf16_f32 v13, v18, v19
	global_store_dwordx4 v[16:17], v[10:13], off sc1
	v_lshlrev_b32_e32 v18, 16, v104
	v_and_b32_e32 v19, 0xffff0000, v104
	v_lshlrev_b32_e32 v10, 16, v102
	v_and_b32_e32 v11, 0xffff0000, v102
	v_lshlrev_b32_e32 v12, 16, v103
	v_and_b32_e32 v13, 0xffff0000, v103
	v_lshlrev_b32_e32 v20, 16, v105
	v_and_b32_e32 v21, 0xffff0000, v105
	v_pk_fma_f32 v[12:13], v[72:73], v[172:173], v[12:13]
	v_pk_fma_f32 v[10:11], v[70:71], v[30:31], v[10:11]
	v_pk_fma_f32 v[20:21], v[68:69], v[26:27], v[20:21]
	v_pk_fma_f32 v[18:19], v[66:67], v[24:25], v[18:19]
	v_cvt_pk_bf16_f32 v10, v10, v11
	v_cvt_pk_bf16_f32 v11, v12, v13
	s_nop 0
	v_cvt_pk_bf16_f32 v12, v18, v19
	v_cvt_pk_bf16_f32 v13, v20, v21
	global_store_dwordx4 v[16:17], v[10:13], off offset:256 sc1
	v_lshlrev_b32_e32 v16, 16, v108
	v_and_b32_e32 v17, 0xffff0000, v108
	v_lshlrev_b32_e32 v10, 16, v106
	v_and_b32_e32 v11, 0xffff0000, v106
	v_lshlrev_b32_e32 v12, 16, v107
	v_and_b32_e32 v13, 0xffff0000, v107
	v_pk_fma_f32 v[12:13], v[64:65], v[176:177], v[12:13]
	v_pk_fma_f32 v[10:11], v[62:63], v[174:175], v[10:11]
	v_pk_fma_f32 v[16:17], v[58:59], v[28:29], v[16:17]
	v_lshlrev_b32_e32 v18, 16, v109
	v_and_b32_e32 v19, 0xffff0000, v109
	v_cvt_pk_bf16_f32 v10, v10, v11
	v_cvt_pk_bf16_f32 v11, v12, v13
	v_cvt_pk_bf16_f32 v12, v16, v17
	v_lshl_add_u64 v[16:17], s[50:51], 0, v[116:117]
	v_pk_fma_f32 v[18:19], v[60:61], v[32:33], v[18:19]
	v_lshl_add_u64 v[16:17], v[16:17], 0, v[178:179]
	v_cvt_pk_bf16_f32 v13, v18, v19
	global_store_dwordx4 v[16:17], v[10:13], off sc1
	v_lshlrev_b32_e32 v18, 16, v112
	v_and_b32_e32 v19, 0xffff0000, v112
	v_lshlrev_b32_e32 v10, 16, v110
	v_and_b32_e32 v11, 0xffff0000, v110
	v_lshlrev_b32_e32 v12, 16, v111
	v_and_b32_e32 v13, 0xffff0000, v111
	v_lshlrev_b32_e32 v20, 16, v113
	v_and_b32_e32 v21, 0xffff0000, v113
	v_pk_fma_f32 v[12:13], v[56:57], v[172:173], v[12:13]
	v_pk_fma_f32 v[10:11], v[54:55], v[30:31], v[10:11]
	v_pk_fma_f32 v[20:21], v[52:53], v[26:27], v[20:21]
	v_pk_fma_f32 v[18:19], v[50:51], v[24:25], v[18:19]
	v_cvt_pk_bf16_f32 v10, v10, v11
	v_cvt_pk_bf16_f32 v11, v12, v13
	s_nop 0
	v_cvt_pk_bf16_f32 v12, v18, v19
	v_cvt_pk_bf16_f32 v13, v20, v21
	global_store_dwordx4 v[16:17], v[10:13], off offset:256 sc1
	s_nop 1
	v_lshlrev_b32_e32 v10, 16, v6
	v_and_b32_e32 v11, 0xffff0000, v6
	v_lshlrev_b32_e32 v6, 16, v7
	v_and_b32_e32 v7, 0xffff0000, v7
	v_lshlrev_b32_e32 v12, 16, v8
	v_and_b32_e32 v13, 0xffff0000, v8
	v_lshlrev_b32_e32 v8, 16, v9
	v_and_b32_e32 v9, 0xffff0000, v9
	v_pk_fma_f32 v[16:17], v[48:49], v[176:177], v[6:7]
	v_pk_fma_f32 v[6:7], v[46:47], v[174:175], v[10:11]
	v_pk_fma_f32 v[10:11], v[44:45], v[32:33], v[8:9]
	v_pk_fma_f32 v[8:9], v[42:43], v[28:29], v[12:13]
	v_cvt_pk_bf16_f32 v6, v6, v7
	v_cvt_pk_bf16_f32 v7, v16, v17
	s_nop 0
	v_cvt_pk_bf16_f32 v8, v8, v9
	v_cvt_pk_bf16_f32 v9, v10, v11
	v_lshl_add_u64 v[10:11], s[50:51], 0, v[14:15]
	v_lshl_add_u64 v[10:11], v[10:11], 0, v[178:179]
	global_store_dwordx4 v[10:11], v[6:9], off sc1
	s_nop 1
	v_lshlrev_b32_e32 v6, 16, v2
	v_and_b32_e32 v7, 0xffff0000, v2
	v_lshlrev_b32_e32 v2, 16, v3
	v_and_b32_e32 v3, 0xffff0000, v3
	v_lshlrev_b32_e32 v8, 16, v4
	v_and_b32_e32 v9, 0xffff0000, v4
	v_lshlrev_b32_e32 v4, 16, v5
	v_and_b32_e32 v5, 0xffff0000, v5
	v_pk_fma_f32 v[10:11], v[40:41], v[172:173], v[2:3]
	v_pk_fma_f32 v[2:3], v[38:39], v[30:31], v[6:7]
	v_pk_fma_f32 v[6:7], v[36:37], v[26:27], v[4:5]
	v_pk_fma_f32 v[4:5], v[34:35], v[24:25], v[8:9]
	v_cvt_pk_bf16_f32 v2, v2, v3
	v_cvt_pk_bf16_f32 v3, v10, v11
	s_nop 0
	v_cvt_pk_bf16_f32 v4, v4, v5
	v_cvt_pk_bf16_f32 v5, v6, v7
.LBB0_1227:
	v_lshl_add_u64 v[6:7], s[50:51], 0, v[14:15]
	v_lshl_add_u64 v[6:7], v[22:23], 1, v[6:7]
	s_and_b64 vcc, exec, s[38:39]
	s_mov_b64 s[4:5], -1
	global_store_dwordx4 v[6:7], v[2:5], off offset:256 sc1
	s_cbranch_vccnz .LBB0_1207
	s_andn2_b64 vcc, exec, s[48:49]
	s_cbranch_vccnz .LBB0_1206
	s_barrier
	s_branch .LBB0_1206

.LBB0_1613:
	s_add_u32 s2, s0, s17
	s_addc_u32 s3, s1, s18
	global_load_dwordx4 v[106:109], v65, s[2:3]
	v_add_co_u32_e32 v84, vcc, s13, v80
	v_lshl_add_u64 v[82:83], s[0:1], 0, v[78:79]
	s_nop 0
	v_addc_co_u32_e32 v85, vcc, -1, v81, vcc
	v_add_co_u32_e32 v82, vcc, 0x11100000, v82
	s_add_i32 s15, s15, s66
	s_nop 0
	v_addc_co_u32_e32 v83, vcc, 0, v83, vcc
	global_load_dwordx2 v[110:111], v[82:83], off
	global_load_dwordx2 v[112:113], v[82:83], off offset:512
	global_load_dwordx2 v[114:115], v[82:83], off offset:1024
	global_load_dwordx2 v[116:117], v[82:83], off offset:1536
	global_load_dwordx2 v[118:119], v[82:83], off offset:2048
	global_load_dwordx2 v[120:121], v[82:83], off offset:2560
	global_load_dwordx2 v[122:123], v[82:83], off offset:3072
	global_load_dwordx2 v[124:125], v[82:83], off offset:3584
	v_lshl_add_u64 v[78:79], v[78:79], 0, s[94:95]
	s_waitcnt vmcnt(8)
	v_readfirstlane_b32 s2, v106
	v_readfirstlane_b32 s3, v107
	s_lshr_b32 s4, s2, 18
	s_lshl_b32 s2, s2, 11
	s_lshr_b32 s11, s3, 18
	s_and_b32 s19, s4, 0x3ffc
	s_and_b32 s4, s2, 0x7ffff800
	s_and_b32 s2, s11, 0x3ffc
	s_add_i32 s11, s81, s19
	s_add_i32 s2, s81, s2
	v_mov_b32_e32 v105, s11
	v_mov_b32_e32 v139, s2
	ds_read_b32 v138, v105
	ds_read_b32 v140, v139
	s_lshl_b32 s3, s3, 11
	v_pk_mul_f32 v[82:83], v[108:109], s[8:9] op_sel_hi:[1,0]
	s_waitcnt vmcnt(7)
	v_lshlrev_b32_e32 v106, 16, v110
	s_waitcnt lgkmcnt(1)
	v_ashrrev_i32_e32 v139, 31, v138
	s_waitcnt lgkmcnt(0)
	v_ashrrev_i32_e32 v141, 31, v140
	v_lshlrev_b64 v[138:139], 19, v[138:139]
	v_lshlrev_b64 v[140:141], 19, v[140:141]
	v_lshl_add_u64 v[138:139], s[6:7], 0, v[138:139]
	v_lshl_add_u64 v[140:141], s[6:7], 0, v[140:141]
	v_lshl_add_u64 v[138:139], v[138:139], 0, s[4:5]
	s_and_b32 s4, s3, 0x7ffff800
	v_lshl_add_u64 v[140:141], v[140:141], 0, s[4:5]
	v_readfirstlane_b32 s2, v138
	v_readfirstlane_b32 s3, v139
	s_nop 4
	global_load_dword v105, v93, s[2:3]
	global_load_dword v139, v93, s[2:3] offset:256
	global_load_dword v143, v93, s[2:3] offset:512
	global_load_dword v145, v93, s[2:3] offset:768
	global_load_dword v147, v93, s[2:3] offset:1024
	global_load_dword v149, v93, s[2:3] offset:1280
	global_load_dword v151, v93, s[2:3] offset:1536
	global_load_dword v153, v93, s[2:3] offset:1792
	v_readfirstlane_b32 s2, v140
	v_readfirstlane_b32 s3, v141
	s_nop 4
	global_load_dword v155, v93, s[2:3]
	global_load_dword v157, v93, s[2:3] offset:256
	global_load_dword v159, v93, s[2:3] offset:512
	global_load_dword v167, v93, s[2:3] offset:768
	global_load_dword v175, v93, s[2:3] offset:1024
	global_load_dword v183, v93, s[2:3] offset:1280
	global_load_dword v191, v93, s[2:3] offset:1536
	global_load_dword v199, v93, s[2:3] offset:1792
	v_and_b32_e32 v107, 0xffff0000, v110
	v_lshlrev_b32_e32 v108, 16, v111
	v_and_b32_e32 v109, 0xffff0000, v111
	s_waitcnt vmcnt(22)
	v_lshlrev_b32_e32 v110, 16, v112
	v_and_b32_e32 v111, 0xffff0000, v112
	v_lshlrev_b32_e32 v112, 16, v113
	v_and_b32_e32 v113, 0xffff0000, v113
	s_waitcnt vmcnt(21)
	v_lshlrev_b32_e32 v126, 16, v114
	v_and_b32_e32 v127, 0xffff0000, v114
	v_lshlrev_b32_e32 v114, 16, v115
	v_and_b32_e32 v115, 0xffff0000, v115
	s_waitcnt vmcnt(16)
	v_lshlrev_b32_e32 v136, 16, v124
	v_and_b32_e32 v137, 0xffff0000, v124
	v_lshlrev_b32_e32 v124, 16, v125
	v_and_b32_e32 v125, 0xffff0000, v125
	v_lshlrev_b32_e32 v128, 16, v116
	v_and_b32_e32 v129, 0xffff0000, v116
	v_lshlrev_b32_e32 v116, 16, v117
	v_and_b32_e32 v117, 0xffff0000, v117
	v_lshlrev_b32_e32 v130, 16, v118
	v_and_b32_e32 v131, 0xffff0000, v118
	v_lshlrev_b32_e32 v118, 16, v119
	v_and_b32_e32 v119, 0xffff0000, v119
	v_lshlrev_b32_e32 v132, 16, v120
	v_and_b32_e32 v133, 0xffff0000, v120
	v_lshlrev_b32_e32 v120, 16, v121
	v_and_b32_e32 v121, 0xffff0000, v121
	v_lshlrev_b32_e32 v134, 16, v122
	v_and_b32_e32 v135, 0xffff0000, v122
	v_lshlrev_b32_e32 v122, 16, v123
	v_and_b32_e32 v123, 0xffff0000, v123
	s_add_u32 s17, s17, s68
	s_addc_u32 s18, s18, s69
	s_cmp_ge_i32 s15, s16
	s_waitcnt vmcnt(15)
	v_cvt_f32_fp8_sdwa v140, v105 src0_sel:BYTE_1
	v_cvt_f32_fp8_sdwa v144, v105 src0_sel:BYTE_3
	s_waitcnt vmcnt(14)
	v_cvt_f32_fp8_sdwa v148, v139 src0_sel:BYTE_1
	v_cvt_f32_fp8_sdwa v152, v139 src0_sel:BYTE_3
	s_waitcnt vmcnt(12)
	v_cvt_f32_fp8_e32 v162, v145
	v_cvt_f32_fp8_sdwa v164, v145 src0_sel:BYTE_1
	v_cvt_f32_fp8_sdwa v166, v145 src0_sel:BYTE_2
	v_cvt_f32_fp8_sdwa v168, v145 src0_sel:BYTE_3
	s_waitcnt vmcnt(10)
	v_cvt_f32_fp8_e32 v178, v149
	v_cvt_f32_fp8_sdwa v180, v149 src0_sel:BYTE_1
	v_cvt_f32_fp8_sdwa v182, v149 src0_sel:BYTE_2
	v_cvt_f32_fp8_sdwa v184, v149 src0_sel:BYTE_3
	s_waitcnt vmcnt(8)
	v_cvt_f32_fp8_e32 v194, v153
	v_cvt_f32_fp8_sdwa v196, v153 src0_sel:BYTE_1
	v_cvt_f32_fp8_sdwa v198, v153 src0_sel:BYTE_2
	v_cvt_f32_fp8_sdwa v200, v153 src0_sel:BYTE_3
	s_waitcnt vmcnt(7)
	v_cvt_f32_fp8_e32 v141, v155
	v_cvt_f32_fp8_sdwa v145, v155 src0_sel:BYTE_2
	s_waitcnt vmcnt(6)
	v_cvt_f32_fp8_e32 v149, v157
	v_cvt_f32_fp8_sdwa v153, v157 src0_sel:BYTE_2
	v_cvt_f32_fp8_e32 v138, v105
	v_cvt_f32_fp8_sdwa v142, v105 src0_sel:BYTE_2
	v_cvt_f32_fp8_e32 v146, v139
	v_cvt_f32_fp8_sdwa v150, v139 src0_sel:BYTE_2
	v_cvt_f32_fp8_e32 v154, v143
	v_cvt_f32_fp8_sdwa v156, v143 src0_sel:BYTE_1
	v_cvt_f32_fp8_sdwa v158, v143 src0_sel:BYTE_2
	v_cvt_f32_fp8_sdwa v160, v143 src0_sel:BYTE_3
	v_cvt_f32_fp8_e32 v170, v147
	v_cvt_f32_fp8_sdwa v172, v147 src0_sel:BYTE_1
	v_cvt_f32_fp8_sdwa v174, v147 src0_sel:BYTE_2
	v_cvt_f32_fp8_sdwa v176, v147 src0_sel:BYTE_3
	v_cvt_f32_fp8_e32 v186, v151
	v_cvt_f32_fp8_sdwa v188, v151 src0_sel:BYTE_1
	v_cvt_f32_fp8_sdwa v190, v151 src0_sel:BYTE_2
	v_cvt_f32_fp8_sdwa v192, v151 src0_sel:BYTE_3
	v_cvt_f32_fp8_sdwa v139, v155 src0_sel:BYTE_1
	v_cvt_f32_fp8_sdwa v143, v155 src0_sel:BYTE_3
	v_cvt_f32_fp8_sdwa v147, v157 src0_sel:BYTE_1
	v_cvt_f32_fp8_sdwa v151, v157 src0_sel:BYTE_3
	s_waitcnt vmcnt(5)
	v_cvt_f32_fp8_e32 v157, v159
	v_cvt_f32_fp8_sdwa v161, v159 src0_sel:BYTE_2
	s_waitcnt vmcnt(4)
	v_cvt_f32_fp8_e32 v165, v167
	v_cvt_f32_fp8_sdwa v169, v167 src0_sel:BYTE_2
	s_waitcnt vmcnt(3)
	v_cvt_f32_fp8_e32 v173, v175
	v_cvt_f32_fp8_sdwa v177, v175 src0_sel:BYTE_2
	s_waitcnt vmcnt(2)
	v_cvt_f32_fp8_e32 v181, v183
	v_cvt_f32_fp8_sdwa v185, v183 src0_sel:BYTE_2
	s_waitcnt vmcnt(1)
	v_cvt_f32_fp8_e32 v189, v191
	v_cvt_f32_fp8_sdwa v193, v191 src0_sel:BYTE_2
	s_waitcnt vmcnt(0)
	v_cvt_f32_fp8_e32 v197, v199
	v_cvt_f32_fp8_sdwa v201, v199 src0_sel:BYTE_2
	v_cvt_f32_fp8_sdwa v155, v159 src0_sel:BYTE_1
	v_cvt_f32_fp8_sdwa v159, v159 src0_sel:BYTE_3
	v_cvt_f32_fp8_sdwa v163, v167 src0_sel:BYTE_1
	v_cvt_f32_fp8_sdwa v167, v167 src0_sel:BYTE_3
	v_cvt_f32_fp8_sdwa v171, v175 src0_sel:BYTE_1
	v_cvt_f32_fp8_sdwa v175, v175 src0_sel:BYTE_3
	v_cvt_f32_fp8_sdwa v179, v183 src0_sel:BYTE_1
	v_cvt_f32_fp8_sdwa v183, v183 src0_sel:BYTE_3
	v_cvt_f32_fp8_sdwa v187, v191 src0_sel:BYTE_1
	v_cvt_f32_fp8_sdwa v191, v191 src0_sel:BYTE_3
	v_cvt_f32_fp8_sdwa v195, v199 src0_sel:BYTE_1
	v_cvt_f32_fp8_sdwa v199, v199 src0_sel:BYTE_3
	v_pk_mul_f32 v[140:141], v[82:83], v[140:141]
	v_pk_mul_f32 v[144:145], v[82:83], v[144:145]
	v_pk_mul_f32 v[148:149], v[82:83], v[148:149]
	v_pk_mul_f32 v[152:153], v[82:83], v[152:153]
	v_pk_mul_f32 v[156:157], v[82:83], v[156:157]
	v_pk_mul_f32 v[160:161], v[82:83], v[160:161]
	v_pk_mul_f32 v[164:165], v[82:83], v[164:165]
	v_pk_mul_f32 v[168:169], v[82:83], v[168:169]
	v_pk_mul_f32 v[172:173], v[82:83], v[172:173]
	v_pk_mul_f32 v[176:177], v[82:83], v[176:177]
	v_pk_mul_f32 v[180:181], v[82:83], v[180:181]
	v_pk_mul_f32 v[184:185], v[82:83], v[184:185]
	v_pk_mul_f32 v[188:189], v[82:83], v[188:189]
	v_pk_mul_f32 v[192:193], v[82:83], v[192:193]
	v_pk_mul_f32 v[196:197], v[82:83], v[196:197]
	v_pk_mul_f32 v[200:201], v[82:83], v[200:201]
	v_pk_fma_f32 v[138:139], v[82:83], v[138:139], v[140:141] op_sel:[0,0,1] op_sel_hi:[1,1,0]
	v_pk_fma_f32 v[140:141], v[82:83], v[142:143], v[144:145] op_sel:[0,0,1] op_sel_hi:[1,1,0]
	v_pk_fma_f32 v[142:143], v[82:83], v[146:147], v[148:149] op_sel:[0,0,1] op_sel_hi:[1,1,0]
	v_pk_fma_f32 v[144:145], v[82:83], v[150:151], v[152:153] op_sel:[0,0,1] op_sel_hi:[1,1,0]
	v_pk_fma_f32 v[146:147], v[82:83], v[154:155], v[156:157] op_sel:[0,0,1] op_sel_hi:[1,1,0]
	v_pk_fma_f32 v[148:149], v[82:83], v[158:159], v[160:161] op_sel:[0,0,1] op_sel_hi:[1,1,0]
	v_pk_fma_f32 v[150:151], v[82:83], v[162:163], v[164:165] op_sel:[0,0,1] op_sel_hi:[1,1,0]
	v_pk_fma_f32 v[152:153], v[82:83], v[166:167], v[168:169] op_sel:[0,0,1] op_sel_hi:[1,1,0]
	v_pk_fma_f32 v[154:155], v[82:83], v[170:171], v[172:173] op_sel:[0,0,1] op_sel_hi:[1,1,0]
	v_pk_fma_f32 v[156:157], v[82:83], v[174:175], v[176:177] op_sel:[0,0,1] op_sel_hi:[1,1,0]
	v_pk_fma_f32 v[158:159], v[82:83], v[178:179], v[180:181] op_sel:[0,0,1] op_sel_hi:[1,1,0]
	v_pk_fma_f32 v[160:161], v[82:83], v[182:183], v[184:185] op_sel:[0,0,1] op_sel_hi:[1,1,0]
	v_pk_fma_f32 v[162:163], v[82:83], v[186:187], v[188:189] op_sel:[0,0,1] op_sel_hi:[1,1,0]
	v_pk_fma_f32 v[164:165], v[82:83], v[190:191], v[192:193] op_sel:[0,0,1] op_sel_hi:[1,1,0]
	v_pk_fma_f32 v[166:167], v[82:83], v[194:195], v[196:197] op_sel:[0,0,1] op_sel_hi:[1,1,0]
	v_pk_fma_f32 v[82:83], v[82:83], v[198:199], v[200:201] op_sel:[0,0,1] op_sel_hi:[1,1,0]
	v_pk_fma_f32 v[108:109], v[10:11], v[140:141], v[108:109]
	v_pk_fma_f32 v[106:107], v[8:9], v[138:139], v[106:107]
	v_pk_fma_f32 v[112:113], v[14:15], v[144:145], v[112:113]
	v_pk_fma_f32 v[110:111], v[12:13], v[142:143], v[110:111]
	v_pk_fma_f32 v[114:115], v[26:27], v[148:149], v[114:115]
	v_pk_fma_f32 v[126:127], v[24:25], v[146:147], v[126:127]
	v_pk_fma_f32 v[82:83], v[62:63], v[82:83], v[124:125]
	v_pk_fma_f32 v[124:125], v[60:61], v[166:167], v[136:137]
	v_mul_f32_e32 v105, v107, v107
	v_mul_f32_e32 v136, v109, v109
	v_mul_f32_e32 v137, v111, v111
	v_mul_f32_e32 v138, v113, v113
	v_pk_fma_f32 v[116:117], v[30:31], v[152:153], v[116:117]
	v_pk_fma_f32 v[128:129], v[28:29], v[150:151], v[128:129]
	v_mul_f32_e32 v139, v127, v127
	v_mul_f32_e32 v140, v115, v115
	v_fmac_f32_e32 v105, v106, v106
	v_fmac_f32_e32 v136, v108, v108
	v_fmac_f32_e32 v137, v110, v110
	v_fmac_f32_e32 v138, v112, v112
	v_pk_fma_f32 v[118:119], v[42:43], v[156:157], v[118:119]
	v_pk_fma_f32 v[130:131], v[40:41], v[154:155], v[130:131]
	v_mul_f32_e32 v141, v129, v129
	v_mul_f32_e32 v142, v117, v117
	v_fmac_f32_e32 v139, v126, v126
	v_fmac_f32_e32 v140, v114, v114
	v_add_f32_e32 v105, v105, v136
	v_add_f32_e32 v136, v137, v138
	v_pk_fma_f32 v[120:121], v[46:47], v[160:161], v[120:121]
	v_pk_fma_f32 v[132:133], v[44:45], v[158:159], v[132:133]
	v_mul_f32_e32 v143, v131, v131
	v_mul_f32_e32 v144, v119, v119
	v_fmac_f32_e32 v141, v128, v128
	v_fmac_f32_e32 v142, v116, v116
	v_add_f32_e32 v137, v139, v140
	v_add_f32_e32 v105, v105, v136
	v_pk_fma_f32 v[122:123], v[58:59], v[164:165], v[122:123]
	v_pk_fma_f32 v[134:135], v[56:57], v[162:163], v[134:135]
	v_mul_f32_e32 v145, v133, v133
	v_mul_f32_e32 v146, v121, v121
	v_fmac_f32_e32 v143, v130, v130
	v_fmac_f32_e32 v144, v118, v118
	v_add_f32_e32 v138, v141, v142
	v_add_f32_e32 v105, v105, v137
	v_mul_f32_e32 v147, v135, v135
	v_mul_f32_e32 v148, v123, v123
	v_fmac_f32_e32 v145, v132, v132
	v_fmac_f32_e32 v146, v120, v120
	v_add_f32_e32 v139, v143, v144
	v_add_f32_e32 v105, v105, v138
	v_mul_f32_e32 v149, v125, v125
	v_mul_f32_e32 v150, v83, v83
	v_fmac_f32_e32 v147, v134, v134
	v_fmac_f32_e32 v148, v122, v122
	v_add_f32_e32 v140, v145, v146
	v_add_f32_e32 v105, v105, v139
	v_fmac_f32_e32 v149, v124, v124
	v_fmac_f32_e32 v150, v82, v82
	v_add_f32_e32 v141, v147, v148
	v_add_f32_e32 v105, v105, v140
	v_add_f32_e32 v142, v149, v150
	v_add_f32_e32 v105, v105, v141
	v_add_f32_e32 v105, v105, v142
	ds_bpermute_b32 v136, v101, v105
	s_waitcnt lgkmcnt(0)
	v_add_f32_e32 v105, v105, v136
	ds_bpermute_b32 v136, v102, v105
	s_waitcnt lgkmcnt(0)
	v_add_f32_e32 v105, v105, v136
	ds_bpermute_b32 v136, v103, v105
	s_waitcnt lgkmcnt(0)
	v_add_f32_e32 v105, v105, v136
	ds_bpermute_b32 v136, v104, v105
	s_waitcnt lgkmcnt(0)
	v_add_f32_e32 v105, v105, v136
	v_mov_b32_e32 v136, v105
	s_nop 1
	v_permlane16_swap_b32_e32 v105, v136
	v_add_f32_e32 v105, v105, v136
	v_mov_b32_e32 v136, v105
	s_nop 1
	v_permlane32_swap_b32_e32 v105, v136
	v_add_f32_e32 v105, v105, v136
	v_fmamk_f32 v105, v105, 0x3a000000, v94
	v_mul_f32_e32 v136, 0x4f800000, v105
	v_cmp_gt_f32_e32 vcc, s12, v105
	s_nop 1
	v_cndmask_b32_e32 v105, v105, v136, vcc
	v_sqrt_f32_e32 v136, v105
	s_nop 0
	v_add_u32_e32 v137, -1, v136
	v_add_u32_e32 v138, 1, v136
	v_fma_f32 v139, -v137, v136, v105
	v_fma_f32 v140, -v138, v136, v105
	v_cmp_ge_f32_e64 s[2:3], 0, v139
	s_nop 1
	v_cndmask_b32_e64 v136, v136, v137, s[2:3]
	v_cmp_lt_f32_e64 s[2:3], 0, v140
	s_nop 1
	v_cndmask_b32_e64 v136, v136, v138, s[2:3]
	v_mul_f32_e32 v137, 0x37800000, v136
	v_cndmask_b32_e32 v136, v136, v137, vcc
	v_cmp_class_f32_e32 vcc, v105, v95
	s_nop 1
	v_cndmask_b32_e32 v105, v136, v105, vcc
	v_div_scale_f32 v136, s[2:3], v105, v105, 1.0
	v_rcp_f32_e32 v138, v136
	v_div_scale_f32 v137, vcc, 1.0, v105, 1.0
	v_fma_f32 v139, -v136, v138, 1.0
	v_fmac_f32_e32 v138, v139, v138
	v_mul_f32_e32 v139, v137, v138
	v_fma_f32 v140, -v136, v139, v137
	v_fmac_f32_e32 v139, v140, v138
	v_fma_f32 v136, -v136, v139, v137
	v_div_fmas_f32 v136, v136, v138, v139
	v_div_fixup_f32 v136, v136, v105, 1.0
	v_pk_mul_f32 v[106:107], v[106:107], v[136:137] op_sel_hi:[1,0]
	v_pk_mul_f32 v[108:109], v[108:109], v[136:137] op_sel_hi:[1,0]
	v_pk_mul_f32 v[110:111], v[110:111], v[136:137] op_sel_hi:[1,0]
	v_pk_mul_f32 v[112:113], v[112:113], v[136:137] op_sel_hi:[1,0]
	v_pk_mul_f32 v[126:127], v[126:127], v[136:137] op_sel_hi:[1,0]
	v_pk_mul_f32 v[114:115], v[114:115], v[136:137] op_sel_hi:[1,0]
	v_pk_mul_f32 v[128:129], v[128:129], v[136:137] op_sel_hi:[1,0]
	v_pk_mul_f32 v[138:139], v[116:117], v[136:137] op_sel_hi:[1,0]
	v_pk_mul_f32 v[130:131], v[130:131], v[136:137] op_sel_hi:[1,0]
	v_pk_mul_f32 v[140:141], v[118:119], v[136:137] op_sel_hi:[1,0]
	v_pk_mul_f32 v[132:133], v[132:133], v[136:137] op_sel_hi:[1,0]
	v_pk_mul_f32 v[142:143], v[120:121], v[136:137] op_sel_hi:[1,0]
	v_pk_mul_f32 v[134:135], v[134:135], v[136:137] op_sel_hi:[1,0]
	v_pk_mul_f32 v[144:145], v[122:123], v[136:137] op_sel_hi:[1,0]
	v_pk_mul_f32 v[146:147], v[124:125], v[136:137] op_sel_hi:[1,0]
	v_pk_mul_f32 v[82:83], v[82:83], v[136:137] op_sel_hi:[1,0]
	v_pk_mul_f32 v[108:109], v[2:3], v[108:109]
	v_pk_mul_f32 v[106:107], v[0:1], v[106:107]
	v_pk_mul_f32 v[112:113], v[6:7], v[112:113]
	v_pk_mul_f32 v[110:111], v[4:5], v[110:111]
	v_pk_mul_f32 v[116:117], v[18:19], v[114:115]
	v_pk_mul_f32 v[114:115], v[16:17], v[126:127]
	v_pk_mul_f32 v[120:121], v[22:23], v[138:139]
	v_pk_mul_f32 v[118:119], v[20:21], v[128:129]
	v_pk_mul_f32 v[124:125], v[34:35], v[140:141]
	v_pk_mul_f32 v[122:123], v[32:33], v[130:131]
	v_pk_mul_f32 v[128:129], v[38:39], v[142:143]
	v_pk_mul_f32 v[126:127], v[36:37], v[132:133]
	v_pk_mul_f32 v[132:133], v[50:51], v[144:145]
	v_pk_mul_f32 v[130:131], v[48:49], v[134:135]
	v_pk_mul_f32 v[136:137], v[54:55], v[82:83]
	v_pk_mul_f32 v[134:135], v[52:53], v[146:147]
	global_store_dwordx4 v[84:85], v[106:109], off offset:-3072 sc1
	global_store_dwordx4 v[84:85], v[110:113], off offset:-2048 sc1
	global_store_dwordx4 v[84:85], v[114:117], off offset:-1024 sc1
	global_store_dwordx4 v[80:81], v[118:121], off offset:-4096 sc1
	global_store_dwordx4 v[80:81], v[122:125], off offset:-3072 sc1
	global_store_dwordx4 v[80:81], v[126:129], off offset:-2048 sc1
	global_store_dwordx4 v[80:81], v[130:133], off offset:-1024 sc1
	global_store_dwordx4 v[80:81], v[134:137], off sc1
	v_lshl_add_u64 v[80:81], v[80:81], 0, s[24:25]
	s_cbranch_scc0 .LBB0_1613
	s_branch .LBB0_1610
